# LDS-DMA in SGPR-base + 32-bit VGPR offset form (drops the 64-bit VALU address add) at 194 sites
# speedup vs baseline: 1.0055x; 1.0055x over previous
.LBB0_411:
	s_add_u32 s14, s14, 0xac00000
	s_addc_u32 s15, s15, 0
	s_add_u32 s16, s16, 0x1f00000
	s_addc_u32 s17, s17, 0
	s_lshl_b32 s8, s8, 5
	s_and_b32 s20, s8, 0x60
	s_add_i32 m0, s45, 0x18000
	v_lshl_add_u64 v[8:9], v[8:9], 0, s[56:57]
	s_lshl_b32 s18, s5, 13
	s_lshl_b32 s19, s20, 7
	s_waitcnt vmcnt(2)
	s_barrier
	global_load_lds_dwordx4 v[8:9], off
	v_lshl_add_u64 v[6:7], v[6:7], 0, s[56:57]
	s_add_i32 m0, s45, 0x1a000
	s_add_i32 s49, s45, 0x8000
	s_add_i32 s52, s45, 0xa000
	global_load_lds_dwordx4 v[6:7], off
	v_lshl_add_u64 v[2:3], v[2:3], 0, s[56:57]
	s_mov_b32 m0, s49
	s_add_u32 s8, s6, 0x40080
	global_load_lds_dwordx4 v[2:3], off
	v_lshl_add_u64 v[2:3], v[4:5], 0, s[56:57]
	s_mov_b32 m0, s52
	s_addc_u32 s9, s7, 0
	global_load_lds_dwordx4 v[2:3], off
	s_add_i32 m0, s45, 0x1c000
	s_nop 0
	global_load_lds_dwordx4 v0, s[8:9]
	v_lshl_add_u64 v[2:3], s[8:9], 0, v[158:159]
	s_add_i32 m0, s45, 0x1e000
	s_cmpk_lt_u32 s4, 0x100
	global_load_lds_dwordx4 v158, s[8:9]
	v_lshrrev_b32_e32 v3, 1, v10
	v_and_b32_e32 v3, 24, v3
	v_and_b32_e32 v2, 15, v10
	v_lshlrev_b32_e32 v4, 1, v3
	v_lshl_or_b32 v185, s5, 6, v2
	v_lshl_or_b32 v2, v2, 6, v4
	v_lshlrev_b32_e32 v4, 2, v10
	v_and_b32_e32 v4, 32, v4
	v_bitop3_b32 v5, v2, s18, v4 bitop3:0xde
	v_bitop3_b32 v186, v2, s19, v4 bitop3:0xde
	v_lshlrev_b32_e32 v2, 14, v11
	v_and_b32_e32 v2, 0xffff8000, v2
	v_or_b32_e32 v187, s20, v3
	v_lshl_add_u32 v2, v12, 11, v2
	v_and_b32_e32 v3, 1, v11
	v_lshl_or_b32 v2, v3, 6, v2
	v_lshl_add_u32 v164, v13, 1, v2
	v_lshlrev_b32_e32 v2, 14, v15
	v_and_b32_e32 v2, 0xffff8000, v2
	s_waitcnt vmcnt(6)
	v_lshl_add_u32 v2, v14, 11, v2
	v_and_b32_e32 v3, 1, v15
	v_lshl_or_b32 v2, v3, 6, v2
	s_cselect_b64 s[18:19], -1, 0
	v_mov_b32_e32 v165, v1
	v_lshl_add_u32 v166, v16, 1, v2
	v_mov_b32_e32 v167, v1
	s_mov_b32 s53, 0
	v_add_u32_e32 v188, 0, v5
	v_readlane_b32 s62, v253, 46
	v_readlane_b32 s4, v253, 61
	s_barrier
	v_readlane_b32 s5, v253, 62
	s_branch .LBB0_414

.Lnobar_e1o:
.LBB0_417:
	s_add_u32 s28, s6, 0xfffc0080
	s_addc_u32 s29, s7, -1
	s_add_i32 s43, 0, 0x10000
	s_cmp_eq_u32 s42, 12
	s_cselect_b32 s31, s5, s29
	s_cselect_b32 s30, s8, s28
	s_cselect_b32 s29, s9, s33
	s_cselect_b32 s28, s21, s23
	s_add_i32 s63, 0, 0x14000
	v_add_u32_e32 v142, s43, v186
	v_add_u32_e32 v168, s63, v186
	ds_read_b128 v[130:133], v142
	ds_read_b128 v[134:137], v142 offset:1024
	ds_read_b128 v[138:141], v142 offset:2048
	ds_read_b128 v[142:145], v142 offset:3072
	ds_read_b128 v[146:149], v168
	ds_read_b128 v[150:153], v168 offset:1024
	ds_read_b128 v[154:157], v168 offset:2048
	ds_read_b128 v[168:171], v168 offset:3072
	s_add_i32 m0, s45, 0xc000
	ds_read_b128 v[172:175], v188
	ds_read_b128 v[176:179], v188 offset:1024
	ds_read_b128 v[180:183], v188 offset:2048
	ds_read_b128 v[190:193], v188 offset:3072
	ds_read_b128 v[194:197], v188 offset:4096
	ds_read_b128 v[198:201], v188 offset:5120
	ds_read_b128 v[202:205], v188 offset:6144
	ds_read_b128 v[206:209], v188 offset:7168
	global_load_lds_dwordx4 v166, s[6:7]
	s_add_i32 m0, s45, 0xe000
	s_nop 0
	global_load_lds_dwordx4 v164, s[6:7]
	s_waitcnt vmcnt(8)
	s_waitcnt lgkmcnt(0)
	s_barrier
	s_setprio 1
	s_waitcnt lgkmcnt(0)
	v_mfma_f32_16x16x32_bf16 v[126:129], v[130:133], v[172:175], v[126:129]
	v_mfma_f32_16x16x32_bf16 v[122:125], v[138:141], v[172:175], v[122:125]
	v_mfma_f32_16x16x32_bf16 v[114:117], v[130:133], v[180:183], v[114:117]
	v_mfma_f32_16x16x32_bf16 v[106:109], v[138:141], v[180:183], v[106:109]
	v_mfma_f32_16x16x32_bf16 v[98:101], v[130:133], v[194:197], v[98:101]
	v_mfma_f32_16x16x32_bf16 v[90:93], v[138:141], v[194:197], v[90:93]
	v_mfma_f32_16x16x32_bf16 v[82:85], v[130:133], v[202:205], v[82:85]
	v_mfma_f32_16x16x32_bf16 v[74:77], v[138:141], v[202:205], v[74:77]
	v_mfma_f32_16x16x32_bf16 v[126:129], v[134:137], v[176:179], v[126:129]
	v_mfma_f32_16x16x32_bf16 v[122:125], v[142:145], v[176:179], v[122:125]
	v_mfma_f32_16x16x32_bf16 v[114:117], v[134:137], v[190:193], v[114:117]
	v_mfma_f32_16x16x32_bf16 v[106:109], v[142:145], v[190:193], v[106:109]
	v_mfma_f32_16x16x32_bf16 v[98:101], v[134:137], v[198:201], v[98:101]
	v_mfma_f32_16x16x32_bf16 v[90:93], v[142:145], v[198:201], v[90:93]
	v_mfma_f32_16x16x32_bf16 v[82:85], v[134:137], v[206:209], v[82:85]
	v_mfma_f32_16x16x32_bf16 v[74:77], v[142:145], v[206:209], v[74:77]
	s_setprio 0
	s_setprio 1
	v_mfma_f32_16x16x32_bf16 v[118:121], v[146:149], v[172:175], v[118:121]
	v_mfma_f32_16x16x32_bf16 v[110:113], v[154:157], v[172:175], v[110:113]
	v_mfma_f32_16x16x32_bf16 v[102:105], v[146:149], v[180:183], v[102:105]
	v_mfma_f32_16x16x32_bf16 v[94:97], v[154:157], v[180:183], v[94:97]
	v_mfma_f32_16x16x32_bf16 v[86:89], v[146:149], v[194:197], v[86:89]
	v_mfma_f32_16x16x32_bf16 v[78:81], v[154:157], v[194:197], v[78:81]
	v_mfma_f32_16x16x32_bf16 v[70:73], v[146:149], v[202:205], v[70:73]
	v_mfma_f32_16x16x32_bf16 v[66:69], v[154:157], v[202:205], v[66:69]
	v_mfma_f32_16x16x32_bf16 v[118:121], v[150:153], v[176:179], v[118:121]
	v_mfma_f32_16x16x32_bf16 v[110:113], v[168:171], v[176:179], v[110:113]
	v_mfma_f32_16x16x32_bf16 v[102:105], v[150:153], v[190:193], v[102:105]
	v_mfma_f32_16x16x32_bf16 v[94:97], v[168:171], v[190:193], v[94:97]
	v_mfma_f32_16x16x32_bf16 v[86:89], v[150:153], v[198:201], v[86:89]
	v_mfma_f32_16x16x32_bf16 v[78:81], v[168:171], v[198:201], v[78:81]
	v_mfma_f32_16x16x32_bf16 v[70:73], v[150:153], v[206:209], v[70:73]
	v_mfma_f32_16x16x32_bf16 v[66:69], v[168:171], v[206:209], v[66:69]
	s_setprio 0
	s_barrier
	s_add_i32 s43, s43, s44
	v_lshl_add_u64 v[216:217], s[28:29], 0, v[0:1]
	s_mov_b32 m0, s43
	ds_read_b128 v[172:175], v188 offset:16384
	ds_read_b128 v[176:179], v188 offset:17408
	ds_read_b128 v[180:183], v188 offset:18432
	ds_read_b128 v[190:193], v188 offset:19456
	ds_read_b128 v[194:197], v188 offset:20480
	ds_read_b128 v[198:201], v188 offset:21504
	ds_read_b128 v[202:205], v188 offset:22528
	ds_read_b128 v[206:209], v188 offset:23552
	global_load_lds_dwordx4 v0, s[28:29]
	s_add_i32 m0, s43, 0x2000
	s_add_u32 s58, s28, 0x40000
	v_lshl_add_u64 v[218:219], s[28:29], 0, v[158:159]
	s_addc_u32 s59, s29, 0
	s_add_i32 s43, s63, s44
	global_load_lds_dwordx4 v158, s[28:29]
	s_mov_b32 m0, s43
	v_lshl_add_u64 v[222:223], s[30:31], 0, v[160:161]
	global_load_lds_dwordx4 v0, s[58:59]
	s_add_i32 m0, s43, 0x2000
	s_nop 0
	global_load_lds_dwordx4 v158, s[58:59]
	s_mov_b32 m0, s45
	v_lshl_add_u64 v[220:221], s[30:31], 0, v[162:163]
	global_load_lds_dwordx4 v162, s[30:31]
	s_mov_b32 m0, s46
	s_nop 0
	global_load_lds_dwordx4 v160, s[30:31]
	s_waitcnt vmcnt(8)
	s_waitcnt lgkmcnt(0)
	s_barrier
	s_setprio 1
	s_waitcnt lgkmcnt(0)
	v_mfma_f32_16x16x32_bf16 v[62:65], v[130:133], v[172:175], v[62:65]
	v_mfma_f32_16x16x32_bf16 v[58:61], v[138:141], v[172:175], v[58:61]
	v_mfma_f32_16x16x32_bf16 v[50:53], v[130:133], v[180:183], v[50:53]
	v_mfma_f32_16x16x32_bf16 v[42:45], v[138:141], v[180:183], v[42:45]
	v_mfma_f32_16x16x32_bf16 v[34:37], v[130:133], v[194:197], v[34:37]
	v_mfma_f32_16x16x32_bf16 v[26:29], v[138:141], v[194:197], v[26:29]
	v_mfma_f32_16x16x32_bf16 v[18:21], v[130:133], v[202:205], v[18:21]
	v_mfma_f32_16x16x32_bf16 v[10:13], v[138:141], v[202:205], v[10:13]
	v_mfma_f32_16x16x32_bf16 v[62:65], v[134:137], v[176:179], v[62:65]
	v_mfma_f32_16x16x32_bf16 v[58:61], v[142:145], v[176:179], v[58:61]
	v_mfma_f32_16x16x32_bf16 v[50:53], v[134:137], v[190:193], v[50:53]
	v_mfma_f32_16x16x32_bf16 v[42:45], v[142:145], v[190:193], v[42:45]
	v_mfma_f32_16x16x32_bf16 v[34:37], v[134:137], v[198:201], v[34:37]
	v_mfma_f32_16x16x32_bf16 v[26:29], v[142:145], v[198:201], v[26:29]
	v_mfma_f32_16x16x32_bf16 v[18:21], v[134:137], v[206:209], v[18:21]
	v_mfma_f32_16x16x32_bf16 v[10:13], v[142:145], v[206:209], v[10:13]
	s_setprio 0
	s_setprio 1
	v_mfma_f32_16x16x32_bf16 v[54:57], v[146:149], v[172:175], v[54:57]
	v_mfma_f32_16x16x32_bf16 v[46:49], v[154:157], v[172:175], v[46:49]
	v_mfma_f32_16x16x32_bf16 v[38:41], v[146:149], v[180:183], v[38:41]
	v_mfma_f32_16x16x32_bf16 v[30:33], v[154:157], v[180:183], v[30:33]
	v_mfma_f32_16x16x32_bf16 v[22:25], v[146:149], v[194:197], v[22:25]
	v_mfma_f32_16x16x32_bf16 v[14:17], v[154:157], v[194:197], v[14:17]
	v_mfma_f32_16x16x32_bf16 v[6:9], v[146:149], v[202:205], v[6:9]
	v_mfma_f32_16x16x32_bf16 v[2:5], v[154:157], v[202:205], v[2:5]
	v_mfma_f32_16x16x32_bf16 v[54:57], v[150:153], v[176:179], v[54:57]
	v_mfma_f32_16x16x32_bf16 v[46:49], v[168:171], v[176:179], v[46:49]
	v_mfma_f32_16x16x32_bf16 v[38:41], v[150:153], v[190:193], v[38:41]
	v_mfma_f32_16x16x32_bf16 v[30:33], v[168:171], v[190:193], v[30:33]
	v_mfma_f32_16x16x32_bf16 v[22:25], v[150:153], v[198:201], v[22:25]
	v_mfma_f32_16x16x32_bf16 v[14:17], v[168:171], v[198:201], v[14:17]
	v_mfma_f32_16x16x32_bf16 v[6:9], v[150:153], v[206:209], v[6:9]
	v_mfma_f32_16x16x32_bf16 v[2:5], v[168:171], v[206:209], v[2:5]
	s_setprio 0
	s_barrier
	s_add_i32 s43, 0, 0x18000
	s_add_i32 s58, 0, 0x1c000
	v_add_u32_e32 v142, s43, v186
	v_add_u32_e32 v168, s58, v186
	ds_read_b128 v[130:133], v142
	ds_read_b128 v[134:137], v142 offset:1024
	ds_read_b128 v[138:141], v142 offset:2048
	ds_read_b128 v[142:145], v142 offset:3072
	ds_read_b128 v[146:149], v168
	ds_read_b128 v[150:153], v168 offset:1024
	ds_read_b128 v[154:157], v168 offset:2048
	ds_read_b128 v[168:171], v168 offset:3072
	s_add_u32 s30, s30, 0x40000
	s_addc_u32 s31, s31, 0
	s_mov_b32 m0, s47
	ds_read_b128 v[172:175], v188 offset:32768
	ds_read_b128 v[176:179], v188 offset:33792
	ds_read_b128 v[180:183], v188 offset:34816
	ds_read_b128 v[190:193], v188 offset:35840
	ds_read_b128 v[194:197], v188 offset:36864
	ds_read_b128 v[198:201], v188 offset:37888
	ds_read_b128 v[202:205], v188 offset:38912
	ds_read_b128 v[206:209], v188 offset:39936
	global_load_lds_dwordx4 v162, s[30:31]
	s_mov_b32 m0, s48
	s_nop 0
	global_load_lds_dwordx4 v160, s[30:31]
	s_waitcnt vmcnt(8)
	s_waitcnt lgkmcnt(0)
	s_barrier
	s_setprio 1
	s_waitcnt lgkmcnt(0)
	v_mfma_f32_16x16x32_bf16 v[126:129], v[130:133], v[172:175], v[126:129]
	v_mfma_f32_16x16x32_bf16 v[122:125], v[138:141], v[172:175], v[122:125]
	v_mfma_f32_16x16x32_bf16 v[114:117], v[130:133], v[180:183], v[114:117]
	v_mfma_f32_16x16x32_bf16 v[106:109], v[138:141], v[180:183], v[106:109]
	v_mfma_f32_16x16x32_bf16 v[98:101], v[130:133], v[194:197], v[98:101]
	v_mfma_f32_16x16x32_bf16 v[90:93], v[138:141], v[194:197], v[90:93]
	v_mfma_f32_16x16x32_bf16 v[82:85], v[130:133], v[202:205], v[82:85]
	v_mfma_f32_16x16x32_bf16 v[74:77], v[138:141], v[202:205], v[74:77]
	v_mfma_f32_16x16x32_bf16 v[126:129], v[134:137], v[176:179], v[126:129]
	v_mfma_f32_16x16x32_bf16 v[122:125], v[142:145], v[176:179], v[122:125]
	v_mfma_f32_16x16x32_bf16 v[114:117], v[134:137], v[190:193], v[114:117]
	v_mfma_f32_16x16x32_bf16 v[106:109], v[142:145], v[190:193], v[106:109]
	v_mfma_f32_16x16x32_bf16 v[98:101], v[134:137], v[198:201], v[98:101]
	v_mfma_f32_16x16x32_bf16 v[90:93], v[142:145], v[198:201], v[90:93]
	v_mfma_f32_16x16x32_bf16 v[82:85], v[134:137], v[206:209], v[82:85]
	v_mfma_f32_16x16x32_bf16 v[74:77], v[142:145], v[206:209], v[74:77]
	s_setprio 0
	s_setprio 1
	v_mfma_f32_16x16x32_bf16 v[118:121], v[146:149], v[172:175], v[118:121]
	v_mfma_f32_16x16x32_bf16 v[110:113], v[154:157], v[172:175], v[110:113]
	v_mfma_f32_16x16x32_bf16 v[102:105], v[146:149], v[180:183], v[102:105]
	v_mfma_f32_16x16x32_bf16 v[94:97], v[154:157], v[180:183], v[94:97]
	v_mfma_f32_16x16x32_bf16 v[86:89], v[146:149], v[194:197], v[86:89]
	v_mfma_f32_16x16x32_bf16 v[78:81], v[154:157], v[194:197], v[78:81]
	v_mfma_f32_16x16x32_bf16 v[70:73], v[146:149], v[202:205], v[70:73]
	v_mfma_f32_16x16x32_bf16 v[66:69], v[154:157], v[202:205], v[66:69]
	v_mfma_f32_16x16x32_bf16 v[118:121], v[150:153], v[176:179], v[118:121]
	v_mfma_f32_16x16x32_bf16 v[110:113], v[168:171], v[176:179], v[110:113]
	v_mfma_f32_16x16x32_bf16 v[102:105], v[150:153], v[190:193], v[102:105]
	v_mfma_f32_16x16x32_bf16 v[94:97], v[168:171], v[190:193], v[94:97]
	v_mfma_f32_16x16x32_bf16 v[86:89], v[150:153], v[198:201], v[86:89]
	v_mfma_f32_16x16x32_bf16 v[78:81], v[168:171], v[198:201], v[78:81]
	v_mfma_f32_16x16x32_bf16 v[70:73], v[150:153], v[206:209], v[70:73]
	v_mfma_f32_16x16x32_bf16 v[66:69], v[168:171], v[206:209], v[66:69]
	s_setprio 0
	s_barrier
	s_add_i32 s30, s43, s44
	v_lshl_add_u64 v[216:217], v[216:217], 0, s[56:57]
	s_mov_b32 m0, s30
	ds_read_b128 v[172:175], v188 offset:49152
	ds_read_b128 v[176:179], v188 offset:50176
	ds_read_b128 v[180:183], v188 offset:51200
	ds_read_b128 v[190:193], v188 offset:52224
	ds_read_b128 v[194:197], v188 offset:53248
	ds_read_b128 v[198:201], v188 offset:54272
	ds_read_b128 v[202:205], v188 offset:55296
	ds_read_b128 v[206:209], v188 offset:56320
	global_load_lds_dwordx4 v[216:217], off
	s_add_i32 m0, s30, 0x2000
	s_add_u32 s28, s28, 0x40080
	v_lshl_add_u64 v[216:217], v[218:219], 0, s[56:57]
	s_addc_u32 s29, s29, 0
	s_add_i32 s30, s58, s44
	global_load_lds_dwordx4 v[216:217], off
	s_mov_b32 m0, s30
	s_nop 0
	global_load_lds_dwordx4 v0, s[28:29]
	s_add_i32 m0, s30, 0x2000
	s_nop 0
	global_load_lds_dwordx4 v158, s[28:29]
	s_mov_b32 m0, s49
	v_lshl_add_u64 v[216:217], v[220:221], 0, s[56:57]
	global_load_lds_dwordx4 v[216:217], off
	s_mov_b32 m0, s52
	v_lshl_add_u64 v[216:217], v[222:223], 0, s[56:57]
	global_load_lds_dwordx4 v[216:217], off
	s_waitcnt vmcnt(8)
	s_waitcnt lgkmcnt(0)
	s_barrier
	s_setprio 1
	s_waitcnt lgkmcnt(0)
	v_mfma_f32_16x16x32_bf16 v[62:65], v[130:133], v[172:175], v[62:65]
	v_mfma_f32_16x16x32_bf16 v[58:61], v[138:141], v[172:175], v[58:61]
	v_mfma_f32_16x16x32_bf16 v[50:53], v[130:133], v[180:183], v[50:53]
	v_mfma_f32_16x16x32_bf16 v[42:45], v[138:141], v[180:183], v[42:45]
	v_mfma_f32_16x16x32_bf16 v[34:37], v[130:133], v[194:197], v[34:37]
	v_mfma_f32_16x16x32_bf16 v[26:29], v[138:141], v[194:197], v[26:29]
	v_mfma_f32_16x16x32_bf16 v[18:21], v[130:133], v[202:205], v[18:21]
	v_mfma_f32_16x16x32_bf16 v[10:13], v[138:141], v[202:205], v[10:13]
	v_mfma_f32_16x16x32_bf16 v[62:65], v[134:137], v[176:179], v[62:65]
	v_mfma_f32_16x16x32_bf16 v[58:61], v[142:145], v[176:179], v[58:61]
	v_mfma_f32_16x16x32_bf16 v[50:53], v[134:137], v[190:193], v[50:53]
	v_mfma_f32_16x16x32_bf16 v[42:45], v[142:145], v[190:193], v[42:45]
	v_mfma_f32_16x16x32_bf16 v[34:37], v[134:137], v[198:201], v[34:37]
	v_mfma_f32_16x16x32_bf16 v[26:29], v[142:145], v[198:201], v[26:29]
	v_mfma_f32_16x16x32_bf16 v[18:21], v[134:137], v[206:209], v[18:21]
	v_mfma_f32_16x16x32_bf16 v[10:13], v[142:145], v[206:209], v[10:13]
	s_setprio 0
	s_setprio 1
	v_mfma_f32_16x16x32_bf16 v[54:57], v[146:149], v[172:175], v[54:57]
	v_mfma_f32_16x16x32_bf16 v[46:49], v[154:157], v[172:175], v[46:49]
	v_mfma_f32_16x16x32_bf16 v[38:41], v[146:149], v[180:183], v[38:41]
	v_mfma_f32_16x16x32_bf16 v[30:33], v[154:157], v[180:183], v[30:33]
	v_mfma_f32_16x16x32_bf16 v[22:25], v[146:149], v[194:197], v[22:25]
	v_mfma_f32_16x16x32_bf16 v[14:17], v[154:157], v[194:197], v[14:17]
	v_mfma_f32_16x16x32_bf16 v[6:9], v[146:149], v[202:205], v[6:9]
	v_mfma_f32_16x16x32_bf16 v[2:5], v[154:157], v[202:205], v[2:5]
	v_mfma_f32_16x16x32_bf16 v[54:57], v[150:153], v[176:179], v[54:57]
	v_mfma_f32_16x16x32_bf16 v[46:49], v[168:171], v[176:179], v[46:49]
	v_mfma_f32_16x16x32_bf16 v[38:41], v[150:153], v[190:193], v[38:41]
	v_mfma_f32_16x16x32_bf16 v[30:33], v[168:171], v[190:193], v[30:33]
	v_mfma_f32_16x16x32_bf16 v[22:25], v[150:153], v[198:201], v[22:25]
	v_mfma_f32_16x16x32_bf16 v[14:17], v[168:171], v[198:201], v[14:17]
	v_mfma_f32_16x16x32_bf16 v[6:9], v[150:153], v[206:209], v[6:9]
	v_mfma_f32_16x16x32_bf16 v[2:5], v[168:171], v[206:209], v[2:5]
	s_setprio 0
	s_barrier
	s_add_i32 s42, s42, 2
	s_add_u32 s23, s23, 0x100
	s_addc_u32 s33, s33, 0
	s_add_u32 s6, s6, 0x100
	s_addc_u32 s7, s7, 0
	s_cmp_gt_u32 s42, 13
	s_cbranch_scc0 .LBB0_417
	s_and_b64 vcc, exec, s[18:19]
	s_cbranch_vccz .LBB0_420
	s_barrier

.LBB0_579:
	v_lshl_add_u64 v[8:9], s[62:63], 0, v[0:1]
	v_mov_b32_e32 v119, v1
	v_lshl_add_u64 v[10:11], s[62:63], 0, v[118:119]
	v_mov_b32_e32 v127, v1
	s_and_b32 s21, s81, 3
	s_add_i32 m0, s4, 0x18000
	v_lshl_add_u64 v[8:9], v[8:9], 0, s[56:57]
	v_lshl_add_u64 v[12:13], s[34:35], 0, v[126:127]
	v_mov_b32_e32 v121, v1
	s_lshl_b32 s18, s82, 13
	s_lshl_b32 s19, s21, 12
	s_waitcnt vmcnt(2)
	s_barrier
	global_load_lds_dwordx4 v[8:9], off
	v_lshl_add_u64 v[8:9], v[10:11], 0, s[56:57]
	s_add_i32 m0, s4, 0x1a000
	s_add_i32 s90, s4, 0x8000
	s_add_i32 s96, s4, 0xa000
	s_waitcnt lgkmcnt(0)
	v_lshl_add_u64 v[14:15], s[34:35], 0, v[120:121]
	global_load_lds_dwordx4 v[8:9], off
	v_lshl_add_u64 v[8:9], v[12:13], 0, s[56:57]
	s_mov_b32 m0, s90
	s_add_u32 s8, s62, 0x40080
	global_load_lds_dwordx4 v[8:9], off
	v_lshl_add_u64 v[8:9], v[14:15], 0, s[56:57]
	s_mov_b32 m0, s96
	s_addc_u32 s9, s63, 0
	global_load_lds_dwordx4 v[8:9], off
	s_add_i32 m0, s4, 0x1c000
	s_nop 0
	global_load_lds_dwordx4 v0, s[8:9]
	v_lshl_add_u64 v[8:9], s[8:9], 0, v[118:119]
	s_add_i32 m0, s4, 0x1e000
	v_and_b32_e32 v167, 15, v166
	global_load_lds_dwordx4 v118, s[8:9]
	v_and_b32_e32 v8, 48, v166
	v_lshlrev_b32_e32 v9, 2, v166
	v_lshl_or_b32 v8, v167, 6, v8
	v_and_b32_e32 v9, 32, v9
	v_bitop3_b32 v10, v8, s18, v9 bitop3:0xde
	v_bitop3_b32 v144, v8, s19, v9 bitop3:0xde
	v_lshlrev_b32_e32 v8, 14, v2
	v_and_b32_e32 v8, 0xffff8000, v8
	v_lshl_add_u32 v3, v3, 11, v8
	v_and_b32_e32 v2, 1, v2
	v_lshl_or_b32 v2, v2, 6, v3
	v_lshl_add_u32 v128, v4, 1, v2
	v_lshlrev_b32_e32 v2, 14, v6
	v_and_b32_e32 v2, 0xffff8000, v2
	v_lshl_add_u32 v2, v5, 11, v2
	v_and_b32_e32 v3, 1, v6
	s_waitcnt vmcnt(6)
	v_lshl_or_b32 v2, v3, 6, v2
	v_mov_b32_e32 v4, v1
	v_mov_b32_e32 v5, v1
	v_readlane_b32 s8, v254, 58
	v_lshl_add_u32 v138, v7, 1, v2
	v_mov_b32_e32 v2, v1
	v_mov_b32_e32 v3, v1
	v_add_u32_e32 v145, 0, v10
	v_mov_b64_e32 v[8:9], v[4:5]
	v_mov_b64_e32 v[20:21], v[4:5]
	v_mov_b64_e32 v[24:25], v[4:5]
	v_mov_b64_e32 v[36:37], v[4:5]
	v_mov_b64_e32 v[40:41], v[4:5]
	v_mov_b64_e32 v[52:53], v[4:5]
	v_mov_b64_e32 v[56:57], v[4:5]
	v_mov_b64_e32 v[12:13], v[4:5]
	v_mov_b64_e32 v[16:17], v[4:5]
	v_mov_b64_e32 v[28:29], v[4:5]
	v_mov_b64_e32 v[32:33], v[4:5]
	v_mov_b64_e32 v[44:45], v[4:5]
	v_mov_b64_e32 v[48:49], v[4:5]
	v_mov_b64_e32 v[60:61], v[4:5]
	v_mov_b64_e32 v[64:65], v[4:5]
	v_mov_b64_e32 v[68:69], v[4:5]
	v_mov_b64_e32 v[72:73], v[4:5]
	v_mov_b64_e32 v[84:85], v[4:5]
	v_mov_b64_e32 v[88:89], v[4:5]
	v_mov_b64_e32 v[100:101], v[4:5]
	v_mov_b64_e32 v[104:105], v[4:5]
	v_mov_b64_e32 v[116:117], v[4:5]
	v_mov_b64_e32 v[124:125], v[4:5]
	v_mov_b64_e32 v[76:77], v[4:5]
	v_mov_b64_e32 v[80:81], v[4:5]
	v_mov_b64_e32 v[92:93], v[4:5]
	v_mov_b64_e32 v[96:97], v[4:5]
	v_mov_b64_e32 v[108:109], v[4:5]
	v_mov_b64_e32 v[112:113], v[4:5]
	v_mov_b64_e32 v[132:133], v[4:5]
	v_mov_b64_e32 v[136:137], v[4:5]
	s_mov_b32 s20, s8
	v_readlane_b32 s8, v254, 54
	v_lshl_or_b32 v240, s82, 6, v167
	v_mov_b32_e32 v129, v1
	v_mov_b32_e32 v139, v1
	s_mov_b32 s68, 0
	v_mov_b64_e32 v[6:7], v[2:3]
	v_mov_b64_e32 v[18:19], v[2:3]
	v_mov_b64_e32 v[22:23], v[2:3]
	v_mov_b64_e32 v[34:35], v[2:3]
	v_mov_b64_e32 v[38:39], v[2:3]
	v_mov_b64_e32 v[50:51], v[2:3]
	v_mov_b64_e32 v[54:55], v[2:3]
	v_mov_b64_e32 v[10:11], v[2:3]
	v_mov_b64_e32 v[14:15], v[2:3]
	v_mov_b64_e32 v[26:27], v[2:3]
	v_mov_b64_e32 v[30:31], v[2:3]
	v_mov_b64_e32 v[42:43], v[2:3]
	v_mov_b64_e32 v[46:47], v[2:3]
	v_mov_b64_e32 v[58:59], v[2:3]
	v_mov_b64_e32 v[62:63], v[2:3]
	v_mov_b64_e32 v[66:67], v[2:3]
	v_mov_b64_e32 v[70:71], v[2:3]
	v_mov_b64_e32 v[82:83], v[2:3]
	v_mov_b64_e32 v[86:87], v[2:3]
	v_mov_b64_e32 v[98:99], v[2:3]
	v_mov_b64_e32 v[102:103], v[2:3]
	v_mov_b64_e32 v[114:115], v[2:3]
	v_mov_b64_e32 v[122:123], v[2:3]
	v_mov_b64_e32 v[74:75], v[2:3]
	v_mov_b64_e32 v[78:79], v[2:3]
	v_mov_b64_e32 v[90:91], v[2:3]
	v_mov_b64_e32 v[94:95], v[2:3]
	v_mov_b64_e32 v[106:107], v[2:3]
	v_mov_b64_e32 v[110:111], v[2:3]
	v_mov_b64_e32 v[130:131], v[2:3]
	v_mov_b64_e32 v[134:135], v[2:3]
	s_mov_b32 s83, s8
	s_barrier
	v_readlane_b32 s9, v254, 55

.LBB0_587:
	s_add_u32 s18, s34, s62
	s_addc_u32 s19, s35, s63
	s_add_u32 s18, s18, 0x100
	s_addc_u32 s19, s19, 0
	s_add_u32 s70, s8, s62
	s_addc_u32 s71, s9, s63
	s_add_i32 s26, 0, 0x10000
	s_cmpk_eq_i32 s62, 0x700
	s_cselect_b32 s77, s47, s19
	s_cselect_b32 s76, s59, s18
	s_cselect_b32 s71, s37, s71
	s_cselect_b32 s70, vcc_lo, s70
	s_add_i32 s27, 0, 0x14000
	v_add_u32_e32 v158, s26, v144
	v_add_u32_e32 v176, s27, v144
	ds_read_b128 v[146:149], v158
	ds_read_b128 v[150:153], v158 offset:1024
	ds_read_b128 v[154:157], v158 offset:2048
	ds_read_b128 v[158:161], v158 offset:3072
	ds_read_b128 v[162:165], v176
	ds_read_b128 v[168:171], v176 offset:1024
	ds_read_b128 v[172:175], v176 offset:2048
	ds_read_b128 v[176:179], v176 offset:3072
	v_lshl_add_u64 v[208:209], v[142:143], 0, s[62:63]
	s_add_i32 m0, s4, 0xc000
	ds_read_b128 v[180:183], v145
	ds_read_b128 v[184:187], v145 offset:1024
	ds_read_b128 v[188:191], v145 offset:2048
	ds_read_b128 v[192:195], v145 offset:3072
	ds_read_b128 v[196:199], v145 offset:4096
	ds_read_b128 v[200:203], v145 offset:5120
	ds_read_b128 v[204:207], v145 offset:6144
	ds_read_b128 v[216:219], v145 offset:7168
	global_load_lds_dwordx4 v[208:209], off
	s_add_i32 m0, s4, 0xe000
	v_lshl_add_u64 v[208:209], v[140:141], 0, s[62:63]
	global_load_lds_dwordx4 v[208:209], off
	s_waitcnt vmcnt(8)
	s_waitcnt lgkmcnt(0)
	s_barrier
	s_setprio 1
	s_waitcnt lgkmcnt(0)
	v_mfma_f32_16x16x32_bf16 v[134:137], v[146:149], v[180:183], v[134:137]
	v_mfma_f32_16x16x32_bf16 v[130:133], v[154:157], v[180:183], v[130:133]
	v_mfma_f32_16x16x32_bf16 v[110:113], v[146:149], v[188:191], v[110:113]
	v_mfma_f32_16x16x32_bf16 v[106:109], v[154:157], v[188:191], v[106:109]
	v_mfma_f32_16x16x32_bf16 v[94:97], v[146:149], v[196:199], v[94:97]
	v_mfma_f32_16x16x32_bf16 v[90:93], v[154:157], v[196:199], v[90:93]
	v_mfma_f32_16x16x32_bf16 v[78:81], v[146:149], v[204:207], v[78:81]
	v_mfma_f32_16x16x32_bf16 v[74:77], v[154:157], v[204:207], v[74:77]
	v_mfma_f32_16x16x32_bf16 v[134:137], v[150:153], v[184:187], v[134:137]
	v_mfma_f32_16x16x32_bf16 v[130:133], v[158:161], v[184:187], v[130:133]
	v_mfma_f32_16x16x32_bf16 v[110:113], v[150:153], v[192:195], v[110:113]
	v_mfma_f32_16x16x32_bf16 v[106:109], v[158:161], v[192:195], v[106:109]
	v_mfma_f32_16x16x32_bf16 v[94:97], v[150:153], v[200:203], v[94:97]
	v_mfma_f32_16x16x32_bf16 v[90:93], v[158:161], v[200:203], v[90:93]
	v_mfma_f32_16x16x32_bf16 v[78:81], v[150:153], v[216:219], v[78:81]
	v_mfma_f32_16x16x32_bf16 v[74:77], v[158:161], v[216:219], v[74:77]
	s_setprio 0
	s_setprio 1
	v_mfma_f32_16x16x32_bf16 v[122:125], v[162:165], v[180:183], v[122:125]
	v_mfma_f32_16x16x32_bf16 v[114:117], v[172:175], v[180:183], v[114:117]
	v_mfma_f32_16x16x32_bf16 v[102:105], v[162:165], v[188:191], v[102:105]
	v_mfma_f32_16x16x32_bf16 v[98:101], v[172:175], v[188:191], v[98:101]
	v_mfma_f32_16x16x32_bf16 v[86:89], v[162:165], v[196:199], v[86:89]
	v_mfma_f32_16x16x32_bf16 v[82:85], v[172:175], v[196:199], v[82:85]
	v_mfma_f32_16x16x32_bf16 v[70:73], v[162:165], v[204:207], v[70:73]
	v_mfma_f32_16x16x32_bf16 v[66:69], v[172:175], v[204:207], v[66:69]
	v_mfma_f32_16x16x32_bf16 v[122:125], v[168:171], v[184:187], v[122:125]
	v_mfma_f32_16x16x32_bf16 v[114:117], v[176:179], v[184:187], v[114:117]
	v_mfma_f32_16x16x32_bf16 v[102:105], v[168:171], v[192:195], v[102:105]
	v_mfma_f32_16x16x32_bf16 v[98:101], v[176:179], v[192:195], v[98:101]
	v_mfma_f32_16x16x32_bf16 v[86:89], v[168:171], v[200:203], v[86:89]
	v_mfma_f32_16x16x32_bf16 v[82:85], v[176:179], v[200:203], v[82:85]
	v_mfma_f32_16x16x32_bf16 v[70:73], v[168:171], v[216:219], v[70:73]
	v_mfma_f32_16x16x32_bf16 v[66:69], v[176:179], v[216:219], v[66:69]
	s_setprio 0
	s_barrier
	s_add_i32 s18, s26, s84
	v_lshl_add_u64 v[208:209], s[70:71], 0, v[0:1]
	s_mov_b32 m0, s18
	ds_read_b128 v[180:183], v145 offset:16384
	ds_read_b128 v[184:187], v145 offset:17408
	ds_read_b128 v[188:191], v145 offset:18432
	ds_read_b128 v[192:195], v145 offset:19456
	ds_read_b128 v[196:199], v145 offset:20480
	ds_read_b128 v[200:203], v145 offset:21504
	ds_read_b128 v[204:207], v145 offset:22528
	ds_read_b128 v[216:219], v145 offset:23552
	global_load_lds_dwordx4 v0, s[70:71]
	s_add_i32 m0, s18, 0x2000
	s_add_u32 s18, s70, 0x40000
	v_lshl_add_u64 v[220:221], s[70:71], 0, v[118:119]
	s_addc_u32 s19, s71, 0
	s_add_i32 s26, s27, s84
	global_load_lds_dwordx4 v118, s[70:71]
	s_mov_b32 m0, s26
	v_lshl_add_u64 v[224:225], s[76:77], 0, v[120:121]
	global_load_lds_dwordx4 v0, s[18:19]
	s_add_i32 m0, s26, 0x2000
	s_nop 0
	global_load_lds_dwordx4 v118, s[18:19]
	s_mov_b32 m0, s4
	v_lshl_add_u64 v[222:223], s[76:77], 0, v[126:127]
	global_load_lds_dwordx4 v126, s[76:77]
	s_mov_b32 m0, s5
	s_nop 0
	global_load_lds_dwordx4 v120, s[76:77]
	s_waitcnt vmcnt(8)
	s_waitcnt lgkmcnt(0)
	s_barrier
	s_setprio 1
	s_waitcnt lgkmcnt(0)
	v_mfma_f32_16x16x32_bf16 v[62:65], v[146:149], v[180:183], v[62:65]
	v_mfma_f32_16x16x32_bf16 v[58:61], v[154:157], v[180:183], v[58:61]
	v_mfma_f32_16x16x32_bf16 v[46:49], v[146:149], v[188:191], v[46:49]
	v_mfma_f32_16x16x32_bf16 v[42:45], v[154:157], v[188:191], v[42:45]
	v_mfma_f32_16x16x32_bf16 v[30:33], v[146:149], v[196:199], v[30:33]
	v_mfma_f32_16x16x32_bf16 v[26:29], v[154:157], v[196:199], v[26:29]
	v_mfma_f32_16x16x32_bf16 v[14:17], v[146:149], v[204:207], v[14:17]
	v_mfma_f32_16x16x32_bf16 v[10:13], v[154:157], v[204:207], v[10:13]
	v_mfma_f32_16x16x32_bf16 v[62:65], v[150:153], v[184:187], v[62:65]
	v_mfma_f32_16x16x32_bf16 v[58:61], v[158:161], v[184:187], v[58:61]
	v_mfma_f32_16x16x32_bf16 v[46:49], v[150:153], v[192:195], v[46:49]
	v_mfma_f32_16x16x32_bf16 v[42:45], v[158:161], v[192:195], v[42:45]
	v_mfma_f32_16x16x32_bf16 v[30:33], v[150:153], v[200:203], v[30:33]
	v_mfma_f32_16x16x32_bf16 v[26:29], v[158:161], v[200:203], v[26:29]
	v_mfma_f32_16x16x32_bf16 v[14:17], v[150:153], v[216:219], v[14:17]
	v_mfma_f32_16x16x32_bf16 v[10:13], v[158:161], v[216:219], v[10:13]
	s_setprio 0
	s_setprio 1
	v_mfma_f32_16x16x32_bf16 v[54:57], v[162:165], v[180:183], v[54:57]
	v_mfma_f32_16x16x32_bf16 v[50:53], v[172:175], v[180:183], v[50:53]
	v_mfma_f32_16x16x32_bf16 v[38:41], v[162:165], v[188:191], v[38:41]
	v_mfma_f32_16x16x32_bf16 v[34:37], v[172:175], v[188:191], v[34:37]
	v_mfma_f32_16x16x32_bf16 v[22:25], v[162:165], v[196:199], v[22:25]
	v_mfma_f32_16x16x32_bf16 v[18:21], v[172:175], v[196:199], v[18:21]
	v_mfma_f32_16x16x32_bf16 v[6:9], v[162:165], v[204:207], v[6:9]
	v_mfma_f32_16x16x32_bf16 v[2:5], v[172:175], v[204:207], v[2:5]
	v_mfma_f32_16x16x32_bf16 v[54:57], v[168:171], v[184:187], v[54:57]
	v_mfma_f32_16x16x32_bf16 v[50:53], v[176:179], v[184:187], v[50:53]
	v_mfma_f32_16x16x32_bf16 v[38:41], v[168:171], v[192:195], v[38:41]
	v_mfma_f32_16x16x32_bf16 v[34:37], v[176:179], v[192:195], v[34:37]
	v_mfma_f32_16x16x32_bf16 v[22:25], v[168:171], v[200:203], v[22:25]
	v_mfma_f32_16x16x32_bf16 v[18:21], v[176:179], v[200:203], v[18:21]
	v_mfma_f32_16x16x32_bf16 v[6:9], v[168:171], v[216:219], v[6:9]
	v_mfma_f32_16x16x32_bf16 v[2:5], v[176:179], v[216:219], v[2:5]
	s_setprio 0
	s_barrier
	s_add_i32 s26, 0, 0x18000
	s_add_i32 s27, 0, 0x1c000
	v_add_u32_e32 v158, s26, v144
	v_add_u32_e32 v176, s27, v144
	ds_read_b128 v[146:149], v158
	ds_read_b128 v[150:153], v158 offset:1024
	ds_read_b128 v[154:157], v158 offset:2048
	ds_read_b128 v[158:161], v158 offset:3072
	ds_read_b128 v[162:165], v176
	ds_read_b128 v[168:171], v176 offset:1024
	ds_read_b128 v[172:175], v176 offset:2048
	ds_read_b128 v[176:179], v176 offset:3072
	s_add_u32 s18, s76, 0x40000
	s_addc_u32 s19, s77, 0
	s_mov_b32 m0, s33
	ds_read_b128 v[180:183], v145 offset:32768
	ds_read_b128 v[184:187], v145 offset:33792
	ds_read_b128 v[188:191], v145 offset:34816
	ds_read_b128 v[192:195], v145 offset:35840
	ds_read_b128 v[196:199], v145 offset:36864
	ds_read_b128 v[200:203], v145 offset:37888
	ds_read_b128 v[204:207], v145 offset:38912
	ds_read_b128 v[216:219], v145 offset:39936
	global_load_lds_dwordx4 v126, s[18:19]
	s_mov_b32 m0, s92
	v_lshl_add_u64 v[242:243], s[18:19], 0, v[120:121]
	global_load_lds_dwordx4 v120, s[18:19]
	s_waitcnt vmcnt(8)
	s_waitcnt lgkmcnt(0)
	s_barrier
	s_setprio 1
	s_waitcnt lgkmcnt(0)
	v_mfma_f32_16x16x32_bf16 v[134:137], v[146:149], v[180:183], v[134:137]
	v_mfma_f32_16x16x32_bf16 v[130:133], v[154:157], v[180:183], v[130:133]
	v_mfma_f32_16x16x32_bf16 v[110:113], v[146:149], v[188:191], v[110:113]
	v_mfma_f32_16x16x32_bf16 v[106:109], v[154:157], v[188:191], v[106:109]
	v_mfma_f32_16x16x32_bf16 v[94:97], v[146:149], v[196:199], v[94:97]
	v_mfma_f32_16x16x32_bf16 v[90:93], v[154:157], v[196:199], v[90:93]
	v_mfma_f32_16x16x32_bf16 v[78:81], v[146:149], v[204:207], v[78:81]
	v_mfma_f32_16x16x32_bf16 v[74:77], v[154:157], v[204:207], v[74:77]
	v_mfma_f32_16x16x32_bf16 v[134:137], v[150:153], v[184:187], v[134:137]
	v_mfma_f32_16x16x32_bf16 v[130:133], v[158:161], v[184:187], v[130:133]
	v_mfma_f32_16x16x32_bf16 v[110:113], v[150:153], v[192:195], v[110:113]
	v_mfma_f32_16x16x32_bf16 v[106:109], v[158:161], v[192:195], v[106:109]
	v_mfma_f32_16x16x32_bf16 v[94:97], v[150:153], v[200:203], v[94:97]
	v_mfma_f32_16x16x32_bf16 v[90:93], v[158:161], v[200:203], v[90:93]
	v_mfma_f32_16x16x32_bf16 v[78:81], v[150:153], v[216:219], v[78:81]
	v_mfma_f32_16x16x32_bf16 v[74:77], v[158:161], v[216:219], v[74:77]
	s_setprio 0
	s_setprio 1
	v_mfma_f32_16x16x32_bf16 v[122:125], v[162:165], v[180:183], v[122:125]
	v_mfma_f32_16x16x32_bf16 v[114:117], v[172:175], v[180:183], v[114:117]
	v_mfma_f32_16x16x32_bf16 v[102:105], v[162:165], v[188:191], v[102:105]
	v_mfma_f32_16x16x32_bf16 v[98:101], v[172:175], v[188:191], v[98:101]
	v_mfma_f32_16x16x32_bf16 v[86:89], v[162:165], v[196:199], v[86:89]
	v_mfma_f32_16x16x32_bf16 v[82:85], v[172:175], v[196:199], v[82:85]
	v_mfma_f32_16x16x32_bf16 v[70:73], v[162:165], v[204:207], v[70:73]
	v_mfma_f32_16x16x32_bf16 v[66:69], v[172:175], v[204:207], v[66:69]
	v_mfma_f32_16x16x32_bf16 v[122:125], v[168:171], v[184:187], v[122:125]
	v_mfma_f32_16x16x32_bf16 v[114:117], v[176:179], v[184:187], v[114:117]
	v_mfma_f32_16x16x32_bf16 v[102:105], v[168:171], v[192:195], v[102:105]
	v_mfma_f32_16x16x32_bf16 v[98:101], v[176:179], v[192:195], v[98:101]
	v_mfma_f32_16x16x32_bf16 v[86:89], v[168:171], v[200:203], v[86:89]
	v_mfma_f32_16x16x32_bf16 v[82:85], v[176:179], v[200:203], v[82:85]
	v_mfma_f32_16x16x32_bf16 v[70:73], v[168:171], v[216:219], v[70:73]
	v_mfma_f32_16x16x32_bf16 v[66:69], v[176:179], v[216:219], v[66:69]
	s_setprio 0
	s_barrier
	s_add_i32 s18, s26, s84
	v_lshl_add_u64 v[208:209], v[208:209], 0, s[56:57]
	s_mov_b32 m0, s18
	ds_read_b128 v[180:183], v145 offset:49152
	ds_read_b128 v[184:187], v145 offset:50176
	ds_read_b128 v[188:191], v145 offset:51200
	ds_read_b128 v[192:195], v145 offset:52224
	ds_read_b128 v[196:199], v145 offset:53248
	ds_read_b128 v[200:203], v145 offset:54272
	ds_read_b128 v[204:207], v145 offset:55296
	ds_read_b128 v[216:219], v145 offset:56320
	global_load_lds_dwordx4 v[208:209], off
	s_add_i32 m0, s18, 0x2000
	s_add_u32 s18, s70, 0x40080
	v_lshl_add_u64 v[208:209], v[220:221], 0, s[56:57]
	s_addc_u32 s19, s71, 0
	s_add_i32 s26, s27, s84
	global_load_lds_dwordx4 v[208:209], off
	s_mov_b32 m0, s26
	s_nop 0
	global_load_lds_dwordx4 v0, s[18:19]
	s_add_i32 m0, s26, 0x2000
	s_nop 0
	global_load_lds_dwordx4 v118, s[18:19]
	s_mov_b32 m0, s90
	v_lshl_add_u64 v[208:209], v[222:223], 0, s[56:57]
	global_load_lds_dwordx4 v[208:209], off
	s_mov_b32 m0, s96
	v_lshl_add_u64 v[208:209], v[224:225], 0, s[56:57]
	global_load_lds_dwordx4 v[208:209], off
	s_waitcnt vmcnt(8)
	s_waitcnt lgkmcnt(0)
	s_barrier
	s_setprio 1
	s_waitcnt lgkmcnt(0)
	v_mfma_f32_16x16x32_bf16 v[62:65], v[146:149], v[180:183], v[62:65]
	v_mfma_f32_16x16x32_bf16 v[58:61], v[154:157], v[180:183], v[58:61]
	v_mfma_f32_16x16x32_bf16 v[46:49], v[146:149], v[188:191], v[46:49]
	v_mfma_f32_16x16x32_bf16 v[42:45], v[154:157], v[188:191], v[42:45]
	v_mfma_f32_16x16x32_bf16 v[30:33], v[146:149], v[196:199], v[30:33]
	v_mfma_f32_16x16x32_bf16 v[26:29], v[154:157], v[196:199], v[26:29]
	v_mfma_f32_16x16x32_bf16 v[14:17], v[146:149], v[204:207], v[14:17]
	v_mfma_f32_16x16x32_bf16 v[10:13], v[154:157], v[204:207], v[10:13]
	v_mfma_f32_16x16x32_bf16 v[62:65], v[150:153], v[184:187], v[62:65]
	v_mfma_f32_16x16x32_bf16 v[58:61], v[158:161], v[184:187], v[58:61]
	v_mfma_f32_16x16x32_bf16 v[46:49], v[150:153], v[192:195], v[46:49]
	v_mfma_f32_16x16x32_bf16 v[42:45], v[158:161], v[192:195], v[42:45]
	v_mfma_f32_16x16x32_bf16 v[30:33], v[150:153], v[200:203], v[30:33]
	v_mfma_f32_16x16x32_bf16 v[26:29], v[158:161], v[200:203], v[26:29]
	v_mfma_f32_16x16x32_bf16 v[14:17], v[150:153], v[216:219], v[14:17]
	v_mfma_f32_16x16x32_bf16 v[10:13], v[158:161], v[216:219], v[10:13]
	s_setprio 0
	s_setprio 1
	v_mfma_f32_16x16x32_bf16 v[54:57], v[162:165], v[180:183], v[54:57]
	v_mfma_f32_16x16x32_bf16 v[50:53], v[172:175], v[180:183], v[50:53]
	v_mfma_f32_16x16x32_bf16 v[38:41], v[162:165], v[188:191], v[38:41]
	v_mfma_f32_16x16x32_bf16 v[34:37], v[172:175], v[188:191], v[34:37]
	v_mfma_f32_16x16x32_bf16 v[22:25], v[162:165], v[196:199], v[22:25]
	v_mfma_f32_16x16x32_bf16 v[18:21], v[172:175], v[196:199], v[18:21]
	v_mfma_f32_16x16x32_bf16 v[6:9], v[162:165], v[204:207], v[6:9]
	v_mfma_f32_16x16x32_bf16 v[2:5], v[172:175], v[204:207], v[2:5]
	v_mfma_f32_16x16x32_bf16 v[54:57], v[168:171], v[184:187], v[54:57]
	v_mfma_f32_16x16x32_bf16 v[50:53], v[176:179], v[184:187], v[50:53]
	v_mfma_f32_16x16x32_bf16 v[38:41], v[168:171], v[192:195], v[38:41]
	v_mfma_f32_16x16x32_bf16 v[34:37], v[176:179], v[192:195], v[34:37]
	v_mfma_f32_16x16x32_bf16 v[22:25], v[168:171], v[200:203], v[22:25]
	v_mfma_f32_16x16x32_bf16 v[18:21], v[176:179], v[200:203], v[18:21]
	v_mfma_f32_16x16x32_bf16 v[6:9], v[168:171], v[216:219], v[6:9]
	v_mfma_f32_16x16x32_bf16 v[2:5], v[176:179], v[216:219], v[2:5]
	s_setprio 0
	s_barrier
	s_add_i32 vcc_hi, vcc_hi, 2
	s_add_u32 s62, s62, 0x100
	s_addc_u32 s63, s63, 0
	s_cmp_gt_u32 vcc_hi, 13
	s_cbranch_scc0 .LBB0_587
	s_add_u32 s62, s8, 0xffffff00
	s_addc_u32 s63, s9, -1
	s_andn2_b64 vcc, exec, s[44:45]
	s_cbranch_vccnz .LBB0_590
	v_mov_b32_e32 v2, 0
	s_mov_b32 s20, s36
	s_mov_b32 s83, s46
	s_mov_b64 s[34:35], s[52:53]
	s_mov_b32 s68, s58
	v_mov_b32_e32 v3, v2
	v_mov_b32_e32 v4, v2
	v_mov_b32_e32 v5, v2
	v_mov_b32_e32 v6, v2
	v_mov_b32_e32 v7, v2
	v_mov_b32_e32 v8, v2
	v_mov_b32_e32 v9, v2
	v_mov_b32_e32 v18, v2
	v_mov_b32_e32 v19, v2
	v_mov_b32_e32 v20, v2
	v_mov_b32_e32 v21, v2
	v_mov_b32_e32 v22, v2
	v_mov_b32_e32 v23, v2
	v_mov_b32_e32 v24, v2
	v_mov_b32_e32 v25, v2
	v_mov_b32_e32 v34, v2
	v_mov_b32_e32 v35, v2
	v_mov_b32_e32 v36, v2
	v_mov_b32_e32 v37, v2
	v_mov_b32_e32 v38, v2
	v_mov_b32_e32 v39, v2
	v_mov_b32_e32 v40, v2
	v_mov_b32_e32 v41, v2
	v_mov_b32_e32 v50, v2
	v_mov_b32_e32 v51, v2
	v_mov_b32_e32 v52, v2
	v_mov_b32_e32 v53, v2
	v_mov_b32_e32 v54, v2
	v_mov_b32_e32 v55, v2
	v_mov_b32_e32 v56, v2
	v_mov_b32_e32 v57, v2
	v_mov_b32_e32 v10, v2
	v_mov_b32_e32 v11, v2
	v_mov_b32_e32 v12, v2
	v_mov_b32_e32 v13, v2
	v_mov_b32_e32 v14, v2
	v_mov_b32_e32 v15, v2
	v_mov_b32_e32 v16, v2
	v_mov_b32_e32 v17, v2
	v_mov_b32_e32 v26, v2
	v_mov_b32_e32 v27, v2
	v_mov_b32_e32 v28, v2
	v_mov_b32_e32 v29, v2
	v_mov_b32_e32 v30, v2
	v_mov_b32_e32 v31, v2
	v_mov_b32_e32 v32, v2
	v_mov_b32_e32 v33, v2
	v_mov_b32_e32 v42, v2
	v_mov_b32_e32 v43, v2
	v_mov_b32_e32 v44, v2
	v_mov_b32_e32 v45, v2
	v_mov_b32_e32 v46, v2
	v_mov_b32_e32 v47, v2
	v_mov_b32_e32 v48, v2
	v_mov_b32_e32 v49, v2
	v_mov_b32_e32 v58, v2
	v_mov_b32_e32 v59, v2
	v_mov_b32_e32 v60, v2
	v_mov_b32_e32 v61, v2
	v_mov_b32_e32 v62, v2
	v_mov_b32_e32 v63, v2
	v_mov_b32_e32 v64, v2
	v_mov_b32_e32 v65, v2
	v_mov_b32_e32 v66, v2
	v_mov_b32_e32 v67, v2
	v_mov_b32_e32 v68, v2
	v_mov_b32_e32 v69, v2
	v_mov_b32_e32 v70, v2
	v_mov_b32_e32 v71, v2
	v_mov_b32_e32 v72, v2
	v_mov_b32_e32 v73, v2
	v_mov_b32_e32 v82, v2
	v_mov_b32_e32 v83, v2
	v_mov_b32_e32 v84, v2
	v_mov_b32_e32 v85, v2
	v_mov_b32_e32 v86, v2
	v_mov_b32_e32 v87, v2
	v_mov_b32_e32 v88, v2
	v_mov_b32_e32 v89, v2
	v_mov_b32_e32 v98, v2
	v_mov_b32_e32 v99, v2
	v_mov_b32_e32 v100, v2
	v_mov_b32_e32 v101, v2
	v_mov_b32_e32 v102, v2
	v_mov_b32_e32 v103, v2
	v_mov_b32_e32 v104, v2
	v_mov_b32_e32 v105, v2
	v_mov_b32_e32 v114, v2
	v_mov_b32_e32 v115, v2
	v_mov_b32_e32 v116, v2
	v_mov_b32_e32 v117, v2
	v_mov_b32_e32 v122, v2
	v_mov_b32_e32 v123, v2
	v_mov_b32_e32 v124, v2
	v_mov_b32_e32 v125, v2
	v_mov_b32_e32 v74, v2
	v_mov_b32_e32 v75, v2
	v_mov_b32_e32 v76, v2
	v_mov_b32_e32 v77, v2
	v_mov_b32_e32 v78, v2
	v_mov_b32_e32 v79, v2
	v_mov_b32_e32 v80, v2
	v_mov_b32_e32 v81, v2
	v_mov_b32_e32 v90, v2
	v_mov_b32_e32 v91, v2
	v_mov_b32_e32 v92, v2
	v_mov_b32_e32 v93, v2
	v_mov_b32_e32 v94, v2
	v_mov_b32_e32 v95, v2
	v_mov_b32_e32 v96, v2
	v_mov_b32_e32 v97, v2
	v_mov_b32_e32 v106, v2
	v_mov_b32_e32 v107, v2
	v_mov_b32_e32 v108, v2
	v_mov_b32_e32 v109, v2
	v_mov_b32_e32 v110, v2
	v_mov_b32_e32 v111, v2
	v_mov_b32_e32 v112, v2
	v_mov_b32_e32 v113, v2
	v_mov_b32_e32 v130, v2
	v_mov_b32_e32 v131, v2
	v_mov_b32_e32 v132, v2
	v_mov_b32_e32 v133, v2
	v_mov_b32_e32 v134, v2
	v_mov_b32_e32 v135, v2
	v_mov_b32_e32 v136, v2
	v_mov_b32_e32 v137, v2
	s_andn2_b64 vcc, exec, s[42:43]
	s_cbranch_vccnz .LBB0_591
	s_branch .LBB0_592

.LBB0_676:
	v_lshl_add_u64 v[8:9], s[48:49], 0, v[0:1]
	v_mov_b32_e32 v119, v1
	v_lshl_add_u64 v[10:11], s[48:49], 0, v[118:119]
	v_mov_b32_e32 v127, v1
	s_and_b32 s19, s71, 3
	s_add_i32 m0, s4, 0x18000
	v_lshl_add_u64 v[8:9], v[8:9], 0, s[56:57]
	v_lshl_add_u64 v[12:13], s[30:31], 0, v[126:127]
	v_mov_b32_e32 v121, v1
	s_lshl_b32 s18, s76, 13
	s_lshl_b32 s34, s19, 12
	s_waitcnt vmcnt(2)
	s_barrier
	global_load_lds_dwordx4 v[8:9], off
	v_lshl_add_u64 v[8:9], v[10:11], 0, s[56:57]
	s_add_i32 m0, s4, 0x1a000
	s_add_i32 s85, s4, 0x8000
	s_add_i32 s90, s4, 0xa000
	v_lshl_add_u64 v[14:15], s[30:31], 0, v[120:121]
	global_load_lds_dwordx4 v[8:9], off
	v_lshl_add_u64 v[8:9], v[12:13], 0, s[56:57]
	s_mov_b32 m0, s85
	s_add_u32 s8, s48, 0x40080
	global_load_lds_dwordx4 v[8:9], off
	v_lshl_add_u64 v[8:9], v[14:15], 0, s[56:57]
	s_mov_b32 m0, s90
	s_addc_u32 s9, s49, 0
	global_load_lds_dwordx4 v[8:9], off
	s_add_i32 m0, s4, 0x1c000
	s_nop 0
	global_load_lds_dwordx4 v0, s[8:9]
	v_lshl_add_u64 v[8:9], s[8:9], 0, v[118:119]
	s_add_i32 m0, s4, 0x1e000
	v_and_b32_e32 v166, 15, v239
	global_load_lds_dwordx4 v118, s[8:9]
	v_and_b32_e32 v8, 48, v239
	v_lshlrev_b32_e32 v9, 2, v239
	v_lshl_or_b32 v8, v166, 6, v8
	v_and_b32_e32 v9, 32, v9
	v_bitop3_b32 v10, v8, s18, v9 bitop3:0xde
	v_bitop3_b32 v144, v8, s34, v9 bitop3:0xde
	v_lshlrev_b32_e32 v8, 14, v2
	v_and_b32_e32 v8, 0xffff8000, v8
	v_lshl_add_u32 v3, v3, 11, v8
	v_and_b32_e32 v2, 1, v2
	v_lshl_or_b32 v2, v2, 6, v3
	v_lshl_add_u32 v128, v4, 1, v2
	v_lshlrev_b32_e32 v2, 14, v6
	v_and_b32_e32 v2, 0xffff8000, v2
	v_lshl_add_u32 v2, v5, 11, v2
	v_and_b32_e32 v3, 1, v6
	s_waitcnt vmcnt(6)
	v_lshl_or_b32 v2, v3, 6, v2
	v_mov_b32_e32 v4, v1
	v_mov_b32_e32 v5, v1
	v_readlane_b32 s8, v254, 58
	v_lshl_add_u32 v138, v7, 1, v2
	v_mov_b32_e32 v2, v1
	v_mov_b32_e32 v3, v1
	v_add_u32_e32 v145, 0, v10
	v_mov_b64_e32 v[8:9], v[4:5]
	v_mov_b64_e32 v[20:21], v[4:5]
	v_mov_b64_e32 v[24:25], v[4:5]
	v_mov_b64_e32 v[36:37], v[4:5]
	v_mov_b64_e32 v[40:41], v[4:5]
	v_mov_b64_e32 v[52:53], v[4:5]
	v_mov_b64_e32 v[56:57], v[4:5]
	v_mov_b64_e32 v[12:13], v[4:5]
	v_mov_b64_e32 v[16:17], v[4:5]
	v_mov_b64_e32 v[28:29], v[4:5]
	v_mov_b64_e32 v[32:33], v[4:5]
	v_mov_b64_e32 v[44:45], v[4:5]
	v_mov_b64_e32 v[48:49], v[4:5]
	v_mov_b64_e32 v[60:61], v[4:5]
	v_mov_b64_e32 v[64:65], v[4:5]
	v_mov_b64_e32 v[68:69], v[4:5]
	v_mov_b64_e32 v[72:73], v[4:5]
	v_mov_b64_e32 v[84:85], v[4:5]
	v_mov_b64_e32 v[88:89], v[4:5]
	v_mov_b64_e32 v[100:101], v[4:5]
	v_mov_b64_e32 v[104:105], v[4:5]
	v_mov_b64_e32 v[116:117], v[4:5]
	v_mov_b64_e32 v[124:125], v[4:5]
	v_mov_b64_e32 v[76:77], v[4:5]
	v_mov_b64_e32 v[80:81], v[4:5]
	v_mov_b64_e32 v[92:93], v[4:5]
	v_mov_b64_e32 v[96:97], v[4:5]
	v_mov_b64_e32 v[108:109], v[4:5]
	v_mov_b64_e32 v[112:113], v[4:5]
	v_mov_b64_e32 v[132:133], v[4:5]
	v_mov_b64_e32 v[136:137], v[4:5]
	s_mov_b32 s18, s8
	v_readlane_b32 s8, v254, 54
	v_lshl_or_b32 v240, s76, 6, v166
	v_mov_b32_e32 v129, v1
	v_mov_b32_e32 v139, v1
	s_mov_b32 s68, 0
	v_mov_b64_e32 v[6:7], v[2:3]
	v_mov_b64_e32 v[18:19], v[2:3]
	v_mov_b64_e32 v[22:23], v[2:3]
	v_mov_b64_e32 v[34:35], v[2:3]
	v_mov_b64_e32 v[38:39], v[2:3]
	v_mov_b64_e32 v[50:51], v[2:3]
	v_mov_b64_e32 v[54:55], v[2:3]
	v_mov_b64_e32 v[10:11], v[2:3]
	v_mov_b64_e32 v[14:15], v[2:3]
	v_mov_b64_e32 v[26:27], v[2:3]
	v_mov_b64_e32 v[30:31], v[2:3]
	v_mov_b64_e32 v[42:43], v[2:3]
	v_mov_b64_e32 v[46:47], v[2:3]
	v_mov_b64_e32 v[58:59], v[2:3]
	v_mov_b64_e32 v[62:63], v[2:3]
	v_mov_b64_e32 v[66:67], v[2:3]
	v_mov_b64_e32 v[70:71], v[2:3]
	v_mov_b64_e32 v[82:83], v[2:3]
	v_mov_b64_e32 v[86:87], v[2:3]
	v_mov_b64_e32 v[98:99], v[2:3]
	v_mov_b64_e32 v[102:103], v[2:3]
	v_mov_b64_e32 v[114:115], v[2:3]
	v_mov_b64_e32 v[122:123], v[2:3]
	v_mov_b64_e32 v[74:75], v[2:3]
	v_mov_b64_e32 v[78:79], v[2:3]
	v_mov_b64_e32 v[90:91], v[2:3]
	v_mov_b64_e32 v[94:95], v[2:3]
	v_mov_b64_e32 v[106:107], v[2:3]
	v_mov_b64_e32 v[110:111], v[2:3]
	v_mov_b64_e32 v[130:131], v[2:3]
	v_mov_b64_e32 v[134:135], v[2:3]
	s_mov_b32 s92, s8
	s_barrier
	v_readlane_b32 s9, v254, 55

.LBB0_684:
	s_add_u32 s52, s30, s48
	s_addc_u32 s53, s31, s49
	s_add_u32 s52, s52, 0x100
	s_addc_u32 s53, s53, 0
	s_add_u32 s95, s8, s48
	s_addc_u32 s96, s9, s49
	s_add_i32 vcc_lo, 0, 0x10000
	s_cmpk_eq_i32 s48, 0x700
	s_cselect_b32 s63, s37, s53
	s_cselect_b32 s62, s59, s52
	s_cselect_b32 s53, s35, s96
	s_cselect_b32 s52, s93, s95
	s_add_i32 s95, 0, 0x14000
	v_add_u32_e32 v158, vcc_lo, v144
	v_add_u32_e32 v167, s95, v144
	ds_read_b128 v[146:149], v158
	ds_read_b128 v[150:153], v158 offset:1024
	ds_read_b128 v[154:157], v158 offset:2048
	ds_read_b128 v[158:161], v158 offset:3072
	ds_read_b128 v[162:165], v167
	ds_read_b128 v[168:171], v167 offset:1024
	ds_read_b128 v[172:175], v167 offset:2048
	ds_read_b128 v[176:179], v167 offset:3072
	v_lshl_add_u64 v[208:209], v[142:143], 0, s[48:49]
	s_add_i32 m0, s4, 0xc000
	ds_read_b128 v[180:183], v145
	ds_read_b128 v[184:187], v145 offset:1024
	ds_read_b128 v[188:191], v145 offset:2048
	ds_read_b128 v[192:195], v145 offset:3072
	ds_read_b128 v[196:199], v145 offset:4096
	ds_read_b128 v[200:203], v145 offset:5120
	ds_read_b128 v[204:207], v145 offset:6144
	ds_read_b128 v[216:219], v145 offset:7168
	global_load_lds_dwordx4 v[208:209], off
	s_add_i32 m0, s4, 0xe000
	v_lshl_add_u64 v[208:209], v[140:141], 0, s[48:49]
	global_load_lds_dwordx4 v[208:209], off
	s_waitcnt vmcnt(8)
	s_waitcnt lgkmcnt(0)
	s_barrier
	s_setprio 1
	s_waitcnt lgkmcnt(0)
	v_mfma_f32_16x16x32_bf16 v[134:137], v[146:149], v[180:183], v[134:137]
	v_mfma_f32_16x16x32_bf16 v[130:133], v[154:157], v[180:183], v[130:133]
	v_mfma_f32_16x16x32_bf16 v[110:113], v[146:149], v[188:191], v[110:113]
	v_mfma_f32_16x16x32_bf16 v[106:109], v[154:157], v[188:191], v[106:109]
	v_mfma_f32_16x16x32_bf16 v[94:97], v[146:149], v[196:199], v[94:97]
	v_mfma_f32_16x16x32_bf16 v[90:93], v[154:157], v[196:199], v[90:93]
	v_mfma_f32_16x16x32_bf16 v[78:81], v[146:149], v[204:207], v[78:81]
	v_mfma_f32_16x16x32_bf16 v[74:77], v[154:157], v[204:207], v[74:77]
	v_mfma_f32_16x16x32_bf16 v[134:137], v[150:153], v[184:187], v[134:137]
	v_mfma_f32_16x16x32_bf16 v[130:133], v[158:161], v[184:187], v[130:133]
	v_mfma_f32_16x16x32_bf16 v[110:113], v[150:153], v[192:195], v[110:113]
	v_mfma_f32_16x16x32_bf16 v[106:109], v[158:161], v[192:195], v[106:109]
	v_mfma_f32_16x16x32_bf16 v[94:97], v[150:153], v[200:203], v[94:97]
	v_mfma_f32_16x16x32_bf16 v[90:93], v[158:161], v[200:203], v[90:93]
	v_mfma_f32_16x16x32_bf16 v[78:81], v[150:153], v[216:219], v[78:81]
	v_mfma_f32_16x16x32_bf16 v[74:77], v[158:161], v[216:219], v[74:77]
	s_setprio 0
	s_setprio 1
	v_mfma_f32_16x16x32_bf16 v[122:125], v[162:165], v[180:183], v[122:125]
	v_mfma_f32_16x16x32_bf16 v[114:117], v[172:175], v[180:183], v[114:117]
	v_mfma_f32_16x16x32_bf16 v[102:105], v[162:165], v[188:191], v[102:105]
	v_mfma_f32_16x16x32_bf16 v[98:101], v[172:175], v[188:191], v[98:101]
	v_mfma_f32_16x16x32_bf16 v[86:89], v[162:165], v[196:199], v[86:89]
	v_mfma_f32_16x16x32_bf16 v[82:85], v[172:175], v[196:199], v[82:85]
	v_mfma_f32_16x16x32_bf16 v[70:73], v[162:165], v[204:207], v[70:73]
	v_mfma_f32_16x16x32_bf16 v[66:69], v[172:175], v[204:207], v[66:69]
	v_mfma_f32_16x16x32_bf16 v[122:125], v[168:171], v[184:187], v[122:125]
	v_mfma_f32_16x16x32_bf16 v[114:117], v[176:179], v[184:187], v[114:117]
	v_mfma_f32_16x16x32_bf16 v[102:105], v[168:171], v[192:195], v[102:105]
	v_mfma_f32_16x16x32_bf16 v[98:101], v[176:179], v[192:195], v[98:101]
	v_mfma_f32_16x16x32_bf16 v[86:89], v[168:171], v[200:203], v[86:89]
	v_mfma_f32_16x16x32_bf16 v[82:85], v[176:179], v[200:203], v[82:85]
	v_mfma_f32_16x16x32_bf16 v[70:73], v[168:171], v[216:219], v[70:73]
	v_mfma_f32_16x16x32_bf16 v[66:69], v[176:179], v[216:219], v[66:69]
	s_setprio 0
	s_barrier
	s_add_i32 s96, vcc_lo, s77
	v_lshl_add_u64 v[208:209], s[52:53], 0, v[0:1]
	s_mov_b32 m0, s96
	ds_read_b128 v[180:183], v145 offset:16384
	ds_read_b128 v[184:187], v145 offset:17408
	ds_read_b128 v[188:191], v145 offset:18432
	ds_read_b128 v[192:195], v145 offset:19456
	ds_read_b128 v[196:199], v145 offset:20480
	ds_read_b128 v[200:203], v145 offset:21504
	ds_read_b128 v[204:207], v145 offset:22528
	ds_read_b128 v[216:219], v145 offset:23552
	global_load_lds_dwordx4 v0, s[52:53]
	s_add_i32 m0, s96, 0x2000
	s_add_u32 vcc_lo, s52, 0x40000
	v_lshl_add_u64 v[220:221], s[52:53], 0, v[118:119]
	s_addc_u32 vcc_hi, s53, 0
	s_add_i32 s95, s95, s77
	global_load_lds_dwordx4 v118, s[52:53]
	v_lshl_add_u64 v[222:223], vcc, 0, v[0:1]
	s_mov_b32 m0, s95
	v_lshl_add_u64 v[224:225], s[62:63], 0, v[120:121]
	global_load_lds_dwordx4 v[222:223], off
	s_add_i32 m0, s95, 0x2000
	v_lshl_add_u64 v[222:223], vcc, 0, v[118:119]
	global_load_lds_dwordx4 v[222:223], off
	s_mov_b32 m0, s4
	v_lshl_add_u64 v[222:223], s[62:63], 0, v[126:127]
	global_load_lds_dwordx4 v126, s[62:63]
	s_mov_b32 m0, s5
	s_nop 0
	global_load_lds_dwordx4 v120, s[62:63]
	s_waitcnt vmcnt(8)
	s_waitcnt lgkmcnt(0)
	s_barrier
	s_setprio 1
	s_waitcnt lgkmcnt(0)
	v_mfma_f32_16x16x32_bf16 v[62:65], v[146:149], v[180:183], v[62:65]
	v_mfma_f32_16x16x32_bf16 v[58:61], v[154:157], v[180:183], v[58:61]
	v_mfma_f32_16x16x32_bf16 v[46:49], v[146:149], v[188:191], v[46:49]
	v_mfma_f32_16x16x32_bf16 v[42:45], v[154:157], v[188:191], v[42:45]
	v_mfma_f32_16x16x32_bf16 v[30:33], v[146:149], v[196:199], v[30:33]
	v_mfma_f32_16x16x32_bf16 v[26:29], v[154:157], v[196:199], v[26:29]
	v_mfma_f32_16x16x32_bf16 v[14:17], v[146:149], v[204:207], v[14:17]
	v_mfma_f32_16x16x32_bf16 v[10:13], v[154:157], v[204:207], v[10:13]
	v_mfma_f32_16x16x32_bf16 v[62:65], v[150:153], v[184:187], v[62:65]
	v_mfma_f32_16x16x32_bf16 v[58:61], v[158:161], v[184:187], v[58:61]
	v_mfma_f32_16x16x32_bf16 v[46:49], v[150:153], v[192:195], v[46:49]
	v_mfma_f32_16x16x32_bf16 v[42:45], v[158:161], v[192:195], v[42:45]
	v_mfma_f32_16x16x32_bf16 v[30:33], v[150:153], v[200:203], v[30:33]
	v_mfma_f32_16x16x32_bf16 v[26:29], v[158:161], v[200:203], v[26:29]
	v_mfma_f32_16x16x32_bf16 v[14:17], v[150:153], v[216:219], v[14:17]
	v_mfma_f32_16x16x32_bf16 v[10:13], v[158:161], v[216:219], v[10:13]
	s_setprio 0
	s_setprio 1
	v_mfma_f32_16x16x32_bf16 v[54:57], v[162:165], v[180:183], v[54:57]
	v_mfma_f32_16x16x32_bf16 v[50:53], v[172:175], v[180:183], v[50:53]
	v_mfma_f32_16x16x32_bf16 v[38:41], v[162:165], v[188:191], v[38:41]
	v_mfma_f32_16x16x32_bf16 v[34:37], v[172:175], v[188:191], v[34:37]
	v_mfma_f32_16x16x32_bf16 v[22:25], v[162:165], v[196:199], v[22:25]
	v_mfma_f32_16x16x32_bf16 v[18:21], v[172:175], v[196:199], v[18:21]
	v_mfma_f32_16x16x32_bf16 v[6:9], v[162:165], v[204:207], v[6:9]
	v_mfma_f32_16x16x32_bf16 v[2:5], v[172:175], v[204:207], v[2:5]
	v_mfma_f32_16x16x32_bf16 v[54:57], v[168:171], v[184:187], v[54:57]
	v_mfma_f32_16x16x32_bf16 v[50:53], v[176:179], v[184:187], v[50:53]
	v_mfma_f32_16x16x32_bf16 v[38:41], v[168:171], v[192:195], v[38:41]
	v_mfma_f32_16x16x32_bf16 v[34:37], v[176:179], v[192:195], v[34:37]
	v_mfma_f32_16x16x32_bf16 v[22:25], v[168:171], v[200:203], v[22:25]
	v_mfma_f32_16x16x32_bf16 v[18:21], v[176:179], v[200:203], v[18:21]
	v_mfma_f32_16x16x32_bf16 v[6:9], v[168:171], v[216:219], v[6:9]
	v_mfma_f32_16x16x32_bf16 v[2:5], v[176:179], v[216:219], v[2:5]
	s_setprio 0
	s_barrier
	s_add_i32 s95, 0, 0x18000
	s_add_i32 s96, 0, 0x1c000
	v_add_u32_e32 v158, s95, v144
	v_add_u32_e32 v167, s96, v144
	ds_read_b128 v[146:149], v158
	ds_read_b128 v[150:153], v158 offset:1024
	ds_read_b128 v[154:157], v158 offset:2048
	ds_read_b128 v[158:161], v158 offset:3072
	ds_read_b128 v[162:165], v167
	ds_read_b128 v[168:171], v167 offset:1024
	ds_read_b128 v[172:175], v167 offset:2048
	ds_read_b128 v[176:179], v167 offset:3072
	s_add_u32 s62, s62, 0x40000
	s_addc_u32 s63, s63, 0
	s_mov_b32 m0, s33
	ds_read_b128 v[180:183], v145 offset:32768
	ds_read_b128 v[184:187], v145 offset:33792
	ds_read_b128 v[188:191], v145 offset:34816
	ds_read_b128 v[192:195], v145 offset:35840
	ds_read_b128 v[196:199], v145 offset:36864
	ds_read_b128 v[200:203], v145 offset:37888
	ds_read_b128 v[204:207], v145 offset:38912
	ds_read_b128 v[216:219], v145 offset:39936
	global_load_lds_dwordx4 v126, s[62:63]
	s_mov_b32 m0, s84
	v_lshl_add_u64 v[242:243], s[62:63], 0, v[120:121]
	global_load_lds_dwordx4 v120, s[62:63]
	s_waitcnt vmcnt(8)
	s_waitcnt lgkmcnt(0)
	s_barrier
	s_setprio 1
	s_waitcnt lgkmcnt(0)
	v_mfma_f32_16x16x32_bf16 v[134:137], v[146:149], v[180:183], v[134:137]
	v_mfma_f32_16x16x32_bf16 v[130:133], v[154:157], v[180:183], v[130:133]
	v_mfma_f32_16x16x32_bf16 v[110:113], v[146:149], v[188:191], v[110:113]
	v_mfma_f32_16x16x32_bf16 v[106:109], v[154:157], v[188:191], v[106:109]
	v_mfma_f32_16x16x32_bf16 v[94:97], v[146:149], v[196:199], v[94:97]
	v_mfma_f32_16x16x32_bf16 v[90:93], v[154:157], v[196:199], v[90:93]
	v_mfma_f32_16x16x32_bf16 v[78:81], v[146:149], v[204:207], v[78:81]
	v_mfma_f32_16x16x32_bf16 v[74:77], v[154:157], v[204:207], v[74:77]
	v_mfma_f32_16x16x32_bf16 v[134:137], v[150:153], v[184:187], v[134:137]
	v_mfma_f32_16x16x32_bf16 v[130:133], v[158:161], v[184:187], v[130:133]
	v_mfma_f32_16x16x32_bf16 v[110:113], v[150:153], v[192:195], v[110:113]
	v_mfma_f32_16x16x32_bf16 v[106:109], v[158:161], v[192:195], v[106:109]
	v_mfma_f32_16x16x32_bf16 v[94:97], v[150:153], v[200:203], v[94:97]
	v_mfma_f32_16x16x32_bf16 v[90:93], v[158:161], v[200:203], v[90:93]
	v_mfma_f32_16x16x32_bf16 v[78:81], v[150:153], v[216:219], v[78:81]
	v_mfma_f32_16x16x32_bf16 v[74:77], v[158:161], v[216:219], v[74:77]
	s_setprio 0
	s_setprio 1
	v_mfma_f32_16x16x32_bf16 v[122:125], v[162:165], v[180:183], v[122:125]
	v_mfma_f32_16x16x32_bf16 v[114:117], v[172:175], v[180:183], v[114:117]
	v_mfma_f32_16x16x32_bf16 v[102:105], v[162:165], v[188:191], v[102:105]
	v_mfma_f32_16x16x32_bf16 v[98:101], v[172:175], v[188:191], v[98:101]
	v_mfma_f32_16x16x32_bf16 v[86:89], v[162:165], v[196:199], v[86:89]
	v_mfma_f32_16x16x32_bf16 v[82:85], v[172:175], v[196:199], v[82:85]
	v_mfma_f32_16x16x32_bf16 v[70:73], v[162:165], v[204:207], v[70:73]
	v_mfma_f32_16x16x32_bf16 v[66:69], v[172:175], v[204:207], v[66:69]
	v_mfma_f32_16x16x32_bf16 v[122:125], v[168:171], v[184:187], v[122:125]
	v_mfma_f32_16x16x32_bf16 v[114:117], v[176:179], v[184:187], v[114:117]
	v_mfma_f32_16x16x32_bf16 v[102:105], v[168:171], v[192:195], v[102:105]
	v_mfma_f32_16x16x32_bf16 v[98:101], v[176:179], v[192:195], v[98:101]
	v_mfma_f32_16x16x32_bf16 v[86:89], v[168:171], v[200:203], v[86:89]
	v_mfma_f32_16x16x32_bf16 v[82:85], v[176:179], v[200:203], v[82:85]
	v_mfma_f32_16x16x32_bf16 v[70:73], v[168:171], v[216:219], v[70:73]
	v_mfma_f32_16x16x32_bf16 v[66:69], v[176:179], v[216:219], v[66:69]
	s_setprio 0
	s_barrier
	s_add_i32 s62, s95, s77
	v_lshl_add_u64 v[208:209], v[208:209], 0, s[56:57]
	s_mov_b32 m0, s62
	ds_read_b128 v[180:183], v145 offset:49152
	ds_read_b128 v[184:187], v145 offset:50176
	ds_read_b128 v[188:191], v145 offset:51200
	ds_read_b128 v[192:195], v145 offset:52224
	ds_read_b128 v[196:199], v145 offset:53248
	ds_read_b128 v[200:203], v145 offset:54272
	ds_read_b128 v[204:207], v145 offset:55296
	ds_read_b128 v[216:219], v145 offset:56320
	global_load_lds_dwordx4 v[208:209], off
	s_add_i32 m0, s62, 0x2000
	s_add_u32 s52, s52, 0x40080
	v_lshl_add_u64 v[208:209], v[220:221], 0, s[56:57]
	s_addc_u32 s53, s53, 0
	s_add_i32 s62, s96, s77
	global_load_lds_dwordx4 v[208:209], off
	s_mov_b32 m0, s62
	s_nop 0
	global_load_lds_dwordx4 v0, s[52:53]
	s_add_i32 m0, s62, 0x2000
	s_nop 0
	global_load_lds_dwordx4 v118, s[52:53]
	s_mov_b32 m0, s85
	v_lshl_add_u64 v[208:209], v[222:223], 0, s[56:57]
	global_load_lds_dwordx4 v[208:209], off
	s_mov_b32 m0, s90
	v_lshl_add_u64 v[208:209], v[224:225], 0, s[56:57]
	global_load_lds_dwordx4 v[208:209], off
	s_waitcnt vmcnt(8)
	s_waitcnt lgkmcnt(0)
	s_barrier
	s_setprio 1
	s_waitcnt lgkmcnt(0)
	v_mfma_f32_16x16x32_bf16 v[62:65], v[146:149], v[180:183], v[62:65]
	v_mfma_f32_16x16x32_bf16 v[58:61], v[154:157], v[180:183], v[58:61]
	v_mfma_f32_16x16x32_bf16 v[46:49], v[146:149], v[188:191], v[46:49]
	v_mfma_f32_16x16x32_bf16 v[42:45], v[154:157], v[188:191], v[42:45]
	v_mfma_f32_16x16x32_bf16 v[30:33], v[146:149], v[196:199], v[30:33]
	v_mfma_f32_16x16x32_bf16 v[26:29], v[154:157], v[196:199], v[26:29]
	v_mfma_f32_16x16x32_bf16 v[14:17], v[146:149], v[204:207], v[14:17]
	v_mfma_f32_16x16x32_bf16 v[10:13], v[154:157], v[204:207], v[10:13]
	v_mfma_f32_16x16x32_bf16 v[62:65], v[150:153], v[184:187], v[62:65]
	v_mfma_f32_16x16x32_bf16 v[58:61], v[158:161], v[184:187], v[58:61]
	v_mfma_f32_16x16x32_bf16 v[46:49], v[150:153], v[192:195], v[46:49]
	v_mfma_f32_16x16x32_bf16 v[42:45], v[158:161], v[192:195], v[42:45]
	v_mfma_f32_16x16x32_bf16 v[30:33], v[150:153], v[200:203], v[30:33]
	v_mfma_f32_16x16x32_bf16 v[26:29], v[158:161], v[200:203], v[26:29]
	v_mfma_f32_16x16x32_bf16 v[14:17], v[150:153], v[216:219], v[14:17]
	v_mfma_f32_16x16x32_bf16 v[10:13], v[158:161], v[216:219], v[10:13]
	s_setprio 0
	s_setprio 1
	v_mfma_f32_16x16x32_bf16 v[54:57], v[162:165], v[180:183], v[54:57]
	v_mfma_f32_16x16x32_bf16 v[50:53], v[172:175], v[180:183], v[50:53]
	v_mfma_f32_16x16x32_bf16 v[38:41], v[162:165], v[188:191], v[38:41]
	v_mfma_f32_16x16x32_bf16 v[34:37], v[172:175], v[188:191], v[34:37]
	v_mfma_f32_16x16x32_bf16 v[22:25], v[162:165], v[196:199], v[22:25]
	v_mfma_f32_16x16x32_bf16 v[18:21], v[172:175], v[196:199], v[18:21]
	v_mfma_f32_16x16x32_bf16 v[6:9], v[162:165], v[204:207], v[6:9]
	v_mfma_f32_16x16x32_bf16 v[2:5], v[172:175], v[204:207], v[2:5]
	v_mfma_f32_16x16x32_bf16 v[54:57], v[168:171], v[184:187], v[54:57]
	v_mfma_f32_16x16x32_bf16 v[50:53], v[176:179], v[184:187], v[50:53]
	v_mfma_f32_16x16x32_bf16 v[38:41], v[168:171], v[192:195], v[38:41]
	v_mfma_f32_16x16x32_bf16 v[34:37], v[176:179], v[192:195], v[34:37]
	v_mfma_f32_16x16x32_bf16 v[22:25], v[168:171], v[200:203], v[22:25]
	v_mfma_f32_16x16x32_bf16 v[18:21], v[176:179], v[200:203], v[18:21]
	v_mfma_f32_16x16x32_bf16 v[6:9], v[168:171], v[216:219], v[6:9]
	v_mfma_f32_16x16x32_bf16 v[2:5], v[176:179], v[216:219], v[2:5]
	s_setprio 0
	s_barrier
	s_add_i32 s94, s94, 2
	s_add_u32 s48, s48, 0x100
	s_addc_u32 s49, s49, 0
	s_cmp_gt_u32 s94, 13
	s_cbranch_scc0 .LBB0_684
	s_add_u32 s48, s8, 0xffffff00
	s_addc_u32 s49, s9, -1
	s_andn2_b64 vcc, exec, s[42:43]
	s_cbranch_vccnz .LBB0_687
	v_mov_b32_e32 v2, 0
	s_mov_b32 s18, s34
	s_mov_b32 s92, s36
	s_mov_b64 s[30:31], s[46:47]
	s_mov_b32 s68, s58
	v_mov_b32_e32 v3, v2
	v_mov_b32_e32 v4, v2
	v_mov_b32_e32 v5, v2
	v_mov_b32_e32 v6, v2
	v_mov_b32_e32 v7, v2
	v_mov_b32_e32 v8, v2
	v_mov_b32_e32 v9, v2
	v_mov_b32_e32 v18, v2
	v_mov_b32_e32 v19, v2
	v_mov_b32_e32 v20, v2
	v_mov_b32_e32 v21, v2
	v_mov_b32_e32 v22, v2
	v_mov_b32_e32 v23, v2
	v_mov_b32_e32 v24, v2
	v_mov_b32_e32 v25, v2
	v_mov_b32_e32 v34, v2
	v_mov_b32_e32 v35, v2
	v_mov_b32_e32 v36, v2
	v_mov_b32_e32 v37, v2
	v_mov_b32_e32 v38, v2
	v_mov_b32_e32 v39, v2
	v_mov_b32_e32 v40, v2
	v_mov_b32_e32 v41, v2
	v_mov_b32_e32 v50, v2
	v_mov_b32_e32 v51, v2
	v_mov_b32_e32 v52, v2
	v_mov_b32_e32 v53, v2
	v_mov_b32_e32 v54, v2
	v_mov_b32_e32 v55, v2
	v_mov_b32_e32 v56, v2
	v_mov_b32_e32 v57, v2
	v_mov_b32_e32 v10, v2
	v_mov_b32_e32 v11, v2
	v_mov_b32_e32 v12, v2
	v_mov_b32_e32 v13, v2
	v_mov_b32_e32 v14, v2
	v_mov_b32_e32 v15, v2
	v_mov_b32_e32 v16, v2
	v_mov_b32_e32 v17, v2
	v_mov_b32_e32 v26, v2
	v_mov_b32_e32 v27, v2
	v_mov_b32_e32 v28, v2
	v_mov_b32_e32 v29, v2
	v_mov_b32_e32 v30, v2
	v_mov_b32_e32 v31, v2
	v_mov_b32_e32 v32, v2
	v_mov_b32_e32 v33, v2
	v_mov_b32_e32 v42, v2
	v_mov_b32_e32 v43, v2
	v_mov_b32_e32 v44, v2
	v_mov_b32_e32 v45, v2
	v_mov_b32_e32 v46, v2
	v_mov_b32_e32 v47, v2
	v_mov_b32_e32 v48, v2
	v_mov_b32_e32 v49, v2
	v_mov_b32_e32 v58, v2
	v_mov_b32_e32 v59, v2
	v_mov_b32_e32 v60, v2
	v_mov_b32_e32 v61, v2
	v_mov_b32_e32 v62, v2
	v_mov_b32_e32 v63, v2
	v_mov_b32_e32 v64, v2
	v_mov_b32_e32 v65, v2
	v_mov_b32_e32 v66, v2
	v_mov_b32_e32 v67, v2
	v_mov_b32_e32 v68, v2
	v_mov_b32_e32 v69, v2
	v_mov_b32_e32 v70, v2
	v_mov_b32_e32 v71, v2
	v_mov_b32_e32 v72, v2
	v_mov_b32_e32 v73, v2
	v_mov_b32_e32 v82, v2
	v_mov_b32_e32 v83, v2
	v_mov_b32_e32 v84, v2
	v_mov_b32_e32 v85, v2
	v_mov_b32_e32 v86, v2
	v_mov_b32_e32 v87, v2
	v_mov_b32_e32 v88, v2
	v_mov_b32_e32 v89, v2
	v_mov_b32_e32 v98, v2
	v_mov_b32_e32 v99, v2
	v_mov_b32_e32 v100, v2
	v_mov_b32_e32 v101, v2
	v_mov_b32_e32 v102, v2
	v_mov_b32_e32 v103, v2
	v_mov_b32_e32 v104, v2
	v_mov_b32_e32 v105, v2
	v_mov_b32_e32 v114, v2
	v_mov_b32_e32 v115, v2
	v_mov_b32_e32 v116, v2
	v_mov_b32_e32 v117, v2
	v_mov_b32_e32 v122, v2
	v_mov_b32_e32 v123, v2
	v_mov_b32_e32 v124, v2
	v_mov_b32_e32 v125, v2
	v_mov_b32_e32 v74, v2
	v_mov_b32_e32 v75, v2
	v_mov_b32_e32 v76, v2
	v_mov_b32_e32 v77, v2
	v_mov_b32_e32 v78, v2
	v_mov_b32_e32 v79, v2
	v_mov_b32_e32 v80, v2
	v_mov_b32_e32 v81, v2
	v_mov_b32_e32 v90, v2
	v_mov_b32_e32 v91, v2
	v_mov_b32_e32 v92, v2
	v_mov_b32_e32 v93, v2
	v_mov_b32_e32 v94, v2
	v_mov_b32_e32 v95, v2
	v_mov_b32_e32 v96, v2
	v_mov_b32_e32 v97, v2
	v_mov_b32_e32 v106, v2
	v_mov_b32_e32 v107, v2
	v_mov_b32_e32 v108, v2
	v_mov_b32_e32 v109, v2
	v_mov_b32_e32 v110, v2
	v_mov_b32_e32 v111, v2
	v_mov_b32_e32 v112, v2
	v_mov_b32_e32 v113, v2
	v_mov_b32_e32 v130, v2
	v_mov_b32_e32 v131, v2
	v_mov_b32_e32 v132, v2
	v_mov_b32_e32 v133, v2
	v_mov_b32_e32 v134, v2
	v_mov_b32_e32 v135, v2
	v_mov_b32_e32 v136, v2
	v_mov_b32_e32 v137, v2
	s_branch .LBB0_688

.LBB0_830:
	s_add_u32 s14, s14, 0xac00000
	s_addc_u32 s15, s15, 0
	s_add_u32 s16, s16, 0x1f00000
	s_addc_u32 s17, s17, 0
	s_lshl_b32 s8, s8, 5
	s_and_b32 s20, s8, 0x60
	s_add_i32 m0, s43, 0x18000
	v_lshl_add_u64 v[8:9], v[8:9], 0, s[56:57]
	s_lshl_b32 s18, s5, 13
	s_lshl_b32 s19, s20, 7
	s_waitcnt vmcnt(2)
	s_barrier
	global_load_lds_dwordx4 v[8:9], off
	v_lshl_add_u64 v[6:7], v[6:7], 0, s[56:57]
	s_add_i32 m0, s43, 0x1a000
	s_add_i32 s47, s43, 0x8000
	s_add_i32 s48, s43, 0xa000
	global_load_lds_dwordx4 v[6:7], off
	v_lshl_add_u64 v[2:3], v[2:3], 0, s[56:57]
	s_mov_b32 m0, s47
	s_add_u32 s8, s6, 0x40080
	global_load_lds_dwordx4 v[2:3], off
	v_lshl_add_u64 v[2:3], v[4:5], 0, s[56:57]
	s_mov_b32 m0, s48
	s_addc_u32 s9, s7, 0
	global_load_lds_dwordx4 v[2:3], off
	s_add_i32 m0, s43, 0x1c000
	s_nop 0
	global_load_lds_dwordx4 v0, s[8:9]
	v_lshl_add_u64 v[2:3], s[8:9], 0, v[158:159]
	s_add_i32 m0, s43, 0x1e000
	s_cmpk_lt_u32 s4, 0x100
	global_load_lds_dwordx4 v158, s[8:9]
	v_lshrrev_b32_e32 v3, 1, v10
	v_and_b32_e32 v3, 24, v3
	v_and_b32_e32 v2, 15, v10
	v_lshlrev_b32_e32 v4, 1, v3
	v_lshl_or_b32 v185, s5, 6, v2
	v_lshl_or_b32 v2, v2, 6, v4
	v_lshlrev_b32_e32 v4, 2, v10
	v_and_b32_e32 v4, 32, v4
	v_bitop3_b32 v5, v2, s18, v4 bitop3:0xde
	v_bitop3_b32 v186, v2, s19, v4 bitop3:0xde
	v_lshlrev_b32_e32 v2, 14, v11
	v_and_b32_e32 v2, 0xffff8000, v2
	v_or_b32_e32 v187, s20, v3
	v_lshl_add_u32 v2, v12, 11, v2
	v_and_b32_e32 v3, 1, v11
	v_lshl_or_b32 v2, v3, 6, v2
	v_lshl_add_u32 v164, v13, 1, v2
	v_lshlrev_b32_e32 v2, 14, v15
	v_and_b32_e32 v2, 0xffff8000, v2
	s_waitcnt vmcnt(6)
	v_lshl_add_u32 v2, v14, 11, v2
	v_and_b32_e32 v3, 1, v15
	v_lshl_or_b32 v2, v3, 6, v2
	s_cselect_b64 s[18:19], -1, 0
	v_mov_b32_e32 v165, v1
	v_lshl_add_u32 v166, v16, 1, v2
	v_mov_b32_e32 v167, v1
	s_mov_b32 s49, 0
	v_add_u32_e32 v188, 0, v5
	v_readlane_b32 s52, v253, 49
	v_readlane_b32 s4, v254, 3
	s_barrier
	v_readlane_b32 s5, v254, 4
	s_branch .LBB0_833

.Lnobar_e1e:
.LBB0_836:
	s_add_u32 s28, s6, 0xfffc0080
	s_addc_u32 s29, s7, -1
	s_add_i32 s41, 0, 0x10000
	s_cmp_eq_u32 s40, 12
	s_cselect_b32 s31, s5, s29
	s_cselect_b32 s30, s8, s28
	s_cselect_b32 s29, s9, s33
	s_cselect_b32 s28, s21, s23
	s_add_i32 s53, 0, 0x14000
	v_add_u32_e32 v142, s41, v186
	v_add_u32_e32 v168, s53, v186
	ds_read_b128 v[130:133], v142
	ds_read_b128 v[134:137], v142 offset:1024
	ds_read_b128 v[138:141], v142 offset:2048
	ds_read_b128 v[142:145], v142 offset:3072
	ds_read_b128 v[146:149], v168
	ds_read_b128 v[150:153], v168 offset:1024
	ds_read_b128 v[154:157], v168 offset:2048
	ds_read_b128 v[168:171], v168 offset:3072
	s_add_i32 m0, s43, 0xc000
	ds_read_b128 v[172:175], v188
	ds_read_b128 v[176:179], v188 offset:1024
	ds_read_b128 v[180:183], v188 offset:2048
	ds_read_b128 v[190:193], v188 offset:3072
	ds_read_b128 v[194:197], v188 offset:4096
	ds_read_b128 v[198:201], v188 offset:5120
	ds_read_b128 v[202:205], v188 offset:6144
	ds_read_b128 v[206:209], v188 offset:7168
	global_load_lds_dwordx4 v166, s[6:7]
	s_add_i32 m0, s43, 0xe000
	s_nop 0
	global_load_lds_dwordx4 v164, s[6:7]
	s_waitcnt vmcnt(8)
	s_waitcnt lgkmcnt(0)
	s_barrier
	s_setprio 1
	s_waitcnt lgkmcnt(0)
	v_mfma_f32_16x16x32_bf16 v[126:129], v[130:133], v[172:175], v[126:129]
	v_mfma_f32_16x16x32_bf16 v[122:125], v[138:141], v[172:175], v[122:125]
	v_mfma_f32_16x16x32_bf16 v[114:117], v[130:133], v[180:183], v[114:117]
	v_mfma_f32_16x16x32_bf16 v[106:109], v[138:141], v[180:183], v[106:109]
	v_mfma_f32_16x16x32_bf16 v[98:101], v[130:133], v[194:197], v[98:101]
	v_mfma_f32_16x16x32_bf16 v[90:93], v[138:141], v[194:197], v[90:93]
	v_mfma_f32_16x16x32_bf16 v[82:85], v[130:133], v[202:205], v[82:85]
	v_mfma_f32_16x16x32_bf16 v[74:77], v[138:141], v[202:205], v[74:77]
	v_mfma_f32_16x16x32_bf16 v[126:129], v[134:137], v[176:179], v[126:129]
	v_mfma_f32_16x16x32_bf16 v[122:125], v[142:145], v[176:179], v[122:125]
	v_mfma_f32_16x16x32_bf16 v[114:117], v[134:137], v[190:193], v[114:117]
	v_mfma_f32_16x16x32_bf16 v[106:109], v[142:145], v[190:193], v[106:109]
	v_mfma_f32_16x16x32_bf16 v[98:101], v[134:137], v[198:201], v[98:101]
	v_mfma_f32_16x16x32_bf16 v[90:93], v[142:145], v[198:201], v[90:93]
	v_mfma_f32_16x16x32_bf16 v[82:85], v[134:137], v[206:209], v[82:85]
	v_mfma_f32_16x16x32_bf16 v[74:77], v[142:145], v[206:209], v[74:77]
	s_setprio 0
	s_setprio 1
	v_mfma_f32_16x16x32_bf16 v[118:121], v[146:149], v[172:175], v[118:121]
	v_mfma_f32_16x16x32_bf16 v[110:113], v[154:157], v[172:175], v[110:113]
	v_mfma_f32_16x16x32_bf16 v[102:105], v[146:149], v[180:183], v[102:105]
	v_mfma_f32_16x16x32_bf16 v[94:97], v[154:157], v[180:183], v[94:97]
	v_mfma_f32_16x16x32_bf16 v[86:89], v[146:149], v[194:197], v[86:89]
	v_mfma_f32_16x16x32_bf16 v[78:81], v[154:157], v[194:197], v[78:81]
	v_mfma_f32_16x16x32_bf16 v[70:73], v[146:149], v[202:205], v[70:73]
	v_mfma_f32_16x16x32_bf16 v[66:69], v[154:157], v[202:205], v[66:69]
	v_mfma_f32_16x16x32_bf16 v[118:121], v[150:153], v[176:179], v[118:121]
	v_mfma_f32_16x16x32_bf16 v[110:113], v[168:171], v[176:179], v[110:113]
	v_mfma_f32_16x16x32_bf16 v[102:105], v[150:153], v[190:193], v[102:105]
	v_mfma_f32_16x16x32_bf16 v[94:97], v[168:171], v[190:193], v[94:97]
	v_mfma_f32_16x16x32_bf16 v[86:89], v[150:153], v[198:201], v[86:89]
	v_mfma_f32_16x16x32_bf16 v[78:81], v[168:171], v[198:201], v[78:81]
	v_mfma_f32_16x16x32_bf16 v[70:73], v[150:153], v[206:209], v[70:73]
	v_mfma_f32_16x16x32_bf16 v[66:69], v[168:171], v[206:209], v[66:69]
	s_setprio 0
	s_barrier
	s_add_i32 s41, s41, s42
	v_lshl_add_u64 v[216:217], s[28:29], 0, v[0:1]
	s_mov_b32 m0, s41
	ds_read_b128 v[172:175], v188 offset:16384
	ds_read_b128 v[176:179], v188 offset:17408
	ds_read_b128 v[180:183], v188 offset:18432
	ds_read_b128 v[190:193], v188 offset:19456
	ds_read_b128 v[194:197], v188 offset:20480
	ds_read_b128 v[198:201], v188 offset:21504
	ds_read_b128 v[202:205], v188 offset:22528
	ds_read_b128 v[206:209], v188 offset:23552
	global_load_lds_dwordx4 v0, s[28:29]
	s_add_i32 m0, s41, 0x2000
	s_add_u32 s58, s28, 0x40000
	v_lshl_add_u64 v[218:219], s[28:29], 0, v[158:159]
	s_addc_u32 s59, s29, 0
	s_add_i32 s41, s53, s42
	global_load_lds_dwordx4 v158, s[28:29]
	s_mov_b32 m0, s41
	v_lshl_add_u64 v[222:223], s[30:31], 0, v[160:161]
	global_load_lds_dwordx4 v0, s[58:59]
	s_add_i32 m0, s41, 0x2000
	s_nop 0
	global_load_lds_dwordx4 v158, s[58:59]
	s_mov_b32 m0, s43
	v_lshl_add_u64 v[220:221], s[30:31], 0, v[162:163]
	global_load_lds_dwordx4 v162, s[30:31]
	s_mov_b32 m0, s44
	s_nop 0
	global_load_lds_dwordx4 v160, s[30:31]
	s_waitcnt vmcnt(8)
	s_waitcnt lgkmcnt(0)
	s_barrier
	s_setprio 1
	s_waitcnt lgkmcnt(0)
	v_mfma_f32_16x16x32_bf16 v[62:65], v[130:133], v[172:175], v[62:65]
	v_mfma_f32_16x16x32_bf16 v[58:61], v[138:141], v[172:175], v[58:61]
	v_mfma_f32_16x16x32_bf16 v[50:53], v[130:133], v[180:183], v[50:53]
	v_mfma_f32_16x16x32_bf16 v[42:45], v[138:141], v[180:183], v[42:45]
	v_mfma_f32_16x16x32_bf16 v[34:37], v[130:133], v[194:197], v[34:37]
	v_mfma_f32_16x16x32_bf16 v[26:29], v[138:141], v[194:197], v[26:29]
	v_mfma_f32_16x16x32_bf16 v[18:21], v[130:133], v[202:205], v[18:21]
	v_mfma_f32_16x16x32_bf16 v[10:13], v[138:141], v[202:205], v[10:13]
	v_mfma_f32_16x16x32_bf16 v[62:65], v[134:137], v[176:179], v[62:65]
	v_mfma_f32_16x16x32_bf16 v[58:61], v[142:145], v[176:179], v[58:61]
	v_mfma_f32_16x16x32_bf16 v[50:53], v[134:137], v[190:193], v[50:53]
	v_mfma_f32_16x16x32_bf16 v[42:45], v[142:145], v[190:193], v[42:45]
	v_mfma_f32_16x16x32_bf16 v[34:37], v[134:137], v[198:201], v[34:37]
	v_mfma_f32_16x16x32_bf16 v[26:29], v[142:145], v[198:201], v[26:29]
	v_mfma_f32_16x16x32_bf16 v[18:21], v[134:137], v[206:209], v[18:21]
	v_mfma_f32_16x16x32_bf16 v[10:13], v[142:145], v[206:209], v[10:13]
	s_setprio 0
	s_setprio 1
	v_mfma_f32_16x16x32_bf16 v[54:57], v[146:149], v[172:175], v[54:57]
	v_mfma_f32_16x16x32_bf16 v[46:49], v[154:157], v[172:175], v[46:49]
	v_mfma_f32_16x16x32_bf16 v[38:41], v[146:149], v[180:183], v[38:41]
	v_mfma_f32_16x16x32_bf16 v[30:33], v[154:157], v[180:183], v[30:33]
	v_mfma_f32_16x16x32_bf16 v[22:25], v[146:149], v[194:197], v[22:25]
	v_mfma_f32_16x16x32_bf16 v[14:17], v[154:157], v[194:197], v[14:17]
	v_mfma_f32_16x16x32_bf16 v[6:9], v[146:149], v[202:205], v[6:9]
	v_mfma_f32_16x16x32_bf16 v[2:5], v[154:157], v[202:205], v[2:5]
	v_mfma_f32_16x16x32_bf16 v[54:57], v[150:153], v[176:179], v[54:57]
	v_mfma_f32_16x16x32_bf16 v[46:49], v[168:171], v[176:179], v[46:49]
	v_mfma_f32_16x16x32_bf16 v[38:41], v[150:153], v[190:193], v[38:41]
	v_mfma_f32_16x16x32_bf16 v[30:33], v[168:171], v[190:193], v[30:33]
	v_mfma_f32_16x16x32_bf16 v[22:25], v[150:153], v[198:201], v[22:25]
	v_mfma_f32_16x16x32_bf16 v[14:17], v[168:171], v[198:201], v[14:17]
	v_mfma_f32_16x16x32_bf16 v[6:9], v[150:153], v[206:209], v[6:9]
	v_mfma_f32_16x16x32_bf16 v[2:5], v[168:171], v[206:209], v[2:5]
	s_setprio 0
	s_barrier
	s_add_i32 s41, 0, 0x18000
	s_add_i32 s53, 0, 0x1c000
	v_add_u32_e32 v142, s41, v186
	v_add_u32_e32 v168, s53, v186
	ds_read_b128 v[130:133], v142
	ds_read_b128 v[134:137], v142 offset:1024
	ds_read_b128 v[138:141], v142 offset:2048
	ds_read_b128 v[142:145], v142 offset:3072
	ds_read_b128 v[146:149], v168
	ds_read_b128 v[150:153], v168 offset:1024
	ds_read_b128 v[154:157], v168 offset:2048
	ds_read_b128 v[168:171], v168 offset:3072
	s_add_u32 s30, s30, 0x40000
	s_addc_u32 s31, s31, 0
	s_mov_b32 m0, s45
	ds_read_b128 v[172:175], v188 offset:32768
	ds_read_b128 v[176:179], v188 offset:33792
	ds_read_b128 v[180:183], v188 offset:34816
	ds_read_b128 v[190:193], v188 offset:35840
	ds_read_b128 v[194:197], v188 offset:36864
	ds_read_b128 v[198:201], v188 offset:37888
	ds_read_b128 v[202:205], v188 offset:38912
	ds_read_b128 v[206:209], v188 offset:39936
	global_load_lds_dwordx4 v162, s[30:31]
	s_mov_b32 m0, s46
	s_nop 0
	global_load_lds_dwordx4 v160, s[30:31]
	s_waitcnt vmcnt(8)
	s_waitcnt lgkmcnt(0)
	s_barrier
	s_setprio 1
	s_waitcnt lgkmcnt(0)
	v_mfma_f32_16x16x32_bf16 v[126:129], v[130:133], v[172:175], v[126:129]
	v_mfma_f32_16x16x32_bf16 v[122:125], v[138:141], v[172:175], v[122:125]
	v_mfma_f32_16x16x32_bf16 v[114:117], v[130:133], v[180:183], v[114:117]
	v_mfma_f32_16x16x32_bf16 v[106:109], v[138:141], v[180:183], v[106:109]
	v_mfma_f32_16x16x32_bf16 v[98:101], v[130:133], v[194:197], v[98:101]
	v_mfma_f32_16x16x32_bf16 v[90:93], v[138:141], v[194:197], v[90:93]
	v_mfma_f32_16x16x32_bf16 v[82:85], v[130:133], v[202:205], v[82:85]
	v_mfma_f32_16x16x32_bf16 v[74:77], v[138:141], v[202:205], v[74:77]
	v_mfma_f32_16x16x32_bf16 v[126:129], v[134:137], v[176:179], v[126:129]
	v_mfma_f32_16x16x32_bf16 v[122:125], v[142:145], v[176:179], v[122:125]
	v_mfma_f32_16x16x32_bf16 v[114:117], v[134:137], v[190:193], v[114:117]
	v_mfma_f32_16x16x32_bf16 v[106:109], v[142:145], v[190:193], v[106:109]
	v_mfma_f32_16x16x32_bf16 v[98:101], v[134:137], v[198:201], v[98:101]
	v_mfma_f32_16x16x32_bf16 v[90:93], v[142:145], v[198:201], v[90:93]
	v_mfma_f32_16x16x32_bf16 v[82:85], v[134:137], v[206:209], v[82:85]
	v_mfma_f32_16x16x32_bf16 v[74:77], v[142:145], v[206:209], v[74:77]
	s_setprio 0
	s_setprio 1
	v_mfma_f32_16x16x32_bf16 v[118:121], v[146:149], v[172:175], v[118:121]
	v_mfma_f32_16x16x32_bf16 v[110:113], v[154:157], v[172:175], v[110:113]
	v_mfma_f32_16x16x32_bf16 v[102:105], v[146:149], v[180:183], v[102:105]
	v_mfma_f32_16x16x32_bf16 v[94:97], v[154:157], v[180:183], v[94:97]
	v_mfma_f32_16x16x32_bf16 v[86:89], v[146:149], v[194:197], v[86:89]
	v_mfma_f32_16x16x32_bf16 v[78:81], v[154:157], v[194:197], v[78:81]
	v_mfma_f32_16x16x32_bf16 v[70:73], v[146:149], v[202:205], v[70:73]
	v_mfma_f32_16x16x32_bf16 v[66:69], v[154:157], v[202:205], v[66:69]
	v_mfma_f32_16x16x32_bf16 v[118:121], v[150:153], v[176:179], v[118:121]
	v_mfma_f32_16x16x32_bf16 v[110:113], v[168:171], v[176:179], v[110:113]
	v_mfma_f32_16x16x32_bf16 v[102:105], v[150:153], v[190:193], v[102:105]
	v_mfma_f32_16x16x32_bf16 v[94:97], v[168:171], v[190:193], v[94:97]
	v_mfma_f32_16x16x32_bf16 v[86:89], v[150:153], v[198:201], v[86:89]
	v_mfma_f32_16x16x32_bf16 v[78:81], v[168:171], v[198:201], v[78:81]
	v_mfma_f32_16x16x32_bf16 v[70:73], v[150:153], v[206:209], v[70:73]
	v_mfma_f32_16x16x32_bf16 v[66:69], v[168:171], v[206:209], v[66:69]
	s_setprio 0
	s_barrier
	s_add_i32 s30, s41, s42
	v_lshl_add_u64 v[216:217], v[216:217], 0, s[56:57]
	s_mov_b32 m0, s30
	ds_read_b128 v[172:175], v188 offset:49152
	ds_read_b128 v[176:179], v188 offset:50176
	ds_read_b128 v[180:183], v188 offset:51200
	ds_read_b128 v[190:193], v188 offset:52224
	ds_read_b128 v[194:197], v188 offset:53248
	ds_read_b128 v[198:201], v188 offset:54272
	ds_read_b128 v[202:205], v188 offset:55296
	ds_read_b128 v[206:209], v188 offset:56320
	global_load_lds_dwordx4 v[216:217], off
	s_add_i32 m0, s30, 0x2000
	s_add_u32 s28, s28, 0x40080
	v_lshl_add_u64 v[216:217], v[218:219], 0, s[56:57]
	s_addc_u32 s29, s29, 0
	s_add_i32 s30, s53, s42
	global_load_lds_dwordx4 v[216:217], off
	s_mov_b32 m0, s30
	s_nop 0
	global_load_lds_dwordx4 v0, s[28:29]
	s_add_i32 m0, s30, 0x2000
	s_nop 0
	global_load_lds_dwordx4 v158, s[28:29]
	s_mov_b32 m0, s47
	v_lshl_add_u64 v[216:217], v[220:221], 0, s[56:57]
	global_load_lds_dwordx4 v[216:217], off
	s_mov_b32 m0, s48
	v_lshl_add_u64 v[216:217], v[222:223], 0, s[56:57]
	global_load_lds_dwordx4 v[216:217], off
	s_waitcnt vmcnt(8)
	s_waitcnt lgkmcnt(0)
	s_barrier
	s_setprio 1
	s_waitcnt lgkmcnt(0)
	v_mfma_f32_16x16x32_bf16 v[62:65], v[130:133], v[172:175], v[62:65]
	v_mfma_f32_16x16x32_bf16 v[58:61], v[138:141], v[172:175], v[58:61]
	v_mfma_f32_16x16x32_bf16 v[50:53], v[130:133], v[180:183], v[50:53]
	v_mfma_f32_16x16x32_bf16 v[42:45], v[138:141], v[180:183], v[42:45]
	v_mfma_f32_16x16x32_bf16 v[34:37], v[130:133], v[194:197], v[34:37]
	v_mfma_f32_16x16x32_bf16 v[26:29], v[138:141], v[194:197], v[26:29]
	v_mfma_f32_16x16x32_bf16 v[18:21], v[130:133], v[202:205], v[18:21]
	v_mfma_f32_16x16x32_bf16 v[10:13], v[138:141], v[202:205], v[10:13]
	v_mfma_f32_16x16x32_bf16 v[62:65], v[134:137], v[176:179], v[62:65]
	v_mfma_f32_16x16x32_bf16 v[58:61], v[142:145], v[176:179], v[58:61]
	v_mfma_f32_16x16x32_bf16 v[50:53], v[134:137], v[190:193], v[50:53]
	v_mfma_f32_16x16x32_bf16 v[42:45], v[142:145], v[190:193], v[42:45]
	v_mfma_f32_16x16x32_bf16 v[34:37], v[134:137], v[198:201], v[34:37]
	v_mfma_f32_16x16x32_bf16 v[26:29], v[142:145], v[198:201], v[26:29]
	v_mfma_f32_16x16x32_bf16 v[18:21], v[134:137], v[206:209], v[18:21]
	v_mfma_f32_16x16x32_bf16 v[10:13], v[142:145], v[206:209], v[10:13]
	s_setprio 0
	s_setprio 1
	v_mfma_f32_16x16x32_bf16 v[54:57], v[146:149], v[172:175], v[54:57]
	v_mfma_f32_16x16x32_bf16 v[46:49], v[154:157], v[172:175], v[46:49]
	v_mfma_f32_16x16x32_bf16 v[38:41], v[146:149], v[180:183], v[38:41]
	v_mfma_f32_16x16x32_bf16 v[30:33], v[154:157], v[180:183], v[30:33]
	v_mfma_f32_16x16x32_bf16 v[22:25], v[146:149], v[194:197], v[22:25]
	v_mfma_f32_16x16x32_bf16 v[14:17], v[154:157], v[194:197], v[14:17]
	v_mfma_f32_16x16x32_bf16 v[6:9], v[146:149], v[202:205], v[6:9]
	v_mfma_f32_16x16x32_bf16 v[2:5], v[154:157], v[202:205], v[2:5]
	v_mfma_f32_16x16x32_bf16 v[54:57], v[150:153], v[176:179], v[54:57]
	v_mfma_f32_16x16x32_bf16 v[46:49], v[168:171], v[176:179], v[46:49]
	v_mfma_f32_16x16x32_bf16 v[38:41], v[150:153], v[190:193], v[38:41]
	v_mfma_f32_16x16x32_bf16 v[30:33], v[168:171], v[190:193], v[30:33]
	v_mfma_f32_16x16x32_bf16 v[22:25], v[150:153], v[198:201], v[22:25]
	v_mfma_f32_16x16x32_bf16 v[14:17], v[168:171], v[198:201], v[14:17]
	v_mfma_f32_16x16x32_bf16 v[6:9], v[150:153], v[206:209], v[6:9]
	v_mfma_f32_16x16x32_bf16 v[2:5], v[168:171], v[206:209], v[2:5]
	s_setprio 0
	s_barrier
	s_add_i32 s40, s40, 2
	s_add_u32 s23, s23, 0x100
	s_addc_u32 s33, s33, 0
	s_add_u32 s6, s6, 0x100
	s_addc_u32 s7, s7, 0
	s_cmp_gt_u32 s40, 13
	s_cbranch_scc0 .LBB0_836
	s_and_b64 vcc, exec, s[18:19]
	s_cbranch_vccz .LBB0_839
	s_barrier

.LBB0_1513:
	v_lshl_add_u64 v[10:11], s[34:35], 0, v[0:1]
	v_mov_b32_e32 v119, v1
	v_lshl_add_u64 v[12:13], s[34:35], 0, v[118:119]
	v_mov_b32_e32 v127, v1
	s_and_b32 s49, s17, 3
	s_add_i32 m0, s4, 0x18000
	v_lshl_add_u64 v[10:11], v[10:11], 0, s[56:57]
	s_waitcnt lgkmcnt(0)
	v_lshl_add_u64 v[14:15], s[26:27], 0, v[126:127]
	v_mov_b32_e32 v121, v1
	s_lshl_b32 s16, s46, 13
	s_lshl_b32 s28, s49, 12
	s_waitcnt vmcnt(2)
	s_barrier
	global_load_lds_dwordx4 v[10:11], off
	v_lshl_add_u64 v[10:11], v[12:13], 0, s[56:57]
	s_add_i32 m0, s4, 0x1a000
	s_add_i32 s77, s4, 0x8000
	s_add_i32 s79, s4, 0xa000
	v_lshl_add_u64 v[16:17], s[26:27], 0, v[120:121]
	global_load_lds_dwordx4 v[10:11], off
	v_lshl_add_u64 v[10:11], v[14:15], 0, s[56:57]
	s_mov_b32 m0, s77
	s_add_u32 s8, s34, 0x60080
	global_load_lds_dwordx4 v[10:11], off
	v_lshl_add_u64 v[10:11], v[16:17], 0, s[56:57]
	s_mov_b32 m0, s79
	s_addc_u32 s9, s35, 0
	global_load_lds_dwordx4 v[10:11], off
	s_add_i32 m0, s4, 0x1c000
	s_nop 0
	global_load_lds_dwordx4 v0, s[8:9]
	v_lshl_add_u64 v[10:11], s[8:9], 0, v[118:119]
	s_add_i32 m0, s4, 0x1e000
	v_and_b32_e32 v167, 15, v166
	global_load_lds_dwordx4 v118, s[8:9]
	v_and_b32_e32 v10, 48, v166
	v_lshlrev_b32_e32 v11, 2, v166
	v_lshl_or_b32 v10, v167, 6, v10
	v_and_b32_e32 v11, 32, v11
	s_waitcnt vmcnt(0)
	v_bitop3_b32 v144, v10, s28, v11 bitop3:0xde
	s_movk_i32 s28, 0x600
	v_bitop3_b32 v12, v10, s16, v11 bitop3:0xde
	v_lshrrev_b32_e32 v10, 1, v2
	v_mul_lo_u32 v2, v3, s28
	s_movk_i32 s16, 0x6000
	v_mad_u64_u32 v[2:3], s[8:9], v10, s16, v[2:3]
	v_or_b32_e32 v2, v2, v4
	v_add_lshl_u32 v128, v2, v5, 1
	v_lshrrev_b32_e32 v3, 1, v7
	v_mul_lo_u32 v2, v6, s28
	v_mad_u64_u32 v[2:3], s[8:9], v3, s16, v[2:3]
	s_waitcnt vmcnt(6)
	v_or_b32_e32 v2, v2, v8
	v_mov_b32_e32 v4, v1
	v_mov_b32_e32 v5, v1
	v_readlane_b32 s8, v254, 58
	v_add_lshl_u32 v138, v2, v9, 1
	v_mov_b32_e32 v2, v1
	v_mov_b32_e32 v3, v1
	v_add_u32_e32 v145, 0, v12
	v_mov_b64_e32 v[8:9], v[4:5]
	v_mov_b64_e32 v[20:21], v[4:5]
	v_mov_b64_e32 v[24:25], v[4:5]
	v_mov_b64_e32 v[36:37], v[4:5]
	v_mov_b64_e32 v[40:41], v[4:5]
	v_mov_b64_e32 v[52:53], v[4:5]
	v_mov_b64_e32 v[56:57], v[4:5]
	v_mov_b64_e32 v[12:13], v[4:5]
	v_mov_b64_e32 v[16:17], v[4:5]
	v_mov_b64_e32 v[28:29], v[4:5]
	v_mov_b64_e32 v[32:33], v[4:5]
	v_mov_b64_e32 v[44:45], v[4:5]
	v_mov_b64_e32 v[48:49], v[4:5]
	v_mov_b64_e32 v[60:61], v[4:5]
	v_mov_b64_e32 v[64:65], v[4:5]
	v_mov_b64_e32 v[68:69], v[4:5]
	v_mov_b64_e32 v[72:73], v[4:5]
	v_mov_b64_e32 v[84:85], v[4:5]
	v_mov_b64_e32 v[88:89], v[4:5]
	v_mov_b64_e32 v[100:101], v[4:5]
	v_mov_b64_e32 v[104:105], v[4:5]
	v_mov_b64_e32 v[116:117], v[4:5]
	v_mov_b64_e32 v[124:125], v[4:5]
	v_mov_b64_e32 v[76:77], v[4:5]
	v_mov_b64_e32 v[80:81], v[4:5]
	v_mov_b64_e32 v[92:93], v[4:5]
	v_mov_b64_e32 v[96:97], v[4:5]
	v_mov_b64_e32 v[108:109], v[4:5]
	v_mov_b64_e32 v[112:113], v[4:5]
	v_mov_b64_e32 v[132:133], v[4:5]
	v_mov_b64_e32 v[136:137], v[4:5]
	s_mov_b32 s16, s8
	v_readlane_b32 s8, v254, 54
	v_lshl_or_b32 v240, s46, 6, v167
	v_mov_b32_e32 v129, v1
	v_mov_b32_e32 v139, v1
	s_mov_b32 s68, 0
	v_mov_b64_e32 v[6:7], v[2:3]
	v_mov_b64_e32 v[18:19], v[2:3]
	v_mov_b64_e32 v[22:23], v[2:3]
	v_mov_b64_e32 v[34:35], v[2:3]
	v_mov_b64_e32 v[38:39], v[2:3]
	v_mov_b64_e32 v[50:51], v[2:3]
	v_mov_b64_e32 v[54:55], v[2:3]
	v_mov_b64_e32 v[10:11], v[2:3]
	v_mov_b64_e32 v[14:15], v[2:3]
	v_mov_b64_e32 v[26:27], v[2:3]
	v_mov_b64_e32 v[30:31], v[2:3]
	v_mov_b64_e32 v[42:43], v[2:3]
	v_mov_b64_e32 v[46:47], v[2:3]
	v_mov_b64_e32 v[58:59], v[2:3]
	v_mov_b64_e32 v[62:63], v[2:3]
	v_mov_b64_e32 v[66:67], v[2:3]
	v_mov_b64_e32 v[70:71], v[2:3]
	v_mov_b64_e32 v[82:83], v[2:3]
	v_mov_b64_e32 v[86:87], v[2:3]
	v_mov_b64_e32 v[98:99], v[2:3]
	v_mov_b64_e32 v[102:103], v[2:3]
	v_mov_b64_e32 v[114:115], v[2:3]
	v_mov_b64_e32 v[122:123], v[2:3]
	v_mov_b64_e32 v[74:75], v[2:3]
	v_mov_b64_e32 v[78:79], v[2:3]
	v_mov_b64_e32 v[90:91], v[2:3]
	v_mov_b64_e32 v[94:95], v[2:3]
	v_mov_b64_e32 v[106:107], v[2:3]
	v_mov_b64_e32 v[110:111], v[2:3]
	v_mov_b64_e32 v[130:131], v[2:3]
	v_mov_b64_e32 v[134:135], v[2:3]
	s_mov_b32 s47, s8
	s_barrier
	v_readlane_b32 s9, v254, 55

.LBB0_1525:
	s_add_u32 s36, s26, s34
	s_addc_u32 s37, s27, s35
	s_add_u32 s36, s36, 0x100
	s_addc_u32 s37, s37, 0
	s_add_u32 s82, s8, s34
	s_addc_u32 s83, s9, s35
	s_add_i32 s84, 0, 0x10000
	s_cmpk_eq_i32 s34, 0xb00
	s_cselect_b32 s45, s31, s37
	s_cselect_b32 s44, s30, s36
	s_cselect_b32 s37, s29, s83
	s_cselect_b32 s36, s28, s82
	s_add_i32 s85, 0, 0x14000
	v_add_u32_e32 v158, s84, v144
	v_add_u32_e32 v176, s85, v144
	ds_read_b128 v[146:149], v158
	ds_read_b128 v[150:153], v158 offset:1024
	ds_read_b128 v[154:157], v158 offset:2048
	ds_read_b128 v[158:161], v158 offset:3072
	ds_read_b128 v[162:165], v176
	ds_read_b128 v[168:171], v176 offset:1024
	ds_read_b128 v[172:175], v176 offset:2048
	ds_read_b128 v[176:179], v176 offset:3072
	v_lshl_add_u64 v[208:209], v[142:143], 0, s[34:35]
	s_add_i32 m0, s4, 0xc000
	ds_read_b128 v[180:183], v145
	ds_read_b128 v[184:187], v145 offset:1024
	ds_read_b128 v[188:191], v145 offset:2048
	ds_read_b128 v[192:195], v145 offset:3072
	ds_read_b128 v[196:199], v145 offset:4096
	ds_read_b128 v[200:203], v145 offset:5120
	ds_read_b128 v[204:207], v145 offset:6144
	ds_read_b128 v[216:219], v145 offset:7168
	global_load_lds_dwordx4 v[208:209], off
	s_add_i32 m0, s4, 0xe000
	v_lshl_add_u64 v[208:209], v[140:141], 0, s[34:35]
	global_load_lds_dwordx4 v[208:209], off
	s_waitcnt vmcnt(8)
	s_waitcnt lgkmcnt(0)
	s_barrier
	s_setprio 1
	s_waitcnt lgkmcnt(0)
	v_mfma_f32_16x16x32_bf16 v[134:137], v[146:149], v[180:183], v[134:137]
	v_mfma_f32_16x16x32_bf16 v[130:133], v[154:157], v[180:183], v[130:133]
	v_mfma_f32_16x16x32_bf16 v[110:113], v[146:149], v[188:191], v[110:113]
	v_mfma_f32_16x16x32_bf16 v[106:109], v[154:157], v[188:191], v[106:109]
	v_mfma_f32_16x16x32_bf16 v[94:97], v[146:149], v[196:199], v[94:97]
	v_mfma_f32_16x16x32_bf16 v[90:93], v[154:157], v[196:199], v[90:93]
	v_mfma_f32_16x16x32_bf16 v[78:81], v[146:149], v[204:207], v[78:81]
	v_mfma_f32_16x16x32_bf16 v[74:77], v[154:157], v[204:207], v[74:77]
	v_mfma_f32_16x16x32_bf16 v[134:137], v[150:153], v[184:187], v[134:137]
	v_mfma_f32_16x16x32_bf16 v[130:133], v[158:161], v[184:187], v[130:133]
	v_mfma_f32_16x16x32_bf16 v[110:113], v[150:153], v[192:195], v[110:113]
	v_mfma_f32_16x16x32_bf16 v[106:109], v[158:161], v[192:195], v[106:109]
	v_mfma_f32_16x16x32_bf16 v[94:97], v[150:153], v[200:203], v[94:97]
	v_mfma_f32_16x16x32_bf16 v[90:93], v[158:161], v[200:203], v[90:93]
	v_mfma_f32_16x16x32_bf16 v[78:81], v[150:153], v[216:219], v[78:81]
	v_mfma_f32_16x16x32_bf16 v[74:77], v[158:161], v[216:219], v[74:77]
	s_setprio 0
	s_setprio 1
	v_mfma_f32_16x16x32_bf16 v[122:125], v[162:165], v[180:183], v[122:125]
	v_mfma_f32_16x16x32_bf16 v[114:117], v[172:175], v[180:183], v[114:117]
	v_mfma_f32_16x16x32_bf16 v[102:105], v[162:165], v[188:191], v[102:105]
	v_mfma_f32_16x16x32_bf16 v[98:101], v[172:175], v[188:191], v[98:101]
	v_mfma_f32_16x16x32_bf16 v[86:89], v[162:165], v[196:199], v[86:89]
	v_mfma_f32_16x16x32_bf16 v[82:85], v[172:175], v[196:199], v[82:85]
	v_mfma_f32_16x16x32_bf16 v[70:73], v[162:165], v[204:207], v[70:73]
	v_mfma_f32_16x16x32_bf16 v[66:69], v[172:175], v[204:207], v[66:69]
	v_mfma_f32_16x16x32_bf16 v[122:125], v[168:171], v[184:187], v[122:125]
	v_mfma_f32_16x16x32_bf16 v[114:117], v[176:179], v[184:187], v[114:117]
	v_mfma_f32_16x16x32_bf16 v[102:105], v[168:171], v[192:195], v[102:105]
	v_mfma_f32_16x16x32_bf16 v[98:101], v[176:179], v[192:195], v[98:101]
	v_mfma_f32_16x16x32_bf16 v[86:89], v[168:171], v[200:203], v[86:89]
	v_mfma_f32_16x16x32_bf16 v[82:85], v[176:179], v[200:203], v[82:85]
	v_mfma_f32_16x16x32_bf16 v[70:73], v[168:171], v[216:219], v[70:73]
	v_mfma_f32_16x16x32_bf16 v[66:69], v[176:179], v[216:219], v[66:69]
	s_setprio 0
	s_barrier
	s_add_i32 s82, s84, s70
	v_lshl_add_u64 v[208:209], s[36:37], 0, v[0:1]
	s_mov_b32 m0, s82
	ds_read_b128 v[180:183], v145 offset:16384
	ds_read_b128 v[184:187], v145 offset:17408
	ds_read_b128 v[188:191], v145 offset:18432
	ds_read_b128 v[192:195], v145 offset:19456
	ds_read_b128 v[196:199], v145 offset:20480
	ds_read_b128 v[200:203], v145 offset:21504
	ds_read_b128 v[204:207], v145 offset:22528
	ds_read_b128 v[216:219], v145 offset:23552
	global_load_lds_dwordx4 v0, s[36:37]
	s_add_i32 m0, s82, 0x2000
	s_add_u32 s82, s36, 0x60000
	v_lshl_add_u64 v[220:221], s[36:37], 0, v[118:119]
	s_addc_u32 s83, s37, 0
	s_add_i32 s84, s85, s70
	global_load_lds_dwordx4 v118, s[36:37]
	s_mov_b32 m0, s84
	v_lshl_add_u64 v[224:225], s[44:45], 0, v[120:121]
	global_load_lds_dwordx4 v0, s[82:83]
	s_add_i32 m0, s84, 0x2000
	s_nop 0
	global_load_lds_dwordx4 v118, s[82:83]
	s_mov_b32 m0, s4
	v_lshl_add_u64 v[222:223], s[44:45], 0, v[126:127]
	global_load_lds_dwordx4 v126, s[44:45]
	s_mov_b32 m0, s33
	s_nop 0
	global_load_lds_dwordx4 v120, s[44:45]
	s_waitcnt vmcnt(8)
	s_waitcnt lgkmcnt(0)
	s_barrier
	s_setprio 1
	s_waitcnt lgkmcnt(0)
	v_mfma_f32_16x16x32_bf16 v[62:65], v[146:149], v[180:183], v[62:65]
	v_mfma_f32_16x16x32_bf16 v[58:61], v[154:157], v[180:183], v[58:61]
	v_mfma_f32_16x16x32_bf16 v[46:49], v[146:149], v[188:191], v[46:49]
	v_mfma_f32_16x16x32_bf16 v[42:45], v[154:157], v[188:191], v[42:45]
	v_mfma_f32_16x16x32_bf16 v[30:33], v[146:149], v[196:199], v[30:33]
	v_mfma_f32_16x16x32_bf16 v[26:29], v[154:157], v[196:199], v[26:29]
	v_mfma_f32_16x16x32_bf16 v[14:17], v[146:149], v[204:207], v[14:17]
	v_mfma_f32_16x16x32_bf16 v[10:13], v[154:157], v[204:207], v[10:13]
	v_mfma_f32_16x16x32_bf16 v[62:65], v[150:153], v[184:187], v[62:65]
	v_mfma_f32_16x16x32_bf16 v[58:61], v[158:161], v[184:187], v[58:61]
	v_mfma_f32_16x16x32_bf16 v[46:49], v[150:153], v[192:195], v[46:49]
	v_mfma_f32_16x16x32_bf16 v[42:45], v[158:161], v[192:195], v[42:45]
	v_mfma_f32_16x16x32_bf16 v[30:33], v[150:153], v[200:203], v[30:33]
	v_mfma_f32_16x16x32_bf16 v[26:29], v[158:161], v[200:203], v[26:29]
	v_mfma_f32_16x16x32_bf16 v[14:17], v[150:153], v[216:219], v[14:17]
	v_mfma_f32_16x16x32_bf16 v[10:13], v[158:161], v[216:219], v[10:13]
	s_setprio 0
	s_setprio 1
	v_mfma_f32_16x16x32_bf16 v[54:57], v[162:165], v[180:183], v[54:57]
	v_mfma_f32_16x16x32_bf16 v[50:53], v[172:175], v[180:183], v[50:53]
	v_mfma_f32_16x16x32_bf16 v[38:41], v[162:165], v[188:191], v[38:41]
	v_mfma_f32_16x16x32_bf16 v[34:37], v[172:175], v[188:191], v[34:37]
	v_mfma_f32_16x16x32_bf16 v[22:25], v[162:165], v[196:199], v[22:25]
	v_mfma_f32_16x16x32_bf16 v[18:21], v[172:175], v[196:199], v[18:21]
	v_mfma_f32_16x16x32_bf16 v[6:9], v[162:165], v[204:207], v[6:9]
	v_mfma_f32_16x16x32_bf16 v[2:5], v[172:175], v[204:207], v[2:5]
	v_mfma_f32_16x16x32_bf16 v[54:57], v[168:171], v[184:187], v[54:57]
	v_mfma_f32_16x16x32_bf16 v[50:53], v[176:179], v[184:187], v[50:53]
	v_mfma_f32_16x16x32_bf16 v[38:41], v[168:171], v[192:195], v[38:41]
	v_mfma_f32_16x16x32_bf16 v[34:37], v[176:179], v[192:195], v[34:37]
	v_mfma_f32_16x16x32_bf16 v[22:25], v[168:171], v[200:203], v[22:25]
	v_mfma_f32_16x16x32_bf16 v[18:21], v[176:179], v[200:203], v[18:21]
	v_mfma_f32_16x16x32_bf16 v[6:9], v[168:171], v[216:219], v[6:9]
	v_mfma_f32_16x16x32_bf16 v[2:5], v[176:179], v[216:219], v[2:5]
	s_setprio 0
	s_barrier
	s_add_i32 s82, 0, 0x18000
	s_add_i32 s83, 0, 0x1c000
	v_add_u32_e32 v158, s82, v144
	v_add_u32_e32 v176, s83, v144
	ds_read_b128 v[146:149], v158
	ds_read_b128 v[150:153], v158 offset:1024
	ds_read_b128 v[154:157], v158 offset:2048
	ds_read_b128 v[158:161], v158 offset:3072
	ds_read_b128 v[162:165], v176
	ds_read_b128 v[168:171], v176 offset:1024
	ds_read_b128 v[172:175], v176 offset:2048
	ds_read_b128 v[176:179], v176 offset:3072
	s_add_u32 s44, s44, 0x60000
	s_addc_u32 s45, s45, 0
	s_mov_b32 m0, s71
	ds_read_b128 v[180:183], v145 offset:32768
	ds_read_b128 v[184:187], v145 offset:33792
	ds_read_b128 v[188:191], v145 offset:34816
	ds_read_b128 v[192:195], v145 offset:35840
	ds_read_b128 v[196:199], v145 offset:36864
	ds_read_b128 v[200:203], v145 offset:37888
	ds_read_b128 v[204:207], v145 offset:38912
	ds_read_b128 v[216:219], v145 offset:39936
	global_load_lds_dwordx4 v126, s[44:45]
	s_mov_b32 m0, s76
	v_lshl_add_u64 v[242:243], s[44:45], 0, v[120:121]
	global_load_lds_dwordx4 v120, s[44:45]
	s_waitcnt vmcnt(8)
	s_waitcnt lgkmcnt(0)
	s_barrier
	s_setprio 1
	s_waitcnt lgkmcnt(0)
	v_mfma_f32_16x16x32_bf16 v[134:137], v[146:149], v[180:183], v[134:137]
	v_mfma_f32_16x16x32_bf16 v[130:133], v[154:157], v[180:183], v[130:133]
	v_mfma_f32_16x16x32_bf16 v[110:113], v[146:149], v[188:191], v[110:113]
	v_mfma_f32_16x16x32_bf16 v[106:109], v[154:157], v[188:191], v[106:109]
	v_mfma_f32_16x16x32_bf16 v[94:97], v[146:149], v[196:199], v[94:97]
	v_mfma_f32_16x16x32_bf16 v[90:93], v[154:157], v[196:199], v[90:93]
	v_mfma_f32_16x16x32_bf16 v[78:81], v[146:149], v[204:207], v[78:81]
	v_mfma_f32_16x16x32_bf16 v[74:77], v[154:157], v[204:207], v[74:77]
	v_mfma_f32_16x16x32_bf16 v[134:137], v[150:153], v[184:187], v[134:137]
	v_mfma_f32_16x16x32_bf16 v[130:133], v[158:161], v[184:187], v[130:133]
	v_mfma_f32_16x16x32_bf16 v[110:113], v[150:153], v[192:195], v[110:113]
	v_mfma_f32_16x16x32_bf16 v[106:109], v[158:161], v[192:195], v[106:109]
	v_mfma_f32_16x16x32_bf16 v[94:97], v[150:153], v[200:203], v[94:97]
	v_mfma_f32_16x16x32_bf16 v[90:93], v[158:161], v[200:203], v[90:93]
	v_mfma_f32_16x16x32_bf16 v[78:81], v[150:153], v[216:219], v[78:81]
	v_mfma_f32_16x16x32_bf16 v[74:77], v[158:161], v[216:219], v[74:77]
	s_setprio 0
	s_setprio 1
	v_mfma_f32_16x16x32_bf16 v[122:125], v[162:165], v[180:183], v[122:125]
	v_mfma_f32_16x16x32_bf16 v[114:117], v[172:175], v[180:183], v[114:117]
	v_mfma_f32_16x16x32_bf16 v[102:105], v[162:165], v[188:191], v[102:105]
	v_mfma_f32_16x16x32_bf16 v[98:101], v[172:175], v[188:191], v[98:101]
	v_mfma_f32_16x16x32_bf16 v[86:89], v[162:165], v[196:199], v[86:89]
	v_mfma_f32_16x16x32_bf16 v[82:85], v[172:175], v[196:199], v[82:85]
	v_mfma_f32_16x16x32_bf16 v[70:73], v[162:165], v[204:207], v[70:73]
	v_mfma_f32_16x16x32_bf16 v[66:69], v[172:175], v[204:207], v[66:69]
	v_mfma_f32_16x16x32_bf16 v[122:125], v[168:171], v[184:187], v[122:125]
	v_mfma_f32_16x16x32_bf16 v[114:117], v[176:179], v[184:187], v[114:117]
	v_mfma_f32_16x16x32_bf16 v[102:105], v[168:171], v[192:195], v[102:105]
	v_mfma_f32_16x16x32_bf16 v[98:101], v[176:179], v[192:195], v[98:101]
	v_mfma_f32_16x16x32_bf16 v[86:89], v[168:171], v[200:203], v[86:89]
	v_mfma_f32_16x16x32_bf16 v[82:85], v[176:179], v[200:203], v[82:85]
	v_mfma_f32_16x16x32_bf16 v[70:73], v[168:171], v[216:219], v[70:73]
	v_mfma_f32_16x16x32_bf16 v[66:69], v[176:179], v[216:219], v[66:69]
	s_setprio 0
	s_barrier
	s_add_i32 s44, s82, s70
	v_lshl_add_u64 v[208:209], v[208:209], 0, s[56:57]
	s_mov_b32 m0, s44
	ds_read_b128 v[180:183], v145 offset:49152
	ds_read_b128 v[184:187], v145 offset:50176
	ds_read_b128 v[188:191], v145 offset:51200
	ds_read_b128 v[192:195], v145 offset:52224
	ds_read_b128 v[196:199], v145 offset:53248
	ds_read_b128 v[200:203], v145 offset:54272
	ds_read_b128 v[204:207], v145 offset:55296
	ds_read_b128 v[216:219], v145 offset:56320
	global_load_lds_dwordx4 v[208:209], off
	s_add_i32 m0, s44, 0x2000
	s_add_u32 s36, s36, 0x60080
	v_lshl_add_u64 v[208:209], v[220:221], 0, s[56:57]
	s_addc_u32 s37, s37, 0
	s_add_i32 s44, s83, s70
	global_load_lds_dwordx4 v[208:209], off
	s_mov_b32 m0, s44
	s_nop 0
	global_load_lds_dwordx4 v0, s[36:37]
	s_add_i32 m0, s44, 0x2000
	s_nop 0
	global_load_lds_dwordx4 v118, s[36:37]
	s_mov_b32 m0, s77
	v_lshl_add_u64 v[208:209], v[222:223], 0, s[56:57]
	global_load_lds_dwordx4 v[208:209], off
	s_mov_b32 m0, s79
	v_lshl_add_u64 v[208:209], v[224:225], 0, s[56:57]
	global_load_lds_dwordx4 v[208:209], off
	s_waitcnt vmcnt(8)
	s_waitcnt lgkmcnt(0)
	s_barrier
	s_setprio 1
	s_waitcnt lgkmcnt(0)
	v_mfma_f32_16x16x32_bf16 v[62:65], v[146:149], v[180:183], v[62:65]
	v_mfma_f32_16x16x32_bf16 v[58:61], v[154:157], v[180:183], v[58:61]
	v_mfma_f32_16x16x32_bf16 v[46:49], v[146:149], v[188:191], v[46:49]
	v_mfma_f32_16x16x32_bf16 v[42:45], v[154:157], v[188:191], v[42:45]
	v_mfma_f32_16x16x32_bf16 v[30:33], v[146:149], v[196:199], v[30:33]
	v_mfma_f32_16x16x32_bf16 v[26:29], v[154:157], v[196:199], v[26:29]
	v_mfma_f32_16x16x32_bf16 v[14:17], v[146:149], v[204:207], v[14:17]
	v_mfma_f32_16x16x32_bf16 v[10:13], v[154:157], v[204:207], v[10:13]
	v_mfma_f32_16x16x32_bf16 v[62:65], v[150:153], v[184:187], v[62:65]
	v_mfma_f32_16x16x32_bf16 v[58:61], v[158:161], v[184:187], v[58:61]
	v_mfma_f32_16x16x32_bf16 v[46:49], v[150:153], v[192:195], v[46:49]
	v_mfma_f32_16x16x32_bf16 v[42:45], v[158:161], v[192:195], v[42:45]
	v_mfma_f32_16x16x32_bf16 v[30:33], v[150:153], v[200:203], v[30:33]
	v_mfma_f32_16x16x32_bf16 v[26:29], v[158:161], v[200:203], v[26:29]
	v_mfma_f32_16x16x32_bf16 v[14:17], v[150:153], v[216:219], v[14:17]
	v_mfma_f32_16x16x32_bf16 v[10:13], v[158:161], v[216:219], v[10:13]
	s_setprio 0
	s_setprio 1
	v_mfma_f32_16x16x32_bf16 v[54:57], v[162:165], v[180:183], v[54:57]
	v_mfma_f32_16x16x32_bf16 v[50:53], v[172:175], v[180:183], v[50:53]
	v_mfma_f32_16x16x32_bf16 v[38:41], v[162:165], v[188:191], v[38:41]
	v_mfma_f32_16x16x32_bf16 v[34:37], v[172:175], v[188:191], v[34:37]
	v_mfma_f32_16x16x32_bf16 v[22:25], v[162:165], v[196:199], v[22:25]
	v_mfma_f32_16x16x32_bf16 v[18:21], v[172:175], v[196:199], v[18:21]
	v_mfma_f32_16x16x32_bf16 v[6:9], v[162:165], v[204:207], v[6:9]
	v_mfma_f32_16x16x32_bf16 v[2:5], v[172:175], v[204:207], v[2:5]
	v_mfma_f32_16x16x32_bf16 v[54:57], v[168:171], v[184:187], v[54:57]
	v_mfma_f32_16x16x32_bf16 v[50:53], v[176:179], v[184:187], v[50:53]
	v_mfma_f32_16x16x32_bf16 v[38:41], v[168:171], v[192:195], v[38:41]
	v_mfma_f32_16x16x32_bf16 v[34:37], v[176:179], v[192:195], v[34:37]
	v_mfma_f32_16x16x32_bf16 v[22:25], v[168:171], v[200:203], v[22:25]
	v_mfma_f32_16x16x32_bf16 v[18:21], v[176:179], v[200:203], v[18:21]
	v_mfma_f32_16x16x32_bf16 v[6:9], v[168:171], v[216:219], v[6:9]
	v_mfma_f32_16x16x32_bf16 v[2:5], v[176:179], v[216:219], v[2:5]
	s_setprio 0
	s_barrier
	s_add_i32 s59, s59, 2
	s_add_u32 s34, s34, 0x100
	s_addc_u32 s35, s35, 0
	s_cmp_gt_u32 s59, 21
	s_cbranch_scc0 .LBB0_1525
	s_add_u32 s34, s8, 0xffffff00
	s_addc_u32 s35, s9, -1
	s_and_b64 vcc, exec, s[42:43]
	s_cbranch_vccnz .LBB0_1528
	v_mov_b32_e32 v2, 0
	s_mov_b32 s16, s80
	s_mov_b32 s47, s81
	s_mov_b64 s[26:27], s[30:31]
	s_mov_b32 s68, s58
	v_mov_b32_e32 v3, v2
	v_mov_b32_e32 v4, v2
	v_mov_b32_e32 v5, v2
	v_mov_b32_e32 v6, v2
	v_mov_b32_e32 v7, v2
	v_mov_b32_e32 v8, v2
	v_mov_b32_e32 v9, v2
	v_mov_b32_e32 v18, v2
	v_mov_b32_e32 v19, v2
	v_mov_b32_e32 v20, v2
	v_mov_b32_e32 v21, v2
	v_mov_b32_e32 v22, v2
	v_mov_b32_e32 v23, v2
	v_mov_b32_e32 v24, v2
	v_mov_b32_e32 v25, v2
	v_mov_b32_e32 v34, v2
	v_mov_b32_e32 v35, v2
	v_mov_b32_e32 v36, v2
	v_mov_b32_e32 v37, v2
	v_mov_b32_e32 v38, v2
	v_mov_b32_e32 v39, v2
	v_mov_b32_e32 v40, v2
	v_mov_b32_e32 v41, v2
	v_mov_b32_e32 v50, v2
	v_mov_b32_e32 v51, v2
	v_mov_b32_e32 v52, v2
	v_mov_b32_e32 v53, v2
	v_mov_b32_e32 v54, v2
	v_mov_b32_e32 v55, v2
	v_mov_b32_e32 v56, v2
	v_mov_b32_e32 v57, v2
	v_mov_b32_e32 v10, v2
	v_mov_b32_e32 v11, v2
	v_mov_b32_e32 v12, v2
	v_mov_b32_e32 v13, v2
	v_mov_b32_e32 v14, v2
	v_mov_b32_e32 v15, v2
	v_mov_b32_e32 v16, v2
	v_mov_b32_e32 v17, v2
	v_mov_b32_e32 v26, v2
	v_mov_b32_e32 v27, v2
	v_mov_b32_e32 v28, v2
	v_mov_b32_e32 v29, v2
	v_mov_b32_e32 v30, v2
	v_mov_b32_e32 v31, v2
	v_mov_b32_e32 v32, v2
	v_mov_b32_e32 v33, v2
	v_mov_b32_e32 v42, v2
	v_mov_b32_e32 v43, v2
	v_mov_b32_e32 v44, v2
	v_mov_b32_e32 v45, v2
	v_mov_b32_e32 v46, v2
	v_mov_b32_e32 v47, v2
	v_mov_b32_e32 v48, v2
	v_mov_b32_e32 v49, v2
	v_mov_b32_e32 v58, v2
	v_mov_b32_e32 v59, v2
	v_mov_b32_e32 v60, v2
	v_mov_b32_e32 v61, v2
	v_mov_b32_e32 v62, v2
	v_mov_b32_e32 v63, v2
	v_mov_b32_e32 v64, v2
	v_mov_b32_e32 v65, v2
	v_mov_b32_e32 v66, v2
	v_mov_b32_e32 v67, v2
	v_mov_b32_e32 v68, v2
	v_mov_b32_e32 v69, v2
	v_mov_b32_e32 v70, v2
	v_mov_b32_e32 v71, v2
	v_mov_b32_e32 v72, v2
	v_mov_b32_e32 v73, v2
	v_mov_b32_e32 v82, v2
	v_mov_b32_e32 v83, v2
	v_mov_b32_e32 v84, v2
	v_mov_b32_e32 v85, v2
	v_mov_b32_e32 v86, v2
	v_mov_b32_e32 v87, v2
	v_mov_b32_e32 v88, v2
	v_mov_b32_e32 v89, v2
	v_mov_b32_e32 v98, v2
	v_mov_b32_e32 v99, v2
	v_mov_b32_e32 v100, v2
	v_mov_b32_e32 v101, v2
	v_mov_b32_e32 v102, v2
	v_mov_b32_e32 v103, v2
	v_mov_b32_e32 v104, v2
	v_mov_b32_e32 v105, v2
	v_mov_b32_e32 v114, v2
	v_mov_b32_e32 v115, v2
	v_mov_b32_e32 v116, v2
	v_mov_b32_e32 v117, v2
	v_mov_b32_e32 v122, v2
	v_mov_b32_e32 v123, v2
	v_mov_b32_e32 v124, v2
	v_mov_b32_e32 v125, v2
	v_mov_b32_e32 v74, v2
	v_mov_b32_e32 v75, v2
	v_mov_b32_e32 v76, v2
	v_mov_b32_e32 v77, v2
	v_mov_b32_e32 v78, v2
	v_mov_b32_e32 v79, v2
	v_mov_b32_e32 v80, v2
	v_mov_b32_e32 v81, v2
	v_mov_b32_e32 v90, v2
	v_mov_b32_e32 v91, v2
	v_mov_b32_e32 v92, v2
	v_mov_b32_e32 v93, v2
	v_mov_b32_e32 v94, v2
	v_mov_b32_e32 v95, v2
	v_mov_b32_e32 v96, v2
	v_mov_b32_e32 v97, v2
	v_mov_b32_e32 v106, v2
	v_mov_b32_e32 v107, v2
	v_mov_b32_e32 v108, v2
	v_mov_b32_e32 v109, v2
	v_mov_b32_e32 v110, v2
	v_mov_b32_e32 v111, v2
	v_mov_b32_e32 v112, v2
	v_mov_b32_e32 v113, v2
	v_mov_b32_e32 v130, v2
	v_mov_b32_e32 v131, v2
	v_mov_b32_e32 v132, v2
	v_mov_b32_e32 v133, v2
	v_mov_b32_e32 v134, v2
	v_mov_b32_e32 v135, v2
	v_mov_b32_e32 v136, v2
	v_mov_b32_e32 v137, v2
	s_andn2_b64 vcc, exec, s[40:41]
	s_cbranch_vccnz .LBB0_1529
	s_branch .LBB0_1531

.LBB0_1611:
	v_lshl_add_u64 v[10:11], s[34:35], 0, v[0:1]
	v_mov_b32_e32 v119, v1
	v_lshl_add_u64 v[12:13], s[34:35], 0, v[118:119]
	v_mov_b32_e32 v127, v1
	s_and_b32 s45, s17, 3
	s_add_i32 m0, s4, 0x18000
	v_lshl_add_u64 v[10:11], v[10:11], 0, s[56:57]
	v_lshl_add_u64 v[14:15], s[26:27], 0, v[126:127]
	v_mov_b32_e32 v121, v1
	s_lshl_b32 s16, s44, 13
	s_lshl_b32 s28, s45, 12
	s_waitcnt vmcnt(2)
	s_barrier
	global_load_lds_dwordx4 v[10:11], off
	v_lshl_add_u64 v[10:11], v[12:13], 0, s[56:57]
	s_add_i32 m0, s4, 0x1a000
	s_add_i32 s70, s4, 0x8000
	s_add_i32 s71, s4, 0xa000
	v_lshl_add_u64 v[16:17], s[26:27], 0, v[120:121]
	global_load_lds_dwordx4 v[10:11], off
	v_lshl_add_u64 v[10:11], v[14:15], 0, s[56:57]
	s_mov_b32 m0, s70
	s_add_u32 s8, s34, 0x60080
	global_load_lds_dwordx4 v[10:11], off
	v_lshl_add_u64 v[10:11], v[16:17], 0, s[56:57]
	s_mov_b32 m0, s71
	s_addc_u32 s9, s35, 0
	global_load_lds_dwordx4 v[10:11], off
	s_add_i32 m0, s4, 0x1c000
	s_nop 0
	global_load_lds_dwordx4 v0, s[8:9]
	v_lshl_add_u64 v[10:11], s[8:9], 0, v[118:119]
	s_add_i32 m0, s4, 0x1e000
	v_and_b32_e32 v166, 15, v239
	global_load_lds_dwordx4 v118, s[8:9]
	v_and_b32_e32 v10, 48, v239
	v_lshlrev_b32_e32 v11, 2, v239
	v_lshl_or_b32 v10, v166, 6, v10
	v_and_b32_e32 v11, 32, v11
	s_waitcnt vmcnt(0)
	v_bitop3_b32 v144, v10, s28, v11 bitop3:0xde
	s_movk_i32 s28, 0x600
	v_bitop3_b32 v12, v10, s16, v11 bitop3:0xde
	v_lshrrev_b32_e32 v10, 1, v2
	v_mul_lo_u32 v2, v3, s28
	s_movk_i32 s16, 0x6000
	v_mad_u64_u32 v[2:3], s[8:9], v10, s16, v[2:3]
	v_or_b32_e32 v2, v2, v4
	v_add_lshl_u32 v128, v2, v5, 1
	v_lshrrev_b32_e32 v3, 1, v7
	v_mul_lo_u32 v2, v6, s28
	v_mad_u64_u32 v[2:3], s[8:9], v3, s16, v[2:3]
	s_waitcnt vmcnt(6)
	v_or_b32_e32 v2, v2, v8
	v_mov_b32_e32 v4, v1
	v_mov_b32_e32 v5, v1
	v_readlane_b32 s8, v254, 58
	v_add_lshl_u32 v138, v2, v9, 1
	v_mov_b32_e32 v2, v1
	v_mov_b32_e32 v3, v1
	v_add_u32_e32 v145, 0, v12
	v_mov_b64_e32 v[8:9], v[4:5]
	v_mov_b64_e32 v[20:21], v[4:5]
	v_mov_b64_e32 v[24:25], v[4:5]
	v_mov_b64_e32 v[36:37], v[4:5]
	v_mov_b64_e32 v[40:41], v[4:5]
	v_mov_b64_e32 v[52:53], v[4:5]
	v_mov_b64_e32 v[56:57], v[4:5]
	v_mov_b64_e32 v[12:13], v[4:5]
	v_mov_b64_e32 v[16:17], v[4:5]
	v_mov_b64_e32 v[28:29], v[4:5]
	v_mov_b64_e32 v[32:33], v[4:5]
	v_mov_b64_e32 v[44:45], v[4:5]
	v_mov_b64_e32 v[48:49], v[4:5]
	v_mov_b64_e32 v[60:61], v[4:5]
	v_mov_b64_e32 v[64:65], v[4:5]
	v_mov_b64_e32 v[68:69], v[4:5]
	v_mov_b64_e32 v[72:73], v[4:5]
	v_mov_b64_e32 v[84:85], v[4:5]
	v_mov_b64_e32 v[88:89], v[4:5]
	v_mov_b64_e32 v[100:101], v[4:5]
	v_mov_b64_e32 v[104:105], v[4:5]
	v_mov_b64_e32 v[116:117], v[4:5]
	v_mov_b64_e32 v[124:125], v[4:5]
	v_mov_b64_e32 v[76:77], v[4:5]
	v_mov_b64_e32 v[80:81], v[4:5]
	v_mov_b64_e32 v[92:93], v[4:5]
	v_mov_b64_e32 v[96:97], v[4:5]
	v_mov_b64_e32 v[108:109], v[4:5]
	v_mov_b64_e32 v[112:113], v[4:5]
	v_mov_b64_e32 v[132:133], v[4:5]
	v_mov_b64_e32 v[136:137], v[4:5]
	s_mov_b32 s16, s8
	v_readlane_b32 s8, v254, 54
	v_lshl_or_b32 v240, s44, 6, v166
	v_mov_b32_e32 v129, v1
	v_mov_b32_e32 v139, v1
	s_mov_b32 s68, 0
	v_mov_b64_e32 v[6:7], v[2:3]
	v_mov_b64_e32 v[18:19], v[2:3]
	v_mov_b64_e32 v[22:23], v[2:3]
	v_mov_b64_e32 v[34:35], v[2:3]
	v_mov_b64_e32 v[38:39], v[2:3]
	v_mov_b64_e32 v[50:51], v[2:3]
	v_mov_b64_e32 v[54:55], v[2:3]
	v_mov_b64_e32 v[10:11], v[2:3]
	v_mov_b64_e32 v[14:15], v[2:3]
	v_mov_b64_e32 v[26:27], v[2:3]
	v_mov_b64_e32 v[30:31], v[2:3]
	v_mov_b64_e32 v[42:43], v[2:3]
	v_mov_b64_e32 v[46:47], v[2:3]
	v_mov_b64_e32 v[58:59], v[2:3]
	v_mov_b64_e32 v[62:63], v[2:3]
	v_mov_b64_e32 v[66:67], v[2:3]
	v_mov_b64_e32 v[70:71], v[2:3]
	v_mov_b64_e32 v[82:83], v[2:3]
	v_mov_b64_e32 v[86:87], v[2:3]
	v_mov_b64_e32 v[98:99], v[2:3]
	v_mov_b64_e32 v[102:103], v[2:3]
	v_mov_b64_e32 v[114:115], v[2:3]
	v_mov_b64_e32 v[122:123], v[2:3]
	v_mov_b64_e32 v[74:75], v[2:3]
	v_mov_b64_e32 v[78:79], v[2:3]
	v_mov_b64_e32 v[90:91], v[2:3]
	v_mov_b64_e32 v[94:95], v[2:3]
	v_mov_b64_e32 v[106:107], v[2:3]
	v_mov_b64_e32 v[110:111], v[2:3]
	v_mov_b64_e32 v[130:131], v[2:3]
	v_mov_b64_e32 v[134:135], v[2:3]
	s_mov_b32 s76, s8
	s_barrier
	v_readlane_b32 s9, v254, 55

.LBB0_1623:
	s_add_u32 s36, s26, s34
	s_addc_u32 s37, s27, s35
	s_add_u32 s36, s36, 0x100
	s_addc_u32 s37, s37, 0
	s_add_u32 s80, s8, s34
	s_addc_u32 s81, s9, s35
	s_add_i32 s82, 0, 0x10000
	s_cmpk_eq_i32 s34, 0xb00
	s_cselect_b32 s43, s31, s37
	s_cselect_b32 s42, s30, s36
	s_cselect_b32 s37, s29, s81
	s_cselect_b32 s36, s28, s80
	s_add_i32 s83, 0, 0x14000
	v_add_u32_e32 v158, s82, v144
	v_add_u32_e32 v167, s83, v144
	ds_read_b128 v[146:149], v158
	ds_read_b128 v[150:153], v158 offset:1024
	ds_read_b128 v[154:157], v158 offset:2048
	ds_read_b128 v[158:161], v158 offset:3072
	ds_read_b128 v[162:165], v167
	ds_read_b128 v[168:171], v167 offset:1024
	ds_read_b128 v[172:175], v167 offset:2048
	ds_read_b128 v[176:179], v167 offset:3072
	v_lshl_add_u64 v[208:209], v[142:143], 0, s[34:35]
	s_add_i32 m0, s4, 0xc000
	ds_read_b128 v[180:183], v145
	ds_read_b128 v[184:187], v145 offset:1024
	ds_read_b128 v[188:191], v145 offset:2048
	ds_read_b128 v[192:195], v145 offset:3072
	ds_read_b128 v[196:199], v145 offset:4096
	ds_read_b128 v[200:203], v145 offset:5120
	ds_read_b128 v[204:207], v145 offset:6144
	ds_read_b128 v[216:219], v145 offset:7168
	global_load_lds_dwordx4 v[208:209], off
	s_add_i32 m0, s4, 0xe000
	v_lshl_add_u64 v[208:209], v[140:141], 0, s[34:35]
	global_load_lds_dwordx4 v[208:209], off
	s_waitcnt vmcnt(8)
	s_waitcnt lgkmcnt(0)
	s_barrier
	s_setprio 1
	s_waitcnt lgkmcnt(0)
	v_mfma_f32_16x16x32_bf16 v[134:137], v[146:149], v[180:183], v[134:137]
	v_mfma_f32_16x16x32_bf16 v[130:133], v[154:157], v[180:183], v[130:133]
	v_mfma_f32_16x16x32_bf16 v[110:113], v[146:149], v[188:191], v[110:113]
	v_mfma_f32_16x16x32_bf16 v[106:109], v[154:157], v[188:191], v[106:109]
	v_mfma_f32_16x16x32_bf16 v[94:97], v[146:149], v[196:199], v[94:97]
	v_mfma_f32_16x16x32_bf16 v[90:93], v[154:157], v[196:199], v[90:93]
	v_mfma_f32_16x16x32_bf16 v[78:81], v[146:149], v[204:207], v[78:81]
	v_mfma_f32_16x16x32_bf16 v[74:77], v[154:157], v[204:207], v[74:77]
	v_mfma_f32_16x16x32_bf16 v[134:137], v[150:153], v[184:187], v[134:137]
	v_mfma_f32_16x16x32_bf16 v[130:133], v[158:161], v[184:187], v[130:133]
	v_mfma_f32_16x16x32_bf16 v[110:113], v[150:153], v[192:195], v[110:113]
	v_mfma_f32_16x16x32_bf16 v[106:109], v[158:161], v[192:195], v[106:109]
	v_mfma_f32_16x16x32_bf16 v[94:97], v[150:153], v[200:203], v[94:97]
	v_mfma_f32_16x16x32_bf16 v[90:93], v[158:161], v[200:203], v[90:93]
	v_mfma_f32_16x16x32_bf16 v[78:81], v[150:153], v[216:219], v[78:81]
	v_mfma_f32_16x16x32_bf16 v[74:77], v[158:161], v[216:219], v[74:77]
	s_setprio 0
	s_setprio 1
	v_mfma_f32_16x16x32_bf16 v[122:125], v[162:165], v[180:183], v[122:125]
	v_mfma_f32_16x16x32_bf16 v[114:117], v[172:175], v[180:183], v[114:117]
	v_mfma_f32_16x16x32_bf16 v[102:105], v[162:165], v[188:191], v[102:105]
	v_mfma_f32_16x16x32_bf16 v[98:101], v[172:175], v[188:191], v[98:101]
	v_mfma_f32_16x16x32_bf16 v[86:89], v[162:165], v[196:199], v[86:89]
	v_mfma_f32_16x16x32_bf16 v[82:85], v[172:175], v[196:199], v[82:85]
	v_mfma_f32_16x16x32_bf16 v[70:73], v[162:165], v[204:207], v[70:73]
	v_mfma_f32_16x16x32_bf16 v[66:69], v[172:175], v[204:207], v[66:69]
	v_mfma_f32_16x16x32_bf16 v[122:125], v[168:171], v[184:187], v[122:125]
	v_mfma_f32_16x16x32_bf16 v[114:117], v[176:179], v[184:187], v[114:117]
	v_mfma_f32_16x16x32_bf16 v[102:105], v[168:171], v[192:195], v[102:105]
	v_mfma_f32_16x16x32_bf16 v[98:101], v[176:179], v[192:195], v[98:101]
	v_mfma_f32_16x16x32_bf16 v[86:89], v[168:171], v[200:203], v[86:89]
	v_mfma_f32_16x16x32_bf16 v[82:85], v[176:179], v[200:203], v[82:85]
	v_mfma_f32_16x16x32_bf16 v[70:73], v[168:171], v[216:219], v[70:73]
	v_mfma_f32_16x16x32_bf16 v[66:69], v[176:179], v[216:219], v[66:69]
	s_setprio 0
	s_barrier
	s_add_i32 s80, s82, s53
	v_lshl_add_u64 v[208:209], s[36:37], 0, v[0:1]
	s_mov_b32 m0, s80
	ds_read_b128 v[180:183], v145 offset:16384
	ds_read_b128 v[184:187], v145 offset:17408
	ds_read_b128 v[188:191], v145 offset:18432
	ds_read_b128 v[192:195], v145 offset:19456
	ds_read_b128 v[196:199], v145 offset:20480
	ds_read_b128 v[200:203], v145 offset:21504
	ds_read_b128 v[204:207], v145 offset:22528
	ds_read_b128 v[216:219], v145 offset:23552
	global_load_lds_dwordx4 v0, s[36:37]
	s_add_i32 m0, s80, 0x2000
	s_add_u32 s80, s36, 0x60000
	v_lshl_add_u64 v[220:221], s[36:37], 0, v[118:119]
	s_addc_u32 s81, s37, 0
	s_add_i32 s82, s83, s53
	global_load_lds_dwordx4 v118, s[36:37]
	s_mov_b32 m0, s82
	v_lshl_add_u64 v[224:225], s[42:43], 0, v[120:121]
	global_load_lds_dwordx4 v0, s[80:81]
	s_add_i32 m0, s82, 0x2000
	s_nop 0
	global_load_lds_dwordx4 v118, s[80:81]
	s_mov_b32 m0, s4
	v_lshl_add_u64 v[222:223], s[42:43], 0, v[126:127]
	global_load_lds_dwordx4 v126, s[42:43]
	s_mov_b32 m0, s33
	s_nop 0
	global_load_lds_dwordx4 v120, s[42:43]
	s_waitcnt vmcnt(8)
	s_waitcnt lgkmcnt(0)
	s_barrier
	s_setprio 1
	s_waitcnt lgkmcnt(0)
	v_mfma_f32_16x16x32_bf16 v[62:65], v[146:149], v[180:183], v[62:65]
	v_mfma_f32_16x16x32_bf16 v[58:61], v[154:157], v[180:183], v[58:61]
	v_mfma_f32_16x16x32_bf16 v[46:49], v[146:149], v[188:191], v[46:49]
	v_mfma_f32_16x16x32_bf16 v[42:45], v[154:157], v[188:191], v[42:45]
	v_mfma_f32_16x16x32_bf16 v[30:33], v[146:149], v[196:199], v[30:33]
	v_mfma_f32_16x16x32_bf16 v[26:29], v[154:157], v[196:199], v[26:29]
	v_mfma_f32_16x16x32_bf16 v[14:17], v[146:149], v[204:207], v[14:17]
	v_mfma_f32_16x16x32_bf16 v[10:13], v[154:157], v[204:207], v[10:13]
	v_mfma_f32_16x16x32_bf16 v[62:65], v[150:153], v[184:187], v[62:65]
	v_mfma_f32_16x16x32_bf16 v[58:61], v[158:161], v[184:187], v[58:61]
	v_mfma_f32_16x16x32_bf16 v[46:49], v[150:153], v[192:195], v[46:49]
	v_mfma_f32_16x16x32_bf16 v[42:45], v[158:161], v[192:195], v[42:45]
	v_mfma_f32_16x16x32_bf16 v[30:33], v[150:153], v[200:203], v[30:33]
	v_mfma_f32_16x16x32_bf16 v[26:29], v[158:161], v[200:203], v[26:29]
	v_mfma_f32_16x16x32_bf16 v[14:17], v[150:153], v[216:219], v[14:17]
	v_mfma_f32_16x16x32_bf16 v[10:13], v[158:161], v[216:219], v[10:13]
	s_setprio 0
	s_setprio 1
	v_mfma_f32_16x16x32_bf16 v[54:57], v[162:165], v[180:183], v[54:57]
	v_mfma_f32_16x16x32_bf16 v[50:53], v[172:175], v[180:183], v[50:53]
	v_mfma_f32_16x16x32_bf16 v[38:41], v[162:165], v[188:191], v[38:41]
	v_mfma_f32_16x16x32_bf16 v[34:37], v[172:175], v[188:191], v[34:37]
	v_mfma_f32_16x16x32_bf16 v[22:25], v[162:165], v[196:199], v[22:25]
	v_mfma_f32_16x16x32_bf16 v[18:21], v[172:175], v[196:199], v[18:21]
	v_mfma_f32_16x16x32_bf16 v[6:9], v[162:165], v[204:207], v[6:9]
	v_mfma_f32_16x16x32_bf16 v[2:5], v[172:175], v[204:207], v[2:5]
	v_mfma_f32_16x16x32_bf16 v[54:57], v[168:171], v[184:187], v[54:57]
	v_mfma_f32_16x16x32_bf16 v[50:53], v[176:179], v[184:187], v[50:53]
	v_mfma_f32_16x16x32_bf16 v[38:41], v[168:171], v[192:195], v[38:41]
	v_mfma_f32_16x16x32_bf16 v[34:37], v[176:179], v[192:195], v[34:37]
	v_mfma_f32_16x16x32_bf16 v[22:25], v[168:171], v[200:203], v[22:25]
	v_mfma_f32_16x16x32_bf16 v[18:21], v[176:179], v[200:203], v[18:21]
	v_mfma_f32_16x16x32_bf16 v[6:9], v[168:171], v[216:219], v[6:9]
	v_mfma_f32_16x16x32_bf16 v[2:5], v[176:179], v[216:219], v[2:5]
	s_setprio 0
	s_barrier
	s_add_i32 s80, 0, 0x18000
	s_add_i32 s81, 0, 0x1c000
	v_add_u32_e32 v158, s80, v144
	v_add_u32_e32 v167, s81, v144
	ds_read_b128 v[146:149], v158
	ds_read_b128 v[150:153], v158 offset:1024
	ds_read_b128 v[154:157], v158 offset:2048
	ds_read_b128 v[158:161], v158 offset:3072
	ds_read_b128 v[162:165], v167
	ds_read_b128 v[168:171], v167 offset:1024
	ds_read_b128 v[172:175], v167 offset:2048
	ds_read_b128 v[176:179], v167 offset:3072
	s_add_u32 s42, s42, 0x60000
	s_addc_u32 s43, s43, 0
	s_mov_b32 m0, s62
	ds_read_b128 v[180:183], v145 offset:32768
	ds_read_b128 v[184:187], v145 offset:33792
	ds_read_b128 v[188:191], v145 offset:34816
	ds_read_b128 v[192:195], v145 offset:35840
	ds_read_b128 v[196:199], v145 offset:36864
	ds_read_b128 v[200:203], v145 offset:37888
	ds_read_b128 v[204:207], v145 offset:38912
	ds_read_b128 v[216:219], v145 offset:39936
	global_load_lds_dwordx4 v126, s[42:43]
	s_mov_b32 m0, s63
	v_lshl_add_u64 v[242:243], s[42:43], 0, v[120:121]
	global_load_lds_dwordx4 v120, s[42:43]
	s_waitcnt vmcnt(8)
	s_waitcnt lgkmcnt(0)
	s_barrier
	s_setprio 1
	s_waitcnt lgkmcnt(0)
	v_mfma_f32_16x16x32_bf16 v[134:137], v[146:149], v[180:183], v[134:137]
	v_mfma_f32_16x16x32_bf16 v[130:133], v[154:157], v[180:183], v[130:133]
	v_mfma_f32_16x16x32_bf16 v[110:113], v[146:149], v[188:191], v[110:113]
	v_mfma_f32_16x16x32_bf16 v[106:109], v[154:157], v[188:191], v[106:109]
	v_mfma_f32_16x16x32_bf16 v[94:97], v[146:149], v[196:199], v[94:97]
	v_mfma_f32_16x16x32_bf16 v[90:93], v[154:157], v[196:199], v[90:93]
	v_mfma_f32_16x16x32_bf16 v[78:81], v[146:149], v[204:207], v[78:81]
	v_mfma_f32_16x16x32_bf16 v[74:77], v[154:157], v[204:207], v[74:77]
	v_mfma_f32_16x16x32_bf16 v[134:137], v[150:153], v[184:187], v[134:137]
	v_mfma_f32_16x16x32_bf16 v[130:133], v[158:161], v[184:187], v[130:133]
	v_mfma_f32_16x16x32_bf16 v[110:113], v[150:153], v[192:195], v[110:113]
	v_mfma_f32_16x16x32_bf16 v[106:109], v[158:161], v[192:195], v[106:109]
	v_mfma_f32_16x16x32_bf16 v[94:97], v[150:153], v[200:203], v[94:97]
	v_mfma_f32_16x16x32_bf16 v[90:93], v[158:161], v[200:203], v[90:93]
	v_mfma_f32_16x16x32_bf16 v[78:81], v[150:153], v[216:219], v[78:81]
	v_mfma_f32_16x16x32_bf16 v[74:77], v[158:161], v[216:219], v[74:77]
	s_setprio 0
	s_setprio 1
	v_mfma_f32_16x16x32_bf16 v[122:125], v[162:165], v[180:183], v[122:125]
	v_mfma_f32_16x16x32_bf16 v[114:117], v[172:175], v[180:183], v[114:117]
	v_mfma_f32_16x16x32_bf16 v[102:105], v[162:165], v[188:191], v[102:105]
	v_mfma_f32_16x16x32_bf16 v[98:101], v[172:175], v[188:191], v[98:101]
	v_mfma_f32_16x16x32_bf16 v[86:89], v[162:165], v[196:199], v[86:89]
	v_mfma_f32_16x16x32_bf16 v[82:85], v[172:175], v[196:199], v[82:85]
	v_mfma_f32_16x16x32_bf16 v[70:73], v[162:165], v[204:207], v[70:73]
	v_mfma_f32_16x16x32_bf16 v[66:69], v[172:175], v[204:207], v[66:69]
	v_mfma_f32_16x16x32_bf16 v[122:125], v[168:171], v[184:187], v[122:125]
	v_mfma_f32_16x16x32_bf16 v[114:117], v[176:179], v[184:187], v[114:117]
	v_mfma_f32_16x16x32_bf16 v[102:105], v[168:171], v[192:195], v[102:105]
	v_mfma_f32_16x16x32_bf16 v[98:101], v[176:179], v[192:195], v[98:101]
	v_mfma_f32_16x16x32_bf16 v[86:89], v[168:171], v[200:203], v[86:89]
	v_mfma_f32_16x16x32_bf16 v[82:85], v[176:179], v[200:203], v[82:85]
	v_mfma_f32_16x16x32_bf16 v[70:73], v[168:171], v[216:219], v[70:73]
	v_mfma_f32_16x16x32_bf16 v[66:69], v[176:179], v[216:219], v[66:69]
	s_setprio 0
	s_barrier
	s_add_i32 s42, s80, s53
	v_lshl_add_u64 v[208:209], v[208:209], 0, s[56:57]
	s_mov_b32 m0, s42
	ds_read_b128 v[180:183], v145 offset:49152
	ds_read_b128 v[184:187], v145 offset:50176
	ds_read_b128 v[188:191], v145 offset:51200
	ds_read_b128 v[192:195], v145 offset:52224
	ds_read_b128 v[196:199], v145 offset:53248
	ds_read_b128 v[200:203], v145 offset:54272
	ds_read_b128 v[204:207], v145 offset:55296
	ds_read_b128 v[216:219], v145 offset:56320
	global_load_lds_dwordx4 v[208:209], off
	s_add_i32 m0, s42, 0x2000
	s_add_u32 s36, s36, 0x60080
	v_lshl_add_u64 v[208:209], v[220:221], 0, s[56:57]
	s_addc_u32 s37, s37, 0
	s_add_i32 s42, s81, s53
	global_load_lds_dwordx4 v[208:209], off
	s_mov_b32 m0, s42
	s_nop 0
	global_load_lds_dwordx4 v0, s[36:37]
	s_add_i32 m0, s42, 0x2000
	s_nop 0
	global_load_lds_dwordx4 v118, s[36:37]
	s_mov_b32 m0, s70
	v_lshl_add_u64 v[208:209], v[222:223], 0, s[56:57]
	global_load_lds_dwordx4 v[208:209], off
	s_mov_b32 m0, s71
	v_lshl_add_u64 v[208:209], v[224:225], 0, s[56:57]
	global_load_lds_dwordx4 v[208:209], off
	s_waitcnt vmcnt(8)
	s_waitcnt lgkmcnt(0)
	s_barrier
	s_setprio 1
	s_waitcnt lgkmcnt(0)
	v_mfma_f32_16x16x32_bf16 v[62:65], v[146:149], v[180:183], v[62:65]
	v_mfma_f32_16x16x32_bf16 v[58:61], v[154:157], v[180:183], v[58:61]
	v_mfma_f32_16x16x32_bf16 v[46:49], v[146:149], v[188:191], v[46:49]
	v_mfma_f32_16x16x32_bf16 v[42:45], v[154:157], v[188:191], v[42:45]
	v_mfma_f32_16x16x32_bf16 v[30:33], v[146:149], v[196:199], v[30:33]
	v_mfma_f32_16x16x32_bf16 v[26:29], v[154:157], v[196:199], v[26:29]
	v_mfma_f32_16x16x32_bf16 v[14:17], v[146:149], v[204:207], v[14:17]
	v_mfma_f32_16x16x32_bf16 v[10:13], v[154:157], v[204:207], v[10:13]
	v_mfma_f32_16x16x32_bf16 v[62:65], v[150:153], v[184:187], v[62:65]
	v_mfma_f32_16x16x32_bf16 v[58:61], v[158:161], v[184:187], v[58:61]
	v_mfma_f32_16x16x32_bf16 v[46:49], v[150:153], v[192:195], v[46:49]
	v_mfma_f32_16x16x32_bf16 v[42:45], v[158:161], v[192:195], v[42:45]
	v_mfma_f32_16x16x32_bf16 v[30:33], v[150:153], v[200:203], v[30:33]
	v_mfma_f32_16x16x32_bf16 v[26:29], v[158:161], v[200:203], v[26:29]
	v_mfma_f32_16x16x32_bf16 v[14:17], v[150:153], v[216:219], v[14:17]
	v_mfma_f32_16x16x32_bf16 v[10:13], v[158:161], v[216:219], v[10:13]
	s_setprio 0
	s_setprio 1
	v_mfma_f32_16x16x32_bf16 v[54:57], v[162:165], v[180:183], v[54:57]
	v_mfma_f32_16x16x32_bf16 v[50:53], v[172:175], v[180:183], v[50:53]
	v_mfma_f32_16x16x32_bf16 v[38:41], v[162:165], v[188:191], v[38:41]
	v_mfma_f32_16x16x32_bf16 v[34:37], v[172:175], v[188:191], v[34:37]
	v_mfma_f32_16x16x32_bf16 v[22:25], v[162:165], v[196:199], v[22:25]
	v_mfma_f32_16x16x32_bf16 v[18:21], v[172:175], v[196:199], v[18:21]
	v_mfma_f32_16x16x32_bf16 v[6:9], v[162:165], v[204:207], v[6:9]
	v_mfma_f32_16x16x32_bf16 v[2:5], v[172:175], v[204:207], v[2:5]
	v_mfma_f32_16x16x32_bf16 v[54:57], v[168:171], v[184:187], v[54:57]
	v_mfma_f32_16x16x32_bf16 v[50:53], v[176:179], v[184:187], v[50:53]
	v_mfma_f32_16x16x32_bf16 v[38:41], v[168:171], v[192:195], v[38:41]
	v_mfma_f32_16x16x32_bf16 v[34:37], v[176:179], v[192:195], v[34:37]
	v_mfma_f32_16x16x32_bf16 v[22:25], v[168:171], v[200:203], v[22:25]
	v_mfma_f32_16x16x32_bf16 v[18:21], v[176:179], v[200:203], v[18:21]
	v_mfma_f32_16x16x32_bf16 v[6:9], v[168:171], v[216:219], v[6:9]
	v_mfma_f32_16x16x32_bf16 v[2:5], v[176:179], v[216:219], v[2:5]
	s_setprio 0
	s_barrier
	s_add_i32 s59, s59, 2
	s_add_u32 s34, s34, 0x100
	s_addc_u32 s35, s35, 0
	s_cmp_gt_u32 s59, 21
	s_cbranch_scc0 .LBB0_1623
	s_add_u32 s34, s8, 0xffffff00
	s_addc_u32 s35, s9, -1
	s_and_b64 vcc, exec, s[40:41]
	s_cbranch_vccnz .LBB0_1626
	v_mov_b32_e32 v2, 0
	s_mov_b32 s16, s77
	s_mov_b32 s76, s79
	s_mov_b64 s[26:27], s[30:31]
	s_mov_b32 s68, s58
	v_mov_b32_e32 v3, v2
	v_mov_b32_e32 v4, v2
	v_mov_b32_e32 v5, v2
	v_mov_b32_e32 v6, v2
	v_mov_b32_e32 v7, v2
	v_mov_b32_e32 v8, v2
	v_mov_b32_e32 v9, v2
	v_mov_b32_e32 v18, v2
	v_mov_b32_e32 v19, v2
	v_mov_b32_e32 v20, v2
	v_mov_b32_e32 v21, v2
	v_mov_b32_e32 v22, v2
	v_mov_b32_e32 v23, v2
	v_mov_b32_e32 v24, v2
	v_mov_b32_e32 v25, v2
	v_mov_b32_e32 v34, v2
	v_mov_b32_e32 v35, v2
	v_mov_b32_e32 v36, v2
	v_mov_b32_e32 v37, v2
	v_mov_b32_e32 v38, v2
	v_mov_b32_e32 v39, v2
	v_mov_b32_e32 v40, v2
	v_mov_b32_e32 v41, v2
	v_mov_b32_e32 v50, v2
	v_mov_b32_e32 v51, v2
	v_mov_b32_e32 v52, v2
	v_mov_b32_e32 v53, v2
	v_mov_b32_e32 v54, v2
	v_mov_b32_e32 v55, v2
	v_mov_b32_e32 v56, v2
	v_mov_b32_e32 v57, v2
	v_mov_b32_e32 v10, v2
	v_mov_b32_e32 v11, v2
	v_mov_b32_e32 v12, v2
	v_mov_b32_e32 v13, v2
	v_mov_b32_e32 v14, v2
	v_mov_b32_e32 v15, v2
	v_mov_b32_e32 v16, v2
	v_mov_b32_e32 v17, v2
	v_mov_b32_e32 v26, v2
	v_mov_b32_e32 v27, v2
	v_mov_b32_e32 v28, v2
	v_mov_b32_e32 v29, v2
	v_mov_b32_e32 v30, v2
	v_mov_b32_e32 v31, v2
	v_mov_b32_e32 v32, v2
	v_mov_b32_e32 v33, v2
	v_mov_b32_e32 v42, v2
	v_mov_b32_e32 v43, v2
	v_mov_b32_e32 v44, v2
	v_mov_b32_e32 v45, v2
	v_mov_b32_e32 v46, v2
	v_mov_b32_e32 v47, v2
	v_mov_b32_e32 v48, v2
	v_mov_b32_e32 v49, v2
	v_mov_b32_e32 v58, v2
	v_mov_b32_e32 v59, v2
	v_mov_b32_e32 v60, v2
	v_mov_b32_e32 v61, v2
	v_mov_b32_e32 v62, v2
	v_mov_b32_e32 v63, v2
	v_mov_b32_e32 v64, v2
	v_mov_b32_e32 v65, v2
	v_mov_b32_e32 v66, v2
	v_mov_b32_e32 v67, v2
	v_mov_b32_e32 v68, v2
	v_mov_b32_e32 v69, v2
	v_mov_b32_e32 v70, v2
	v_mov_b32_e32 v71, v2
	v_mov_b32_e32 v72, v2
	v_mov_b32_e32 v73, v2
	v_mov_b32_e32 v82, v2
	v_mov_b32_e32 v83, v2
	v_mov_b32_e32 v84, v2
	v_mov_b32_e32 v85, v2
	v_mov_b32_e32 v86, v2
	v_mov_b32_e32 v87, v2
	v_mov_b32_e32 v88, v2
	v_mov_b32_e32 v89, v2
	v_mov_b32_e32 v98, v2
	v_mov_b32_e32 v99, v2
	v_mov_b32_e32 v100, v2
	v_mov_b32_e32 v101, v2
	v_mov_b32_e32 v102, v2
	v_mov_b32_e32 v103, v2
	v_mov_b32_e32 v104, v2
	v_mov_b32_e32 v105, v2
	v_mov_b32_e32 v114, v2
	v_mov_b32_e32 v115, v2
	v_mov_b32_e32 v116, v2
	v_mov_b32_e32 v117, v2
	v_mov_b32_e32 v122, v2
	v_mov_b32_e32 v123, v2
	v_mov_b32_e32 v124, v2
	v_mov_b32_e32 v125, v2
	v_mov_b32_e32 v74, v2
	v_mov_b32_e32 v75, v2
	v_mov_b32_e32 v76, v2
	v_mov_b32_e32 v77, v2
	v_mov_b32_e32 v78, v2
	v_mov_b32_e32 v79, v2
	v_mov_b32_e32 v80, v2
	v_mov_b32_e32 v81, v2
	v_mov_b32_e32 v90, v2
	v_mov_b32_e32 v91, v2
	v_mov_b32_e32 v92, v2
	v_mov_b32_e32 v93, v2
	v_mov_b32_e32 v94, v2
	v_mov_b32_e32 v95, v2
	v_mov_b32_e32 v96, v2
	v_mov_b32_e32 v97, v2
	v_mov_b32_e32 v106, v2
	v_mov_b32_e32 v107, v2
	v_mov_b32_e32 v108, v2
	v_mov_b32_e32 v109, v2
	v_mov_b32_e32 v110, v2
	v_mov_b32_e32 v111, v2
	v_mov_b32_e32 v112, v2
	v_mov_b32_e32 v113, v2
	v_mov_b32_e32 v130, v2
	v_mov_b32_e32 v131, v2
	v_mov_b32_e32 v132, v2
	v_mov_b32_e32 v133, v2
	v_mov_b32_e32 v134, v2
	v_mov_b32_e32 v135, v2
	v_mov_b32_e32 v136, v2
	v_mov_b32_e32 v137, v2
	s_andn2_b64 vcc, exec, s[38:39]
	s_cbranch_vccnz .LBB0_1627
	s_branch .LBB0_1628

.LBB0_1773:
	s_add_u32 s14, s14, 0xac00000
	s_addc_u32 s15, s15, 0
	s_add_u32 s16, s16, 0x1f00000
	s_addc_u32 s17, s17, 0
	s_lshl_b32 s19, s19, 5
	s_and_b32 s23, s19, 0x60
	s_lshl_b32 s22, s8, 13
	s_lshl_b32 s24, s23, 7
	s_add_u32 s20, s18, 0x980080
	v_mov_b32_e32 v163, v1
	s_addc_u32 s21, s9, 0
	v_mov_b32_e32 v159, v1
	s_add_i32 m0, s37, 0x18000
	s_waitcnt lgkmcnt(0)
	s_waitcnt vmcnt(2)
	s_barrier
	global_load_lds_dwordx4 v162, s[20:21]
	v_lshl_add_u64 v[14:15], s[20:21], 0, v[158:159]
	s_add_i32 m0, s37, 0x1a000
	s_add_i32 s47, s37, 0x8000
	s_add_i32 s48, s37, 0xa000
	global_load_lds_dwordx4 v158, s[20:21]
	v_lshl_add_u64 v[2:3], v[2:3], 0, s[56:57]
	s_mov_b32 m0, s47
	s_add_u32 s18, s18, 0x9c0080
	global_load_lds_dwordx4 v[2:3], off
	v_lshl_add_u64 v[2:3], v[4:5], 0, s[56:57]
	s_mov_b32 m0, s48
	s_addc_u32 s19, s9, 0
	global_load_lds_dwordx4 v[2:3], off
	s_add_i32 m0, s37, 0x1c000
	s_nop 0
	global_load_lds_dwordx4 v162, s[18:19]
	v_lshl_add_u64 v[2:3], s[18:19], 0, v[158:159]
	s_add_i32 m0, s37, 0x1e000
	s_cmpk_lt_u32 s4, 0x100
	global_load_lds_dwordx4 v158, s[18:19]
	v_lshrrev_b32_e32 v3, 1, v6
	v_and_b32_e32 v3, 24, v3
	v_and_b32_e32 v2, 15, v6
	v_lshlrev_b32_e32 v4, 1, v3
	v_lshl_or_b32 v180, s8, 6, v2
	v_lshl_or_b32 v2, v2, 6, v4
	v_lshlrev_b32_e32 v4, 2, v6
	v_and_b32_e32 v4, 32, v4
	v_bitop3_b32 v5, v2, s22, v4 bitop3:0xde
	v_bitop3_b32 v181, v2, s24, v4 bitop3:0xde
	v_lshlrev_b32_e32 v2, 14, v7
	v_and_b32_e32 v2, 0xffff8000, v2
	v_or_b32_e32 v182, s23, v3
	v_lshl_add_u32 v2, v8, 11, v2
	v_and_b32_e32 v3, 1, v7
	v_lshl_or_b32 v2, v3, 6, v2
	v_lshl_add_u32 v164, v9, 1, v2
	v_lshlrev_b32_e32 v2, 14, v11
	v_and_b32_e32 v2, 0xffff8000, v2
	s_waitcnt vmcnt(6)
	v_lshl_add_u32 v2, v10, 11, v2
	v_and_b32_e32 v3, 1, v11
	v_lshl_or_b32 v2, v3, 6, v2
	v_readlane_b32 s8, v254, 7
	s_cselect_b64 s[18:19], -1, 0
	v_mov_b32_e32 v165, v1
	v_lshl_add_u32 v166, v12, 1, v2
	v_mov_b32_e32 v167, v1
	s_mov_b32 s52, 0
	v_add_u32_e32 v183, 0, v5
	s_mov_b32 s4, s8
	s_mov_b64 s[28:29], s[10:11]
	s_mov_b32 s49, 0
	s_barrier
	v_readlane_b32 s9, v254, 8
	s_branch .LBB0_1776

.LBB0_1783:
	s_add_u32 s28, s6, 0xfffc0080
	s_addc_u32 s29, s7, -1
	s_add_i32 s53, 0, 0x10000
	s_cmp_eq_u32 s41, 12
	s_cselect_b32 s31, s8, s29
	s_cselect_b32 s30, s9, s28
	s_cselect_b32 s29, s21, s40
	s_cselect_b32 s28, s23, s33
	s_add_i32 s62, 0, 0x14000
	v_add_u32_e32 v142, s53, v181
	v_add_u32_e32 v168, s62, v181
	ds_read_b128 v[130:133], v142
	ds_read_b128 v[134:137], v142 offset:1024
	ds_read_b128 v[138:141], v142 offset:2048
	ds_read_b128 v[142:145], v142 offset:3072
	ds_read_b128 v[146:149], v168
	ds_read_b128 v[150:153], v168 offset:1024
	ds_read_b128 v[154:157], v168 offset:2048
	ds_read_b128 v[168:171], v168 offset:3072
	s_add_i32 m0, s37, 0xc000
	ds_read_b128 v[172:175], v183
	ds_read_b128 v[184:187], v183 offset:1024
	ds_read_b128 v[188:191], v183 offset:2048
	ds_read_b128 v[192:195], v183 offset:3072
	ds_read_b128 v[196:199], v183 offset:4096
	ds_read_b128 v[200:203], v183 offset:5120
	ds_read_b128 v[204:207], v183 offset:6144
	ds_read_b128 v[216:219], v183 offset:7168
	global_load_lds_dwordx4 v166, s[6:7]
	s_add_i32 m0, s37, 0xe000
	s_nop 0
	global_load_lds_dwordx4 v164, s[6:7]
	s_waitcnt vmcnt(8)
	s_waitcnt lgkmcnt(0)
	s_barrier
	s_setprio 1
	s_waitcnt lgkmcnt(0)
	v_mfma_f32_16x16x32_bf16 v[126:129], v[130:133], v[172:175], v[126:129]
	v_mfma_f32_16x16x32_bf16 v[122:125], v[138:141], v[172:175], v[122:125]
	v_mfma_f32_16x16x32_bf16 v[114:117], v[130:133], v[188:191], v[114:117]
	v_mfma_f32_16x16x32_bf16 v[106:109], v[138:141], v[188:191], v[106:109]
	v_mfma_f32_16x16x32_bf16 v[98:101], v[130:133], v[196:199], v[98:101]
	v_mfma_f32_16x16x32_bf16 v[90:93], v[138:141], v[196:199], v[90:93]
	v_mfma_f32_16x16x32_bf16 v[82:85], v[130:133], v[204:207], v[82:85]
	v_mfma_f32_16x16x32_bf16 v[74:77], v[138:141], v[204:207], v[74:77]
	v_mfma_f32_16x16x32_bf16 v[126:129], v[134:137], v[184:187], v[126:129]
	v_mfma_f32_16x16x32_bf16 v[122:125], v[142:145], v[184:187], v[122:125]
	v_mfma_f32_16x16x32_bf16 v[114:117], v[134:137], v[192:195], v[114:117]
	v_mfma_f32_16x16x32_bf16 v[106:109], v[142:145], v[192:195], v[106:109]
	v_mfma_f32_16x16x32_bf16 v[98:101], v[134:137], v[200:203], v[98:101]
	v_mfma_f32_16x16x32_bf16 v[90:93], v[142:145], v[200:203], v[90:93]
	v_mfma_f32_16x16x32_bf16 v[82:85], v[134:137], v[216:219], v[82:85]
	v_mfma_f32_16x16x32_bf16 v[74:77], v[142:145], v[216:219], v[74:77]
	s_setprio 0
	s_setprio 1
	v_mfma_f32_16x16x32_bf16 v[118:121], v[146:149], v[172:175], v[118:121]
	v_mfma_f32_16x16x32_bf16 v[110:113], v[154:157], v[172:175], v[110:113]
	v_mfma_f32_16x16x32_bf16 v[102:105], v[146:149], v[188:191], v[102:105]
	v_mfma_f32_16x16x32_bf16 v[94:97], v[154:157], v[188:191], v[94:97]
	v_mfma_f32_16x16x32_bf16 v[86:89], v[146:149], v[196:199], v[86:89]
	v_mfma_f32_16x16x32_bf16 v[78:81], v[154:157], v[196:199], v[78:81]
	v_mfma_f32_16x16x32_bf16 v[70:73], v[146:149], v[204:207], v[70:73]
	v_mfma_f32_16x16x32_bf16 v[66:69], v[154:157], v[204:207], v[66:69]
	v_mfma_f32_16x16x32_bf16 v[118:121], v[150:153], v[184:187], v[118:121]
	v_mfma_f32_16x16x32_bf16 v[110:113], v[168:171], v[184:187], v[110:113]
	v_mfma_f32_16x16x32_bf16 v[102:105], v[150:153], v[192:195], v[102:105]
	v_mfma_f32_16x16x32_bf16 v[94:97], v[168:171], v[192:195], v[94:97]
	v_mfma_f32_16x16x32_bf16 v[86:89], v[150:153], v[200:203], v[86:89]
	v_mfma_f32_16x16x32_bf16 v[78:81], v[168:171], v[200:203], v[78:81]
	v_mfma_f32_16x16x32_bf16 v[70:73], v[150:153], v[216:219], v[70:73]
	v_mfma_f32_16x16x32_bf16 v[66:69], v[168:171], v[216:219], v[66:69]
	s_setprio 0
	s_barrier
	s_add_i32 s53, s53, s36
	v_lshl_add_u64 v[176:177], s[28:29], 0, v[162:163]
	s_mov_b32 m0, s53
	ds_read_b128 v[172:175], v183 offset:16384
	ds_read_b128 v[184:187], v183 offset:17408
	ds_read_b128 v[188:191], v183 offset:18432
	ds_read_b128 v[192:195], v183 offset:19456
	ds_read_b128 v[196:199], v183 offset:20480
	ds_read_b128 v[200:203], v183 offset:21504
	ds_read_b128 v[204:207], v183 offset:22528
	ds_read_b128 v[216:219], v183 offset:23552
	global_load_lds_dwordx4 v162, s[28:29]
	s_add_i32 m0, s53, 0x2000
	s_add_u32 s58, s28, 0x40000
	v_lshl_add_u64 v[208:209], s[28:29], 0, v[158:159]
	s_addc_u32 s59, s29, 0
	s_add_i32 s53, s62, s36
	global_load_lds_dwordx4 v158, s[28:29]
	s_mov_b32 m0, s53
	v_lshl_add_u64 v[222:223], s[30:31], 0, v[160:161]
	global_load_lds_dwordx4 v162, s[58:59]
	s_add_i32 m0, s53, 0x2000
	s_nop 0
	global_load_lds_dwordx4 v158, s[58:59]
	s_mov_b32 m0, s37
	v_lshl_add_u64 v[220:221], s[30:31], 0, v[0:1]
	global_load_lds_dwordx4 v0, s[30:31]
	s_mov_b32 m0, s44
	s_nop 0
	global_load_lds_dwordx4 v160, s[30:31]
	s_waitcnt vmcnt(8)
	s_waitcnt lgkmcnt(0)
	s_barrier
	s_setprio 1
	s_waitcnt lgkmcnt(0)
	v_mfma_f32_16x16x32_bf16 v[62:65], v[130:133], v[172:175], v[62:65]
	v_mfma_f32_16x16x32_bf16 v[58:61], v[138:141], v[172:175], v[58:61]
	v_mfma_f32_16x16x32_bf16 v[50:53], v[130:133], v[188:191], v[50:53]
	v_mfma_f32_16x16x32_bf16 v[42:45], v[138:141], v[188:191], v[42:45]
	v_mfma_f32_16x16x32_bf16 v[34:37], v[130:133], v[196:199], v[34:37]
	v_mfma_f32_16x16x32_bf16 v[26:29], v[138:141], v[196:199], v[26:29]
	v_mfma_f32_16x16x32_bf16 v[18:21], v[130:133], v[204:207], v[18:21]
	v_mfma_f32_16x16x32_bf16 v[10:13], v[138:141], v[204:207], v[10:13]
	v_mfma_f32_16x16x32_bf16 v[62:65], v[134:137], v[184:187], v[62:65]
	v_mfma_f32_16x16x32_bf16 v[58:61], v[142:145], v[184:187], v[58:61]
	v_mfma_f32_16x16x32_bf16 v[50:53], v[134:137], v[192:195], v[50:53]
	v_mfma_f32_16x16x32_bf16 v[42:45], v[142:145], v[192:195], v[42:45]
	v_mfma_f32_16x16x32_bf16 v[34:37], v[134:137], v[200:203], v[34:37]
	v_mfma_f32_16x16x32_bf16 v[26:29], v[142:145], v[200:203], v[26:29]
	v_mfma_f32_16x16x32_bf16 v[18:21], v[134:137], v[216:219], v[18:21]
	v_mfma_f32_16x16x32_bf16 v[10:13], v[142:145], v[216:219], v[10:13]
	s_setprio 0
	s_setprio 1
	v_mfma_f32_16x16x32_bf16 v[54:57], v[146:149], v[172:175], v[54:57]
	v_mfma_f32_16x16x32_bf16 v[46:49], v[154:157], v[172:175], v[46:49]
	v_mfma_f32_16x16x32_bf16 v[38:41], v[146:149], v[188:191], v[38:41]
	v_mfma_f32_16x16x32_bf16 v[30:33], v[154:157], v[188:191], v[30:33]
	v_mfma_f32_16x16x32_bf16 v[22:25], v[146:149], v[196:199], v[22:25]
	v_mfma_f32_16x16x32_bf16 v[14:17], v[154:157], v[196:199], v[14:17]
	v_mfma_f32_16x16x32_bf16 v[6:9], v[146:149], v[204:207], v[6:9]
	v_mfma_f32_16x16x32_bf16 v[2:5], v[154:157], v[204:207], v[2:5]
	v_mfma_f32_16x16x32_bf16 v[54:57], v[150:153], v[184:187], v[54:57]
	v_mfma_f32_16x16x32_bf16 v[46:49], v[168:171], v[184:187], v[46:49]
	v_mfma_f32_16x16x32_bf16 v[38:41], v[150:153], v[192:195], v[38:41]
	v_mfma_f32_16x16x32_bf16 v[30:33], v[168:171], v[192:195], v[30:33]
	v_mfma_f32_16x16x32_bf16 v[22:25], v[150:153], v[200:203], v[22:25]
	v_mfma_f32_16x16x32_bf16 v[14:17], v[168:171], v[200:203], v[14:17]
	v_mfma_f32_16x16x32_bf16 v[6:9], v[150:153], v[216:219], v[6:9]
	v_mfma_f32_16x16x32_bf16 v[2:5], v[168:171], v[216:219], v[2:5]
	s_setprio 0
	s_barrier
	s_add_i32 s53, 0, 0x18000
	s_add_i32 s58, 0, 0x1c000
	v_add_u32_e32 v142, s53, v181
	v_add_u32_e32 v168, s58, v181
	ds_read_b128 v[130:133], v142
	ds_read_b128 v[134:137], v142 offset:1024
	ds_read_b128 v[138:141], v142 offset:2048
	ds_read_b128 v[142:145], v142 offset:3072
	ds_read_b128 v[146:149], v168
	ds_read_b128 v[150:153], v168 offset:1024
	ds_read_b128 v[154:157], v168 offset:2048
	ds_read_b128 v[168:171], v168 offset:3072
	s_add_u32 s30, s30, 0x40000
	s_addc_u32 s31, s31, 0
	s_mov_b32 m0, s45
	ds_read_b128 v[172:175], v183 offset:32768
	ds_read_b128 v[184:187], v183 offset:33792
	ds_read_b128 v[188:191], v183 offset:34816
	ds_read_b128 v[192:195], v183 offset:35840
	ds_read_b128 v[196:199], v183 offset:36864
	ds_read_b128 v[200:203], v183 offset:37888
	ds_read_b128 v[204:207], v183 offset:38912
	ds_read_b128 v[216:219], v183 offset:39936
	global_load_lds_dwordx4 v0, s[30:31]
	s_mov_b32 m0, s46
	v_lshl_add_u64 v[224:225], s[30:31], 0, v[160:161]
	global_load_lds_dwordx4 v160, s[30:31]
	s_waitcnt vmcnt(8)
	s_waitcnt lgkmcnt(0)
	s_barrier
	s_setprio 1
	s_waitcnt lgkmcnt(0)
	v_mfma_f32_16x16x32_bf16 v[126:129], v[130:133], v[172:175], v[126:129]
	v_mfma_f32_16x16x32_bf16 v[122:125], v[138:141], v[172:175], v[122:125]
	v_mfma_f32_16x16x32_bf16 v[114:117], v[130:133], v[188:191], v[114:117]
	v_mfma_f32_16x16x32_bf16 v[106:109], v[138:141], v[188:191], v[106:109]
	v_mfma_f32_16x16x32_bf16 v[98:101], v[130:133], v[196:199], v[98:101]
	v_mfma_f32_16x16x32_bf16 v[90:93], v[138:141], v[196:199], v[90:93]
	v_mfma_f32_16x16x32_bf16 v[82:85], v[130:133], v[204:207], v[82:85]
	v_mfma_f32_16x16x32_bf16 v[74:77], v[138:141], v[204:207], v[74:77]
	v_mfma_f32_16x16x32_bf16 v[126:129], v[134:137], v[184:187], v[126:129]
	v_mfma_f32_16x16x32_bf16 v[122:125], v[142:145], v[184:187], v[122:125]
	v_mfma_f32_16x16x32_bf16 v[114:117], v[134:137], v[192:195], v[114:117]
	v_mfma_f32_16x16x32_bf16 v[106:109], v[142:145], v[192:195], v[106:109]
	v_mfma_f32_16x16x32_bf16 v[98:101], v[134:137], v[200:203], v[98:101]
	v_mfma_f32_16x16x32_bf16 v[90:93], v[142:145], v[200:203], v[90:93]
	v_mfma_f32_16x16x32_bf16 v[82:85], v[134:137], v[216:219], v[82:85]
	v_mfma_f32_16x16x32_bf16 v[74:77], v[142:145], v[216:219], v[74:77]
	s_setprio 0
	s_setprio 1
	v_mfma_f32_16x16x32_bf16 v[118:121], v[146:149], v[172:175], v[118:121]
	v_mfma_f32_16x16x32_bf16 v[110:113], v[154:157], v[172:175], v[110:113]
	v_mfma_f32_16x16x32_bf16 v[102:105], v[146:149], v[188:191], v[102:105]
	v_mfma_f32_16x16x32_bf16 v[94:97], v[154:157], v[188:191], v[94:97]
	v_mfma_f32_16x16x32_bf16 v[86:89], v[146:149], v[196:199], v[86:89]
	v_mfma_f32_16x16x32_bf16 v[78:81], v[154:157], v[196:199], v[78:81]
	v_mfma_f32_16x16x32_bf16 v[70:73], v[146:149], v[204:207], v[70:73]
	v_mfma_f32_16x16x32_bf16 v[66:69], v[154:157], v[204:207], v[66:69]
	v_mfma_f32_16x16x32_bf16 v[118:121], v[150:153], v[184:187], v[118:121]
	v_mfma_f32_16x16x32_bf16 v[110:113], v[168:171], v[184:187], v[110:113]
	v_mfma_f32_16x16x32_bf16 v[102:105], v[150:153], v[192:195], v[102:105]
	v_mfma_f32_16x16x32_bf16 v[94:97], v[168:171], v[192:195], v[94:97]
	v_mfma_f32_16x16x32_bf16 v[86:89], v[150:153], v[200:203], v[86:89]
	v_mfma_f32_16x16x32_bf16 v[78:81], v[168:171], v[200:203], v[78:81]
	v_mfma_f32_16x16x32_bf16 v[70:73], v[150:153], v[216:219], v[70:73]
	v_mfma_f32_16x16x32_bf16 v[66:69], v[168:171], v[216:219], v[66:69]
	s_setprio 0
	s_barrier
	s_add_i32 s30, s53, s36
	v_lshl_add_u64 v[176:177], v[176:177], 0, s[56:57]
	s_mov_b32 m0, s30
	ds_read_b128 v[172:175], v183 offset:49152
	ds_read_b128 v[184:187], v183 offset:50176
	ds_read_b128 v[188:191], v183 offset:51200
	ds_read_b128 v[192:195], v183 offset:52224
	ds_read_b128 v[196:199], v183 offset:53248
	ds_read_b128 v[200:203], v183 offset:54272
	ds_read_b128 v[204:207], v183 offset:55296
	ds_read_b128 v[216:219], v183 offset:56320
	global_load_lds_dwordx4 v[176:177], off
	s_add_i32 m0, s30, 0x2000
	s_add_u32 s28, s28, 0x40080
	v_lshl_add_u64 v[176:177], v[208:209], 0, s[56:57]
	s_addc_u32 s29, s29, 0
	s_add_i32 s30, s58, s36
	global_load_lds_dwordx4 v[176:177], off
	s_mov_b32 m0, s30
	s_nop 0
	global_load_lds_dwordx4 v162, s[28:29]
	s_add_i32 m0, s30, 0x2000
	s_nop 0
	global_load_lds_dwordx4 v158, s[28:29]
	s_mov_b32 m0, s47
	v_lshl_add_u64 v[176:177], v[220:221], 0, s[56:57]
	global_load_lds_dwordx4 v[176:177], off
	s_mov_b32 m0, s48
	v_lshl_add_u64 v[176:177], v[222:223], 0, s[56:57]
	global_load_lds_dwordx4 v[176:177], off
	s_waitcnt vmcnt(8)
	s_waitcnt lgkmcnt(0)
	s_barrier
	s_setprio 1
	s_waitcnt lgkmcnt(0)
	v_mfma_f32_16x16x32_bf16 v[62:65], v[130:133], v[172:175], v[62:65]
	v_mfma_f32_16x16x32_bf16 v[58:61], v[138:141], v[172:175], v[58:61]
	v_mfma_f32_16x16x32_bf16 v[50:53], v[130:133], v[188:191], v[50:53]
	v_mfma_f32_16x16x32_bf16 v[42:45], v[138:141], v[188:191], v[42:45]
	v_mfma_f32_16x16x32_bf16 v[34:37], v[130:133], v[196:199], v[34:37]
	v_mfma_f32_16x16x32_bf16 v[26:29], v[138:141], v[196:199], v[26:29]
	v_mfma_f32_16x16x32_bf16 v[18:21], v[130:133], v[204:207], v[18:21]
	v_mfma_f32_16x16x32_bf16 v[10:13], v[138:141], v[204:207], v[10:13]
	v_mfma_f32_16x16x32_bf16 v[62:65], v[134:137], v[184:187], v[62:65]
	v_mfma_f32_16x16x32_bf16 v[58:61], v[142:145], v[184:187], v[58:61]
	v_mfma_f32_16x16x32_bf16 v[50:53], v[134:137], v[192:195], v[50:53]
	v_mfma_f32_16x16x32_bf16 v[42:45], v[142:145], v[192:195], v[42:45]
	v_mfma_f32_16x16x32_bf16 v[34:37], v[134:137], v[200:203], v[34:37]
	v_mfma_f32_16x16x32_bf16 v[26:29], v[142:145], v[200:203], v[26:29]
	v_mfma_f32_16x16x32_bf16 v[18:21], v[134:137], v[216:219], v[18:21]
	v_mfma_f32_16x16x32_bf16 v[10:13], v[142:145], v[216:219], v[10:13]
	s_setprio 0
	s_setprio 1
	v_mfma_f32_16x16x32_bf16 v[54:57], v[146:149], v[172:175], v[54:57]
	v_mfma_f32_16x16x32_bf16 v[46:49], v[154:157], v[172:175], v[46:49]
	v_mfma_f32_16x16x32_bf16 v[38:41], v[146:149], v[188:191], v[38:41]
	v_mfma_f32_16x16x32_bf16 v[30:33], v[154:157], v[188:191], v[30:33]
	v_mfma_f32_16x16x32_bf16 v[22:25], v[146:149], v[196:199], v[22:25]
	v_mfma_f32_16x16x32_bf16 v[14:17], v[154:157], v[196:199], v[14:17]
	v_mfma_f32_16x16x32_bf16 v[6:9], v[146:149], v[204:207], v[6:9]
	v_mfma_f32_16x16x32_bf16 v[2:5], v[154:157], v[204:207], v[2:5]
	v_mfma_f32_16x16x32_bf16 v[54:57], v[150:153], v[184:187], v[54:57]
	v_mfma_f32_16x16x32_bf16 v[46:49], v[168:171], v[184:187], v[46:49]
	v_mfma_f32_16x16x32_bf16 v[38:41], v[150:153], v[192:195], v[38:41]
	v_mfma_f32_16x16x32_bf16 v[30:33], v[168:171], v[192:195], v[30:33]
	v_mfma_f32_16x16x32_bf16 v[22:25], v[150:153], v[200:203], v[22:25]
	v_mfma_f32_16x16x32_bf16 v[14:17], v[168:171], v[200:203], v[14:17]
	v_mfma_f32_16x16x32_bf16 v[6:9], v[150:153], v[216:219], v[6:9]
	v_mfma_f32_16x16x32_bf16 v[2:5], v[168:171], v[216:219], v[2:5]
	s_setprio 0
	s_barrier
	s_add_i32 s41, s41, 2
	s_add_u32 s33, s33, 0x100
	s_addc_u32 s40, s40, 0
	s_add_u32 s6, s6, 0x100
	s_addc_u32 s7, s7, 0
	s_cmp_gt_u32 s41, 13
	s_cbranch_scc0 .LBB0_1783
	s_and_b64 vcc, exec, s[18:19]
	s_cbranch_vccz .LBB0_1786
	s_barrier

.LBB0_1793:
	s_add_u32 s10, s10, 0x2300000
	s_addc_u32 s11, s11, 0
	s_lshl_b32 s9, s9, 5
	s_and_b32 s9, s9, 0x60
	s_add_i32 m0, s36, 0x18000
	v_lshl_add_u64 v[8:9], v[8:9], 0, s[56:57]
	s_lshl_b32 s13, s8, 13
	s_lshl_b32 s16, s9, 7
	s_waitcnt vmcnt(2)
	s_barrier
	global_load_lds_dwordx4 v[8:9], off
	v_lshl_add_u64 v[6:7], v[6:7], 0, s[56:57]
	s_add_i32 m0, s36, 0x1a000
	s_add_i32 s38, s36, 0x8000
	s_add_i32 s39, s36, 0xa000
	global_load_lds_dwordx4 v[6:7], off
	v_lshl_add_u64 v[2:3], v[2:3], 0, s[56:57]
	s_mov_b32 m0, s38
	s_add_u32 s14, s24, 0x40080
	global_load_lds_dwordx4 v[2:3], off
	v_lshl_add_u64 v[2:3], v[4:5], 0, s[56:57]
	s_mov_b32 m0, s39
	s_addc_u32 s15, s25, 0
	global_load_lds_dwordx4 v[2:3], off
	s_add_i32 m0, s36, 0x1c000
	s_nop 0
	global_load_lds_dwordx4 v134, s[14:15]
	v_lshl_add_u64 v[2:3], s[14:15], 0, v[130:131]
	s_add_i32 m0, s36, 0x1e000
	s_cmpk_lt_u32 s12, 0x100
	global_load_lds_dwordx4 v130, s[14:15]
	v_lshrrev_b32_e32 v3, 1, v10
	v_and_b32_e32 v3, 24, v3
	v_and_b32_e32 v2, 15, v10
	v_lshlrev_b32_e32 v4, 1, v3
	v_lshl_or_b32 v0, s8, 6, v2
	v_lshl_or_b32 v2, v2, 6, v4
	v_lshlrev_b32_e32 v4, 2, v10
	v_and_b32_e32 v4, 32, v4
	v_bitop3_b32 v5, v2, s13, v4 bitop3:0xde
	s_waitcnt vmcnt(0)
	v_bitop3_b32 v144, v2, s16, v4 bitop3:0xde
	v_lshlrev_b32_e32 v2, 14, v11
	v_and_b32_e32 v2, 0xffff8000, v2
	v_or_b32_e32 v145, s9, v3
	v_lshl_add_u32 v2, v12, 11, v2
	v_and_b32_e32 v3, 1, v11
	v_lshl_or_b32 v2, v3, 6, v2
	v_lshl_add_u32 v138, v13, 1, v2
	v_lshlrev_b32_e32 v2, 14, v15
	v_and_b32_e32 v2, 0xffff8000, v2
	s_waitcnt vmcnt(6)
	v_lshl_add_u32 v2, v14, 11, v2
	v_and_b32_e32 v3, 1, v15
	v_lshl_or_b32 v2, v3, 6, v2
	v_readlane_b32 s8, v254, 27
	s_cselect_b64 s[12:13], -1, 0
	v_mov_b32_e32 v139, v1
	v_lshl_add_u32 v140, v16, 1, v2
	v_mov_b32_e32 v141, v1
	s_mov_b32 s40, 0
	v_add_u32_e32 v146, 0, v5
	v_readlane_b32 s41, v254, 23
	s_mov_b32 s44, s8
	s_barrier
	v_readlane_b32 s9, v254, 28
	s_branch .LBB0_1796

.LBB0_1799:
	s_add_u32 s26, s24, 0xfffc0080
	s_addc_u32 s27, s25, -1
	s_add_i32 s48, 0, 0x10000
	s_cmp_eq_u32 s47, 12
	s_cselect_b32 s29, s8, s27
	s_cselect_b32 s28, s9, s26
	v_add_u32_e32 v142, s48, v144
	s_cselect_b32 s27, s15, s46
	s_cselect_b32 s26, s17, s45
	s_add_i32 s52, 0, 0x14000
	ds_read_b128 v[148:151], v142
	ds_read_b128 v[152:155], v142 offset:1024
	ds_read_b128 v[156:159], v142 offset:2048
	ds_read_b128 v[160:163], v142 offset:3072
	v_add_u32_e32 v142, s52, v144
	ds_read_b128 v[164:167], v142
	ds_read_b128 v[168:171], v142 offset:1024
	ds_read_b128 v[172:175], v142 offset:2048
	ds_read_b128 v[180:183], v142 offset:3072
	s_add_i32 m0, s36, 0xc000
	ds_read_b128 v[184:187], v146
	ds_read_b128 v[188:191], v146 offset:1024
	ds_read_b128 v[192:195], v146 offset:2048
	ds_read_b128 v[196:199], v146 offset:3072
	ds_read_b128 v[200:203], v146 offset:4096
	ds_read_b128 v[204:207], v146 offset:5120
	ds_read_b128 v[216:219], v146 offset:6144
	ds_read_b128 v[220:223], v146 offset:7168
	global_load_lds_dwordx4 v140, s[24:25]
	s_add_i32 m0, s36, 0xe000
	s_nop 0
	global_load_lds_dwordx4 v138, s[24:25]
	s_waitcnt vmcnt(8)
	s_waitcnt lgkmcnt(0)
	s_barrier
	s_setprio 1
	s_waitcnt lgkmcnt(0)
	v_mfma_f32_16x16x32_bf16 v[126:129], v[148:151], v[184:187], v[126:129]
	v_mfma_f32_16x16x32_bf16 v[122:125], v[156:159], v[184:187], v[122:125]
	v_mfma_f32_16x16x32_bf16 v[118:121], v[148:151], v[192:195], v[118:121]
	v_mfma_f32_16x16x32_bf16 v[110:113], v[156:159], v[192:195], v[110:113]
	v_mfma_f32_16x16x32_bf16 v[102:105], v[148:151], v[200:203], v[102:105]
	v_mfma_f32_16x16x32_bf16 v[94:97], v[156:159], v[200:203], v[94:97]
	v_mfma_f32_16x16x32_bf16 v[86:89], v[148:151], v[216:219], v[86:89]
	v_mfma_f32_16x16x32_bf16 v[78:81], v[156:159], v[216:219], v[78:81]
	v_mfma_f32_16x16x32_bf16 v[126:129], v[152:155], v[188:191], v[126:129]
	v_mfma_f32_16x16x32_bf16 v[122:125], v[160:163], v[188:191], v[122:125]
	v_mfma_f32_16x16x32_bf16 v[118:121], v[152:155], v[196:199], v[118:121]
	v_mfma_f32_16x16x32_bf16 v[110:113], v[160:163], v[196:199], v[110:113]
	v_mfma_f32_16x16x32_bf16 v[102:105], v[152:155], v[204:207], v[102:105]
	v_mfma_f32_16x16x32_bf16 v[94:97], v[160:163], v[204:207], v[94:97]
	v_mfma_f32_16x16x32_bf16 v[86:89], v[152:155], v[220:223], v[86:89]
	v_mfma_f32_16x16x32_bf16 v[78:81], v[160:163], v[220:223], v[78:81]
	s_setprio 0
	s_setprio 1
	v_mfma_f32_16x16x32_bf16 v[114:117], v[164:167], v[184:187], v[114:117]
	v_mfma_f32_16x16x32_bf16 v[106:109], v[172:175], v[184:187], v[106:109]
	v_mfma_f32_16x16x32_bf16 v[98:101], v[164:167], v[192:195], v[98:101]
	v_mfma_f32_16x16x32_bf16 v[90:93], v[172:175], v[192:195], v[90:93]
	v_mfma_f32_16x16x32_bf16 v[82:85], v[164:167], v[200:203], v[82:85]
	v_mfma_f32_16x16x32_bf16 v[74:77], v[172:175], v[200:203], v[74:77]
	v_mfma_f32_16x16x32_bf16 v[70:73], v[164:167], v[216:219], v[70:73]
	v_mfma_f32_16x16x32_bf16 v[66:69], v[172:175], v[216:219], v[66:69]
	v_mfma_f32_16x16x32_bf16 v[114:117], v[168:171], v[188:191], v[114:117]
	v_mfma_f32_16x16x32_bf16 v[106:109], v[180:183], v[188:191], v[106:109]
	v_mfma_f32_16x16x32_bf16 v[98:101], v[168:171], v[196:199], v[98:101]
	v_mfma_f32_16x16x32_bf16 v[90:93], v[180:183], v[196:199], v[90:93]
	v_mfma_f32_16x16x32_bf16 v[82:85], v[168:171], v[204:207], v[82:85]
	v_mfma_f32_16x16x32_bf16 v[74:77], v[180:183], v[204:207], v[74:77]
	v_mfma_f32_16x16x32_bf16 v[70:73], v[168:171], v[220:223], v[70:73]
	v_mfma_f32_16x16x32_bf16 v[66:69], v[180:183], v[220:223], v[66:69]
	s_setprio 0
	s_barrier
	s_add_i32 s48, s48, s35
	v_lshl_add_u64 v[142:143], s[26:27], 0, v[134:135]
	s_mov_b32 m0, s48
	ds_read_b128 v[184:187], v146 offset:16384
	ds_read_b128 v[188:191], v146 offset:17408
	ds_read_b128 v[192:195], v146 offset:18432
	ds_read_b128 v[196:199], v146 offset:19456
	ds_read_b128 v[200:203], v146 offset:20480
	ds_read_b128 v[204:207], v146 offset:21504
	ds_read_b128 v[216:219], v146 offset:22528
	ds_read_b128 v[220:223], v146 offset:23552
	global_load_lds_dwordx4 v134, s[26:27]
	s_add_i32 m0, s48, 0x2000
	s_add_u32 s48, s26, 0x40000
	v_lshl_add_u64 v[176:177], s[26:27], 0, v[130:131]
	s_addc_u32 s49, s27, 0
	s_add_i32 s52, s52, s35
	global_load_lds_dwordx4 v130, s[26:27]
	s_mov_b32 m0, s52
	v_lshl_add_u64 v[224:225], s[28:29], 0, v[132:133]
	global_load_lds_dwordx4 v134, s[48:49]
	s_add_i32 m0, s52, 0x2000
	s_nop 0
	global_load_lds_dwordx4 v130, s[48:49]
	s_mov_b32 m0, s36
	v_lshl_add_u64 v[208:209], s[28:29], 0, v[136:137]
	global_load_lds_dwordx4 v136, s[28:29]
	s_mov_b32 m0, s37
	s_nop 0
	global_load_lds_dwordx4 v132, s[28:29]
	s_waitcnt vmcnt(8)
	s_waitcnt lgkmcnt(0)
	s_barrier
	s_setprio 1
	s_waitcnt lgkmcnt(0)
	v_mfma_f32_16x16x32_bf16 v[62:65], v[148:151], v[184:187], v[62:65]
	v_mfma_f32_16x16x32_bf16 v[58:61], v[156:159], v[184:187], v[58:61]
	v_mfma_f32_16x16x32_bf16 v[54:57], v[148:151], v[192:195], v[54:57]
	v_mfma_f32_16x16x32_bf16 v[46:49], v[156:159], v[192:195], v[46:49]
	v_mfma_f32_16x16x32_bf16 v[38:41], v[148:151], v[200:203], v[38:41]
	v_mfma_f32_16x16x32_bf16 v[30:33], v[156:159], v[200:203], v[30:33]
	v_mfma_f32_16x16x32_bf16 v[22:25], v[148:151], v[216:219], v[22:25]
	v_mfma_f32_16x16x32_bf16 v[14:17], v[156:159], v[216:219], v[14:17]
	v_mfma_f32_16x16x32_bf16 v[62:65], v[152:155], v[188:191], v[62:65]
	v_mfma_f32_16x16x32_bf16 v[58:61], v[160:163], v[188:191], v[58:61]
	v_mfma_f32_16x16x32_bf16 v[54:57], v[152:155], v[196:199], v[54:57]
	v_mfma_f32_16x16x32_bf16 v[46:49], v[160:163], v[196:199], v[46:49]
	v_mfma_f32_16x16x32_bf16 v[38:41], v[152:155], v[204:207], v[38:41]
	v_mfma_f32_16x16x32_bf16 v[30:33], v[160:163], v[204:207], v[30:33]
	v_mfma_f32_16x16x32_bf16 v[22:25], v[152:155], v[220:223], v[22:25]
	v_mfma_f32_16x16x32_bf16 v[14:17], v[160:163], v[220:223], v[14:17]
	s_setprio 0
	s_setprio 1
	v_mfma_f32_16x16x32_bf16 v[50:53], v[164:167], v[184:187], v[50:53]
	v_mfma_f32_16x16x32_bf16 v[42:45], v[172:175], v[184:187], v[42:45]
	v_mfma_f32_16x16x32_bf16 v[34:37], v[164:167], v[192:195], v[34:37]
	v_mfma_f32_16x16x32_bf16 v[26:29], v[172:175], v[192:195], v[26:29]
	v_mfma_f32_16x16x32_bf16 v[18:21], v[164:167], v[200:203], v[18:21]
	v_mfma_f32_16x16x32_bf16 v[10:13], v[172:175], v[200:203], v[10:13]
	v_mfma_f32_16x16x32_bf16 v[6:9], v[164:167], v[216:219], v[6:9]
	v_mfma_f32_16x16x32_bf16 v[2:5], v[172:175], v[216:219], v[2:5]
	v_mfma_f32_16x16x32_bf16 v[50:53], v[168:171], v[188:191], v[50:53]
	v_mfma_f32_16x16x32_bf16 v[42:45], v[180:183], v[188:191], v[42:45]
	v_mfma_f32_16x16x32_bf16 v[34:37], v[168:171], v[196:199], v[34:37]
	v_mfma_f32_16x16x32_bf16 v[26:29], v[180:183], v[196:199], v[26:29]
	v_mfma_f32_16x16x32_bf16 v[18:21], v[168:171], v[204:207], v[18:21]
	v_mfma_f32_16x16x32_bf16 v[10:13], v[180:183], v[204:207], v[10:13]
	v_mfma_f32_16x16x32_bf16 v[6:9], v[168:171], v[220:223], v[6:9]
	v_mfma_f32_16x16x32_bf16 v[2:5], v[180:183], v[220:223], v[2:5]
	s_setprio 0
	s_barrier
	s_add_i32 s48, 0, 0x18000
	v_add_u32_e32 v147, s48, v144
	s_add_i32 s49, 0, 0x1c000
	ds_read_b128 v[148:151], v147
	ds_read_b128 v[152:155], v147 offset:1024
	ds_read_b128 v[156:159], v147 offset:2048
	ds_read_b128 v[160:163], v147 offset:3072
	v_add_u32_e32 v147, s49, v144
	ds_read_b128 v[164:167], v147
	ds_read_b128 v[168:171], v147 offset:1024
	ds_read_b128 v[172:175], v147 offset:2048
	ds_read_b128 v[180:183], v147 offset:3072
	s_add_u32 s28, s28, 0x40000
	s_addc_u32 s29, s29, 0
	s_mov_b32 m0, s4
	ds_read_b128 v[184:187], v146 offset:32768
	ds_read_b128 v[188:191], v146 offset:33792
	ds_read_b128 v[192:195], v146 offset:34816
	ds_read_b128 v[196:199], v146 offset:35840
	ds_read_b128 v[200:203], v146 offset:36864
	ds_read_b128 v[204:207], v146 offset:37888
	ds_read_b128 v[216:219], v146 offset:38912
	ds_read_b128 v[220:223], v146 offset:39936
	global_load_lds_dwordx4 v136, s[28:29]
	s_mov_b32 m0, s33
	s_nop 0
	global_load_lds_dwordx4 v132, s[28:29]
	s_waitcnt vmcnt(8)
	s_waitcnt lgkmcnt(0)
	s_barrier
	s_setprio 1
	s_waitcnt lgkmcnt(0)
	v_mfma_f32_16x16x32_bf16 v[126:129], v[148:151], v[184:187], v[126:129]
	v_mfma_f32_16x16x32_bf16 v[122:125], v[156:159], v[184:187], v[122:125]
	v_mfma_f32_16x16x32_bf16 v[118:121], v[148:151], v[192:195], v[118:121]
	v_mfma_f32_16x16x32_bf16 v[110:113], v[156:159], v[192:195], v[110:113]
	v_mfma_f32_16x16x32_bf16 v[102:105], v[148:151], v[200:203], v[102:105]
	v_mfma_f32_16x16x32_bf16 v[94:97], v[156:159], v[200:203], v[94:97]
	v_mfma_f32_16x16x32_bf16 v[86:89], v[148:151], v[216:219], v[86:89]
	v_mfma_f32_16x16x32_bf16 v[78:81], v[156:159], v[216:219], v[78:81]
	v_mfma_f32_16x16x32_bf16 v[126:129], v[152:155], v[188:191], v[126:129]
	v_mfma_f32_16x16x32_bf16 v[122:125], v[160:163], v[188:191], v[122:125]
	v_mfma_f32_16x16x32_bf16 v[118:121], v[152:155], v[196:199], v[118:121]
	v_mfma_f32_16x16x32_bf16 v[110:113], v[160:163], v[196:199], v[110:113]
	v_mfma_f32_16x16x32_bf16 v[102:105], v[152:155], v[204:207], v[102:105]
	v_mfma_f32_16x16x32_bf16 v[94:97], v[160:163], v[204:207], v[94:97]
	v_mfma_f32_16x16x32_bf16 v[86:89], v[152:155], v[220:223], v[86:89]
	v_mfma_f32_16x16x32_bf16 v[78:81], v[160:163], v[220:223], v[78:81]
	s_setprio 0
	s_setprio 1
	v_mfma_f32_16x16x32_bf16 v[114:117], v[164:167], v[184:187], v[114:117]
	v_mfma_f32_16x16x32_bf16 v[106:109], v[172:175], v[184:187], v[106:109]
	v_mfma_f32_16x16x32_bf16 v[98:101], v[164:167], v[192:195], v[98:101]
	v_mfma_f32_16x16x32_bf16 v[90:93], v[172:175], v[192:195], v[90:93]
	v_mfma_f32_16x16x32_bf16 v[82:85], v[164:167], v[200:203], v[82:85]
	v_mfma_f32_16x16x32_bf16 v[74:77], v[172:175], v[200:203], v[74:77]
	v_mfma_f32_16x16x32_bf16 v[70:73], v[164:167], v[216:219], v[70:73]
	v_mfma_f32_16x16x32_bf16 v[66:69], v[172:175], v[216:219], v[66:69]
	v_mfma_f32_16x16x32_bf16 v[114:117], v[168:171], v[188:191], v[114:117]
	v_mfma_f32_16x16x32_bf16 v[106:109], v[180:183], v[188:191], v[106:109]
	v_mfma_f32_16x16x32_bf16 v[98:101], v[168:171], v[196:199], v[98:101]
	v_mfma_f32_16x16x32_bf16 v[90:93], v[180:183], v[196:199], v[90:93]
	v_mfma_f32_16x16x32_bf16 v[82:85], v[168:171], v[204:207], v[82:85]
	v_mfma_f32_16x16x32_bf16 v[74:77], v[180:183], v[204:207], v[74:77]
	v_mfma_f32_16x16x32_bf16 v[70:73], v[168:171], v[220:223], v[70:73]
	v_mfma_f32_16x16x32_bf16 v[66:69], v[180:183], v[220:223], v[66:69]
	s_setprio 0
	s_barrier
	s_add_i32 s28, s48, s35
	v_lshl_add_u64 v[142:143], v[142:143], 0, s[56:57]
	s_mov_b32 m0, s28
	ds_read_b128 v[184:187], v146 offset:49152
	ds_read_b128 v[188:191], v146 offset:50176
	ds_read_b128 v[192:195], v146 offset:51200
	ds_read_b128 v[196:199], v146 offset:52224
	ds_read_b128 v[200:203], v146 offset:53248
	ds_read_b128 v[204:207], v146 offset:54272
	ds_read_b128 v[216:219], v146 offset:55296
	ds_read_b128 v[220:223], v146 offset:56320
	global_load_lds_dwordx4 v[142:143], off
	s_add_i32 m0, s28, 0x2000
	s_add_u32 s26, s26, 0x40080
	v_lshl_add_u64 v[142:143], v[176:177], 0, s[56:57]
	s_addc_u32 s27, s27, 0
	s_add_i32 s28, s49, s35
	global_load_lds_dwordx4 v[142:143], off
	s_mov_b32 m0, s28
	s_nop 0
	global_load_lds_dwordx4 v134, s[26:27]
	s_add_i32 m0, s28, 0x2000
	s_nop 0
	global_load_lds_dwordx4 v130, s[26:27]
	s_mov_b32 m0, s38
	v_lshl_add_u64 v[142:143], v[208:209], 0, s[56:57]
	global_load_lds_dwordx4 v[142:143], off
	s_mov_b32 m0, s39
	v_lshl_add_u64 v[142:143], v[224:225], 0, s[56:57]
	global_load_lds_dwordx4 v[142:143], off
	s_waitcnt vmcnt(8)
	s_waitcnt lgkmcnt(0)
	s_barrier
	s_setprio 1
	s_waitcnt lgkmcnt(0)
	v_mfma_f32_16x16x32_bf16 v[62:65], v[148:151], v[184:187], v[62:65]
	v_mfma_f32_16x16x32_bf16 v[58:61], v[156:159], v[184:187], v[58:61]
	v_mfma_f32_16x16x32_bf16 v[54:57], v[148:151], v[192:195], v[54:57]
	v_mfma_f32_16x16x32_bf16 v[46:49], v[156:159], v[192:195], v[46:49]
	v_mfma_f32_16x16x32_bf16 v[38:41], v[148:151], v[200:203], v[38:41]
	v_mfma_f32_16x16x32_bf16 v[30:33], v[156:159], v[200:203], v[30:33]
	v_mfma_f32_16x16x32_bf16 v[22:25], v[148:151], v[216:219], v[22:25]
	v_mfma_f32_16x16x32_bf16 v[14:17], v[156:159], v[216:219], v[14:17]
	v_mfma_f32_16x16x32_bf16 v[62:65], v[152:155], v[188:191], v[62:65]
	v_mfma_f32_16x16x32_bf16 v[58:61], v[160:163], v[188:191], v[58:61]
	v_mfma_f32_16x16x32_bf16 v[54:57], v[152:155], v[196:199], v[54:57]
	v_mfma_f32_16x16x32_bf16 v[46:49], v[160:163], v[196:199], v[46:49]
	v_mfma_f32_16x16x32_bf16 v[38:41], v[152:155], v[204:207], v[38:41]
	v_mfma_f32_16x16x32_bf16 v[30:33], v[160:163], v[204:207], v[30:33]
	v_mfma_f32_16x16x32_bf16 v[22:25], v[152:155], v[220:223], v[22:25]
	v_mfma_f32_16x16x32_bf16 v[14:17], v[160:163], v[220:223], v[14:17]
	s_setprio 0
	s_setprio 1
	v_mfma_f32_16x16x32_bf16 v[50:53], v[164:167], v[184:187], v[50:53]
	v_mfma_f32_16x16x32_bf16 v[42:45], v[172:175], v[184:187], v[42:45]
	v_mfma_f32_16x16x32_bf16 v[34:37], v[164:167], v[192:195], v[34:37]
	v_mfma_f32_16x16x32_bf16 v[26:29], v[172:175], v[192:195], v[26:29]
	v_mfma_f32_16x16x32_bf16 v[18:21], v[164:167], v[200:203], v[18:21]
	v_mfma_f32_16x16x32_bf16 v[10:13], v[172:175], v[200:203], v[10:13]
	v_mfma_f32_16x16x32_bf16 v[6:9], v[164:167], v[216:219], v[6:9]
	v_mfma_f32_16x16x32_bf16 v[2:5], v[172:175], v[216:219], v[2:5]
	v_mfma_f32_16x16x32_bf16 v[50:53], v[168:171], v[188:191], v[50:53]
	v_mfma_f32_16x16x32_bf16 v[42:45], v[180:183], v[188:191], v[42:45]
	v_mfma_f32_16x16x32_bf16 v[34:37], v[168:171], v[196:199], v[34:37]
	v_mfma_f32_16x16x32_bf16 v[26:29], v[180:183], v[196:199], v[26:29]
	v_mfma_f32_16x16x32_bf16 v[18:21], v[168:171], v[204:207], v[18:21]
	v_mfma_f32_16x16x32_bf16 v[10:13], v[180:183], v[204:207], v[10:13]
	v_mfma_f32_16x16x32_bf16 v[6:9], v[168:171], v[220:223], v[6:9]
	v_mfma_f32_16x16x32_bf16 v[2:5], v[180:183], v[220:223], v[2:5]
	s_setprio 0
	s_barrier
	s_add_i32 s47, s47, 2
	s_add_u32 s45, s45, 0x100
	s_addc_u32 s46, s46, 0
	s_add_u32 s24, s24, 0x100
	s_addc_u32 s25, s25, 0
	s_cmp_gt_u32 s47, 13
	s_cbranch_scc0 .LBB0_1799
	s_and_b64 vcc, exec, s[12:13]
	s_cbranch_vccz .LBB0_1802
	s_barrier

.LBB0_2358:
	v_mov_b32_e32 v127, v1
	v_lshl_add_u64 v[2:3], s[30:31], 0, v[126:127]
	v_mov_b32_e32 v123, v1
	v_lshl_add_u64 v[4:5], s[30:31], 0, v[122:123]
	v_mov_b32_e32 v129, v1
	s_and_b32 s17, s85, 3
	s_add_i32 m0, s65, 0x18000
	v_lshl_add_u64 v[2:3], v[2:3], 0, s[56:57]
	v_lshl_add_u64 v[6:7], s[34:35], 0, v[128:129]
	v_mov_b32_e32 v125, v1
	s_lshl_b32 s10, s93, 13
	s_lshl_b32 s11, s17, 12
	s_waitcnt vmcnt(2)
	s_barrier
	global_load_lds_dwordx4 v[2:3], off
	v_lshl_add_u64 v[2:3], v[4:5], 0, s[56:57]
	s_add_i32 m0, s65, 0x1a000
	s_add_i32 s68, s65, 0x8000
	s_add_i32 s22, s65, 0xa000
	v_lshl_add_u64 v[8:9], s[34:35], 0, v[124:125]
	global_load_lds_dwordx4 v[2:3], off
	v_lshl_add_u64 v[2:3], v[6:7], 0, s[56:57]
	s_mov_b32 m0, s68
	s_add_u32 s36, s30, 0x10080
	global_load_lds_dwordx4 v[2:3], off
	v_lshl_add_u64 v[2:3], v[8:9], 0, s[56:57]
	s_mov_b32 m0, s22
	s_addc_u32 s37, s31, 0
	global_load_lds_dwordx4 v[2:3], off
	s_add_i32 m0, s65, 0x1c000
	s_nop 0
	global_load_lds_dwordx4 v126, s[36:37]
	v_lshl_add_u64 v[2:3], s[36:37], 0, v[122:123]
	s_add_i32 m0, s65, 0x1e000
	v_and_b32_e32 v166, 15, v0
	global_load_lds_dwordx4 v122, s[36:37]
	v_and_b32_e32 v2, 48, v0
	v_lshlrev_b32_e32 v3, 2, v0
	v_lshl_or_b32 v2, v166, 6, v2
	v_and_b32_e32 v3, 32, v3
	v_bitop3_b32 v6, v2, s10, v3 bitop3:0xde
	s_waitcnt vmcnt(6)
	v_mov_b32_e32 v4, v1
	v_mov_b32_e32 v5, v1
	v_readlane_b32 s8, v254, 58
	v_bitop3_b32 v138, v2, s11, v3 bitop3:0xde
	v_mov_b32_e32 v2, v1
	v_mov_b32_e32 v3, v1
	v_add_u32_e32 v139, 0, v6
	v_mov_b64_e32 v[8:9], v[4:5]
	v_mov_b64_e32 v[20:21], v[4:5]
	v_mov_b64_e32 v[24:25], v[4:5]
	v_mov_b64_e32 v[36:37], v[4:5]
	v_mov_b64_e32 v[40:41], v[4:5]
	v_mov_b64_e32 v[52:53], v[4:5]
	v_mov_b64_e32 v[56:57], v[4:5]
	v_mov_b64_e32 v[12:13], v[4:5]
	s_waitcnt lgkmcnt(0)
	v_mov_b64_e32 v[16:17], v[4:5]
	v_mov_b64_e32 v[28:29], v[4:5]
	v_mov_b64_e32 v[32:33], v[4:5]
	v_mov_b64_e32 v[44:45], v[4:5]
	v_mov_b64_e32 v[48:49], v[4:5]
	v_mov_b64_e32 v[60:61], v[4:5]
	v_mov_b64_e32 v[64:65], v[4:5]
	v_mov_b64_e32 v[68:69], v[4:5]
	v_mov_b64_e32 v[72:73], v[4:5]
	v_mov_b64_e32 v[84:85], v[4:5]
	v_mov_b64_e32 v[88:89], v[4:5]
	v_mov_b64_e32 v[100:101], v[4:5]
	v_mov_b64_e32 v[104:105], v[4:5]
	v_mov_b64_e32 v[116:117], v[4:5]
	v_mov_b64_e32 v[120:121], v[4:5]
	v_mov_b64_e32 v[76:77], v[4:5]
	v_mov_b64_e32 v[80:81], v[4:5]
	v_mov_b64_e32 v[92:93], v[4:5]
	v_mov_b64_e32 v[96:97], v[4:5]
	v_mov_b64_e32 v[108:109], v[4:5]
	v_mov_b64_e32 v[112:113], v[4:5]
	v_mov_b64_e32 v[132:133], v[4:5]
	v_mov_b64_e32 v[136:137], v[4:5]
	s_mov_b32 s16, s8
	v_readlane_b32 s8, v254, 54
	v_lshl_or_b32 v240, s93, 6, v166
	s_mov_b32 s58, 0
	v_mov_b64_e32 v[6:7], v[2:3]
	v_mov_b64_e32 v[18:19], v[2:3]
	v_mov_b64_e32 v[22:23], v[2:3]
	v_mov_b64_e32 v[34:35], v[2:3]
	v_mov_b64_e32 v[38:39], v[2:3]
	v_mov_b64_e32 v[50:51], v[2:3]
	v_mov_b64_e32 v[54:55], v[2:3]
	v_mov_b64_e32 v[10:11], v[2:3]
	v_mov_b64_e32 v[14:15], v[2:3]
	v_mov_b64_e32 v[26:27], v[2:3]
	v_mov_b64_e32 v[30:31], v[2:3]
	v_mov_b64_e32 v[42:43], v[2:3]
	v_mov_b64_e32 v[46:47], v[2:3]
	v_mov_b64_e32 v[58:59], v[2:3]
	v_mov_b64_e32 v[62:63], v[2:3]
	v_mov_b64_e32 v[66:67], v[2:3]
	v_mov_b64_e32 v[70:71], v[2:3]
	v_mov_b64_e32 v[82:83], v[2:3]
	v_mov_b64_e32 v[86:87], v[2:3]
	v_mov_b64_e32 v[98:99], v[2:3]
	v_mov_b64_e32 v[102:103], v[2:3]
	v_mov_b64_e32 v[114:115], v[2:3]
	v_mov_b64_e32 v[118:119], v[2:3]
	v_mov_b64_e32 v[74:75], v[2:3]
	v_mov_b64_e32 v[78:79], v[2:3]
	v_mov_b64_e32 v[90:91], v[2:3]
	v_mov_b64_e32 v[94:95], v[2:3]
	v_mov_b64_e32 v[106:107], v[2:3]
	v_mov_b64_e32 v[110:111], v[2:3]
	v_mov_b64_e32 v[130:131], v[2:3]
	v_mov_b64_e32 v[134:135], v[2:3]
	s_mov_b32 s94, s8
	s_barrier
	v_readlane_b32 s9, v254, 55
	s_branch .LBB0_2360

.LBB0_2367:
	s_add_u32 s10, s34, s38
	s_addc_u32 s11, s35, 0
	s_add_u32 s39, s10, 0x100
	s_addc_u32 s76, s11, 0
	s_and_b64 s[70:71], s[62:63], exec
	s_cselect_b32 s77, s45, s76
	s_cselect_b32 s76, s59, s39
	s_add_u32 s38, s30, s38
	s_addc_u32 s39, s31, 0
	s_add_u32 s70, s38, 0x100
	s_addc_u32 s71, s39, 0
	s_add_i32 s91, 0, 0x10000
	s_and_b64 s[38:39], s[62:63], exec
	s_cselect_b32 s79, s37, s71
	s_cselect_b32 s78, s82, s70
	s_add_i32 s38, 0, 0x14000
	s_add_u32 s10, s10, 0x10080
	s_addc_u32 s11, s11, 0
	s_add_i32 s8, s91, s95
	s_add_i32 m0, s65, 0xc000
	s_add_i32 s14, s65, 0xe000
	s_add_i32 s9, s8, 0x2000
	s_add_u32 s80, s78, 0x10000
	s_addc_u32 s81, s79, 0
	s_add_i32 s50, s38, s95
	v_add_u32_e32 v152, s91, v138
	v_add_u32_e32 v164, s38, v138
	s_add_i32 s74, s50, 0x2000
	s_add_i32 vcc_hi, 0, 0x18000
	s_add_i32 s39, 0, 0x1c000
	ds_read_b128 v[140:143], v152
	ds_read_b128 v[144:147], v152 offset:1024
	ds_read_b128 v[148:151], v152 offset:2048
	ds_read_b128 v[152:155], v152 offset:3072
	ds_read_b128 v[156:159], v164
	ds_read_b128 v[160:163], v164 offset:1024
	ds_read_b128 v[168:171], v164 offset:2048
	ds_read_b128 v[172:175], v164 offset:3072
	s_add_u32 s70, s76, 0x10000
	s_addc_u32 s71, s77, 0
	s_add_i32 vcc_lo, vcc_hi, s95
	s_add_i32 s64, vcc_lo, 0x2000
	s_add_u32 s62, s78, 0x10080
	s_addc_u32 s63, s79, 0
	s_add_i32 s91, s39, s95
	s_add_i32 s38, s91, 0x2000
	ds_read_b128 v[176:179], v139
	ds_read_b128 v[180:183], v139 offset:1024
	ds_read_b128 v[184:187], v139 offset:2048
	ds_read_b128 v[188:191], v139 offset:3072
	ds_read_b128 v[192:195], v139 offset:4096
	ds_read_b128 v[196:199], v139 offset:5120
	ds_read_b128 v[200:203], v139 offset:6144
	ds_read_b128 v[204:207], v139 offset:7168
	global_load_lds_dwordx4 v128, s[10:11]
	s_mov_b32 m0, s14
	s_nop 0
	global_load_lds_dwordx4 v124, s[10:11]
	s_waitcnt vmcnt(8)
	s_waitcnt lgkmcnt(0)
	s_barrier
	s_setprio 1
	s_waitcnt lgkmcnt(0)
	v_mfma_f32_16x16x32_bf16 v[134:137], v[140:143], v[176:179], v[134:137]
	v_mfma_f32_16x16x32_bf16 v[130:133], v[148:151], v[176:179], v[130:133]
	v_mfma_f32_16x16x32_bf16 v[110:113], v[140:143], v[184:187], v[110:113]
	v_mfma_f32_16x16x32_bf16 v[106:109], v[148:151], v[184:187], v[106:109]
	v_mfma_f32_16x16x32_bf16 v[94:97], v[140:143], v[192:195], v[94:97]
	v_mfma_f32_16x16x32_bf16 v[90:93], v[148:151], v[192:195], v[90:93]
	v_mfma_f32_16x16x32_bf16 v[78:81], v[140:143], v[200:203], v[78:81]
	v_mfma_f32_16x16x32_bf16 v[74:77], v[148:151], v[200:203], v[74:77]
	v_mfma_f32_16x16x32_bf16 v[134:137], v[144:147], v[180:183], v[134:137]
	v_mfma_f32_16x16x32_bf16 v[130:133], v[152:155], v[180:183], v[130:133]
	v_mfma_f32_16x16x32_bf16 v[110:113], v[144:147], v[188:191], v[110:113]
	v_mfma_f32_16x16x32_bf16 v[106:109], v[152:155], v[188:191], v[106:109]
	v_mfma_f32_16x16x32_bf16 v[94:97], v[144:147], v[196:199], v[94:97]
	v_mfma_f32_16x16x32_bf16 v[90:93], v[152:155], v[196:199], v[90:93]
	v_mfma_f32_16x16x32_bf16 v[78:81], v[144:147], v[204:207], v[78:81]
	v_mfma_f32_16x16x32_bf16 v[74:77], v[152:155], v[204:207], v[74:77]
	s_setprio 0
	s_setprio 1
	v_mfma_f32_16x16x32_bf16 v[118:121], v[156:159], v[176:179], v[118:121]
	v_mfma_f32_16x16x32_bf16 v[114:117], v[168:171], v[176:179], v[114:117]
	v_mfma_f32_16x16x32_bf16 v[102:105], v[156:159], v[184:187], v[102:105]
	v_mfma_f32_16x16x32_bf16 v[98:101], v[168:171], v[184:187], v[98:101]
	v_mfma_f32_16x16x32_bf16 v[86:89], v[156:159], v[192:195], v[86:89]
	v_mfma_f32_16x16x32_bf16 v[82:85], v[168:171], v[192:195], v[82:85]
	v_mfma_f32_16x16x32_bf16 v[70:73], v[156:159], v[200:203], v[70:73]
	v_mfma_f32_16x16x32_bf16 v[66:69], v[168:171], v[200:203], v[66:69]
	v_mfma_f32_16x16x32_bf16 v[118:121], v[160:163], v[180:183], v[118:121]
	v_mfma_f32_16x16x32_bf16 v[114:117], v[172:175], v[180:183], v[114:117]
	v_mfma_f32_16x16x32_bf16 v[102:105], v[160:163], v[188:191], v[102:105]
	v_mfma_f32_16x16x32_bf16 v[98:101], v[172:175], v[188:191], v[98:101]
	v_mfma_f32_16x16x32_bf16 v[86:89], v[160:163], v[196:199], v[86:89]
	v_mfma_f32_16x16x32_bf16 v[82:85], v[172:175], v[196:199], v[82:85]
	v_mfma_f32_16x16x32_bf16 v[70:73], v[160:163], v[204:207], v[70:73]
	v_mfma_f32_16x16x32_bf16 v[66:69], v[172:175], v[204:207], v[66:69]
	s_setprio 0
	s_barrier
	s_mov_b32 m0, s8
	v_lshl_add_u64 v[164:165], s[78:79], 0, v[126:127]
	ds_read_b128 v[176:179], v139 offset:16384
	ds_read_b128 v[180:183], v139 offset:17408
	ds_read_b128 v[184:187], v139 offset:18432
	ds_read_b128 v[188:191], v139 offset:19456
	ds_read_b128 v[192:195], v139 offset:20480
	ds_read_b128 v[196:199], v139 offset:21504
	ds_read_b128 v[200:203], v139 offset:22528
	ds_read_b128 v[204:207], v139 offset:23552
	global_load_lds_dwordx4 v126, s[78:79]
	v_lshl_add_u64 v[208:209], s[78:79], 0, v[122:123]
	s_mov_b32 m0, s9
	s_nop 0
	global_load_lds_dwordx4 v122, s[78:79]
	s_mov_b32 m0, s50
	v_lshl_add_u64 v[218:219], s[76:77], 0, v[124:125]
	global_load_lds_dwordx4 v126, s[80:81]
	s_mov_b32 m0, s74
	s_nop 0
	global_load_lds_dwordx4 v122, s[80:81]
	s_mov_b32 m0, s65
	v_lshl_add_u64 v[216:217], s[76:77], 0, v[128:129]
	global_load_lds_dwordx4 v128, s[76:77]
	s_mov_b32 m0, s15
	s_nop 0
	global_load_lds_dwordx4 v124, s[76:77]
	s_waitcnt vmcnt(8)
	s_waitcnt lgkmcnt(0)
	s_barrier
	s_setprio 1
	s_waitcnt lgkmcnt(0)
	v_mfma_f32_16x16x32_bf16 v[62:65], v[140:143], v[176:179], v[62:65]
	v_mfma_f32_16x16x32_bf16 v[58:61], v[148:151], v[176:179], v[58:61]
	v_mfma_f32_16x16x32_bf16 v[46:49], v[140:143], v[184:187], v[46:49]
	v_mfma_f32_16x16x32_bf16 v[42:45], v[148:151], v[184:187], v[42:45]
	v_mfma_f32_16x16x32_bf16 v[30:33], v[140:143], v[192:195], v[30:33]
	v_mfma_f32_16x16x32_bf16 v[26:29], v[148:151], v[192:195], v[26:29]
	v_mfma_f32_16x16x32_bf16 v[14:17], v[140:143], v[200:203], v[14:17]
	v_mfma_f32_16x16x32_bf16 v[10:13], v[148:151], v[200:203], v[10:13]
	v_mfma_f32_16x16x32_bf16 v[62:65], v[144:147], v[180:183], v[62:65]
	v_mfma_f32_16x16x32_bf16 v[58:61], v[152:155], v[180:183], v[58:61]
	v_mfma_f32_16x16x32_bf16 v[46:49], v[144:147], v[188:191], v[46:49]
	v_mfma_f32_16x16x32_bf16 v[42:45], v[152:155], v[188:191], v[42:45]
	v_mfma_f32_16x16x32_bf16 v[30:33], v[144:147], v[196:199], v[30:33]
	v_mfma_f32_16x16x32_bf16 v[26:29], v[152:155], v[196:199], v[26:29]
	v_mfma_f32_16x16x32_bf16 v[14:17], v[144:147], v[204:207], v[14:17]
	v_mfma_f32_16x16x32_bf16 v[10:13], v[152:155], v[204:207], v[10:13]
	s_setprio 0
	s_setprio 1
	v_mfma_f32_16x16x32_bf16 v[54:57], v[156:159], v[176:179], v[54:57]
	v_mfma_f32_16x16x32_bf16 v[50:53], v[168:171], v[176:179], v[50:53]
	v_mfma_f32_16x16x32_bf16 v[38:41], v[156:159], v[184:187], v[38:41]
	v_mfma_f32_16x16x32_bf16 v[34:37], v[168:171], v[184:187], v[34:37]
	v_mfma_f32_16x16x32_bf16 v[22:25], v[156:159], v[192:195], v[22:25]
	v_mfma_f32_16x16x32_bf16 v[18:21], v[168:171], v[192:195], v[18:21]
	v_mfma_f32_16x16x32_bf16 v[6:9], v[156:159], v[200:203], v[6:9]
	v_mfma_f32_16x16x32_bf16 v[2:5], v[168:171], v[200:203], v[2:5]
	v_mfma_f32_16x16x32_bf16 v[54:57], v[160:163], v[180:183], v[54:57]
	v_mfma_f32_16x16x32_bf16 v[50:53], v[172:175], v[180:183], v[50:53]
	v_mfma_f32_16x16x32_bf16 v[38:41], v[160:163], v[188:191], v[38:41]
	v_mfma_f32_16x16x32_bf16 v[34:37], v[172:175], v[188:191], v[34:37]
	v_mfma_f32_16x16x32_bf16 v[22:25], v[160:163], v[196:199], v[22:25]
	v_mfma_f32_16x16x32_bf16 v[18:21], v[172:175], v[196:199], v[18:21]
	v_mfma_f32_16x16x32_bf16 v[6:9], v[160:163], v[204:207], v[6:9]
	v_mfma_f32_16x16x32_bf16 v[2:5], v[172:175], v[204:207], v[2:5]
	s_setprio 0
	s_barrier
	v_add_u32_e32 v152, vcc_hi, v138
	v_add_u32_e32 v167, s39, v138
	ds_read_b128 v[140:143], v152
	ds_read_b128 v[144:147], v152 offset:1024
	ds_read_b128 v[148:151], v152 offset:2048
	ds_read_b128 v[152:155], v152 offset:3072
	ds_read_b128 v[156:159], v167
	ds_read_b128 v[160:163], v167 offset:1024
	ds_read_b128 v[168:171], v167 offset:2048
	ds_read_b128 v[172:175], v167 offset:3072
	s_mov_b32 m0, s84
	ds_read_b128 v[176:179], v139 offset:32768
	ds_read_b128 v[180:183], v139 offset:33792
	ds_read_b128 v[184:187], v139 offset:34816
	ds_read_b128 v[188:191], v139 offset:35840
	ds_read_b128 v[192:195], v139 offset:36864
	ds_read_b128 v[196:199], v139 offset:37888
	ds_read_b128 v[200:203], v139 offset:38912
	ds_read_b128 v[204:207], v139 offset:39936
	global_load_lds_dwordx4 v128, s[70:71]
	s_mov_b32 m0, s90
	v_lshl_add_u64 v[220:221], s[70:71], 0, v[124:125]
	global_load_lds_dwordx4 v124, s[70:71]
	s_waitcnt vmcnt(8)
	s_waitcnt lgkmcnt(0)
	s_barrier
	s_setprio 1
	s_waitcnt lgkmcnt(0)
	v_mfma_f32_16x16x32_bf16 v[134:137], v[140:143], v[176:179], v[134:137]
	v_mfma_f32_16x16x32_bf16 v[130:133], v[148:151], v[176:179], v[130:133]
	v_mfma_f32_16x16x32_bf16 v[110:113], v[140:143], v[184:187], v[110:113]
	v_mfma_f32_16x16x32_bf16 v[106:109], v[148:151], v[184:187], v[106:109]
	v_mfma_f32_16x16x32_bf16 v[94:97], v[140:143], v[192:195], v[94:97]
	v_mfma_f32_16x16x32_bf16 v[90:93], v[148:151], v[192:195], v[90:93]
	v_mfma_f32_16x16x32_bf16 v[78:81], v[140:143], v[200:203], v[78:81]
	v_mfma_f32_16x16x32_bf16 v[74:77], v[148:151], v[200:203], v[74:77]
	v_mfma_f32_16x16x32_bf16 v[134:137], v[144:147], v[180:183], v[134:137]
	v_mfma_f32_16x16x32_bf16 v[130:133], v[152:155], v[180:183], v[130:133]
	v_mfma_f32_16x16x32_bf16 v[110:113], v[144:147], v[188:191], v[110:113]
	v_mfma_f32_16x16x32_bf16 v[106:109], v[152:155], v[188:191], v[106:109]
	v_mfma_f32_16x16x32_bf16 v[94:97], v[144:147], v[196:199], v[94:97]
	v_mfma_f32_16x16x32_bf16 v[90:93], v[152:155], v[196:199], v[90:93]
	v_mfma_f32_16x16x32_bf16 v[78:81], v[144:147], v[204:207], v[78:81]
	v_mfma_f32_16x16x32_bf16 v[74:77], v[152:155], v[204:207], v[74:77]
	s_setprio 0
	s_setprio 1
	v_mfma_f32_16x16x32_bf16 v[118:121], v[156:159], v[176:179], v[118:121]
	v_mfma_f32_16x16x32_bf16 v[114:117], v[168:171], v[176:179], v[114:117]
	v_mfma_f32_16x16x32_bf16 v[102:105], v[156:159], v[184:187], v[102:105]
	v_mfma_f32_16x16x32_bf16 v[98:101], v[168:171], v[184:187], v[98:101]
	v_mfma_f32_16x16x32_bf16 v[86:89], v[156:159], v[192:195], v[86:89]
	v_mfma_f32_16x16x32_bf16 v[82:85], v[168:171], v[192:195], v[82:85]
	v_mfma_f32_16x16x32_bf16 v[70:73], v[156:159], v[200:203], v[70:73]
	v_mfma_f32_16x16x32_bf16 v[66:69], v[168:171], v[200:203], v[66:69]
	v_mfma_f32_16x16x32_bf16 v[118:121], v[160:163], v[180:183], v[118:121]
	v_mfma_f32_16x16x32_bf16 v[114:117], v[172:175], v[180:183], v[114:117]
	v_mfma_f32_16x16x32_bf16 v[102:105], v[160:163], v[188:191], v[102:105]
	v_mfma_f32_16x16x32_bf16 v[98:101], v[172:175], v[188:191], v[98:101]
	v_mfma_f32_16x16x32_bf16 v[86:89], v[160:163], v[196:199], v[86:89]
	v_mfma_f32_16x16x32_bf16 v[82:85], v[172:175], v[196:199], v[82:85]
	v_mfma_f32_16x16x32_bf16 v[70:73], v[160:163], v[204:207], v[70:73]
	v_mfma_f32_16x16x32_bf16 v[66:69], v[172:175], v[204:207], v[66:69]
	s_setprio 0
	s_barrier
	s_mov_b32 m0, vcc_lo
	v_lshl_add_u64 v[164:165], v[164:165], 0, s[56:57]
	ds_read_b128 v[176:179], v139 offset:49152
	ds_read_b128 v[180:183], v139 offset:50176
	ds_read_b128 v[184:187], v139 offset:51200
	ds_read_b128 v[188:191], v139 offset:52224
	ds_read_b128 v[192:195], v139 offset:53248
	ds_read_b128 v[196:199], v139 offset:54272
	ds_read_b128 v[200:203], v139 offset:55296
	ds_read_b128 v[204:207], v139 offset:56320
	global_load_lds_dwordx4 v[164:165], off
	s_mov_b32 m0, s64
	v_lshl_add_u64 v[164:165], v[208:209], 0, s[56:57]
	global_load_lds_dwordx4 v[164:165], off
	s_mov_b32 m0, s91
	s_nop 0
	global_load_lds_dwordx4 v126, s[62:63]
	s_mov_b32 m0, s38
	s_nop 0
	global_load_lds_dwordx4 v122, s[62:63]
	s_mov_b32 m0, s68
	v_lshl_add_u64 v[164:165], v[216:217], 0, s[56:57]
	global_load_lds_dwordx4 v[164:165], off
	s_mov_b32 m0, s22
	v_lshl_add_u64 v[164:165], v[218:219], 0, s[56:57]
	global_load_lds_dwordx4 v[164:165], off
	s_waitcnt vmcnt(8)
	s_waitcnt lgkmcnt(0)
	s_barrier
	s_setprio 1
	s_waitcnt lgkmcnt(0)
	v_mfma_f32_16x16x32_bf16 v[62:65], v[140:143], v[176:179], v[62:65]
	v_mfma_f32_16x16x32_bf16 v[58:61], v[148:151], v[176:179], v[58:61]
	v_mfma_f32_16x16x32_bf16 v[46:49], v[140:143], v[184:187], v[46:49]
	v_mfma_f32_16x16x32_bf16 v[42:45], v[148:151], v[184:187], v[42:45]
	v_mfma_f32_16x16x32_bf16 v[30:33], v[140:143], v[192:195], v[30:33]
	v_mfma_f32_16x16x32_bf16 v[26:29], v[148:151], v[192:195], v[26:29]
	v_mfma_f32_16x16x32_bf16 v[14:17], v[140:143], v[200:203], v[14:17]
	v_mfma_f32_16x16x32_bf16 v[10:13], v[148:151], v[200:203], v[10:13]
	v_mfma_f32_16x16x32_bf16 v[62:65], v[144:147], v[180:183], v[62:65]
	v_mfma_f32_16x16x32_bf16 v[58:61], v[152:155], v[180:183], v[58:61]
	v_mfma_f32_16x16x32_bf16 v[46:49], v[144:147], v[188:191], v[46:49]
	v_mfma_f32_16x16x32_bf16 v[42:45], v[152:155], v[188:191], v[42:45]
	v_mfma_f32_16x16x32_bf16 v[30:33], v[144:147], v[196:199], v[30:33]
	v_mfma_f32_16x16x32_bf16 v[26:29], v[152:155], v[196:199], v[26:29]
	v_mfma_f32_16x16x32_bf16 v[14:17], v[144:147], v[204:207], v[14:17]
	v_mfma_f32_16x16x32_bf16 v[10:13], v[152:155], v[204:207], v[10:13]
	s_setprio 0
	s_setprio 1
	v_mfma_f32_16x16x32_bf16 v[54:57], v[156:159], v[176:179], v[54:57]
	v_mfma_f32_16x16x32_bf16 v[50:53], v[168:171], v[176:179], v[50:53]
	v_mfma_f32_16x16x32_bf16 v[38:41], v[156:159], v[184:187], v[38:41]
	v_mfma_f32_16x16x32_bf16 v[34:37], v[168:171], v[184:187], v[34:37]
	v_mfma_f32_16x16x32_bf16 v[22:25], v[156:159], v[192:195], v[22:25]
	v_mfma_f32_16x16x32_bf16 v[18:21], v[168:171], v[192:195], v[18:21]
	v_mfma_f32_16x16x32_bf16 v[6:9], v[156:159], v[200:203], v[6:9]
	v_mfma_f32_16x16x32_bf16 v[2:5], v[168:171], v[200:203], v[2:5]
	v_mfma_f32_16x16x32_bf16 v[54:57], v[160:163], v[180:183], v[54:57]
	v_mfma_f32_16x16x32_bf16 v[50:53], v[172:175], v[180:183], v[50:53]
	v_mfma_f32_16x16x32_bf16 v[38:41], v[160:163], v[188:191], v[38:41]
	v_mfma_f32_16x16x32_bf16 v[34:37], v[172:175], v[188:191], v[34:37]
	v_mfma_f32_16x16x32_bf16 v[22:25], v[160:163], v[196:199], v[22:25]
	v_mfma_f32_16x16x32_bf16 v[18:21], v[172:175], v[196:199], v[18:21]
	v_mfma_f32_16x16x32_bf16 v[6:9], v[160:163], v[204:207], v[6:9]
	v_mfma_f32_16x16x32_bf16 v[2:5], v[172:175], v[204:207], v[2:5]
	s_setprio 0
	s_barrier
	s_movk_i32 s38, 0x100
	s_andn2_b64 vcc, exec, s[52:53]
	s_mov_b64 s[62:63], -1
	s_mov_b64 s[52:53], 0
	s_cbranch_vccz .LBB0_2367
	s_andn2_b64 vcc, exec, s[42:43]
	s_cbranch_vccnz .LBB0_2359
	v_mov_b32_e32 v2, 0
	s_mov_b32 s16, s36
	s_mov_b32 s94, s44
	s_mov_b64 s[30:31], s[48:49]
	s_mov_b64 s[34:35], s[46:47]
	s_mov_b32 s58, s23
	v_mov_b32_e32 v3, v2
	v_mov_b32_e32 v4, v2
	v_mov_b32_e32 v5, v2
	v_mov_b32_e32 v6, v2
	v_mov_b32_e32 v7, v2
	v_mov_b32_e32 v8, v2
	v_mov_b32_e32 v9, v2
	v_mov_b32_e32 v18, v2
	v_mov_b32_e32 v19, v2
	v_mov_b32_e32 v20, v2
	v_mov_b32_e32 v21, v2
	v_mov_b32_e32 v22, v2
	v_mov_b32_e32 v23, v2
	v_mov_b32_e32 v24, v2
	v_mov_b32_e32 v25, v2
	v_mov_b32_e32 v34, v2
	v_mov_b32_e32 v35, v2
	v_mov_b32_e32 v36, v2
	v_mov_b32_e32 v37, v2
	v_mov_b32_e32 v38, v2
	v_mov_b32_e32 v39, v2
	v_mov_b32_e32 v40, v2
	v_mov_b32_e32 v41, v2
	v_mov_b32_e32 v50, v2
	v_mov_b32_e32 v51, v2
	v_mov_b32_e32 v52, v2
	v_mov_b32_e32 v53, v2
	v_mov_b32_e32 v54, v2
	v_mov_b32_e32 v55, v2
	v_mov_b32_e32 v56, v2
	v_mov_b32_e32 v57, v2
	v_mov_b32_e32 v10, v2
	v_mov_b32_e32 v11, v2
	v_mov_b32_e32 v12, v2
	v_mov_b32_e32 v13, v2
	v_mov_b32_e32 v14, v2
	v_mov_b32_e32 v15, v2
	v_mov_b32_e32 v16, v2
	v_mov_b32_e32 v17, v2
	v_mov_b32_e32 v26, v2
	v_mov_b32_e32 v27, v2
	v_mov_b32_e32 v28, v2
	v_mov_b32_e32 v29, v2
	v_mov_b32_e32 v30, v2
	v_mov_b32_e32 v31, v2
	v_mov_b32_e32 v32, v2
	v_mov_b32_e32 v33, v2
	v_mov_b32_e32 v42, v2
	v_mov_b32_e32 v43, v2
	v_mov_b32_e32 v44, v2
	v_mov_b32_e32 v45, v2
	v_mov_b32_e32 v46, v2
	v_mov_b32_e32 v47, v2
	v_mov_b32_e32 v48, v2
	v_mov_b32_e32 v49, v2
	v_mov_b32_e32 v58, v2
	v_mov_b32_e32 v59, v2
	v_mov_b32_e32 v60, v2
	v_mov_b32_e32 v61, v2
	v_mov_b32_e32 v62, v2
	v_mov_b32_e32 v63, v2
	v_mov_b32_e32 v64, v2
	v_mov_b32_e32 v65, v2
	v_mov_b32_e32 v66, v2
	v_mov_b32_e32 v67, v2
	v_mov_b32_e32 v68, v2
	v_mov_b32_e32 v69, v2
	v_mov_b32_e32 v70, v2
	v_mov_b32_e32 v71, v2
	v_mov_b32_e32 v72, v2
	v_mov_b32_e32 v73, v2
	v_mov_b32_e32 v82, v2
	v_mov_b32_e32 v83, v2
	v_mov_b32_e32 v84, v2
	v_mov_b32_e32 v85, v2
	v_mov_b32_e32 v86, v2
	v_mov_b32_e32 v87, v2
	v_mov_b32_e32 v88, v2
	v_mov_b32_e32 v89, v2
	v_mov_b32_e32 v98, v2
	v_mov_b32_e32 v99, v2
	v_mov_b32_e32 v100, v2
	v_mov_b32_e32 v101, v2
	v_mov_b32_e32 v102, v2
	v_mov_b32_e32 v103, v2
	v_mov_b32_e32 v104, v2
	v_mov_b32_e32 v105, v2
	v_mov_b32_e32 v114, v2
	v_mov_b32_e32 v115, v2
	v_mov_b32_e32 v116, v2
	v_mov_b32_e32 v117, v2
	v_mov_b32_e32 v118, v2
	v_mov_b32_e32 v119, v2
	v_mov_b32_e32 v120, v2
	v_mov_b32_e32 v121, v2
	v_mov_b32_e32 v74, v2
	v_mov_b32_e32 v75, v2
	v_mov_b32_e32 v76, v2
	v_mov_b32_e32 v77, v2
	v_mov_b32_e32 v78, v2
	v_mov_b32_e32 v79, v2
	v_mov_b32_e32 v80, v2
	v_mov_b32_e32 v81, v2
	v_mov_b32_e32 v90, v2
	v_mov_b32_e32 v91, v2
	v_mov_b32_e32 v92, v2
	v_mov_b32_e32 v93, v2
	v_mov_b32_e32 v94, v2
	v_mov_b32_e32 v95, v2
	v_mov_b32_e32 v96, v2
	v_mov_b32_e32 v97, v2
	v_mov_b32_e32 v106, v2
	v_mov_b32_e32 v107, v2
	v_mov_b32_e32 v108, v2
	v_mov_b32_e32 v109, v2
	v_mov_b32_e32 v110, v2
	v_mov_b32_e32 v111, v2
	v_mov_b32_e32 v112, v2
	v_mov_b32_e32 v113, v2
	v_mov_b32_e32 v130, v2
	v_mov_b32_e32 v131, v2
	v_mov_b32_e32 v132, v2
	v_mov_b32_e32 v133, v2
	v_mov_b32_e32 v134, v2
	v_mov_b32_e32 v135, v2
	v_mov_b32_e32 v136, v2
	v_mov_b32_e32 v137, v2
	s_branch .LBB0_2359

.LBB0_2458:
	v_mov_b32_e32 v127, v1
	v_lshl_add_u64 v[2:3], s[28:29], 0, v[126:127]
	v_mov_b32_e32 v123, v1
	v_lshl_add_u64 v[4:5], s[28:29], 0, v[122:123]
	v_mov_b32_e32 v129, v1
	s_and_b32 s15, s79, 3
	s_add_i32 m0, s82, 0x18000
	v_lshl_add_u64 v[2:3], v[2:3], 0, s[56:57]
	v_lshl_add_u64 v[6:7], s[30:31], 0, v[128:129]
	v_mov_b32_e32 v125, v1
	s_lshl_b32 s8, s80, 13
	s_lshl_b32 s9, s15, 12
	s_waitcnt vmcnt(2)
	s_barrier
	global_load_lds_dwordx4 v[2:3], off
	v_lshl_add_u64 v[2:3], v[4:5], 0, s[56:57]
	s_add_i32 m0, s82, 0x1a000
	s_add_i32 s68, s82, 0x8000
	s_add_i32 s93, s82, 0xa000
	v_lshl_add_u64 v[8:9], s[30:31], 0, v[124:125]
	global_load_lds_dwordx4 v[2:3], off
	v_lshl_add_u64 v[2:3], v[6:7], 0, s[56:57]
	s_mov_b32 m0, s68
	s_add_u32 s10, s28, 0x10080
	global_load_lds_dwordx4 v[2:3], off
	v_lshl_add_u64 v[2:3], v[8:9], 0, s[56:57]
	s_mov_b32 m0, s93
	s_addc_u32 s11, s29, 0
	global_load_lds_dwordx4 v[2:3], off
	s_add_i32 m0, s82, 0x1c000
	s_nop 0
	global_load_lds_dwordx4 v126, s[10:11]
	v_lshl_add_u64 v[2:3], s[10:11], 0, v[122:123]
	s_add_i32 m0, s82, 0x1e000
	v_and_b32_e32 v0, 15, v239
	global_load_lds_dwordx4 v122, s[10:11]
	v_and_b32_e32 v2, 48, v239
	v_lshlrev_b32_e32 v3, 2, v239
	v_lshl_or_b32 v2, v0, 6, v2
	v_and_b32_e32 v3, 32, v3
	v_bitop3_b32 v6, v2, s8, v3 bitop3:0xde
	s_waitcnt vmcnt(6)
	v_mov_b32_e32 v4, v1
	v_mov_b32_e32 v5, v1
	v_readlane_b32 s8, v254, 58
	v_bitop3_b32 v138, v2, s9, v3 bitop3:0xde
	v_mov_b32_e32 v2, v1
	v_mov_b32_e32 v3, v1
	v_add_u32_e32 v139, 0, v6
	v_mov_b64_e32 v[8:9], v[4:5]
	v_mov_b64_e32 v[20:21], v[4:5]
	v_mov_b64_e32 v[24:25], v[4:5]
	v_mov_b64_e32 v[36:37], v[4:5]
	v_mov_b64_e32 v[40:41], v[4:5]
	v_mov_b64_e32 v[52:53], v[4:5]
	v_mov_b64_e32 v[56:57], v[4:5]
	v_mov_b64_e32 v[12:13], v[4:5]
	v_mov_b64_e32 v[16:17], v[4:5]
	v_mov_b64_e32 v[28:29], v[4:5]
	v_mov_b64_e32 v[32:33], v[4:5]
	v_mov_b64_e32 v[44:45], v[4:5]
	v_mov_b64_e32 v[48:49], v[4:5]
	v_mov_b64_e32 v[60:61], v[4:5]
	v_mov_b64_e32 v[64:65], v[4:5]
	v_mov_b64_e32 v[68:69], v[4:5]
	v_mov_b64_e32 v[72:73], v[4:5]
	v_mov_b64_e32 v[84:85], v[4:5]
	v_mov_b64_e32 v[88:89], v[4:5]
	v_mov_b64_e32 v[100:101], v[4:5]
	v_mov_b64_e32 v[104:105], v[4:5]
	v_mov_b64_e32 v[116:117], v[4:5]
	v_mov_b64_e32 v[120:121], v[4:5]
	v_mov_b64_e32 v[76:77], v[4:5]
	v_mov_b64_e32 v[80:81], v[4:5]
	v_mov_b64_e32 v[92:93], v[4:5]
	v_mov_b64_e32 v[96:97], v[4:5]
	v_mov_b64_e32 v[108:109], v[4:5]
	v_mov_b64_e32 v[112:113], v[4:5]
	v_mov_b64_e32 v[132:133], v[4:5]
	v_mov_b64_e32 v[136:137], v[4:5]
	s_mov_b32 s14, s8
	v_readlane_b32 s8, v254, 54
	v_lshl_or_b32 v240, s80, 6, v0
	s_mov_b32 s94, 0
	v_mov_b64_e32 v[6:7], v[2:3]
	v_mov_b64_e32 v[18:19], v[2:3]
	v_mov_b64_e32 v[22:23], v[2:3]
	v_mov_b64_e32 v[34:35], v[2:3]
	v_mov_b64_e32 v[38:39], v[2:3]
	v_mov_b64_e32 v[50:51], v[2:3]
	v_mov_b64_e32 v[54:55], v[2:3]
	v_mov_b64_e32 v[10:11], v[2:3]
	v_mov_b64_e32 v[14:15], v[2:3]
	v_mov_b64_e32 v[26:27], v[2:3]
	v_mov_b64_e32 v[30:31], v[2:3]
	v_mov_b64_e32 v[42:43], v[2:3]
	v_mov_b64_e32 v[46:47], v[2:3]
	v_mov_b64_e32 v[58:59], v[2:3]
	v_mov_b64_e32 v[62:63], v[2:3]
	v_mov_b64_e32 v[66:67], v[2:3]
	v_mov_b64_e32 v[70:71], v[2:3]
	v_mov_b64_e32 v[82:83], v[2:3]
	v_mov_b64_e32 v[86:87], v[2:3]
	v_mov_b64_e32 v[98:99], v[2:3]
	v_mov_b64_e32 v[102:103], v[2:3]
	v_mov_b64_e32 v[114:115], v[2:3]
	v_mov_b64_e32 v[118:119], v[2:3]
	v_mov_b64_e32 v[74:75], v[2:3]
	v_mov_b64_e32 v[78:79], v[2:3]
	v_mov_b64_e32 v[90:91], v[2:3]
	v_mov_b64_e32 v[94:95], v[2:3]
	v_mov_b64_e32 v[106:107], v[2:3]
	v_mov_b64_e32 v[110:111], v[2:3]
	v_mov_b64_e32 v[130:131], v[2:3]
	v_mov_b64_e32 v[134:135], v[2:3]
	s_mov_b32 s95, s8
	s_barrier
	v_readlane_b32 s9, v254, 55
	s_branch .LBB0_2460

.LBB0_2467:
	s_add_u32 s8, s30, s12
	s_addc_u32 s9, s31, 0
	s_add_u32 s13, s8, 0x100
	s_addc_u32 s50, s9, 0
	s_and_b64 s[10:11], s[48:49], exec
	s_cselect_b32 s63, s37, s50
	s_cselect_b32 s62, s59, s13
	s_add_u32 s10, s28, s12
	s_addc_u32 s11, s29, 0
	s_add_u32 s12, s10, 0x100
	s_addc_u32 s13, s11, 0
	s_add_i32 s50, 0, 0x10000
	s_and_b64 s[10:11], s[48:49], exec
	s_cselect_b32 s71, s35, s13
	s_cselect_b32 s70, s96, s12
	s_add_i32 s12, 0, 0x14000
	s_add_u32 s10, s8, 0x10080
	s_addc_u32 s11, s9, 0
	s_add_i32 s9, s50, s81
	s_add_i32 m0, s82, 0xc000
	s_add_i32 s8, s82, 0xe000
	s_add_i32 s64, s9, 0x2000
	s_add_u32 s76, s70, 0x10000
	s_addc_u32 s77, s71, 0
	s_add_i32 s65, s12, s81
	v_add_u32_e32 v152, s50, v138
	v_add_u32_e32 v168, s12, v138
	s_add_i32 s74, s65, 0x2000
	s_add_i32 s91, 0, 0x18000
	s_add_i32 s13, 0, 0x1c000
	ds_read_b128 v[140:143], v152
	ds_read_b128 v[144:147], v152 offset:1024
	ds_read_b128 v[148:151], v152 offset:2048
	ds_read_b128 v[152:155], v152 offset:3072
	ds_read_b128 v[156:159], v168
	ds_read_b128 v[160:163], v168 offset:1024
	ds_read_b128 v[164:167], v168 offset:2048
	ds_read_b128 v[168:171], v168 offset:3072
	s_add_u32 s52, s62, 0x10000
	s_addc_u32 s53, s63, 0
	s_add_i32 vcc_hi, s91, s81
	s_add_i32 vcc_lo, vcc_hi, 0x2000
	s_add_u32 s48, s70, 0x10080
	s_addc_u32 s49, s71, 0
	s_add_i32 s50, s13, s81
	s_add_i32 s12, s50, 0x2000
	ds_read_b128 v[172:175], v139
	ds_read_b128 v[176:179], v139 offset:1024
	ds_read_b128 v[180:183], v139 offset:2048
	ds_read_b128 v[184:187], v139 offset:3072
	ds_read_b128 v[188:191], v139 offset:4096
	ds_read_b128 v[192:195], v139 offset:5120
	ds_read_b128 v[196:199], v139 offset:6144
	ds_read_b128 v[200:203], v139 offset:7168
	global_load_lds_dwordx4 v128, s[10:11]
	s_mov_b32 m0, s8
	s_nop 0
	global_load_lds_dwordx4 v124, s[10:11]
	s_waitcnt vmcnt(8)
	s_waitcnt lgkmcnt(0)
	s_barrier
	s_setprio 1
	s_waitcnt lgkmcnt(0)
	v_mfma_f32_16x16x32_bf16 v[134:137], v[140:143], v[172:175], v[134:137]
	v_mfma_f32_16x16x32_bf16 v[130:133], v[148:151], v[172:175], v[130:133]
	v_mfma_f32_16x16x32_bf16 v[110:113], v[140:143], v[180:183], v[110:113]
	v_mfma_f32_16x16x32_bf16 v[106:109], v[148:151], v[180:183], v[106:109]
	v_mfma_f32_16x16x32_bf16 v[94:97], v[140:143], v[188:191], v[94:97]
	v_mfma_f32_16x16x32_bf16 v[90:93], v[148:151], v[188:191], v[90:93]
	v_mfma_f32_16x16x32_bf16 v[78:81], v[140:143], v[196:199], v[78:81]
	v_mfma_f32_16x16x32_bf16 v[74:77], v[148:151], v[196:199], v[74:77]
	v_mfma_f32_16x16x32_bf16 v[134:137], v[144:147], v[176:179], v[134:137]
	v_mfma_f32_16x16x32_bf16 v[130:133], v[152:155], v[176:179], v[130:133]
	v_mfma_f32_16x16x32_bf16 v[110:113], v[144:147], v[184:187], v[110:113]
	v_mfma_f32_16x16x32_bf16 v[106:109], v[152:155], v[184:187], v[106:109]
	v_mfma_f32_16x16x32_bf16 v[94:97], v[144:147], v[192:195], v[94:97]
	v_mfma_f32_16x16x32_bf16 v[90:93], v[152:155], v[192:195], v[90:93]
	v_mfma_f32_16x16x32_bf16 v[78:81], v[144:147], v[200:203], v[78:81]
	v_mfma_f32_16x16x32_bf16 v[74:77], v[152:155], v[200:203], v[74:77]
	s_setprio 0
	s_setprio 1
	v_mfma_f32_16x16x32_bf16 v[118:121], v[156:159], v[172:175], v[118:121]
	v_mfma_f32_16x16x32_bf16 v[114:117], v[164:167], v[172:175], v[114:117]
	v_mfma_f32_16x16x32_bf16 v[102:105], v[156:159], v[180:183], v[102:105]
	v_mfma_f32_16x16x32_bf16 v[98:101], v[164:167], v[180:183], v[98:101]
	v_mfma_f32_16x16x32_bf16 v[86:89], v[156:159], v[188:191], v[86:89]
	v_mfma_f32_16x16x32_bf16 v[82:85], v[164:167], v[188:191], v[82:85]
	v_mfma_f32_16x16x32_bf16 v[70:73], v[156:159], v[196:199], v[70:73]
	v_mfma_f32_16x16x32_bf16 v[66:69], v[164:167], v[196:199], v[66:69]
	v_mfma_f32_16x16x32_bf16 v[118:121], v[160:163], v[176:179], v[118:121]
	v_mfma_f32_16x16x32_bf16 v[114:117], v[168:171], v[176:179], v[114:117]
	v_mfma_f32_16x16x32_bf16 v[102:105], v[160:163], v[184:187], v[102:105]
	v_mfma_f32_16x16x32_bf16 v[98:101], v[168:171], v[184:187], v[98:101]
	v_mfma_f32_16x16x32_bf16 v[86:89], v[160:163], v[192:195], v[86:89]
	v_mfma_f32_16x16x32_bf16 v[82:85], v[168:171], v[192:195], v[82:85]
	v_mfma_f32_16x16x32_bf16 v[70:73], v[160:163], v[200:203], v[70:73]
	v_mfma_f32_16x16x32_bf16 v[66:69], v[168:171], v[200:203], v[66:69]
	s_setprio 0
	s_barrier
	s_mov_b32 m0, s9
	v_lshl_add_u64 v[204:205], s[70:71], 0, v[126:127]
	ds_read_b128 v[172:175], v139 offset:16384
	ds_read_b128 v[176:179], v139 offset:17408
	ds_read_b128 v[180:183], v139 offset:18432
	ds_read_b128 v[184:187], v139 offset:19456
	ds_read_b128 v[188:191], v139 offset:20480
	ds_read_b128 v[192:195], v139 offset:21504
	ds_read_b128 v[196:199], v139 offset:22528
	ds_read_b128 v[200:203], v139 offset:23552
	global_load_lds_dwordx4 v126, s[70:71]
	v_lshl_add_u64 v[206:207], s[70:71], 0, v[122:123]
	s_mov_b32 m0, s64
	s_nop 0
	global_load_lds_dwordx4 v122, s[70:71]
	s_mov_b32 m0, s65
	v_lshl_add_u64 v[216:217], s[62:63], 0, v[124:125]
	global_load_lds_dwordx4 v126, s[76:77]
	s_mov_b32 m0, s74
	s_nop 0
	global_load_lds_dwordx4 v122, s[76:77]
	s_mov_b32 m0, s82
	v_lshl_add_u64 v[208:209], s[62:63], 0, v[128:129]
	global_load_lds_dwordx4 v128, s[62:63]
	s_mov_b32 m0, s92
	s_nop 0
	global_load_lds_dwordx4 v124, s[62:63]
	s_waitcnt vmcnt(8)
	s_waitcnt lgkmcnt(0)
	s_barrier
	s_setprio 1
	s_waitcnt lgkmcnt(0)
	v_mfma_f32_16x16x32_bf16 v[62:65], v[140:143], v[172:175], v[62:65]
	v_mfma_f32_16x16x32_bf16 v[58:61], v[148:151], v[172:175], v[58:61]
	v_mfma_f32_16x16x32_bf16 v[46:49], v[140:143], v[180:183], v[46:49]
	v_mfma_f32_16x16x32_bf16 v[42:45], v[148:151], v[180:183], v[42:45]
	v_mfma_f32_16x16x32_bf16 v[30:33], v[140:143], v[188:191], v[30:33]
	v_mfma_f32_16x16x32_bf16 v[26:29], v[148:151], v[188:191], v[26:29]
	v_mfma_f32_16x16x32_bf16 v[14:17], v[140:143], v[196:199], v[14:17]
	v_mfma_f32_16x16x32_bf16 v[10:13], v[148:151], v[196:199], v[10:13]
	v_mfma_f32_16x16x32_bf16 v[62:65], v[144:147], v[176:179], v[62:65]
	v_mfma_f32_16x16x32_bf16 v[58:61], v[152:155], v[176:179], v[58:61]
	v_mfma_f32_16x16x32_bf16 v[46:49], v[144:147], v[184:187], v[46:49]
	v_mfma_f32_16x16x32_bf16 v[42:45], v[152:155], v[184:187], v[42:45]
	v_mfma_f32_16x16x32_bf16 v[30:33], v[144:147], v[192:195], v[30:33]
	v_mfma_f32_16x16x32_bf16 v[26:29], v[152:155], v[192:195], v[26:29]
	v_mfma_f32_16x16x32_bf16 v[14:17], v[144:147], v[200:203], v[14:17]
	v_mfma_f32_16x16x32_bf16 v[10:13], v[152:155], v[200:203], v[10:13]
	s_setprio 0
	s_setprio 1
	v_mfma_f32_16x16x32_bf16 v[54:57], v[156:159], v[172:175], v[54:57]
	v_mfma_f32_16x16x32_bf16 v[50:53], v[164:167], v[172:175], v[50:53]
	v_mfma_f32_16x16x32_bf16 v[38:41], v[156:159], v[180:183], v[38:41]
	v_mfma_f32_16x16x32_bf16 v[34:37], v[164:167], v[180:183], v[34:37]
	v_mfma_f32_16x16x32_bf16 v[22:25], v[156:159], v[188:191], v[22:25]
	v_mfma_f32_16x16x32_bf16 v[18:21], v[164:167], v[188:191], v[18:21]
	v_mfma_f32_16x16x32_bf16 v[6:9], v[156:159], v[196:199], v[6:9]
	v_mfma_f32_16x16x32_bf16 v[2:5], v[164:167], v[196:199], v[2:5]
	v_mfma_f32_16x16x32_bf16 v[54:57], v[160:163], v[176:179], v[54:57]
	v_mfma_f32_16x16x32_bf16 v[50:53], v[168:171], v[176:179], v[50:53]
	v_mfma_f32_16x16x32_bf16 v[38:41], v[160:163], v[184:187], v[38:41]
	v_mfma_f32_16x16x32_bf16 v[34:37], v[168:171], v[184:187], v[34:37]
	v_mfma_f32_16x16x32_bf16 v[22:25], v[160:163], v[192:195], v[22:25]
	v_mfma_f32_16x16x32_bf16 v[18:21], v[168:171], v[192:195], v[18:21]
	v_mfma_f32_16x16x32_bf16 v[6:9], v[160:163], v[200:203], v[6:9]
	v_mfma_f32_16x16x32_bf16 v[2:5], v[168:171], v[200:203], v[2:5]
	s_setprio 0
	s_barrier
	v_add_u32_e32 v152, s91, v138
	v_add_u32_e32 v168, s13, v138
	ds_read_b128 v[140:143], v152
	ds_read_b128 v[144:147], v152 offset:1024
	ds_read_b128 v[148:151], v152 offset:2048
	ds_read_b128 v[152:155], v152 offset:3072
	ds_read_b128 v[156:159], v168
	ds_read_b128 v[160:163], v168 offset:1024
	ds_read_b128 v[164:167], v168 offset:2048
	ds_read_b128 v[168:171], v168 offset:3072
	s_mov_b32 m0, s84
	ds_read_b128 v[172:175], v139 offset:32768
	ds_read_b128 v[176:179], v139 offset:33792
	ds_read_b128 v[180:183], v139 offset:34816
	ds_read_b128 v[184:187], v139 offset:35840
	ds_read_b128 v[188:191], v139 offset:36864
	ds_read_b128 v[192:195], v139 offset:37888
	ds_read_b128 v[196:199], v139 offset:38912
	ds_read_b128 v[200:203], v139 offset:39936
	global_load_lds_dwordx4 v128, s[52:53]
	s_mov_b32 m0, s90
	s_nop 0
	global_load_lds_dwordx4 v124, s[52:53]
	s_waitcnt vmcnt(8)
	s_waitcnt lgkmcnt(0)
	s_barrier
	s_setprio 1
	s_waitcnt lgkmcnt(0)
	v_mfma_f32_16x16x32_bf16 v[134:137], v[140:143], v[172:175], v[134:137]
	v_mfma_f32_16x16x32_bf16 v[130:133], v[148:151], v[172:175], v[130:133]
	v_mfma_f32_16x16x32_bf16 v[110:113], v[140:143], v[180:183], v[110:113]
	v_mfma_f32_16x16x32_bf16 v[106:109], v[148:151], v[180:183], v[106:109]
	v_mfma_f32_16x16x32_bf16 v[94:97], v[140:143], v[188:191], v[94:97]
	v_mfma_f32_16x16x32_bf16 v[90:93], v[148:151], v[188:191], v[90:93]
	v_mfma_f32_16x16x32_bf16 v[78:81], v[140:143], v[196:199], v[78:81]
	v_mfma_f32_16x16x32_bf16 v[74:77], v[148:151], v[196:199], v[74:77]
	v_mfma_f32_16x16x32_bf16 v[134:137], v[144:147], v[176:179], v[134:137]
	v_mfma_f32_16x16x32_bf16 v[130:133], v[152:155], v[176:179], v[130:133]
	v_mfma_f32_16x16x32_bf16 v[110:113], v[144:147], v[184:187], v[110:113]
	v_mfma_f32_16x16x32_bf16 v[106:109], v[152:155], v[184:187], v[106:109]
	v_mfma_f32_16x16x32_bf16 v[94:97], v[144:147], v[192:195], v[94:97]
	v_mfma_f32_16x16x32_bf16 v[90:93], v[152:155], v[192:195], v[90:93]
	v_mfma_f32_16x16x32_bf16 v[78:81], v[144:147], v[200:203], v[78:81]
	v_mfma_f32_16x16x32_bf16 v[74:77], v[152:155], v[200:203], v[74:77]
	s_setprio 0
	s_setprio 1
	v_mfma_f32_16x16x32_bf16 v[118:121], v[156:159], v[172:175], v[118:121]
	v_mfma_f32_16x16x32_bf16 v[114:117], v[164:167], v[172:175], v[114:117]
	v_mfma_f32_16x16x32_bf16 v[102:105], v[156:159], v[180:183], v[102:105]
	v_mfma_f32_16x16x32_bf16 v[98:101], v[164:167], v[180:183], v[98:101]
	v_mfma_f32_16x16x32_bf16 v[86:89], v[156:159], v[188:191], v[86:89]
	v_mfma_f32_16x16x32_bf16 v[82:85], v[164:167], v[188:191], v[82:85]
	v_mfma_f32_16x16x32_bf16 v[70:73], v[156:159], v[196:199], v[70:73]
	v_mfma_f32_16x16x32_bf16 v[66:69], v[164:167], v[196:199], v[66:69]
	v_mfma_f32_16x16x32_bf16 v[118:121], v[160:163], v[176:179], v[118:121]
	v_mfma_f32_16x16x32_bf16 v[114:117], v[168:171], v[176:179], v[114:117]
	v_mfma_f32_16x16x32_bf16 v[102:105], v[160:163], v[184:187], v[102:105]
	v_mfma_f32_16x16x32_bf16 v[98:101], v[168:171], v[184:187], v[98:101]
	v_mfma_f32_16x16x32_bf16 v[86:89], v[160:163], v[192:195], v[86:89]
	v_mfma_f32_16x16x32_bf16 v[82:85], v[168:171], v[192:195], v[82:85]
	v_mfma_f32_16x16x32_bf16 v[70:73], v[160:163], v[200:203], v[70:73]
	v_mfma_f32_16x16x32_bf16 v[66:69], v[168:171], v[200:203], v[66:69]
	s_setprio 0
	s_barrier
	s_mov_b32 m0, vcc_hi
	v_lshl_add_u64 v[204:205], v[204:205], 0, s[56:57]
	ds_read_b128 v[172:175], v139 offset:49152
	ds_read_b128 v[176:179], v139 offset:50176
	ds_read_b128 v[180:183], v139 offset:51200
	ds_read_b128 v[184:187], v139 offset:52224
	ds_read_b128 v[188:191], v139 offset:53248
	ds_read_b128 v[192:195], v139 offset:54272
	ds_read_b128 v[196:199], v139 offset:55296
	ds_read_b128 v[200:203], v139 offset:56320
	global_load_lds_dwordx4 v[204:205], off
	s_mov_b32 m0, vcc_lo
	v_lshl_add_u64 v[204:205], v[206:207], 0, s[56:57]
	global_load_lds_dwordx4 v[204:205], off
	s_mov_b32 m0, s50
	s_nop 0
	global_load_lds_dwordx4 v126, s[48:49]
	s_mov_b32 m0, s12
	s_nop 0
	global_load_lds_dwordx4 v122, s[48:49]
	s_mov_b32 m0, s68
	v_lshl_add_u64 v[204:205], v[208:209], 0, s[56:57]
	global_load_lds_dwordx4 v[204:205], off
	s_mov_b32 m0, s93
	v_lshl_add_u64 v[204:205], v[216:217], 0, s[56:57]
	global_load_lds_dwordx4 v[204:205], off
	s_waitcnt vmcnt(8)
	s_waitcnt lgkmcnt(0)
	s_barrier
	s_setprio 1
	s_waitcnt lgkmcnt(0)
	v_mfma_f32_16x16x32_bf16 v[62:65], v[140:143], v[172:175], v[62:65]
	v_mfma_f32_16x16x32_bf16 v[58:61], v[148:151], v[172:175], v[58:61]
	v_mfma_f32_16x16x32_bf16 v[46:49], v[140:143], v[180:183], v[46:49]
	v_mfma_f32_16x16x32_bf16 v[42:45], v[148:151], v[180:183], v[42:45]
	v_mfma_f32_16x16x32_bf16 v[30:33], v[140:143], v[188:191], v[30:33]
	v_mfma_f32_16x16x32_bf16 v[26:29], v[148:151], v[188:191], v[26:29]
	v_mfma_f32_16x16x32_bf16 v[14:17], v[140:143], v[196:199], v[14:17]
	v_mfma_f32_16x16x32_bf16 v[10:13], v[148:151], v[196:199], v[10:13]
	v_mfma_f32_16x16x32_bf16 v[62:65], v[144:147], v[176:179], v[62:65]
	v_mfma_f32_16x16x32_bf16 v[58:61], v[152:155], v[176:179], v[58:61]
	v_mfma_f32_16x16x32_bf16 v[46:49], v[144:147], v[184:187], v[46:49]
	v_mfma_f32_16x16x32_bf16 v[42:45], v[152:155], v[184:187], v[42:45]
	v_mfma_f32_16x16x32_bf16 v[30:33], v[144:147], v[192:195], v[30:33]
	v_mfma_f32_16x16x32_bf16 v[26:29], v[152:155], v[192:195], v[26:29]
	v_mfma_f32_16x16x32_bf16 v[14:17], v[144:147], v[200:203], v[14:17]
	v_mfma_f32_16x16x32_bf16 v[10:13], v[152:155], v[200:203], v[10:13]
	s_setprio 0
	s_setprio 1
	v_mfma_f32_16x16x32_bf16 v[54:57], v[156:159], v[172:175], v[54:57]
	v_mfma_f32_16x16x32_bf16 v[50:53], v[164:167], v[172:175], v[50:53]
	v_mfma_f32_16x16x32_bf16 v[38:41], v[156:159], v[180:183], v[38:41]
	v_mfma_f32_16x16x32_bf16 v[34:37], v[164:167], v[180:183], v[34:37]
	v_mfma_f32_16x16x32_bf16 v[22:25], v[156:159], v[188:191], v[22:25]
	v_mfma_f32_16x16x32_bf16 v[18:21], v[164:167], v[188:191], v[18:21]
	v_mfma_f32_16x16x32_bf16 v[6:9], v[156:159], v[196:199], v[6:9]
	v_mfma_f32_16x16x32_bf16 v[2:5], v[164:167], v[196:199], v[2:5]
	v_mfma_f32_16x16x32_bf16 v[54:57], v[160:163], v[176:179], v[54:57]
	v_mfma_f32_16x16x32_bf16 v[50:53], v[168:171], v[176:179], v[50:53]
	v_mfma_f32_16x16x32_bf16 v[38:41], v[160:163], v[184:187], v[38:41]
	v_mfma_f32_16x16x32_bf16 v[34:37], v[168:171], v[184:187], v[34:37]
	v_mfma_f32_16x16x32_bf16 v[22:25], v[160:163], v[192:195], v[22:25]
	v_mfma_f32_16x16x32_bf16 v[18:21], v[168:171], v[192:195], v[18:21]
	v_mfma_f32_16x16x32_bf16 v[6:9], v[160:163], v[200:203], v[6:9]
	v_mfma_f32_16x16x32_bf16 v[2:5], v[168:171], v[200:203], v[2:5]
	s_setprio 0
	s_barrier
	s_movk_i32 s12, 0x100
	s_andn2_b64 vcc, exec, s[46:47]
	s_mov_b64 s[48:49], -1
	s_mov_b64 s[46:47], 0
	s_cbranch_vccz .LBB0_2467
	s_andn2_b64 vcc, exec, s[40:41]
	s_cbranch_vccnz .LBB0_2459
	v_mov_b32_e32 v2, 0
	s_mov_b32 s14, s34
	s_mov_b32 s95, s36
	s_mov_b64 s[28:29], s[44:45]
	s_mov_b64 s[30:31], s[42:43]
	s_mov_b32 s94, s58
	v_mov_b32_e32 v3, v2
	v_mov_b32_e32 v4, v2
	v_mov_b32_e32 v5, v2
	v_mov_b32_e32 v6, v2
	v_mov_b32_e32 v7, v2
	v_mov_b32_e32 v8, v2
	v_mov_b32_e32 v9, v2
	v_mov_b32_e32 v18, v2
	v_mov_b32_e32 v19, v2
	v_mov_b32_e32 v20, v2
	v_mov_b32_e32 v21, v2
	v_mov_b32_e32 v22, v2
	v_mov_b32_e32 v23, v2
	v_mov_b32_e32 v24, v2
	v_mov_b32_e32 v25, v2
	v_mov_b32_e32 v34, v2
	v_mov_b32_e32 v35, v2
	v_mov_b32_e32 v36, v2
	v_mov_b32_e32 v37, v2
	v_mov_b32_e32 v38, v2
	v_mov_b32_e32 v39, v2
	v_mov_b32_e32 v40, v2
	v_mov_b32_e32 v41, v2
	v_mov_b32_e32 v50, v2
	v_mov_b32_e32 v51, v2
	v_mov_b32_e32 v52, v2
	v_mov_b32_e32 v53, v2
	v_mov_b32_e32 v54, v2
	v_mov_b32_e32 v55, v2
	v_mov_b32_e32 v56, v2
	v_mov_b32_e32 v57, v2
	v_mov_b32_e32 v10, v2
	v_mov_b32_e32 v11, v2
	v_mov_b32_e32 v12, v2
	v_mov_b32_e32 v13, v2
	v_mov_b32_e32 v14, v2
	v_mov_b32_e32 v15, v2
	v_mov_b32_e32 v16, v2
	v_mov_b32_e32 v17, v2
	v_mov_b32_e32 v26, v2
	v_mov_b32_e32 v27, v2
	v_mov_b32_e32 v28, v2
	v_mov_b32_e32 v29, v2
	v_mov_b32_e32 v30, v2
	v_mov_b32_e32 v31, v2
	v_mov_b32_e32 v32, v2
	v_mov_b32_e32 v33, v2
	v_mov_b32_e32 v42, v2
	v_mov_b32_e32 v43, v2
	v_mov_b32_e32 v44, v2
	v_mov_b32_e32 v45, v2
	v_mov_b32_e32 v46, v2
	v_mov_b32_e32 v47, v2
	v_mov_b32_e32 v48, v2
	v_mov_b32_e32 v49, v2
	v_mov_b32_e32 v58, v2
	v_mov_b32_e32 v59, v2
	v_mov_b32_e32 v60, v2
	v_mov_b32_e32 v61, v2
	v_mov_b32_e32 v62, v2
	v_mov_b32_e32 v63, v2
	v_mov_b32_e32 v64, v2
	v_mov_b32_e32 v65, v2
	v_mov_b32_e32 v66, v2
	v_mov_b32_e32 v67, v2
	v_mov_b32_e32 v68, v2
	v_mov_b32_e32 v69, v2
	v_mov_b32_e32 v70, v2
	v_mov_b32_e32 v71, v2
	v_mov_b32_e32 v72, v2
	v_mov_b32_e32 v73, v2
	v_mov_b32_e32 v82, v2
	v_mov_b32_e32 v83, v2
	v_mov_b32_e32 v84, v2
	v_mov_b32_e32 v85, v2
	v_mov_b32_e32 v86, v2
	v_mov_b32_e32 v87, v2
	v_mov_b32_e32 v88, v2
	v_mov_b32_e32 v89, v2
	v_mov_b32_e32 v98, v2
	v_mov_b32_e32 v99, v2
	v_mov_b32_e32 v100, v2
	v_mov_b32_e32 v101, v2
	v_mov_b32_e32 v102, v2
	v_mov_b32_e32 v103, v2
	v_mov_b32_e32 v104, v2
	v_mov_b32_e32 v105, v2
	v_mov_b32_e32 v114, v2
	v_mov_b32_e32 v115, v2
	v_mov_b32_e32 v116, v2
	v_mov_b32_e32 v117, v2
	v_mov_b32_e32 v118, v2
	v_mov_b32_e32 v119, v2
	v_mov_b32_e32 v120, v2
	v_mov_b32_e32 v121, v2
	v_mov_b32_e32 v74, v2
	v_mov_b32_e32 v75, v2
	v_mov_b32_e32 v76, v2
	v_mov_b32_e32 v77, v2
	v_mov_b32_e32 v78, v2
	v_mov_b32_e32 v79, v2
	v_mov_b32_e32 v80, v2
	v_mov_b32_e32 v81, v2
	v_mov_b32_e32 v90, v2
	v_mov_b32_e32 v91, v2
	v_mov_b32_e32 v92, v2
	v_mov_b32_e32 v93, v2
	v_mov_b32_e32 v94, v2
	v_mov_b32_e32 v95, v2
	v_mov_b32_e32 v96, v2
	v_mov_b32_e32 v97, v2
	v_mov_b32_e32 v106, v2
	v_mov_b32_e32 v107, v2
	v_mov_b32_e32 v108, v2
	v_mov_b32_e32 v109, v2
	v_mov_b32_e32 v110, v2
	v_mov_b32_e32 v111, v2
	v_mov_b32_e32 v112, v2
	v_mov_b32_e32 v113, v2
	v_mov_b32_e32 v130, v2
	v_mov_b32_e32 v131, v2
	v_mov_b32_e32 v132, v2
	v_mov_b32_e32 v133, v2
	v_mov_b32_e32 v134, v2
	v_mov_b32_e32 v135, v2
	v_mov_b32_e32 v136, v2
	v_mov_b32_e32 v137, v2
	s_branch .LBB0_2459

.LBB0_2616:
	s_add_u32 s12, s12, 0xac00000
	s_addc_u32 s13, s13, 0
	s_add_u32 s14, s14, 0x1f00000
	s_addc_u32 s15, s15, 0
	s_lshl_b32 s17, s17, 5
	s_and_b32 s21, s17, 0x60
	s_add_i32 m0, s36, 0x18000
	v_lshl_add_u64 v[8:9], v[8:9], 0, s[56:57]
	s_lshl_b32 s20, s16, 13
	s_lshl_b32 s17, s21, 7
	s_waitcnt vmcnt(2)
	s_barrier
	global_load_lds_dwordx4 v[8:9], off
	v_lshl_add_u64 v[6:7], v[6:7], 0, s[56:57]
	s_add_i32 m0, s36, 0x1a000
	s_add_i32 s44, s36, 0x8000
	s_add_i32 s45, s36, 0xa000
	global_load_lds_dwordx4 v[6:7], off
	v_lshl_add_u64 v[2:3], v[2:3], 0, s[56:57]
	s_mov_b32 m0, s44
	s_add_u32 s18, s6, 0x40080
	global_load_lds_dwordx4 v[2:3], off
	v_lshl_add_u64 v[2:3], v[4:5], 0, s[56:57]
	s_mov_b32 m0, s45
	s_addc_u32 s19, s7, 0
	global_load_lds_dwordx4 v[2:3], off
	s_add_i32 m0, s36, 0x1c000
	s_nop 0
	global_load_lds_dwordx4 v162, s[18:19]
	v_lshl_add_u64 v[2:3], s[18:19], 0, v[158:159]
	s_add_i32 m0, s36, 0x1e000
	s_cmpk_lt_u32 s4, 0x100
	global_load_lds_dwordx4 v158, s[18:19]
	v_lshrrev_b32_e32 v3, 1, v0
	v_and_b32_e32 v3, 24, v3
	v_and_b32_e32 v2, 15, v0
	v_lshlrev_b32_e32 v4, 1, v3
	v_lshlrev_b32_e32 v0, 2, v0
	v_lshl_or_b32 v180, s16, 6, v2
	v_lshl_or_b32 v2, v2, 6, v4
	v_and_b32_e32 v0, 32, v0
	v_bitop3_b32 v4, v2, s20, v0 bitop3:0xde
	v_bitop3_b32 v181, v2, s17, v0 bitop3:0xde
	v_lshlrev_b32_e32 v0, 14, v10
	v_and_b32_e32 v0, 0xffff8000, v0
	v_lshl_add_u32 v0, v11, 11, v0
	v_and_b32_e32 v2, 1, v10
	v_lshl_or_b32 v0, v2, 6, v0
	v_lshl_add_u32 v166, v12, 1, v0
	v_lshlrev_b32_e32 v0, 14, v14
	v_and_b32_e32 v0, 0xffff8000, v0
	s_waitcnt vmcnt(6)
	v_lshl_add_u32 v0, v13, 11, v0
	v_and_b32_e32 v2, 1, v14
	v_lshl_or_b32 v0, v2, 6, v0
	v_readlane_b32 s18, v254, 13
	s_cselect_b64 s[16:17], -1, 0
	v_or_b32_e32 v182, s21, v3
	v_mov_b32_e32 v167, v1
	v_lshl_add_u32 v168, v15, 1, v0
	v_mov_b32_e32 v169, v1
	s_mov_b32 s46, 0
	v_add_u32_e32 v183, 0, v4
	v_readlane_b32 s47, v253, 52
	s_mov_b32 s4, s18
	s_barrier
	v_readlane_b32 s19, v254, 14
	s_branch .LBB0_2619

.Lnobar_c6:
.LBB0_2626:
	s_add_u32 s26, s6, 0xfffc0080
	s_addc_u32 s27, s7, -1
	s_add_i32 s50, 0, 0x10000
	s_cmp_eq_u32 s49, 12
	s_cselect_b32 s29, s21, s27
	s_cselect_b32 s28, s33, s26
	v_add_u32_e32 v0, s50, v181
	s_cselect_b32 s27, s19, s48
	s_cselect_b32 s26, s40, s41
	s_add_i32 s58, 0, 0x14000
	ds_read_b128 v[130:133], v0
	ds_read_b128 v[134:137], v0 offset:1024
	ds_read_b128 v[138:141], v0 offset:2048
	ds_read_b128 v[142:145], v0 offset:3072
	v_add_u32_e32 v0, s58, v181
	ds_read_b128 v[146:149], v0
	ds_read_b128 v[150:153], v0 offset:1024
	ds_read_b128 v[154:157], v0 offset:2048
	ds_read_b128 v[170:173], v0 offset:3072
	s_add_i32 m0, s36, 0xc000
	ds_read_b128 v[174:177], v183
	ds_read_b128 v[184:187], v183 offset:1024
	ds_read_b128 v[188:191], v183 offset:2048
	ds_read_b128 v[192:195], v183 offset:3072
	ds_read_b128 v[196:199], v183 offset:4096
	ds_read_b128 v[200:203], v183 offset:5120
	ds_read_b128 v[204:207], v183 offset:6144
	ds_read_b128 v[216:219], v183 offset:7168
	global_load_lds_dwordx4 v168, s[6:7]
	s_add_i32 m0, s36, 0xe000
	s_nop 0
	global_load_lds_dwordx4 v166, s[6:7]
	s_waitcnt vmcnt(8)
	s_waitcnt lgkmcnt(0)
	s_barrier
	s_setprio 1
	s_waitcnt lgkmcnt(0)
	v_mfma_f32_16x16x32_bf16 v[126:129], v[130:133], v[174:177], v[126:129]
	v_mfma_f32_16x16x32_bf16 v[122:125], v[138:141], v[174:177], v[122:125]
	v_mfma_f32_16x16x32_bf16 v[110:113], v[130:133], v[188:191], v[110:113]
	v_mfma_f32_16x16x32_bf16 v[106:109], v[138:141], v[188:191], v[106:109]
	v_mfma_f32_16x16x32_bf16 v[94:97], v[130:133], v[196:199], v[94:97]
	v_mfma_f32_16x16x32_bf16 v[90:93], v[138:141], v[196:199], v[90:93]
	v_mfma_f32_16x16x32_bf16 v[78:81], v[130:133], v[204:207], v[78:81]
	v_mfma_f32_16x16x32_bf16 v[74:77], v[138:141], v[204:207], v[74:77]
	v_mfma_f32_16x16x32_bf16 v[126:129], v[134:137], v[184:187], v[126:129]
	v_mfma_f32_16x16x32_bf16 v[122:125], v[142:145], v[184:187], v[122:125]
	v_mfma_f32_16x16x32_bf16 v[110:113], v[134:137], v[192:195], v[110:113]
	v_mfma_f32_16x16x32_bf16 v[106:109], v[142:145], v[192:195], v[106:109]
	v_mfma_f32_16x16x32_bf16 v[94:97], v[134:137], v[200:203], v[94:97]
	v_mfma_f32_16x16x32_bf16 v[90:93], v[142:145], v[200:203], v[90:93]
	v_mfma_f32_16x16x32_bf16 v[78:81], v[134:137], v[216:219], v[78:81]
	v_mfma_f32_16x16x32_bf16 v[74:77], v[142:145], v[216:219], v[74:77]
	s_setprio 0
	s_setprio 1
	v_mfma_f32_16x16x32_bf16 v[118:121], v[146:149], v[174:177], v[118:121]
	v_mfma_f32_16x16x32_bf16 v[114:117], v[154:157], v[174:177], v[114:117]
	v_mfma_f32_16x16x32_bf16 v[102:105], v[146:149], v[188:191], v[102:105]
	v_mfma_f32_16x16x32_bf16 v[98:101], v[154:157], v[188:191], v[98:101]
	v_mfma_f32_16x16x32_bf16 v[86:89], v[146:149], v[196:199], v[86:89]
	v_mfma_f32_16x16x32_bf16 v[82:85], v[154:157], v[196:199], v[82:85]
	v_mfma_f32_16x16x32_bf16 v[70:73], v[146:149], v[204:207], v[70:73]
	v_mfma_f32_16x16x32_bf16 v[66:69], v[154:157], v[204:207], v[66:69]
	v_mfma_f32_16x16x32_bf16 v[118:121], v[150:153], v[184:187], v[118:121]
	v_mfma_f32_16x16x32_bf16 v[114:117], v[170:173], v[184:187], v[114:117]
	v_mfma_f32_16x16x32_bf16 v[102:105], v[150:153], v[192:195], v[102:105]
	v_mfma_f32_16x16x32_bf16 v[98:101], v[170:173], v[192:195], v[98:101]
	v_mfma_f32_16x16x32_bf16 v[86:89], v[150:153], v[200:203], v[86:89]
	v_mfma_f32_16x16x32_bf16 v[82:85], v[170:173], v[200:203], v[82:85]
	v_mfma_f32_16x16x32_bf16 v[70:73], v[150:153], v[216:219], v[70:73]
	v_mfma_f32_16x16x32_bf16 v[66:69], v[170:173], v[216:219], v[66:69]
	s_setprio 0
	s_barrier
	s_add_i32 s50, s50, s35
	v_lshl_add_u64 v[178:179], s[26:27], 0, v[162:163]
	s_mov_b32 m0, s50
	ds_read_b128 v[174:177], v183 offset:16384
	ds_read_b128 v[184:187], v183 offset:17408
	ds_read_b128 v[188:191], v183 offset:18432
	ds_read_b128 v[192:195], v183 offset:19456
	ds_read_b128 v[196:199], v183 offset:20480
	ds_read_b128 v[200:203], v183 offset:21504
	ds_read_b128 v[204:207], v183 offset:22528
	ds_read_b128 v[216:219], v183 offset:23552
	global_load_lds_dwordx4 v162, s[26:27]
	s_add_i32 m0, s50, 0x2000
	s_add_u32 s52, s26, 0x40000
	v_lshl_add_u64 v[208:209], s[26:27], 0, v[158:159]
	s_addc_u32 s53, s27, 0
	s_add_i32 s50, s58, s35
	global_load_lds_dwordx4 v158, s[26:27]
	s_mov_b32 m0, s50
	v_lshl_add_u64 v[222:223], s[28:29], 0, v[160:161]
	global_load_lds_dwordx4 v162, s[52:53]
	s_add_i32 m0, s50, 0x2000
	s_nop 0
	global_load_lds_dwordx4 v158, s[52:53]
	s_mov_b32 m0, s36
	v_lshl_add_u64 v[220:221], s[28:29], 0, v[164:165]
	global_load_lds_dwordx4 v164, s[28:29]
	s_mov_b32 m0, s37
	s_nop 0
	global_load_lds_dwordx4 v160, s[28:29]
	s_waitcnt vmcnt(8)
	s_waitcnt lgkmcnt(0)
	s_barrier
	s_setprio 1
	s_waitcnt lgkmcnt(0)
	v_mfma_f32_16x16x32_bf16 v[62:65], v[130:133], v[174:177], v[62:65]
	v_mfma_f32_16x16x32_bf16 v[58:61], v[138:141], v[174:177], v[58:61]
	v_mfma_f32_16x16x32_bf16 v[46:49], v[130:133], v[188:191], v[46:49]
	v_mfma_f32_16x16x32_bf16 v[42:45], v[138:141], v[188:191], v[42:45]
	v_mfma_f32_16x16x32_bf16 v[30:33], v[130:133], v[196:199], v[30:33]
	v_mfma_f32_16x16x32_bf16 v[26:29], v[138:141], v[196:199], v[26:29]
	v_mfma_f32_16x16x32_bf16 v[14:17], v[130:133], v[204:207], v[14:17]
	v_mfma_f32_16x16x32_bf16 v[10:13], v[138:141], v[204:207], v[10:13]
	v_mfma_f32_16x16x32_bf16 v[62:65], v[134:137], v[184:187], v[62:65]
	v_mfma_f32_16x16x32_bf16 v[58:61], v[142:145], v[184:187], v[58:61]
	v_mfma_f32_16x16x32_bf16 v[46:49], v[134:137], v[192:195], v[46:49]
	v_mfma_f32_16x16x32_bf16 v[42:45], v[142:145], v[192:195], v[42:45]
	v_mfma_f32_16x16x32_bf16 v[30:33], v[134:137], v[200:203], v[30:33]
	v_mfma_f32_16x16x32_bf16 v[26:29], v[142:145], v[200:203], v[26:29]
	v_mfma_f32_16x16x32_bf16 v[14:17], v[134:137], v[216:219], v[14:17]
	v_mfma_f32_16x16x32_bf16 v[10:13], v[142:145], v[216:219], v[10:13]
	s_setprio 0
	s_setprio 1
	v_mfma_f32_16x16x32_bf16 v[54:57], v[146:149], v[174:177], v[54:57]
	v_mfma_f32_16x16x32_bf16 v[50:53], v[154:157], v[174:177], v[50:53]
	v_mfma_f32_16x16x32_bf16 v[38:41], v[146:149], v[188:191], v[38:41]
	v_mfma_f32_16x16x32_bf16 v[34:37], v[154:157], v[188:191], v[34:37]
	v_mfma_f32_16x16x32_bf16 v[22:25], v[146:149], v[196:199], v[22:25]
	v_mfma_f32_16x16x32_bf16 v[18:21], v[154:157], v[196:199], v[18:21]
	v_mfma_f32_16x16x32_bf16 v[6:9], v[146:149], v[204:207], v[6:9]
	v_mfma_f32_16x16x32_bf16 v[2:5], v[154:157], v[204:207], v[2:5]
	v_mfma_f32_16x16x32_bf16 v[54:57], v[150:153], v[184:187], v[54:57]
	v_mfma_f32_16x16x32_bf16 v[50:53], v[170:173], v[184:187], v[50:53]
	v_mfma_f32_16x16x32_bf16 v[38:41], v[150:153], v[192:195], v[38:41]
	v_mfma_f32_16x16x32_bf16 v[34:37], v[170:173], v[192:195], v[34:37]
	v_mfma_f32_16x16x32_bf16 v[22:25], v[150:153], v[200:203], v[22:25]
	v_mfma_f32_16x16x32_bf16 v[18:21], v[170:173], v[200:203], v[18:21]
	v_mfma_f32_16x16x32_bf16 v[6:9], v[150:153], v[216:219], v[6:9]
	v_mfma_f32_16x16x32_bf16 v[2:5], v[170:173], v[216:219], v[2:5]
	s_setprio 0
	s_barrier
	s_add_i32 s50, 0, 0x18000
	v_add_u32_e32 v0, s50, v181
	s_add_i32 s52, 0, 0x1c000
	ds_read_b128 v[130:133], v0
	ds_read_b128 v[134:137], v0 offset:1024
	ds_read_b128 v[138:141], v0 offset:2048
	ds_read_b128 v[142:145], v0 offset:3072
	v_add_u32_e32 v0, s52, v181
	ds_read_b128 v[146:149], v0
	ds_read_b128 v[150:153], v0 offset:1024
	ds_read_b128 v[154:157], v0 offset:2048
	ds_read_b128 v[170:173], v0 offset:3072
	s_add_u32 s28, s28, 0x40000
	s_addc_u32 s29, s29, 0
	s_mov_b32 m0, s42
	ds_read_b128 v[174:177], v183 offset:32768
	ds_read_b128 v[184:187], v183 offset:33792
	ds_read_b128 v[188:191], v183 offset:34816
	ds_read_b128 v[192:195], v183 offset:35840
	ds_read_b128 v[196:199], v183 offset:36864
	ds_read_b128 v[200:203], v183 offset:37888
	ds_read_b128 v[204:207], v183 offset:38912
	ds_read_b128 v[216:219], v183 offset:39936
	global_load_lds_dwordx4 v164, s[28:29]
	s_mov_b32 m0, s43
	s_nop 0
	global_load_lds_dwordx4 v160, s[28:29]
	s_waitcnt vmcnt(8)
	s_waitcnt lgkmcnt(0)
	s_barrier
	s_setprio 1
	s_waitcnt lgkmcnt(0)
	v_mfma_f32_16x16x32_bf16 v[126:129], v[130:133], v[174:177], v[126:129]
	v_mfma_f32_16x16x32_bf16 v[122:125], v[138:141], v[174:177], v[122:125]
	v_mfma_f32_16x16x32_bf16 v[110:113], v[130:133], v[188:191], v[110:113]
	v_mfma_f32_16x16x32_bf16 v[106:109], v[138:141], v[188:191], v[106:109]
	v_mfma_f32_16x16x32_bf16 v[94:97], v[130:133], v[196:199], v[94:97]
	v_mfma_f32_16x16x32_bf16 v[90:93], v[138:141], v[196:199], v[90:93]
	v_mfma_f32_16x16x32_bf16 v[78:81], v[130:133], v[204:207], v[78:81]
	v_mfma_f32_16x16x32_bf16 v[74:77], v[138:141], v[204:207], v[74:77]
	v_mfma_f32_16x16x32_bf16 v[126:129], v[134:137], v[184:187], v[126:129]
	v_mfma_f32_16x16x32_bf16 v[122:125], v[142:145], v[184:187], v[122:125]
	v_mfma_f32_16x16x32_bf16 v[110:113], v[134:137], v[192:195], v[110:113]
	v_mfma_f32_16x16x32_bf16 v[106:109], v[142:145], v[192:195], v[106:109]
	v_mfma_f32_16x16x32_bf16 v[94:97], v[134:137], v[200:203], v[94:97]
	v_mfma_f32_16x16x32_bf16 v[90:93], v[142:145], v[200:203], v[90:93]
	v_mfma_f32_16x16x32_bf16 v[78:81], v[134:137], v[216:219], v[78:81]
	v_mfma_f32_16x16x32_bf16 v[74:77], v[142:145], v[216:219], v[74:77]
	s_setprio 0
	s_setprio 1
	v_mfma_f32_16x16x32_bf16 v[118:121], v[146:149], v[174:177], v[118:121]
	v_mfma_f32_16x16x32_bf16 v[114:117], v[154:157], v[174:177], v[114:117]
	v_mfma_f32_16x16x32_bf16 v[102:105], v[146:149], v[188:191], v[102:105]
	v_mfma_f32_16x16x32_bf16 v[98:101], v[154:157], v[188:191], v[98:101]
	v_mfma_f32_16x16x32_bf16 v[86:89], v[146:149], v[196:199], v[86:89]
	v_mfma_f32_16x16x32_bf16 v[82:85], v[154:157], v[196:199], v[82:85]
	v_mfma_f32_16x16x32_bf16 v[70:73], v[146:149], v[204:207], v[70:73]
	v_mfma_f32_16x16x32_bf16 v[66:69], v[154:157], v[204:207], v[66:69]
	v_mfma_f32_16x16x32_bf16 v[118:121], v[150:153], v[184:187], v[118:121]
	v_mfma_f32_16x16x32_bf16 v[114:117], v[170:173], v[184:187], v[114:117]
	v_mfma_f32_16x16x32_bf16 v[102:105], v[150:153], v[192:195], v[102:105]
	v_mfma_f32_16x16x32_bf16 v[98:101], v[170:173], v[192:195], v[98:101]
	v_mfma_f32_16x16x32_bf16 v[86:89], v[150:153], v[200:203], v[86:89]
	v_mfma_f32_16x16x32_bf16 v[82:85], v[170:173], v[200:203], v[82:85]
	v_mfma_f32_16x16x32_bf16 v[70:73], v[150:153], v[216:219], v[70:73]
	v_mfma_f32_16x16x32_bf16 v[66:69], v[170:173], v[216:219], v[66:69]
	s_setprio 0
	s_barrier
	s_add_i32 s28, s50, s35
	v_lshl_add_u64 v[178:179], v[178:179], 0, s[56:57]
	s_mov_b32 m0, s28
	ds_read_b128 v[174:177], v183 offset:49152
	ds_read_b128 v[184:187], v183 offset:50176
	ds_read_b128 v[188:191], v183 offset:51200
	ds_read_b128 v[192:195], v183 offset:52224
	ds_read_b128 v[196:199], v183 offset:53248
	ds_read_b128 v[200:203], v183 offset:54272
	ds_read_b128 v[204:207], v183 offset:55296
	ds_read_b128 v[216:219], v183 offset:56320
	global_load_lds_dwordx4 v[178:179], off
	s_add_i32 m0, s28, 0x2000
	s_add_u32 s26, s26, 0x40080
	v_lshl_add_u64 v[178:179], v[208:209], 0, s[56:57]
	s_addc_u32 s27, s27, 0
	s_add_i32 s28, s52, s35
	global_load_lds_dwordx4 v[178:179], off
	s_mov_b32 m0, s28
	s_nop 0
	global_load_lds_dwordx4 v162, s[26:27]
	s_add_i32 m0, s28, 0x2000
	s_nop 0
	global_load_lds_dwordx4 v158, s[26:27]
	s_mov_b32 m0, s44
	v_lshl_add_u64 v[178:179], v[220:221], 0, s[56:57]
	global_load_lds_dwordx4 v[178:179], off
	s_mov_b32 m0, s45
	v_lshl_add_u64 v[178:179], v[222:223], 0, s[56:57]
	global_load_lds_dwordx4 v[178:179], off
	s_waitcnt vmcnt(8)
	s_waitcnt lgkmcnt(0)
	s_barrier
	s_setprio 1
	s_waitcnt lgkmcnt(0)
	v_mfma_f32_16x16x32_bf16 v[62:65], v[130:133], v[174:177], v[62:65]
	v_mfma_f32_16x16x32_bf16 v[58:61], v[138:141], v[174:177], v[58:61]
	v_mfma_f32_16x16x32_bf16 v[46:49], v[130:133], v[188:191], v[46:49]
	v_mfma_f32_16x16x32_bf16 v[42:45], v[138:141], v[188:191], v[42:45]
	v_mfma_f32_16x16x32_bf16 v[30:33], v[130:133], v[196:199], v[30:33]
	v_mfma_f32_16x16x32_bf16 v[26:29], v[138:141], v[196:199], v[26:29]
	v_mfma_f32_16x16x32_bf16 v[14:17], v[130:133], v[204:207], v[14:17]
	v_mfma_f32_16x16x32_bf16 v[10:13], v[138:141], v[204:207], v[10:13]
	v_mfma_f32_16x16x32_bf16 v[62:65], v[134:137], v[184:187], v[62:65]
	v_mfma_f32_16x16x32_bf16 v[58:61], v[142:145], v[184:187], v[58:61]
	v_mfma_f32_16x16x32_bf16 v[46:49], v[134:137], v[192:195], v[46:49]
	v_mfma_f32_16x16x32_bf16 v[42:45], v[142:145], v[192:195], v[42:45]
	v_mfma_f32_16x16x32_bf16 v[30:33], v[134:137], v[200:203], v[30:33]
	v_mfma_f32_16x16x32_bf16 v[26:29], v[142:145], v[200:203], v[26:29]
	v_mfma_f32_16x16x32_bf16 v[14:17], v[134:137], v[216:219], v[14:17]
	v_mfma_f32_16x16x32_bf16 v[10:13], v[142:145], v[216:219], v[10:13]
	s_setprio 0
	s_setprio 1
	v_mfma_f32_16x16x32_bf16 v[54:57], v[146:149], v[174:177], v[54:57]
	v_mfma_f32_16x16x32_bf16 v[50:53], v[154:157], v[174:177], v[50:53]
	v_mfma_f32_16x16x32_bf16 v[38:41], v[146:149], v[188:191], v[38:41]
	v_mfma_f32_16x16x32_bf16 v[34:37], v[154:157], v[188:191], v[34:37]
	v_mfma_f32_16x16x32_bf16 v[22:25], v[146:149], v[196:199], v[22:25]
	v_mfma_f32_16x16x32_bf16 v[18:21], v[154:157], v[196:199], v[18:21]
	v_mfma_f32_16x16x32_bf16 v[6:9], v[146:149], v[204:207], v[6:9]
	v_mfma_f32_16x16x32_bf16 v[2:5], v[154:157], v[204:207], v[2:5]
	v_mfma_f32_16x16x32_bf16 v[54:57], v[150:153], v[184:187], v[54:57]
	v_mfma_f32_16x16x32_bf16 v[50:53], v[170:173], v[184:187], v[50:53]
	v_mfma_f32_16x16x32_bf16 v[38:41], v[150:153], v[192:195], v[38:41]
	v_mfma_f32_16x16x32_bf16 v[34:37], v[170:173], v[192:195], v[34:37]
	v_mfma_f32_16x16x32_bf16 v[22:25], v[150:153], v[200:203], v[22:25]
	v_mfma_f32_16x16x32_bf16 v[18:21], v[170:173], v[200:203], v[18:21]
	v_mfma_f32_16x16x32_bf16 v[6:9], v[150:153], v[216:219], v[6:9]
	v_mfma_f32_16x16x32_bf16 v[2:5], v[170:173], v[216:219], v[2:5]
	s_setprio 0
	s_barrier
	s_add_i32 s49, s49, 2
	s_add_u32 s41, s41, 0x100
	s_addc_u32 s48, s48, 0
	s_add_u32 s6, s6, 0x100
	s_addc_u32 s7, s7, 0
	s_cmp_gt_u32 s49, 13
	s_cbranch_scc0 .LBB0_2626
	s_and_b64 vcc, exec, s[16:17]
	s_cbranch_vccz .LBB0_2629
	s_barrier

.LBB0_2695:
	v_mov_b32_e32 v127, v1
	v_lshl_add_u64 v[8:9], s[36:37], 0, v[126:127]
	v_mov_b32_e32 v119, v1
	v_lshl_add_u64 v[10:11], s[36:37], 0, v[118:119]
	v_mov_b32_e32 v129, v1
	s_and_b32 s62, s13, 3
	s_add_i32 m0, s4, 0x18000
	v_lshl_add_u64 v[8:9], v[8:9], 0, s[56:57]
	v_lshl_add_u64 v[12:13], s[24:25], 0, v[128:129]
	v_mov_b32_e32 v121, v1
	s_lshl_b32 s12, s52, 13
	s_lshl_b32 s28, s62, 12
	s_waitcnt vmcnt(2)
	s_barrier
	global_load_lds_dwordx4 v[8:9], off
	v_lshl_add_u64 v[8:9], v[10:11], 0, s[56:57]
	s_add_i32 m0, s4, 0x1a000
	s_add_i32 s80, s4, 0x8000
	s_add_i32 s81, s4, 0xa000
	s_waitcnt lgkmcnt(0)
	v_lshl_add_u64 v[14:15], s[24:25], 0, v[120:121]
	global_load_lds_dwordx4 v[8:9], off
	v_lshl_add_u64 v[8:9], v[12:13], 0, s[56:57]
	s_mov_b32 m0, s80
	s_add_u32 s26, s36, 0x100080
	global_load_lds_dwordx4 v[8:9], off
	v_lshl_add_u64 v[8:9], v[14:15], 0, s[56:57]
	s_mov_b32 m0, s81
	s_addc_u32 s27, s37, 0
	global_load_lds_dwordx4 v[8:9], off
	s_add_i32 m0, s4, 0x1c000
	s_nop 0
	global_load_lds_dwordx4 v126, s[26:27]
	v_lshl_add_u64 v[8:9], s[26:27], 0, v[118:119]
	s_add_i32 m0, s4, 0x1e000
	v_and_b32_e32 v166, 15, v0
	global_load_lds_dwordx4 v118, s[26:27]
	v_and_b32_e32 v8, 48, v0
	v_lshlrev_b32_e32 v9, 2, v0
	v_lshl_or_b32 v8, v166, 6, v8
	v_and_b32_e32 v9, 32, v9
	v_bitop3_b32 v10, v8, s12, v9 bitop3:0xde
	v_bitop3_b32 v146, v8, s28, v9 bitop3:0xde
	v_lshlrev_b32_e32 v8, 16, v2
	v_and_b32_e32 v8, 0xfffe0000, v8
	v_lshl_add_u32 v3, v3, 13, v8
	v_and_b32_e32 v2, 1, v2
	v_lshl_or_b32 v2, v2, 6, v3
	v_lshl_add_u32 v138, v4, 1, v2
	v_lshlrev_b32_e32 v2, 16, v6
	v_and_b32_e32 v2, 0xfffe0000, v2
	v_lshl_add_u32 v2, v5, 13, v2
	v_and_b32_e32 v3, 1, v6
	s_waitcnt vmcnt(6)
	v_lshl_or_b32 v2, v3, 6, v2
	v_mov_b32_e32 v4, v1
	v_mov_b32_e32 v5, v1
	v_lshl_add_u32 v140, v7, 1, v2
	v_mov_b32_e32 v2, v1
	v_mov_b32_e32 v3, v1
	v_add_u32_e32 v147, 0, v10
	v_mov_b64_e32 v[8:9], v[4:5]
	v_mov_b64_e32 v[20:21], v[4:5]
	v_mov_b64_e32 v[24:25], v[4:5]
	v_mov_b64_e32 v[36:37], v[4:5]
	v_mov_b64_e32 v[40:41], v[4:5]
	v_mov_b64_e32 v[52:53], v[4:5]
	v_mov_b64_e32 v[56:57], v[4:5]
	v_mov_b64_e32 v[12:13], v[4:5]
	v_mov_b64_e32 v[16:17], v[4:5]
	v_mov_b64_e32 v[28:29], v[4:5]
	v_mov_b64_e32 v[32:33], v[4:5]
	v_mov_b64_e32 v[44:45], v[4:5]
	v_mov_b64_e32 v[48:49], v[4:5]
	v_mov_b64_e32 v[60:61], v[4:5]
	v_mov_b64_e32 v[64:65], v[4:5]
	v_mov_b64_e32 v[68:69], v[4:5]
	v_mov_b64_e32 v[72:73], v[4:5]
	v_mov_b64_e32 v[84:85], v[4:5]
	v_mov_b64_e32 v[88:89], v[4:5]
	v_mov_b64_e32 v[100:101], v[4:5]
	v_mov_b64_e32 v[104:105], v[4:5]
	v_mov_b64_e32 v[116:117], v[4:5]
	v_mov_b64_e32 v[124:125], v[4:5]
	v_mov_b64_e32 v[76:77], v[4:5]
	v_mov_b64_e32 v[80:81], v[4:5]
	v_mov_b64_e32 v[92:93], v[4:5]
	v_mov_b64_e32 v[96:97], v[4:5]
	v_mov_b64_e32 v[108:109], v[4:5]
	v_mov_b64_e32 v[112:113], v[4:5]
	v_mov_b64_e32 v[132:133], v[4:5]
	v_mov_b64_e32 v[136:137], v[4:5]
	v_readlane_b32 s26, v254, 54
	v_lshl_or_b32 v240, s52, 6, v166
	v_mov_b32_e32 v139, v1
	v_mov_b32_e32 v141, v1
	s_mov_b32 s68, 0
	v_mov_b64_e32 v[6:7], v[2:3]
	v_mov_b64_e32 v[18:19], v[2:3]
	v_mov_b64_e32 v[22:23], v[2:3]
	v_mov_b64_e32 v[34:35], v[2:3]
	v_mov_b64_e32 v[38:39], v[2:3]
	v_mov_b64_e32 v[50:51], v[2:3]
	v_mov_b64_e32 v[54:55], v[2:3]
	v_mov_b64_e32 v[10:11], v[2:3]
	v_mov_b64_e32 v[14:15], v[2:3]
	v_mov_b64_e32 v[26:27], v[2:3]
	v_mov_b64_e32 v[30:31], v[2:3]
	v_mov_b64_e32 v[42:43], v[2:3]
	v_mov_b64_e32 v[46:47], v[2:3]
	v_mov_b64_e32 v[58:59], v[2:3]
	v_mov_b64_e32 v[62:63], v[2:3]
	v_mov_b64_e32 v[66:67], v[2:3]
	v_mov_b64_e32 v[70:71], v[2:3]
	v_mov_b64_e32 v[82:83], v[2:3]
	v_mov_b64_e32 v[86:87], v[2:3]
	v_mov_b64_e32 v[98:99], v[2:3]
	v_mov_b64_e32 v[102:103], v[2:3]
	v_mov_b64_e32 v[114:115], v[2:3]
	v_mov_b64_e32 v[122:123], v[2:3]
	v_mov_b64_e32 v[74:75], v[2:3]
	v_mov_b64_e32 v[78:79], v[2:3]
	v_mov_b64_e32 v[90:91], v[2:3]
	v_mov_b64_e32 v[94:95], v[2:3]
	v_mov_b64_e32 v[106:107], v[2:3]
	v_mov_b64_e32 v[110:111], v[2:3]
	v_mov_b64_e32 v[130:131], v[2:3]
	v_mov_b64_e32 v[134:135], v[2:3]
	v_readlane_b32 s12, v254, 58
	s_mov_b32 s53, s26
	s_barrier
	v_readlane_b32 s27, v254, 55

.LBB0_2703:
	s_add_u32 s44, s24, s36
	s_addc_u32 s45, s25, s37
	s_add_u32 s44, s44, 0x100
	s_addc_u32 s45, s45, 0
	s_add_u32 s50, s59, s36
	s_addc_u32 s64, s82, s37
	s_add_i32 s65, 0, 0x10000
	s_cmpk_eq_i32 s36, 0x1f00
	s_cselect_b32 s47, s29, s45
	s_cselect_b32 s46, s83, s44
	s_cselect_b32 s45, s27, s64
	s_cselect_b32 s44, s84, s50
	s_add_i32 s50, 0, 0x14000
	v_add_u32_e32 v160, s65, v146
	v_add_u32_e32 v164, s50, v146
	ds_read_b128 v[148:151], v160
	ds_read_b128 v[152:155], v160 offset:1024
	ds_read_b128 v[156:159], v160 offset:2048
	ds_read_b128 v[160:163], v160 offset:3072
	ds_read_b128 v[168:171], v164
	ds_read_b128 v[172:175], v164 offset:1024
	ds_read_b128 v[176:179], v164 offset:2048
	ds_read_b128 v[180:183], v164 offset:3072
	v_lshl_add_u64 v[164:165], v[144:145], 0, s[36:37]
	s_add_i32 m0, s4, 0xc000
	ds_read_b128 v[184:187], v147
	ds_read_b128 v[188:191], v147 offset:1024
	ds_read_b128 v[192:195], v147 offset:2048
	ds_read_b128 v[196:199], v147 offset:3072
	ds_read_b128 v[200:203], v147 offset:4096
	ds_read_b128 v[204:207], v147 offset:5120
	ds_read_b128 v[216:219], v147 offset:6144
	ds_read_b128 v[220:223], v147 offset:7168
	global_load_lds_dwordx4 v[164:165], off
	s_add_i32 m0, s4, 0xe000
	v_lshl_add_u64 v[164:165], v[142:143], 0, s[36:37]
	global_load_lds_dwordx4 v[164:165], off
	s_waitcnt vmcnt(8)
	s_waitcnt lgkmcnt(0)
	s_barrier
	s_setprio 1
	s_waitcnt lgkmcnt(0)
	v_mfma_f32_16x16x32_bf16 v[134:137], v[148:151], v[184:187], v[134:137]
	v_mfma_f32_16x16x32_bf16 v[130:133], v[156:159], v[184:187], v[130:133]
	v_mfma_f32_16x16x32_bf16 v[110:113], v[148:151], v[192:195], v[110:113]
	v_mfma_f32_16x16x32_bf16 v[106:109], v[156:159], v[192:195], v[106:109]
	v_mfma_f32_16x16x32_bf16 v[94:97], v[148:151], v[200:203], v[94:97]
	v_mfma_f32_16x16x32_bf16 v[90:93], v[156:159], v[200:203], v[90:93]
	v_mfma_f32_16x16x32_bf16 v[78:81], v[148:151], v[216:219], v[78:81]
	v_mfma_f32_16x16x32_bf16 v[74:77], v[156:159], v[216:219], v[74:77]
	v_mfma_f32_16x16x32_bf16 v[134:137], v[152:155], v[188:191], v[134:137]
	v_mfma_f32_16x16x32_bf16 v[130:133], v[160:163], v[188:191], v[130:133]
	v_mfma_f32_16x16x32_bf16 v[110:113], v[152:155], v[196:199], v[110:113]
	v_mfma_f32_16x16x32_bf16 v[106:109], v[160:163], v[196:199], v[106:109]
	v_mfma_f32_16x16x32_bf16 v[94:97], v[152:155], v[204:207], v[94:97]
	v_mfma_f32_16x16x32_bf16 v[90:93], v[160:163], v[204:207], v[90:93]
	v_mfma_f32_16x16x32_bf16 v[78:81], v[152:155], v[220:223], v[78:81]
	v_mfma_f32_16x16x32_bf16 v[74:77], v[160:163], v[220:223], v[74:77]
	s_setprio 0
	s_setprio 1
	v_mfma_f32_16x16x32_bf16 v[122:125], v[168:171], v[184:187], v[122:125]
	v_mfma_f32_16x16x32_bf16 v[114:117], v[176:179], v[184:187], v[114:117]
	v_mfma_f32_16x16x32_bf16 v[102:105], v[168:171], v[192:195], v[102:105]
	v_mfma_f32_16x16x32_bf16 v[98:101], v[176:179], v[192:195], v[98:101]
	v_mfma_f32_16x16x32_bf16 v[86:89], v[168:171], v[200:203], v[86:89]
	v_mfma_f32_16x16x32_bf16 v[82:85], v[176:179], v[200:203], v[82:85]
	v_mfma_f32_16x16x32_bf16 v[70:73], v[168:171], v[216:219], v[70:73]
	v_mfma_f32_16x16x32_bf16 v[66:69], v[176:179], v[216:219], v[66:69]
	v_mfma_f32_16x16x32_bf16 v[122:125], v[172:175], v[188:191], v[122:125]
	v_mfma_f32_16x16x32_bf16 v[114:117], v[180:183], v[188:191], v[114:117]
	v_mfma_f32_16x16x32_bf16 v[102:105], v[172:175], v[196:199], v[102:105]
	v_mfma_f32_16x16x32_bf16 v[98:101], v[180:183], v[196:199], v[98:101]
	v_mfma_f32_16x16x32_bf16 v[86:89], v[172:175], v[204:207], v[86:89]
	v_mfma_f32_16x16x32_bf16 v[82:85], v[180:183], v[204:207], v[82:85]
	v_mfma_f32_16x16x32_bf16 v[70:73], v[172:175], v[220:223], v[70:73]
	v_mfma_f32_16x16x32_bf16 v[66:69], v[180:183], v[220:223], v[66:69]
	s_setprio 0
	s_barrier
	s_add_i32 s64, s65, s77
	v_lshl_add_u64 v[164:165], s[44:45], 0, v[126:127]
	s_mov_b32 m0, s64
	ds_read_b128 v[184:187], v147 offset:16384
	ds_read_b128 v[188:191], v147 offset:17408
	ds_read_b128 v[192:195], v147 offset:18432
	ds_read_b128 v[196:199], v147 offset:19456
	ds_read_b128 v[200:203], v147 offset:20480
	ds_read_b128 v[204:207], v147 offset:21504
	ds_read_b128 v[216:219], v147 offset:22528
	ds_read_b128 v[220:223], v147 offset:23552
	global_load_lds_dwordx4 v126, s[44:45]
	s_add_i32 m0, s64, 0x2000
	s_add_u32 s92, s44, 0x100000
	v_lshl_add_u64 v[208:209], s[44:45], 0, v[118:119]
	s_addc_u32 s93, s45, 0
	s_add_i32 s50, s50, s77
	global_load_lds_dwordx4 v118, s[44:45]
	s_mov_b32 m0, s50
	v_lshl_add_u64 v[242:243], s[46:47], 0, v[120:121]
	global_load_lds_dwordx4 v126, s[92:93]
	s_add_i32 m0, s50, 0x2000
	s_nop 0
	global_load_lds_dwordx4 v118, s[92:93]
	s_mov_b32 m0, s4
	v_lshl_add_u64 v[224:225], s[46:47], 0, v[128:129]
	global_load_lds_dwordx4 v128, s[46:47]
	s_mov_b32 m0, s33
	s_nop 0
	global_load_lds_dwordx4 v120, s[46:47]
	s_waitcnt vmcnt(8)
	s_waitcnt lgkmcnt(0)
	s_barrier
	s_setprio 1
	s_waitcnt lgkmcnt(0)
	v_mfma_f32_16x16x32_bf16 v[62:65], v[148:151], v[184:187], v[62:65]
	v_mfma_f32_16x16x32_bf16 v[58:61], v[156:159], v[184:187], v[58:61]
	v_mfma_f32_16x16x32_bf16 v[46:49], v[148:151], v[192:195], v[46:49]
	v_mfma_f32_16x16x32_bf16 v[42:45], v[156:159], v[192:195], v[42:45]
	v_mfma_f32_16x16x32_bf16 v[30:33], v[148:151], v[200:203], v[30:33]
	v_mfma_f32_16x16x32_bf16 v[26:29], v[156:159], v[200:203], v[26:29]
	v_mfma_f32_16x16x32_bf16 v[14:17], v[148:151], v[216:219], v[14:17]
	v_mfma_f32_16x16x32_bf16 v[10:13], v[156:159], v[216:219], v[10:13]
	v_mfma_f32_16x16x32_bf16 v[62:65], v[152:155], v[188:191], v[62:65]
	v_mfma_f32_16x16x32_bf16 v[58:61], v[160:163], v[188:191], v[58:61]
	v_mfma_f32_16x16x32_bf16 v[46:49], v[152:155], v[196:199], v[46:49]
	v_mfma_f32_16x16x32_bf16 v[42:45], v[160:163], v[196:199], v[42:45]
	v_mfma_f32_16x16x32_bf16 v[30:33], v[152:155], v[204:207], v[30:33]
	v_mfma_f32_16x16x32_bf16 v[26:29], v[160:163], v[204:207], v[26:29]
	v_mfma_f32_16x16x32_bf16 v[14:17], v[152:155], v[220:223], v[14:17]
	v_mfma_f32_16x16x32_bf16 v[10:13], v[160:163], v[220:223], v[10:13]
	s_setprio 0
	s_setprio 1
	v_mfma_f32_16x16x32_bf16 v[54:57], v[168:171], v[184:187], v[54:57]
	v_mfma_f32_16x16x32_bf16 v[50:53], v[176:179], v[184:187], v[50:53]
	v_mfma_f32_16x16x32_bf16 v[38:41], v[168:171], v[192:195], v[38:41]
	v_mfma_f32_16x16x32_bf16 v[34:37], v[176:179], v[192:195], v[34:37]
	v_mfma_f32_16x16x32_bf16 v[22:25], v[168:171], v[200:203], v[22:25]
	v_mfma_f32_16x16x32_bf16 v[18:21], v[176:179], v[200:203], v[18:21]
	v_mfma_f32_16x16x32_bf16 v[6:9], v[168:171], v[216:219], v[6:9]
	v_mfma_f32_16x16x32_bf16 v[2:5], v[176:179], v[216:219], v[2:5]
	v_mfma_f32_16x16x32_bf16 v[54:57], v[172:175], v[188:191], v[54:57]
	v_mfma_f32_16x16x32_bf16 v[50:53], v[180:183], v[188:191], v[50:53]
	v_mfma_f32_16x16x32_bf16 v[38:41], v[172:175], v[196:199], v[38:41]
	v_mfma_f32_16x16x32_bf16 v[34:37], v[180:183], v[196:199], v[34:37]
	v_mfma_f32_16x16x32_bf16 v[22:25], v[172:175], v[204:207], v[22:25]
	v_mfma_f32_16x16x32_bf16 v[18:21], v[180:183], v[204:207], v[18:21]
	v_mfma_f32_16x16x32_bf16 v[6:9], v[172:175], v[220:223], v[6:9]
	v_mfma_f32_16x16x32_bf16 v[2:5], v[180:183], v[220:223], v[2:5]
	s_setprio 0
	s_barrier
	s_add_i32 s50, 0, 0x18000
	s_add_i32 s64, 0, 0x1c000
	v_add_u32_e32 v160, s50, v146
	v_add_u32_e32 v167, s64, v146
	ds_read_b128 v[148:151], v160
	ds_read_b128 v[152:155], v160 offset:1024
	ds_read_b128 v[156:159], v160 offset:2048
	ds_read_b128 v[160:163], v160 offset:3072
	ds_read_b128 v[168:171], v167
	ds_read_b128 v[172:175], v167 offset:1024
	ds_read_b128 v[176:179], v167 offset:2048
	ds_read_b128 v[180:183], v167 offset:3072
	s_add_u32 s46, s46, 0x100000
	s_addc_u32 s47, s47, 0
	s_mov_b32 m0, s78
	ds_read_b128 v[184:187], v147 offset:32768
	ds_read_b128 v[188:191], v147 offset:33792
	ds_read_b128 v[192:195], v147 offset:34816
	ds_read_b128 v[196:199], v147 offset:35840
	ds_read_b128 v[200:203], v147 offset:36864
	ds_read_b128 v[204:207], v147 offset:37888
	ds_read_b128 v[216:219], v147 offset:38912
	ds_read_b128 v[220:223], v147 offset:39936
	global_load_lds_dwordx4 v128, s[46:47]
	s_mov_b32 m0, s79
	v_lshl_add_u64 v[244:245], s[46:47], 0, v[120:121]
	global_load_lds_dwordx4 v120, s[46:47]
	s_waitcnt vmcnt(8)
	s_waitcnt lgkmcnt(0)
	s_barrier
	s_setprio 1
	s_waitcnt lgkmcnt(0)
	v_mfma_f32_16x16x32_bf16 v[134:137], v[148:151], v[184:187], v[134:137]
	v_mfma_f32_16x16x32_bf16 v[130:133], v[156:159], v[184:187], v[130:133]
	v_mfma_f32_16x16x32_bf16 v[110:113], v[148:151], v[192:195], v[110:113]
	v_mfma_f32_16x16x32_bf16 v[106:109], v[156:159], v[192:195], v[106:109]
	v_mfma_f32_16x16x32_bf16 v[94:97], v[148:151], v[200:203], v[94:97]
	v_mfma_f32_16x16x32_bf16 v[90:93], v[156:159], v[200:203], v[90:93]
	v_mfma_f32_16x16x32_bf16 v[78:81], v[148:151], v[216:219], v[78:81]
	v_mfma_f32_16x16x32_bf16 v[74:77], v[156:159], v[216:219], v[74:77]
	v_mfma_f32_16x16x32_bf16 v[134:137], v[152:155], v[188:191], v[134:137]
	v_mfma_f32_16x16x32_bf16 v[130:133], v[160:163], v[188:191], v[130:133]
	v_mfma_f32_16x16x32_bf16 v[110:113], v[152:155], v[196:199], v[110:113]
	v_mfma_f32_16x16x32_bf16 v[106:109], v[160:163], v[196:199], v[106:109]
	v_mfma_f32_16x16x32_bf16 v[94:97], v[152:155], v[204:207], v[94:97]
	v_mfma_f32_16x16x32_bf16 v[90:93], v[160:163], v[204:207], v[90:93]
	v_mfma_f32_16x16x32_bf16 v[78:81], v[152:155], v[220:223], v[78:81]
	v_mfma_f32_16x16x32_bf16 v[74:77], v[160:163], v[220:223], v[74:77]
	s_setprio 0
	s_setprio 1
	v_mfma_f32_16x16x32_bf16 v[122:125], v[168:171], v[184:187], v[122:125]
	v_mfma_f32_16x16x32_bf16 v[114:117], v[176:179], v[184:187], v[114:117]
	v_mfma_f32_16x16x32_bf16 v[102:105], v[168:171], v[192:195], v[102:105]
	v_mfma_f32_16x16x32_bf16 v[98:101], v[176:179], v[192:195], v[98:101]
	v_mfma_f32_16x16x32_bf16 v[86:89], v[168:171], v[200:203], v[86:89]
	v_mfma_f32_16x16x32_bf16 v[82:85], v[176:179], v[200:203], v[82:85]
	v_mfma_f32_16x16x32_bf16 v[70:73], v[168:171], v[216:219], v[70:73]
	v_mfma_f32_16x16x32_bf16 v[66:69], v[176:179], v[216:219], v[66:69]
	v_mfma_f32_16x16x32_bf16 v[122:125], v[172:175], v[188:191], v[122:125]
	v_mfma_f32_16x16x32_bf16 v[114:117], v[180:183], v[188:191], v[114:117]
	v_mfma_f32_16x16x32_bf16 v[102:105], v[172:175], v[196:199], v[102:105]
	v_mfma_f32_16x16x32_bf16 v[98:101], v[180:183], v[196:199], v[98:101]
	v_mfma_f32_16x16x32_bf16 v[86:89], v[172:175], v[204:207], v[86:89]
	v_mfma_f32_16x16x32_bf16 v[82:85], v[180:183], v[204:207], v[82:85]
	v_mfma_f32_16x16x32_bf16 v[70:73], v[172:175], v[220:223], v[70:73]
	v_mfma_f32_16x16x32_bf16 v[66:69], v[180:183], v[220:223], v[66:69]
	s_setprio 0
	s_barrier
	s_add_i32 s46, s50, s77
	v_lshl_add_u64 v[164:165], v[164:165], 0, s[56:57]
	s_mov_b32 m0, s46
	ds_read_b128 v[184:187], v147 offset:49152
	ds_read_b128 v[188:191], v147 offset:50176
	ds_read_b128 v[192:195], v147 offset:51200
	ds_read_b128 v[196:199], v147 offset:52224
	ds_read_b128 v[200:203], v147 offset:53248
	ds_read_b128 v[204:207], v147 offset:54272
	ds_read_b128 v[216:219], v147 offset:55296
	ds_read_b128 v[220:223], v147 offset:56320
	global_load_lds_dwordx4 v[164:165], off
	s_add_i32 m0, s46, 0x2000
	s_add_u32 s44, s44, 0x100080
	v_lshl_add_u64 v[164:165], v[208:209], 0, s[56:57]
	s_addc_u32 s45, s45, 0
	s_add_i32 s46, s64, s77
	global_load_lds_dwordx4 v[164:165], off
	s_mov_b32 m0, s46
	s_nop 0
	global_load_lds_dwordx4 v126, s[44:45]
	s_add_i32 m0, s46, 0x2000
	s_nop 0
	global_load_lds_dwordx4 v118, s[44:45]
	s_mov_b32 m0, s80
	v_lshl_add_u64 v[164:165], v[224:225], 0, s[56:57]
	global_load_lds_dwordx4 v[164:165], off
	s_mov_b32 m0, s81
	v_lshl_add_u64 v[164:165], v[242:243], 0, s[56:57]
	global_load_lds_dwordx4 v[164:165], off
	s_waitcnt vmcnt(8)
	s_waitcnt lgkmcnt(0)
	s_barrier
	s_setprio 1
	s_waitcnt lgkmcnt(0)
	v_mfma_f32_16x16x32_bf16 v[62:65], v[148:151], v[184:187], v[62:65]
	v_mfma_f32_16x16x32_bf16 v[58:61], v[156:159], v[184:187], v[58:61]
	v_mfma_f32_16x16x32_bf16 v[46:49], v[148:151], v[192:195], v[46:49]
	v_mfma_f32_16x16x32_bf16 v[42:45], v[156:159], v[192:195], v[42:45]
	v_mfma_f32_16x16x32_bf16 v[30:33], v[148:151], v[200:203], v[30:33]
	v_mfma_f32_16x16x32_bf16 v[26:29], v[156:159], v[200:203], v[26:29]
	v_mfma_f32_16x16x32_bf16 v[14:17], v[148:151], v[216:219], v[14:17]
	v_mfma_f32_16x16x32_bf16 v[10:13], v[156:159], v[216:219], v[10:13]
	v_mfma_f32_16x16x32_bf16 v[62:65], v[152:155], v[188:191], v[62:65]
	v_mfma_f32_16x16x32_bf16 v[58:61], v[160:163], v[188:191], v[58:61]
	v_mfma_f32_16x16x32_bf16 v[46:49], v[152:155], v[196:199], v[46:49]
	v_mfma_f32_16x16x32_bf16 v[42:45], v[160:163], v[196:199], v[42:45]
	v_mfma_f32_16x16x32_bf16 v[30:33], v[152:155], v[204:207], v[30:33]
	v_mfma_f32_16x16x32_bf16 v[26:29], v[160:163], v[204:207], v[26:29]
	v_mfma_f32_16x16x32_bf16 v[14:17], v[152:155], v[220:223], v[14:17]
	v_mfma_f32_16x16x32_bf16 v[10:13], v[160:163], v[220:223], v[10:13]
	s_setprio 0
	s_setprio 1
	v_mfma_f32_16x16x32_bf16 v[54:57], v[168:171], v[184:187], v[54:57]
	v_mfma_f32_16x16x32_bf16 v[50:53], v[176:179], v[184:187], v[50:53]
	v_mfma_f32_16x16x32_bf16 v[38:41], v[168:171], v[192:195], v[38:41]
	v_mfma_f32_16x16x32_bf16 v[34:37], v[176:179], v[192:195], v[34:37]
	v_mfma_f32_16x16x32_bf16 v[22:25], v[168:171], v[200:203], v[22:25]
	v_mfma_f32_16x16x32_bf16 v[18:21], v[176:179], v[200:203], v[18:21]
	v_mfma_f32_16x16x32_bf16 v[6:9], v[168:171], v[216:219], v[6:9]
	v_mfma_f32_16x16x32_bf16 v[2:5], v[176:179], v[216:219], v[2:5]
	v_mfma_f32_16x16x32_bf16 v[54:57], v[172:175], v[188:191], v[54:57]
	v_mfma_f32_16x16x32_bf16 v[50:53], v[180:183], v[188:191], v[50:53]
	v_mfma_f32_16x16x32_bf16 v[38:41], v[172:175], v[196:199], v[38:41]
	v_mfma_f32_16x16x32_bf16 v[34:37], v[180:183], v[196:199], v[34:37]
	v_mfma_f32_16x16x32_bf16 v[22:25], v[172:175], v[204:207], v[22:25]
	v_mfma_f32_16x16x32_bf16 v[18:21], v[180:183], v[204:207], v[18:21]
	v_mfma_f32_16x16x32_bf16 v[6:9], v[172:175], v[220:223], v[6:9]
	v_mfma_f32_16x16x32_bf16 v[2:5], v[180:183], v[220:223], v[2:5]
	s_setprio 0
	s_barrier
	s_add_i32 s85, s85, 2
	s_add_u32 s36, s36, 0x100
	s_addc_u32 s37, s37, 0
	s_cmp_gt_u32 s85, 61
	s_cbranch_scc0 .LBB0_2703
	s_add_u32 s36, s59, 0xffffff00
	s_addc_u32 s37, s82, -1
	s_andn2_b64 vcc, exec, s[42:43]
	s_cbranch_vccnz .LBB0_2706
	v_mov_b32_e32 v2, 0
	s_mov_b32 s12, s26
	s_mov_b32 s53, s28
	s_mov_b64 s[24:25], s[34:35]
	s_mov_b32 s68, s58
	v_mov_b32_e32 v3, v2
	v_mov_b32_e32 v4, v2
	v_mov_b32_e32 v5, v2
	v_mov_b32_e32 v6, v2
	v_mov_b32_e32 v7, v2
	v_mov_b32_e32 v8, v2
	v_mov_b32_e32 v9, v2
	v_mov_b32_e32 v18, v2
	v_mov_b32_e32 v19, v2
	v_mov_b32_e32 v20, v2
	v_mov_b32_e32 v21, v2
	v_mov_b32_e32 v22, v2
	v_mov_b32_e32 v23, v2
	v_mov_b32_e32 v24, v2
	v_mov_b32_e32 v25, v2
	v_mov_b32_e32 v34, v2
	v_mov_b32_e32 v35, v2
	v_mov_b32_e32 v36, v2
	v_mov_b32_e32 v37, v2
	v_mov_b32_e32 v38, v2
	v_mov_b32_e32 v39, v2
	v_mov_b32_e32 v40, v2
	v_mov_b32_e32 v41, v2
	v_mov_b32_e32 v50, v2
	v_mov_b32_e32 v51, v2
	v_mov_b32_e32 v52, v2
	v_mov_b32_e32 v53, v2
	v_mov_b32_e32 v54, v2
	v_mov_b32_e32 v55, v2
	v_mov_b32_e32 v56, v2
	v_mov_b32_e32 v57, v2
	v_mov_b32_e32 v10, v2
	v_mov_b32_e32 v11, v2
	v_mov_b32_e32 v12, v2
	v_mov_b32_e32 v13, v2
	v_mov_b32_e32 v14, v2
	v_mov_b32_e32 v15, v2
	v_mov_b32_e32 v16, v2
	v_mov_b32_e32 v17, v2
	v_mov_b32_e32 v26, v2
	v_mov_b32_e32 v27, v2
	v_mov_b32_e32 v28, v2
	v_mov_b32_e32 v29, v2
	v_mov_b32_e32 v30, v2
	v_mov_b32_e32 v31, v2
	v_mov_b32_e32 v32, v2
	v_mov_b32_e32 v33, v2
	v_mov_b32_e32 v42, v2
	v_mov_b32_e32 v43, v2
	v_mov_b32_e32 v44, v2
	v_mov_b32_e32 v45, v2
	v_mov_b32_e32 v46, v2
	v_mov_b32_e32 v47, v2
	v_mov_b32_e32 v48, v2
	v_mov_b32_e32 v49, v2
	v_mov_b32_e32 v58, v2
	v_mov_b32_e32 v59, v2
	v_mov_b32_e32 v60, v2
	v_mov_b32_e32 v61, v2
	v_mov_b32_e32 v62, v2
	v_mov_b32_e32 v63, v2
	v_mov_b32_e32 v64, v2
	v_mov_b32_e32 v65, v2
	v_mov_b32_e32 v66, v2
	v_mov_b32_e32 v67, v2
	v_mov_b32_e32 v68, v2
	v_mov_b32_e32 v69, v2
	v_mov_b32_e32 v70, v2
	v_mov_b32_e32 v71, v2
	v_mov_b32_e32 v72, v2
	v_mov_b32_e32 v73, v2
	v_mov_b32_e32 v82, v2
	v_mov_b32_e32 v83, v2
	v_mov_b32_e32 v84, v2
	v_mov_b32_e32 v85, v2
	v_mov_b32_e32 v86, v2
	v_mov_b32_e32 v87, v2
	v_mov_b32_e32 v88, v2
	v_mov_b32_e32 v89, v2
	v_mov_b32_e32 v98, v2
	v_mov_b32_e32 v99, v2
	v_mov_b32_e32 v100, v2
	v_mov_b32_e32 v101, v2
	v_mov_b32_e32 v102, v2
	v_mov_b32_e32 v103, v2
	v_mov_b32_e32 v104, v2
	v_mov_b32_e32 v105, v2
	v_mov_b32_e32 v114, v2
	v_mov_b32_e32 v115, v2
	v_mov_b32_e32 v116, v2
	v_mov_b32_e32 v117, v2
	v_mov_b32_e32 v122, v2
	v_mov_b32_e32 v123, v2
	v_mov_b32_e32 v124, v2
	v_mov_b32_e32 v125, v2
	v_mov_b32_e32 v74, v2
	v_mov_b32_e32 v75, v2
	v_mov_b32_e32 v76, v2
	v_mov_b32_e32 v77, v2
	v_mov_b32_e32 v78, v2
	v_mov_b32_e32 v79, v2
	v_mov_b32_e32 v80, v2
	v_mov_b32_e32 v81, v2
	v_mov_b32_e32 v90, v2
	v_mov_b32_e32 v91, v2
	v_mov_b32_e32 v92, v2
	v_mov_b32_e32 v93, v2
	v_mov_b32_e32 v94, v2
	v_mov_b32_e32 v95, v2
	v_mov_b32_e32 v96, v2
	v_mov_b32_e32 v97, v2
	v_mov_b32_e32 v106, v2
	v_mov_b32_e32 v107, v2
	v_mov_b32_e32 v108, v2
	v_mov_b32_e32 v109, v2
	v_mov_b32_e32 v110, v2
	v_mov_b32_e32 v111, v2
	v_mov_b32_e32 v112, v2
	v_mov_b32_e32 v113, v2
	v_mov_b32_e32 v130, v2
	v_mov_b32_e32 v131, v2
	v_mov_b32_e32 v132, v2
	v_mov_b32_e32 v133, v2
	v_mov_b32_e32 v134, v2
	v_mov_b32_e32 v135, v2
	v_mov_b32_e32 v136, v2
	v_mov_b32_e32 v137, v2
	s_movk_i32 s92, 0x2b20
	s_andn2_b64 vcc, exec, s[40:41]
	s_cbranch_vccnz .LBB0_2707
	s_branch .LBB0_2708

.LBB0_2788:
	v_mov_b32_e32 v127, v1
	v_lshl_add_u64 v[8:9], s[36:37], 0, v[126:127]
	v_mov_b32_e32 v119, v1
	v_lshl_add_u64 v[10:11], s[36:37], 0, v[118:119]
	v_mov_b32_e32 v129, v1
	s_and_b32 s52, s13, 3
	s_add_i32 m0, s4, 0x18000
	v_lshl_add_u64 v[8:9], v[8:9], 0, s[56:57]
	v_lshl_add_u64 v[12:13], s[24:25], 0, v[128:129]
	v_mov_b32_e32 v121, v1
	s_lshl_b32 s12, s48, 13
	s_lshl_b32 s28, s52, 12
	s_waitcnt vmcnt(2)
	s_barrier
	global_load_lds_dwordx4 v[8:9], off
	v_lshl_add_u64 v[8:9], v[10:11], 0, s[56:57]
	s_add_i32 m0, s4, 0x1a000
	s_add_i32 s78, s4, 0x8000
	s_add_i32 s79, s4, 0xa000
	v_lshl_add_u64 v[14:15], s[24:25], 0, v[120:121]
	global_load_lds_dwordx4 v[8:9], off
	v_lshl_add_u64 v[8:9], v[12:13], 0, s[56:57]
	s_mov_b32 m0, s78
	s_add_u32 s26, s36, 0x100080
	global_load_lds_dwordx4 v[8:9], off
	v_lshl_add_u64 v[8:9], v[14:15], 0, s[56:57]
	s_mov_b32 m0, s79
	s_addc_u32 s27, s37, 0
	global_load_lds_dwordx4 v[8:9], off
	s_add_i32 m0, s4, 0x1c000
	s_nop 0
	global_load_lds_dwordx4 v126, s[26:27]
	v_lshl_add_u64 v[8:9], s[26:27], 0, v[118:119]
	s_add_i32 m0, s4, 0x1e000
	v_and_b32_e32 v166, 15, v0
	global_load_lds_dwordx4 v118, s[26:27]
	v_and_b32_e32 v8, 48, v0
	v_lshlrev_b32_e32 v9, 2, v0
	v_lshl_or_b32 v8, v166, 6, v8
	v_and_b32_e32 v9, 32, v9
	v_bitop3_b32 v10, v8, s12, v9 bitop3:0xde
	v_bitop3_b32 v146, v8, s28, v9 bitop3:0xde
	v_lshlrev_b32_e32 v8, 16, v2
	v_and_b32_e32 v8, 0xfffe0000, v8
	v_lshl_add_u32 v3, v3, 13, v8
	v_and_b32_e32 v2, 1, v2
	v_lshl_or_b32 v2, v2, 6, v3
	v_lshl_add_u32 v138, v4, 1, v2
	v_lshlrev_b32_e32 v2, 16, v6
	v_and_b32_e32 v2, 0xfffe0000, v2
	v_lshl_add_u32 v2, v5, 13, v2
	v_and_b32_e32 v3, 1, v6
	s_waitcnt vmcnt(6)
	v_lshl_or_b32 v2, v3, 6, v2
	v_mov_b32_e32 v4, v1
	v_mov_b32_e32 v5, v1
	v_lshl_add_u32 v140, v7, 1, v2
	v_mov_b32_e32 v2, v1
	v_mov_b32_e32 v3, v1
	v_add_u32_e32 v147, 0, v10
	v_mov_b64_e32 v[8:9], v[4:5]
	v_mov_b64_e32 v[20:21], v[4:5]
	v_mov_b64_e32 v[24:25], v[4:5]
	v_mov_b64_e32 v[36:37], v[4:5]
	v_mov_b64_e32 v[40:41], v[4:5]
	v_mov_b64_e32 v[52:53], v[4:5]
	v_mov_b64_e32 v[56:57], v[4:5]
	v_mov_b64_e32 v[12:13], v[4:5]
	v_mov_b64_e32 v[16:17], v[4:5]
	v_mov_b64_e32 v[28:29], v[4:5]
	v_mov_b64_e32 v[32:33], v[4:5]
	v_mov_b64_e32 v[44:45], v[4:5]
	v_mov_b64_e32 v[48:49], v[4:5]
	v_mov_b64_e32 v[60:61], v[4:5]
	v_mov_b64_e32 v[64:65], v[4:5]
	v_mov_b64_e32 v[68:69], v[4:5]
	v_mov_b64_e32 v[72:73], v[4:5]
	v_mov_b64_e32 v[84:85], v[4:5]
	v_mov_b64_e32 v[88:89], v[4:5]
	v_mov_b64_e32 v[100:101], v[4:5]
	v_mov_b64_e32 v[104:105], v[4:5]
	v_mov_b64_e32 v[116:117], v[4:5]
	v_mov_b64_e32 v[124:125], v[4:5]
	v_mov_b64_e32 v[76:77], v[4:5]
	v_mov_b64_e32 v[80:81], v[4:5]
	v_mov_b64_e32 v[92:93], v[4:5]
	v_mov_b64_e32 v[96:97], v[4:5]
	v_mov_b64_e32 v[108:109], v[4:5]
	v_mov_b64_e32 v[112:113], v[4:5]
	v_mov_b64_e32 v[132:133], v[4:5]
	v_mov_b64_e32 v[136:137], v[4:5]
	v_readlane_b32 s26, v254, 54
	v_lshl_or_b32 v240, s48, 6, v166
	v_mov_b32_e32 v139, v1
	v_mov_b32_e32 v141, v1
	s_mov_b32 s68, 0
	v_mov_b64_e32 v[6:7], v[2:3]
	v_mov_b64_e32 v[18:19], v[2:3]
	v_mov_b64_e32 v[22:23], v[2:3]
	v_mov_b64_e32 v[34:35], v[2:3]
	v_mov_b64_e32 v[38:39], v[2:3]
	v_mov_b64_e32 v[50:51], v[2:3]
	v_mov_b64_e32 v[54:55], v[2:3]
	v_mov_b64_e32 v[10:11], v[2:3]
	v_mov_b64_e32 v[14:15], v[2:3]
	v_mov_b64_e32 v[26:27], v[2:3]
	v_mov_b64_e32 v[30:31], v[2:3]
	v_mov_b64_e32 v[42:43], v[2:3]
	v_mov_b64_e32 v[46:47], v[2:3]
	v_mov_b64_e32 v[58:59], v[2:3]
	v_mov_b64_e32 v[62:63], v[2:3]
	v_mov_b64_e32 v[66:67], v[2:3]
	v_mov_b64_e32 v[70:71], v[2:3]
	v_mov_b64_e32 v[82:83], v[2:3]
	v_mov_b64_e32 v[86:87], v[2:3]
	v_mov_b64_e32 v[98:99], v[2:3]
	v_mov_b64_e32 v[102:103], v[2:3]
	v_mov_b64_e32 v[114:115], v[2:3]
	v_mov_b64_e32 v[122:123], v[2:3]
	v_mov_b64_e32 v[74:75], v[2:3]
	v_mov_b64_e32 v[78:79], v[2:3]
	v_mov_b64_e32 v[90:91], v[2:3]
	v_mov_b64_e32 v[94:95], v[2:3]
	v_mov_b64_e32 v[106:107], v[2:3]
	v_mov_b64_e32 v[110:111], v[2:3]
	v_mov_b64_e32 v[130:131], v[2:3]
	v_mov_b64_e32 v[134:135], v[2:3]
	v_readlane_b32 s12, v254, 58
	s_mov_b32 s80, s26
	s_barrier
	v_readlane_b32 s27, v254, 55

.LBB0_2796:
	s_add_u32 s44, s24, s36
	s_addc_u32 s45, s25, s37
	s_add_u32 s44, s44, 0x100
	s_addc_u32 s45, s45, 0
	s_add_u32 s50, s59, s36
	s_addc_u32 s64, s81, s37
	s_add_i32 s65, 0, 0x10000
	s_cmpk_eq_i32 s36, 0x1f00
	s_cselect_b32 s47, s29, s45
	s_cselect_b32 s46, s82, s44
	s_cselect_b32 s45, s27, s64
	s_cselect_b32 s44, s83, s50
	s_add_i32 s50, 0, 0x14000
	v_add_u32_e32 v160, s65, v146
	v_add_u32_e32 v164, s50, v146
	ds_read_b128 v[148:151], v160
	ds_read_b128 v[152:155], v160 offset:1024
	ds_read_b128 v[156:159], v160 offset:2048
	ds_read_b128 v[160:163], v160 offset:3072
	ds_read_b128 v[168:171], v164
	ds_read_b128 v[172:175], v164 offset:1024
	ds_read_b128 v[176:179], v164 offset:2048
	ds_read_b128 v[180:183], v164 offset:3072
	v_lshl_add_u64 v[164:165], v[144:145], 0, s[36:37]
	s_add_i32 m0, s4, 0xc000
	ds_read_b128 v[184:187], v147
	ds_read_b128 v[188:191], v147 offset:1024
	ds_read_b128 v[192:195], v147 offset:2048
	ds_read_b128 v[196:199], v147 offset:3072
	ds_read_b128 v[200:203], v147 offset:4096
	ds_read_b128 v[204:207], v147 offset:5120
	ds_read_b128 v[216:219], v147 offset:6144
	ds_read_b128 v[220:223], v147 offset:7168
	global_load_lds_dwordx4 v[164:165], off
	s_add_i32 m0, s4, 0xe000
	v_lshl_add_u64 v[164:165], v[142:143], 0, s[36:37]
	global_load_lds_dwordx4 v[164:165], off
	s_waitcnt vmcnt(8)
	s_waitcnt lgkmcnt(0)
	s_barrier
	s_setprio 1
	s_waitcnt lgkmcnt(0)
	v_mfma_f32_16x16x32_bf16 v[134:137], v[148:151], v[184:187], v[134:137]
	v_mfma_f32_16x16x32_bf16 v[130:133], v[156:159], v[184:187], v[130:133]
	v_mfma_f32_16x16x32_bf16 v[110:113], v[148:151], v[192:195], v[110:113]
	v_mfma_f32_16x16x32_bf16 v[106:109], v[156:159], v[192:195], v[106:109]
	v_mfma_f32_16x16x32_bf16 v[94:97], v[148:151], v[200:203], v[94:97]
	v_mfma_f32_16x16x32_bf16 v[90:93], v[156:159], v[200:203], v[90:93]
	v_mfma_f32_16x16x32_bf16 v[78:81], v[148:151], v[216:219], v[78:81]
	v_mfma_f32_16x16x32_bf16 v[74:77], v[156:159], v[216:219], v[74:77]
	v_mfma_f32_16x16x32_bf16 v[134:137], v[152:155], v[188:191], v[134:137]
	v_mfma_f32_16x16x32_bf16 v[130:133], v[160:163], v[188:191], v[130:133]
	v_mfma_f32_16x16x32_bf16 v[110:113], v[152:155], v[196:199], v[110:113]
	v_mfma_f32_16x16x32_bf16 v[106:109], v[160:163], v[196:199], v[106:109]
	v_mfma_f32_16x16x32_bf16 v[94:97], v[152:155], v[204:207], v[94:97]
	v_mfma_f32_16x16x32_bf16 v[90:93], v[160:163], v[204:207], v[90:93]
	v_mfma_f32_16x16x32_bf16 v[78:81], v[152:155], v[220:223], v[78:81]
	v_mfma_f32_16x16x32_bf16 v[74:77], v[160:163], v[220:223], v[74:77]
	s_setprio 0
	s_setprio 1
	v_mfma_f32_16x16x32_bf16 v[122:125], v[168:171], v[184:187], v[122:125]
	v_mfma_f32_16x16x32_bf16 v[114:117], v[176:179], v[184:187], v[114:117]
	v_mfma_f32_16x16x32_bf16 v[102:105], v[168:171], v[192:195], v[102:105]
	v_mfma_f32_16x16x32_bf16 v[98:101], v[176:179], v[192:195], v[98:101]
	v_mfma_f32_16x16x32_bf16 v[86:89], v[168:171], v[200:203], v[86:89]
	v_mfma_f32_16x16x32_bf16 v[82:85], v[176:179], v[200:203], v[82:85]
	v_mfma_f32_16x16x32_bf16 v[70:73], v[168:171], v[216:219], v[70:73]
	v_mfma_f32_16x16x32_bf16 v[66:69], v[176:179], v[216:219], v[66:69]
	v_mfma_f32_16x16x32_bf16 v[122:125], v[172:175], v[188:191], v[122:125]
	v_mfma_f32_16x16x32_bf16 v[114:117], v[180:183], v[188:191], v[114:117]
	v_mfma_f32_16x16x32_bf16 v[102:105], v[172:175], v[196:199], v[102:105]
	v_mfma_f32_16x16x32_bf16 v[98:101], v[180:183], v[196:199], v[98:101]
	v_mfma_f32_16x16x32_bf16 v[86:89], v[172:175], v[204:207], v[86:89]
	v_mfma_f32_16x16x32_bf16 v[82:85], v[180:183], v[204:207], v[82:85]
	v_mfma_f32_16x16x32_bf16 v[70:73], v[172:175], v[220:223], v[70:73]
	v_mfma_f32_16x16x32_bf16 v[66:69], v[180:183], v[220:223], v[66:69]
	s_setprio 0
	s_barrier
	s_add_i32 s64, s65, s71
	v_lshl_add_u64 v[164:165], s[44:45], 0, v[126:127]
	s_mov_b32 m0, s64
	ds_read_b128 v[184:187], v147 offset:16384
	ds_read_b128 v[188:191], v147 offset:17408
	ds_read_b128 v[192:195], v147 offset:18432
	ds_read_b128 v[196:199], v147 offset:19456
	ds_read_b128 v[200:203], v147 offset:20480
	ds_read_b128 v[204:207], v147 offset:21504
	ds_read_b128 v[216:219], v147 offset:22528
	ds_read_b128 v[220:223], v147 offset:23552
	global_load_lds_dwordx4 v126, s[44:45]
	s_add_i32 m0, s64, 0x2000
	s_add_u32 s92, s44, 0x100000
	v_lshl_add_u64 v[208:209], s[44:45], 0, v[118:119]
	s_addc_u32 s93, s45, 0
	s_add_i32 s50, s50, s71
	global_load_lds_dwordx4 v118, s[44:45]
	s_mov_b32 m0, s50
	v_lshl_add_u64 v[242:243], s[46:47], 0, v[120:121]
	global_load_lds_dwordx4 v126, s[92:93]
	s_add_i32 m0, s50, 0x2000
	s_nop 0
	global_load_lds_dwordx4 v118, s[92:93]
	s_mov_b32 m0, s4
	v_lshl_add_u64 v[224:225], s[46:47], 0, v[128:129]
	global_load_lds_dwordx4 v128, s[46:47]
	s_mov_b32 m0, s33
	s_nop 0
	global_load_lds_dwordx4 v120, s[46:47]
	s_waitcnt vmcnt(8)
	s_waitcnt lgkmcnt(0)
	s_barrier
	s_setprio 1
	s_waitcnt lgkmcnt(0)
	v_mfma_f32_16x16x32_bf16 v[62:65], v[148:151], v[184:187], v[62:65]
	v_mfma_f32_16x16x32_bf16 v[58:61], v[156:159], v[184:187], v[58:61]
	v_mfma_f32_16x16x32_bf16 v[46:49], v[148:151], v[192:195], v[46:49]
	v_mfma_f32_16x16x32_bf16 v[42:45], v[156:159], v[192:195], v[42:45]
	v_mfma_f32_16x16x32_bf16 v[30:33], v[148:151], v[200:203], v[30:33]
	v_mfma_f32_16x16x32_bf16 v[26:29], v[156:159], v[200:203], v[26:29]
	v_mfma_f32_16x16x32_bf16 v[14:17], v[148:151], v[216:219], v[14:17]
	v_mfma_f32_16x16x32_bf16 v[10:13], v[156:159], v[216:219], v[10:13]
	v_mfma_f32_16x16x32_bf16 v[62:65], v[152:155], v[188:191], v[62:65]
	v_mfma_f32_16x16x32_bf16 v[58:61], v[160:163], v[188:191], v[58:61]
	v_mfma_f32_16x16x32_bf16 v[46:49], v[152:155], v[196:199], v[46:49]
	v_mfma_f32_16x16x32_bf16 v[42:45], v[160:163], v[196:199], v[42:45]
	v_mfma_f32_16x16x32_bf16 v[30:33], v[152:155], v[204:207], v[30:33]
	v_mfma_f32_16x16x32_bf16 v[26:29], v[160:163], v[204:207], v[26:29]
	v_mfma_f32_16x16x32_bf16 v[14:17], v[152:155], v[220:223], v[14:17]
	v_mfma_f32_16x16x32_bf16 v[10:13], v[160:163], v[220:223], v[10:13]
	s_setprio 0
	s_setprio 1
	v_mfma_f32_16x16x32_bf16 v[54:57], v[168:171], v[184:187], v[54:57]
	v_mfma_f32_16x16x32_bf16 v[50:53], v[176:179], v[184:187], v[50:53]
	v_mfma_f32_16x16x32_bf16 v[38:41], v[168:171], v[192:195], v[38:41]
	v_mfma_f32_16x16x32_bf16 v[34:37], v[176:179], v[192:195], v[34:37]
	v_mfma_f32_16x16x32_bf16 v[22:25], v[168:171], v[200:203], v[22:25]
	v_mfma_f32_16x16x32_bf16 v[18:21], v[176:179], v[200:203], v[18:21]
	v_mfma_f32_16x16x32_bf16 v[6:9], v[168:171], v[216:219], v[6:9]
	v_mfma_f32_16x16x32_bf16 v[2:5], v[176:179], v[216:219], v[2:5]
	v_mfma_f32_16x16x32_bf16 v[54:57], v[172:175], v[188:191], v[54:57]
	v_mfma_f32_16x16x32_bf16 v[50:53], v[180:183], v[188:191], v[50:53]
	v_mfma_f32_16x16x32_bf16 v[38:41], v[172:175], v[196:199], v[38:41]
	v_mfma_f32_16x16x32_bf16 v[34:37], v[180:183], v[196:199], v[34:37]
	v_mfma_f32_16x16x32_bf16 v[22:25], v[172:175], v[204:207], v[22:25]
	v_mfma_f32_16x16x32_bf16 v[18:21], v[180:183], v[204:207], v[18:21]
	v_mfma_f32_16x16x32_bf16 v[6:9], v[172:175], v[220:223], v[6:9]
	v_mfma_f32_16x16x32_bf16 v[2:5], v[180:183], v[220:223], v[2:5]
	s_setprio 0
	s_barrier
	s_add_i32 s50, 0, 0x18000
	s_add_i32 s64, 0, 0x1c000
	v_add_u32_e32 v160, s50, v146
	v_add_u32_e32 v167, s64, v146
	ds_read_b128 v[148:151], v160
	ds_read_b128 v[152:155], v160 offset:1024
	ds_read_b128 v[156:159], v160 offset:2048
	ds_read_b128 v[160:163], v160 offset:3072
	ds_read_b128 v[168:171], v167
	ds_read_b128 v[172:175], v167 offset:1024
	ds_read_b128 v[176:179], v167 offset:2048
	ds_read_b128 v[180:183], v167 offset:3072
	s_add_u32 s46, s46, 0x100000
	s_addc_u32 s47, s47, 0
	s_mov_b32 m0, s76
	ds_read_b128 v[184:187], v147 offset:32768
	ds_read_b128 v[188:191], v147 offset:33792
	ds_read_b128 v[192:195], v147 offset:34816
	ds_read_b128 v[196:199], v147 offset:35840
	ds_read_b128 v[200:203], v147 offset:36864
	ds_read_b128 v[204:207], v147 offset:37888
	ds_read_b128 v[216:219], v147 offset:38912
	ds_read_b128 v[220:223], v147 offset:39936
	global_load_lds_dwordx4 v128, s[46:47]
	s_mov_b32 m0, s77
	v_lshl_add_u64 v[244:245], s[46:47], 0, v[120:121]
	global_load_lds_dwordx4 v120, s[46:47]
	s_waitcnt vmcnt(8)
	s_waitcnt lgkmcnt(0)
	s_barrier
	s_setprio 1
	s_waitcnt lgkmcnt(0)
	v_mfma_f32_16x16x32_bf16 v[134:137], v[148:151], v[184:187], v[134:137]
	v_mfma_f32_16x16x32_bf16 v[130:133], v[156:159], v[184:187], v[130:133]
	v_mfma_f32_16x16x32_bf16 v[110:113], v[148:151], v[192:195], v[110:113]
	v_mfma_f32_16x16x32_bf16 v[106:109], v[156:159], v[192:195], v[106:109]
	v_mfma_f32_16x16x32_bf16 v[94:97], v[148:151], v[200:203], v[94:97]
	v_mfma_f32_16x16x32_bf16 v[90:93], v[156:159], v[200:203], v[90:93]
	v_mfma_f32_16x16x32_bf16 v[78:81], v[148:151], v[216:219], v[78:81]
	v_mfma_f32_16x16x32_bf16 v[74:77], v[156:159], v[216:219], v[74:77]
	v_mfma_f32_16x16x32_bf16 v[134:137], v[152:155], v[188:191], v[134:137]
	v_mfma_f32_16x16x32_bf16 v[130:133], v[160:163], v[188:191], v[130:133]
	v_mfma_f32_16x16x32_bf16 v[110:113], v[152:155], v[196:199], v[110:113]
	v_mfma_f32_16x16x32_bf16 v[106:109], v[160:163], v[196:199], v[106:109]
	v_mfma_f32_16x16x32_bf16 v[94:97], v[152:155], v[204:207], v[94:97]
	v_mfma_f32_16x16x32_bf16 v[90:93], v[160:163], v[204:207], v[90:93]
	v_mfma_f32_16x16x32_bf16 v[78:81], v[152:155], v[220:223], v[78:81]
	v_mfma_f32_16x16x32_bf16 v[74:77], v[160:163], v[220:223], v[74:77]
	s_setprio 0
	s_setprio 1
	v_mfma_f32_16x16x32_bf16 v[122:125], v[168:171], v[184:187], v[122:125]
	v_mfma_f32_16x16x32_bf16 v[114:117], v[176:179], v[184:187], v[114:117]
	v_mfma_f32_16x16x32_bf16 v[102:105], v[168:171], v[192:195], v[102:105]
	v_mfma_f32_16x16x32_bf16 v[98:101], v[176:179], v[192:195], v[98:101]
	v_mfma_f32_16x16x32_bf16 v[86:89], v[168:171], v[200:203], v[86:89]
	v_mfma_f32_16x16x32_bf16 v[82:85], v[176:179], v[200:203], v[82:85]
	v_mfma_f32_16x16x32_bf16 v[70:73], v[168:171], v[216:219], v[70:73]
	v_mfma_f32_16x16x32_bf16 v[66:69], v[176:179], v[216:219], v[66:69]
	v_mfma_f32_16x16x32_bf16 v[122:125], v[172:175], v[188:191], v[122:125]
	v_mfma_f32_16x16x32_bf16 v[114:117], v[180:183], v[188:191], v[114:117]
	v_mfma_f32_16x16x32_bf16 v[102:105], v[172:175], v[196:199], v[102:105]
	v_mfma_f32_16x16x32_bf16 v[98:101], v[180:183], v[196:199], v[98:101]
	v_mfma_f32_16x16x32_bf16 v[86:89], v[172:175], v[204:207], v[86:89]
	v_mfma_f32_16x16x32_bf16 v[82:85], v[180:183], v[204:207], v[82:85]
	v_mfma_f32_16x16x32_bf16 v[70:73], v[172:175], v[220:223], v[70:73]
	v_mfma_f32_16x16x32_bf16 v[66:69], v[180:183], v[220:223], v[66:69]
	s_setprio 0
	s_barrier
	s_add_i32 s46, s50, s71
	v_lshl_add_u64 v[164:165], v[164:165], 0, s[56:57]
	s_mov_b32 m0, s46
	ds_read_b128 v[184:187], v147 offset:49152
	ds_read_b128 v[188:191], v147 offset:50176
	ds_read_b128 v[192:195], v147 offset:51200
	ds_read_b128 v[196:199], v147 offset:52224
	ds_read_b128 v[200:203], v147 offset:53248
	ds_read_b128 v[204:207], v147 offset:54272
	ds_read_b128 v[216:219], v147 offset:55296
	ds_read_b128 v[220:223], v147 offset:56320
	global_load_lds_dwordx4 v[164:165], off
	s_add_i32 m0, s46, 0x2000
	s_add_u32 s44, s44, 0x100080
	v_lshl_add_u64 v[164:165], v[208:209], 0, s[56:57]
	s_addc_u32 s45, s45, 0
	s_add_i32 s46, s64, s71
	global_load_lds_dwordx4 v[164:165], off
	s_mov_b32 m0, s46
	s_nop 0
	global_load_lds_dwordx4 v126, s[44:45]
	s_add_i32 m0, s46, 0x2000
	s_nop 0
	global_load_lds_dwordx4 v118, s[44:45]
	s_mov_b32 m0, s78
	v_lshl_add_u64 v[164:165], v[224:225], 0, s[56:57]
	global_load_lds_dwordx4 v[164:165], off
	s_mov_b32 m0, s79
	v_lshl_add_u64 v[164:165], v[242:243], 0, s[56:57]
	global_load_lds_dwordx4 v[164:165], off
	s_waitcnt vmcnt(8)
	s_waitcnt lgkmcnt(0)
	s_barrier
	s_setprio 1
	s_waitcnt lgkmcnt(0)
	v_mfma_f32_16x16x32_bf16 v[62:65], v[148:151], v[184:187], v[62:65]
	v_mfma_f32_16x16x32_bf16 v[58:61], v[156:159], v[184:187], v[58:61]
	v_mfma_f32_16x16x32_bf16 v[46:49], v[148:151], v[192:195], v[46:49]
	v_mfma_f32_16x16x32_bf16 v[42:45], v[156:159], v[192:195], v[42:45]
	v_mfma_f32_16x16x32_bf16 v[30:33], v[148:151], v[200:203], v[30:33]
	v_mfma_f32_16x16x32_bf16 v[26:29], v[156:159], v[200:203], v[26:29]
	v_mfma_f32_16x16x32_bf16 v[14:17], v[148:151], v[216:219], v[14:17]
	v_mfma_f32_16x16x32_bf16 v[10:13], v[156:159], v[216:219], v[10:13]
	v_mfma_f32_16x16x32_bf16 v[62:65], v[152:155], v[188:191], v[62:65]
	v_mfma_f32_16x16x32_bf16 v[58:61], v[160:163], v[188:191], v[58:61]
	v_mfma_f32_16x16x32_bf16 v[46:49], v[152:155], v[196:199], v[46:49]
	v_mfma_f32_16x16x32_bf16 v[42:45], v[160:163], v[196:199], v[42:45]
	v_mfma_f32_16x16x32_bf16 v[30:33], v[152:155], v[204:207], v[30:33]
	v_mfma_f32_16x16x32_bf16 v[26:29], v[160:163], v[204:207], v[26:29]
	v_mfma_f32_16x16x32_bf16 v[14:17], v[152:155], v[220:223], v[14:17]
	v_mfma_f32_16x16x32_bf16 v[10:13], v[160:163], v[220:223], v[10:13]
	s_setprio 0
	s_setprio 1
	v_mfma_f32_16x16x32_bf16 v[54:57], v[168:171], v[184:187], v[54:57]
	v_mfma_f32_16x16x32_bf16 v[50:53], v[176:179], v[184:187], v[50:53]
	v_mfma_f32_16x16x32_bf16 v[38:41], v[168:171], v[192:195], v[38:41]
	v_mfma_f32_16x16x32_bf16 v[34:37], v[176:179], v[192:195], v[34:37]
	v_mfma_f32_16x16x32_bf16 v[22:25], v[168:171], v[200:203], v[22:25]
	v_mfma_f32_16x16x32_bf16 v[18:21], v[176:179], v[200:203], v[18:21]
	v_mfma_f32_16x16x32_bf16 v[6:9], v[168:171], v[216:219], v[6:9]
	v_mfma_f32_16x16x32_bf16 v[2:5], v[176:179], v[216:219], v[2:5]
	v_mfma_f32_16x16x32_bf16 v[54:57], v[172:175], v[188:191], v[54:57]
	v_mfma_f32_16x16x32_bf16 v[50:53], v[180:183], v[188:191], v[50:53]
	v_mfma_f32_16x16x32_bf16 v[38:41], v[172:175], v[196:199], v[38:41]
	v_mfma_f32_16x16x32_bf16 v[34:37], v[180:183], v[196:199], v[34:37]
	v_mfma_f32_16x16x32_bf16 v[22:25], v[172:175], v[204:207], v[22:25]
	v_mfma_f32_16x16x32_bf16 v[18:21], v[180:183], v[204:207], v[18:21]
	v_mfma_f32_16x16x32_bf16 v[6:9], v[172:175], v[220:223], v[6:9]
	v_mfma_f32_16x16x32_bf16 v[2:5], v[180:183], v[220:223], v[2:5]
	s_setprio 0
	s_barrier
	s_add_i32 s84, s84, 2
	s_add_u32 s36, s36, 0x100
	s_addc_u32 s37, s37, 0
	s_cmp_gt_u32 s84, 61
	s_cbranch_scc0 .LBB0_2796
	s_add_u32 s36, s59, 0xffffff00
	s_addc_u32 s37, s81, -1
	s_andn2_b64 vcc, exec, s[42:43]
	s_cbranch_vccnz .LBB0_2799
	v_mov_b32_e32 v2, 0
	s_mov_b32 s12, s26
	s_mov_b32 s80, s28
	s_mov_b64 s[24:25], s[34:35]
	s_mov_b32 s68, s58
	v_mov_b32_e32 v3, v2
	v_mov_b32_e32 v4, v2
	v_mov_b32_e32 v5, v2
	v_mov_b32_e32 v6, v2
	v_mov_b32_e32 v7, v2
	v_mov_b32_e32 v8, v2
	v_mov_b32_e32 v9, v2
	v_mov_b32_e32 v18, v2
	v_mov_b32_e32 v19, v2
	v_mov_b32_e32 v20, v2
	v_mov_b32_e32 v21, v2
	v_mov_b32_e32 v22, v2
	v_mov_b32_e32 v23, v2
	v_mov_b32_e32 v24, v2
	v_mov_b32_e32 v25, v2
	v_mov_b32_e32 v34, v2
	v_mov_b32_e32 v35, v2
	v_mov_b32_e32 v36, v2
	v_mov_b32_e32 v37, v2
	v_mov_b32_e32 v38, v2
	v_mov_b32_e32 v39, v2
	v_mov_b32_e32 v40, v2
	v_mov_b32_e32 v41, v2
	v_mov_b32_e32 v50, v2
	v_mov_b32_e32 v51, v2
	v_mov_b32_e32 v52, v2
	v_mov_b32_e32 v53, v2
	v_mov_b32_e32 v54, v2
	v_mov_b32_e32 v55, v2
	v_mov_b32_e32 v56, v2
	v_mov_b32_e32 v57, v2
	v_mov_b32_e32 v10, v2
	v_mov_b32_e32 v11, v2
	v_mov_b32_e32 v12, v2
	v_mov_b32_e32 v13, v2
	v_mov_b32_e32 v14, v2
	v_mov_b32_e32 v15, v2
	v_mov_b32_e32 v16, v2
	v_mov_b32_e32 v17, v2
	v_mov_b32_e32 v26, v2
	v_mov_b32_e32 v27, v2
	v_mov_b32_e32 v28, v2
	v_mov_b32_e32 v29, v2
	v_mov_b32_e32 v30, v2
	v_mov_b32_e32 v31, v2
	v_mov_b32_e32 v32, v2
	v_mov_b32_e32 v33, v2
	v_mov_b32_e32 v42, v2
	v_mov_b32_e32 v43, v2
	v_mov_b32_e32 v44, v2
	v_mov_b32_e32 v45, v2
	v_mov_b32_e32 v46, v2
	v_mov_b32_e32 v47, v2
	v_mov_b32_e32 v48, v2
	v_mov_b32_e32 v49, v2
	v_mov_b32_e32 v58, v2
	v_mov_b32_e32 v59, v2
	v_mov_b32_e32 v60, v2
	v_mov_b32_e32 v61, v2
	v_mov_b32_e32 v62, v2
	v_mov_b32_e32 v63, v2
	v_mov_b32_e32 v64, v2
	v_mov_b32_e32 v65, v2
	v_mov_b32_e32 v66, v2
	v_mov_b32_e32 v67, v2
	v_mov_b32_e32 v68, v2
	v_mov_b32_e32 v69, v2
	v_mov_b32_e32 v70, v2
	v_mov_b32_e32 v71, v2
	v_mov_b32_e32 v72, v2
	v_mov_b32_e32 v73, v2
	v_mov_b32_e32 v82, v2
	v_mov_b32_e32 v83, v2
	v_mov_b32_e32 v84, v2
	v_mov_b32_e32 v85, v2
	v_mov_b32_e32 v86, v2
	v_mov_b32_e32 v87, v2
	v_mov_b32_e32 v88, v2
	v_mov_b32_e32 v89, v2
	v_mov_b32_e32 v98, v2
	v_mov_b32_e32 v99, v2
	v_mov_b32_e32 v100, v2
	v_mov_b32_e32 v101, v2
	v_mov_b32_e32 v102, v2
	v_mov_b32_e32 v103, v2
	v_mov_b32_e32 v104, v2
	v_mov_b32_e32 v105, v2
	v_mov_b32_e32 v114, v2
	v_mov_b32_e32 v115, v2
	v_mov_b32_e32 v116, v2
	v_mov_b32_e32 v117, v2
	v_mov_b32_e32 v122, v2
	v_mov_b32_e32 v123, v2
	v_mov_b32_e32 v124, v2
	v_mov_b32_e32 v125, v2
	v_mov_b32_e32 v74, v2
	v_mov_b32_e32 v75, v2
	v_mov_b32_e32 v76, v2
	v_mov_b32_e32 v77, v2
	v_mov_b32_e32 v78, v2
	v_mov_b32_e32 v79, v2
	v_mov_b32_e32 v80, v2
	v_mov_b32_e32 v81, v2
	v_mov_b32_e32 v90, v2
	v_mov_b32_e32 v91, v2
	v_mov_b32_e32 v92, v2
	v_mov_b32_e32 v93, v2
	v_mov_b32_e32 v94, v2
	v_mov_b32_e32 v95, v2
	v_mov_b32_e32 v96, v2
	v_mov_b32_e32 v97, v2
	v_mov_b32_e32 v106, v2
	v_mov_b32_e32 v107, v2
	v_mov_b32_e32 v108, v2
	v_mov_b32_e32 v109, v2
	v_mov_b32_e32 v110, v2
	v_mov_b32_e32 v111, v2
	v_mov_b32_e32 v112, v2
	v_mov_b32_e32 v113, v2
	v_mov_b32_e32 v130, v2
	v_mov_b32_e32 v131, v2
	v_mov_b32_e32 v132, v2
	v_mov_b32_e32 v133, v2
	v_mov_b32_e32 v134, v2
	v_mov_b32_e32 v135, v2
	v_mov_b32_e32 v136, v2
	v_mov_b32_e32 v137, v2
	s_movk_i32 s92, 0x2b20
	s_andn2_b64 vcc, exec, s[40:41]
	s_cbranch_vccnz .LBB0_2800
	s_branch .LBB0_2801

.LBB0_2883:
	v_mov_b32_e32 v127, v1
	v_lshl_add_u64 v[8:9], s[36:37], 0, v[126:127]
	v_mov_b32_e32 v123, v1
	v_lshl_add_u64 v[10:11], s[36:37], 0, v[122:123]
	v_mov_b32_e32 v129, v1
	s_and_b32 s53, s21, 3
	s_add_i32 m0, s4, 0x18000
	v_lshl_add_u64 v[8:9], v[8:9], 0, s[56:57]
	v_lshl_add_u64 v[12:13], s[24:25], 0, v[128:129]
	v_mov_b32_e32 v125, v1
	s_lshl_b32 s20, s49, 13
	s_lshl_b32 s28, s53, 12
	s_waitcnt vmcnt(2)
	s_barrier
	global_load_lds_dwordx4 v[8:9], off
	v_lshl_add_u64 v[8:9], v[10:11], 0, s[56:57]
	s_add_i32 m0, s4, 0x1a000
	s_add_i32 s79, s4, 0x8000
	s_add_i32 s80, s4, 0xa000
	s_waitcnt lgkmcnt(0)
	v_lshl_add_u64 v[14:15], s[24:25], 0, v[124:125]
	global_load_lds_dwordx4 v[8:9], off
	v_lshl_add_u64 v[8:9], v[12:13], 0, s[56:57]
	s_mov_b32 m0, s79
	s_add_u32 s26, s36, 0x100080
	global_load_lds_dwordx4 v[8:9], off
	v_lshl_add_u64 v[8:9], v[14:15], 0, s[56:57]
	s_mov_b32 m0, s80
	s_addc_u32 s27, s37, 0
	global_load_lds_dwordx4 v[8:9], off
	s_add_i32 m0, s4, 0x1c000
	s_nop 0
	global_load_lds_dwordx4 v126, s[26:27]
	v_lshl_add_u64 v[8:9], s[26:27], 0, v[122:123]
	s_add_i32 m0, s4, 0x1e000
	v_and_b32_e32 v166, 15, v0
	global_load_lds_dwordx4 v122, s[26:27]
	v_and_b32_e32 v8, 48, v0
	v_lshlrev_b32_e32 v9, 2, v0
	v_lshl_or_b32 v8, v166, 6, v8
	v_and_b32_e32 v9, 32, v9
	v_bitop3_b32 v10, v8, s20, v9 bitop3:0xde
	v_bitop3_b32 v146, v8, s28, v9 bitop3:0xde
	v_lshlrev_b32_e32 v8, 16, v2
	v_and_b32_e32 v8, 0xfffe0000, v8
	v_lshl_add_u32 v3, v3, 13, v8
	v_and_b32_e32 v2, 1, v2
	v_lshl_or_b32 v2, v2, 6, v3
	v_lshl_add_u32 v138, v4, 1, v2
	v_lshlrev_b32_e32 v2, 16, v6
	v_and_b32_e32 v2, 0xfffe0000, v2
	v_lshl_add_u32 v2, v5, 13, v2
	v_and_b32_e32 v3, 1, v6
	s_waitcnt vmcnt(6)
	v_lshl_or_b32 v2, v3, 6, v2
	v_mov_b32_e32 v4, v1
	v_mov_b32_e32 v5, v1
	v_lshl_add_u32 v140, v7, 1, v2
	v_mov_b32_e32 v2, v1
	v_mov_b32_e32 v3, v1
	v_add_u32_e32 v147, 0, v10
	v_mov_b64_e32 v[8:9], v[4:5]
	v_mov_b64_e32 v[20:21], v[4:5]
	v_mov_b64_e32 v[24:25], v[4:5]
	v_mov_b64_e32 v[36:37], v[4:5]
	v_mov_b64_e32 v[40:41], v[4:5]
	v_mov_b64_e32 v[52:53], v[4:5]
	v_mov_b64_e32 v[56:57], v[4:5]
	v_mov_b64_e32 v[12:13], v[4:5]
	v_mov_b64_e32 v[16:17], v[4:5]
	v_mov_b64_e32 v[28:29], v[4:5]
	v_mov_b64_e32 v[32:33], v[4:5]
	v_mov_b64_e32 v[44:45], v[4:5]
	v_mov_b64_e32 v[48:49], v[4:5]
	v_mov_b64_e32 v[60:61], v[4:5]
	v_mov_b64_e32 v[64:65], v[4:5]
	v_mov_b64_e32 v[68:69], v[4:5]
	v_mov_b64_e32 v[72:73], v[4:5]
	v_mov_b64_e32 v[84:85], v[4:5]
	v_mov_b64_e32 v[88:89], v[4:5]
	v_mov_b64_e32 v[100:101], v[4:5]
	v_mov_b64_e32 v[104:105], v[4:5]
	v_mov_b64_e32 v[116:117], v[4:5]
	v_mov_b64_e32 v[120:121], v[4:5]
	v_mov_b64_e32 v[76:77], v[4:5]
	v_mov_b64_e32 v[80:81], v[4:5]
	v_mov_b64_e32 v[92:93], v[4:5]
	v_mov_b64_e32 v[96:97], v[4:5]
	v_mov_b64_e32 v[108:109], v[4:5]
	v_mov_b64_e32 v[112:113], v[4:5]
	v_mov_b64_e32 v[132:133], v[4:5]
	v_mov_b64_e32 v[136:137], v[4:5]
	v_readlane_b32 s26, v254, 54
	v_lshl_or_b32 v224, s49, 6, v166
	v_mov_b32_e32 v139, v1
	v_mov_b32_e32 v141, v1
	s_mov_b32 s68, 0
	v_mov_b64_e32 v[6:7], v[2:3]
	v_mov_b64_e32 v[18:19], v[2:3]
	v_mov_b64_e32 v[22:23], v[2:3]
	v_mov_b64_e32 v[34:35], v[2:3]
	v_mov_b64_e32 v[38:39], v[2:3]
	v_mov_b64_e32 v[50:51], v[2:3]
	v_mov_b64_e32 v[54:55], v[2:3]
	v_mov_b64_e32 v[10:11], v[2:3]
	v_mov_b64_e32 v[14:15], v[2:3]
	v_mov_b64_e32 v[26:27], v[2:3]
	v_mov_b64_e32 v[30:31], v[2:3]
	v_mov_b64_e32 v[42:43], v[2:3]
	v_mov_b64_e32 v[46:47], v[2:3]
	v_mov_b64_e32 v[58:59], v[2:3]
	v_mov_b64_e32 v[62:63], v[2:3]
	v_mov_b64_e32 v[66:67], v[2:3]
	v_mov_b64_e32 v[70:71], v[2:3]
	v_mov_b64_e32 v[82:83], v[2:3]
	v_mov_b64_e32 v[86:87], v[2:3]
	v_mov_b64_e32 v[98:99], v[2:3]
	v_mov_b64_e32 v[102:103], v[2:3]
	v_mov_b64_e32 v[114:115], v[2:3]
	v_mov_b64_e32 v[118:119], v[2:3]
	v_mov_b64_e32 v[74:75], v[2:3]
	v_mov_b64_e32 v[78:79], v[2:3]
	v_mov_b64_e32 v[90:91], v[2:3]
	v_mov_b64_e32 v[94:95], v[2:3]
	v_mov_b64_e32 v[106:107], v[2:3]
	v_mov_b64_e32 v[110:111], v[2:3]
	v_mov_b64_e32 v[130:131], v[2:3]
	v_mov_b64_e32 v[134:135], v[2:3]
	v_readlane_b32 s20, v254, 58
	s_mov_b32 s52, s26
	s_barrier
	v_readlane_b32 s27, v254, 55

.LBB0_2891:
	s_add_u32 s44, s24, s36
	s_addc_u32 s45, s25, s37
	s_add_u32 s44, s44, 0x100
	s_addc_u32 s45, s45, 0
	s_add_u32 s50, s59, s36
	s_addc_u32 s64, s81, s37
	s_add_i32 s65, 0, 0x10000
	s_cmpk_eq_i32 s36, 0x1f00
	s_cselect_b32 s47, s29, s45
	s_cselect_b32 s46, s82, s44
	s_cselect_b32 s45, s27, s64
	s_cselect_b32 s44, s83, s50
	s_add_i32 s50, 0, 0x14000
	v_add_u32_e32 v160, s65, v146
	v_add_u32_e32 v164, s50, v146
	ds_read_b128 v[148:151], v160
	ds_read_b128 v[152:155], v160 offset:1024
	ds_read_b128 v[156:159], v160 offset:2048
	ds_read_b128 v[160:163], v160 offset:3072
	ds_read_b128 v[168:171], v164
	ds_read_b128 v[172:175], v164 offset:1024
	ds_read_b128 v[176:179], v164 offset:2048
	ds_read_b128 v[180:183], v164 offset:3072
	v_lshl_add_u64 v[164:165], v[144:145], 0, s[36:37]
	s_add_i32 m0, s4, 0xc000
	ds_read_b128 v[184:187], v147
	ds_read_b128 v[188:191], v147 offset:1024
	ds_read_b128 v[192:195], v147 offset:2048
	ds_read_b128 v[196:199], v147 offset:3072
	ds_read_b128 v[200:203], v147 offset:4096
	ds_read_b128 v[204:207], v147 offset:5120
	ds_read_b128 v[216:219], v147 offset:6144
	ds_read_b128 v[220:223], v147 offset:7168
	global_load_lds_dwordx4 v[164:165], off
	s_add_i32 m0, s4, 0xe000
	v_lshl_add_u64 v[164:165], v[142:143], 0, s[36:37]
	global_load_lds_dwordx4 v[164:165], off
	s_waitcnt vmcnt(8)
	s_waitcnt lgkmcnt(0)
	s_barrier
	s_setprio 1
	s_waitcnt lgkmcnt(0)
	v_mfma_f32_16x16x32_bf16 v[134:137], v[148:151], v[184:187], v[134:137]
	v_mfma_f32_16x16x32_bf16 v[130:133], v[156:159], v[184:187], v[130:133]
	v_mfma_f32_16x16x32_bf16 v[110:113], v[148:151], v[192:195], v[110:113]
	v_mfma_f32_16x16x32_bf16 v[106:109], v[156:159], v[192:195], v[106:109]
	v_mfma_f32_16x16x32_bf16 v[94:97], v[148:151], v[200:203], v[94:97]
	v_mfma_f32_16x16x32_bf16 v[90:93], v[156:159], v[200:203], v[90:93]
	v_mfma_f32_16x16x32_bf16 v[78:81], v[148:151], v[216:219], v[78:81]
	v_mfma_f32_16x16x32_bf16 v[74:77], v[156:159], v[216:219], v[74:77]
	v_mfma_f32_16x16x32_bf16 v[134:137], v[152:155], v[188:191], v[134:137]
	v_mfma_f32_16x16x32_bf16 v[130:133], v[160:163], v[188:191], v[130:133]
	v_mfma_f32_16x16x32_bf16 v[110:113], v[152:155], v[196:199], v[110:113]
	v_mfma_f32_16x16x32_bf16 v[106:109], v[160:163], v[196:199], v[106:109]
	v_mfma_f32_16x16x32_bf16 v[94:97], v[152:155], v[204:207], v[94:97]
	v_mfma_f32_16x16x32_bf16 v[90:93], v[160:163], v[204:207], v[90:93]
	v_mfma_f32_16x16x32_bf16 v[78:81], v[152:155], v[220:223], v[78:81]
	v_mfma_f32_16x16x32_bf16 v[74:77], v[160:163], v[220:223], v[74:77]
	s_setprio 0
	s_setprio 1
	v_mfma_f32_16x16x32_bf16 v[118:121], v[168:171], v[184:187], v[118:121]
	v_mfma_f32_16x16x32_bf16 v[114:117], v[176:179], v[184:187], v[114:117]
	v_mfma_f32_16x16x32_bf16 v[102:105], v[168:171], v[192:195], v[102:105]
	v_mfma_f32_16x16x32_bf16 v[98:101], v[176:179], v[192:195], v[98:101]
	v_mfma_f32_16x16x32_bf16 v[86:89], v[168:171], v[200:203], v[86:89]
	v_mfma_f32_16x16x32_bf16 v[82:85], v[176:179], v[200:203], v[82:85]
	v_mfma_f32_16x16x32_bf16 v[70:73], v[168:171], v[216:219], v[70:73]
	v_mfma_f32_16x16x32_bf16 v[66:69], v[176:179], v[216:219], v[66:69]
	v_mfma_f32_16x16x32_bf16 v[118:121], v[172:175], v[188:191], v[118:121]
	v_mfma_f32_16x16x32_bf16 v[114:117], v[180:183], v[188:191], v[114:117]
	v_mfma_f32_16x16x32_bf16 v[102:105], v[172:175], v[196:199], v[102:105]
	v_mfma_f32_16x16x32_bf16 v[98:101], v[180:183], v[196:199], v[98:101]
	v_mfma_f32_16x16x32_bf16 v[86:89], v[172:175], v[204:207], v[86:89]
	v_mfma_f32_16x16x32_bf16 v[82:85], v[180:183], v[204:207], v[82:85]
	v_mfma_f32_16x16x32_bf16 v[70:73], v[172:175], v[220:223], v[70:73]
	v_mfma_f32_16x16x32_bf16 v[66:69], v[180:183], v[220:223], v[66:69]
	s_setprio 0
	s_barrier
	s_add_i32 s64, s65, s76
	v_lshl_add_u64 v[164:165], s[44:45], 0, v[126:127]
	s_mov_b32 m0, s64
	ds_read_b128 v[184:187], v147 offset:16384
	ds_read_b128 v[188:191], v147 offset:17408
	ds_read_b128 v[192:195], v147 offset:18432
	ds_read_b128 v[196:199], v147 offset:19456
	ds_read_b128 v[200:203], v147 offset:20480
	ds_read_b128 v[204:207], v147 offset:21504
	ds_read_b128 v[216:219], v147 offset:22528
	ds_read_b128 v[220:223], v147 offset:23552
	global_load_lds_dwordx4 v126, s[44:45]
	s_add_i32 m0, s64, 0x2000
	s_add_u32 s92, s44, 0x100000
	v_lshl_add_u64 v[208:209], s[44:45], 0, v[122:123]
	s_addc_u32 s93, s45, 0
	s_add_i32 s50, s50, s76
	global_load_lds_dwordx4 v122, s[44:45]
	s_mov_b32 m0, s50
	v_lshl_add_u64 v[242:243], s[46:47], 0, v[124:125]
	global_load_lds_dwordx4 v126, s[92:93]
	s_add_i32 m0, s50, 0x2000
	s_nop 0
	global_load_lds_dwordx4 v122, s[92:93]
	s_mov_b32 m0, s4
	v_lshl_add_u64 v[240:241], s[46:47], 0, v[128:129]
	global_load_lds_dwordx4 v128, s[46:47]
	s_mov_b32 m0, s33
	s_nop 0
	global_load_lds_dwordx4 v124, s[46:47]
	s_waitcnt vmcnt(8)
	s_waitcnt lgkmcnt(0)
	s_barrier
	s_setprio 1
	s_waitcnt lgkmcnt(0)
	v_mfma_f32_16x16x32_bf16 v[62:65], v[148:151], v[184:187], v[62:65]
	v_mfma_f32_16x16x32_bf16 v[58:61], v[156:159], v[184:187], v[58:61]
	v_mfma_f32_16x16x32_bf16 v[46:49], v[148:151], v[192:195], v[46:49]
	v_mfma_f32_16x16x32_bf16 v[42:45], v[156:159], v[192:195], v[42:45]
	v_mfma_f32_16x16x32_bf16 v[30:33], v[148:151], v[200:203], v[30:33]
	v_mfma_f32_16x16x32_bf16 v[26:29], v[156:159], v[200:203], v[26:29]
	v_mfma_f32_16x16x32_bf16 v[14:17], v[148:151], v[216:219], v[14:17]
	v_mfma_f32_16x16x32_bf16 v[10:13], v[156:159], v[216:219], v[10:13]
	v_mfma_f32_16x16x32_bf16 v[62:65], v[152:155], v[188:191], v[62:65]
	v_mfma_f32_16x16x32_bf16 v[58:61], v[160:163], v[188:191], v[58:61]
	v_mfma_f32_16x16x32_bf16 v[46:49], v[152:155], v[196:199], v[46:49]
	v_mfma_f32_16x16x32_bf16 v[42:45], v[160:163], v[196:199], v[42:45]
	v_mfma_f32_16x16x32_bf16 v[30:33], v[152:155], v[204:207], v[30:33]
	v_mfma_f32_16x16x32_bf16 v[26:29], v[160:163], v[204:207], v[26:29]
	v_mfma_f32_16x16x32_bf16 v[14:17], v[152:155], v[220:223], v[14:17]
	v_mfma_f32_16x16x32_bf16 v[10:13], v[160:163], v[220:223], v[10:13]
	s_setprio 0
	s_setprio 1
	v_mfma_f32_16x16x32_bf16 v[54:57], v[168:171], v[184:187], v[54:57]
	v_mfma_f32_16x16x32_bf16 v[50:53], v[176:179], v[184:187], v[50:53]
	v_mfma_f32_16x16x32_bf16 v[38:41], v[168:171], v[192:195], v[38:41]
	v_mfma_f32_16x16x32_bf16 v[34:37], v[176:179], v[192:195], v[34:37]
	v_mfma_f32_16x16x32_bf16 v[22:25], v[168:171], v[200:203], v[22:25]
	v_mfma_f32_16x16x32_bf16 v[18:21], v[176:179], v[200:203], v[18:21]
	v_mfma_f32_16x16x32_bf16 v[6:9], v[168:171], v[216:219], v[6:9]
	v_mfma_f32_16x16x32_bf16 v[2:5], v[176:179], v[216:219], v[2:5]
	v_mfma_f32_16x16x32_bf16 v[54:57], v[172:175], v[188:191], v[54:57]
	v_mfma_f32_16x16x32_bf16 v[50:53], v[180:183], v[188:191], v[50:53]
	v_mfma_f32_16x16x32_bf16 v[38:41], v[172:175], v[196:199], v[38:41]
	v_mfma_f32_16x16x32_bf16 v[34:37], v[180:183], v[196:199], v[34:37]
	v_mfma_f32_16x16x32_bf16 v[22:25], v[172:175], v[204:207], v[22:25]
	v_mfma_f32_16x16x32_bf16 v[18:21], v[180:183], v[204:207], v[18:21]
	v_mfma_f32_16x16x32_bf16 v[6:9], v[172:175], v[220:223], v[6:9]
	v_mfma_f32_16x16x32_bf16 v[2:5], v[180:183], v[220:223], v[2:5]
	s_setprio 0
	s_barrier
	s_add_i32 s50, 0, 0x18000
	s_add_i32 s64, 0, 0x1c000
	v_add_u32_e32 v160, s50, v146
	v_add_u32_e32 v167, s64, v146
	ds_read_b128 v[148:151], v160
	ds_read_b128 v[152:155], v160 offset:1024
	ds_read_b128 v[156:159], v160 offset:2048
	ds_read_b128 v[160:163], v160 offset:3072
	ds_read_b128 v[168:171], v167
	ds_read_b128 v[172:175], v167 offset:1024
	ds_read_b128 v[176:179], v167 offset:2048
	ds_read_b128 v[180:183], v167 offset:3072
	s_add_u32 s46, s46, 0x100000
	s_addc_u32 s47, s47, 0
	s_mov_b32 m0, s77
	ds_read_b128 v[184:187], v147 offset:32768
	ds_read_b128 v[188:191], v147 offset:33792
	ds_read_b128 v[192:195], v147 offset:34816
	ds_read_b128 v[196:199], v147 offset:35840
	ds_read_b128 v[200:203], v147 offset:36864
	ds_read_b128 v[204:207], v147 offset:37888
	ds_read_b128 v[216:219], v147 offset:38912
	ds_read_b128 v[220:223], v147 offset:39936
	global_load_lds_dwordx4 v128, s[46:47]
	s_mov_b32 m0, s78
	v_lshl_add_u64 v[244:245], s[46:47], 0, v[124:125]
	global_load_lds_dwordx4 v124, s[46:47]
	s_waitcnt vmcnt(8)
	s_waitcnt lgkmcnt(0)
	s_barrier
	s_setprio 1
	s_waitcnt lgkmcnt(0)
	v_mfma_f32_16x16x32_bf16 v[134:137], v[148:151], v[184:187], v[134:137]
	v_mfma_f32_16x16x32_bf16 v[130:133], v[156:159], v[184:187], v[130:133]
	v_mfma_f32_16x16x32_bf16 v[110:113], v[148:151], v[192:195], v[110:113]
	v_mfma_f32_16x16x32_bf16 v[106:109], v[156:159], v[192:195], v[106:109]
	v_mfma_f32_16x16x32_bf16 v[94:97], v[148:151], v[200:203], v[94:97]
	v_mfma_f32_16x16x32_bf16 v[90:93], v[156:159], v[200:203], v[90:93]
	v_mfma_f32_16x16x32_bf16 v[78:81], v[148:151], v[216:219], v[78:81]
	v_mfma_f32_16x16x32_bf16 v[74:77], v[156:159], v[216:219], v[74:77]
	v_mfma_f32_16x16x32_bf16 v[134:137], v[152:155], v[188:191], v[134:137]
	v_mfma_f32_16x16x32_bf16 v[130:133], v[160:163], v[188:191], v[130:133]
	v_mfma_f32_16x16x32_bf16 v[110:113], v[152:155], v[196:199], v[110:113]
	v_mfma_f32_16x16x32_bf16 v[106:109], v[160:163], v[196:199], v[106:109]
	v_mfma_f32_16x16x32_bf16 v[94:97], v[152:155], v[204:207], v[94:97]
	v_mfma_f32_16x16x32_bf16 v[90:93], v[160:163], v[204:207], v[90:93]
	v_mfma_f32_16x16x32_bf16 v[78:81], v[152:155], v[220:223], v[78:81]
	v_mfma_f32_16x16x32_bf16 v[74:77], v[160:163], v[220:223], v[74:77]
	s_setprio 0
	s_setprio 1
	v_mfma_f32_16x16x32_bf16 v[118:121], v[168:171], v[184:187], v[118:121]
	v_mfma_f32_16x16x32_bf16 v[114:117], v[176:179], v[184:187], v[114:117]
	v_mfma_f32_16x16x32_bf16 v[102:105], v[168:171], v[192:195], v[102:105]
	v_mfma_f32_16x16x32_bf16 v[98:101], v[176:179], v[192:195], v[98:101]
	v_mfma_f32_16x16x32_bf16 v[86:89], v[168:171], v[200:203], v[86:89]
	v_mfma_f32_16x16x32_bf16 v[82:85], v[176:179], v[200:203], v[82:85]
	v_mfma_f32_16x16x32_bf16 v[70:73], v[168:171], v[216:219], v[70:73]
	v_mfma_f32_16x16x32_bf16 v[66:69], v[176:179], v[216:219], v[66:69]
	v_mfma_f32_16x16x32_bf16 v[118:121], v[172:175], v[188:191], v[118:121]
	v_mfma_f32_16x16x32_bf16 v[114:117], v[180:183], v[188:191], v[114:117]
	v_mfma_f32_16x16x32_bf16 v[102:105], v[172:175], v[196:199], v[102:105]
	v_mfma_f32_16x16x32_bf16 v[98:101], v[180:183], v[196:199], v[98:101]
	v_mfma_f32_16x16x32_bf16 v[86:89], v[172:175], v[204:207], v[86:89]
	v_mfma_f32_16x16x32_bf16 v[82:85], v[180:183], v[204:207], v[82:85]
	v_mfma_f32_16x16x32_bf16 v[70:73], v[172:175], v[220:223], v[70:73]
	v_mfma_f32_16x16x32_bf16 v[66:69], v[180:183], v[220:223], v[66:69]
	s_setprio 0
	s_barrier
	s_add_i32 s46, s50, s76
	v_lshl_add_u64 v[164:165], v[164:165], 0, s[56:57]
	s_mov_b32 m0, s46
	ds_read_b128 v[184:187], v147 offset:49152
	ds_read_b128 v[188:191], v147 offset:50176
	ds_read_b128 v[192:195], v147 offset:51200
	ds_read_b128 v[196:199], v147 offset:52224
	ds_read_b128 v[200:203], v147 offset:53248
	ds_read_b128 v[204:207], v147 offset:54272
	ds_read_b128 v[216:219], v147 offset:55296
	ds_read_b128 v[220:223], v147 offset:56320
	global_load_lds_dwordx4 v[164:165], off
	s_add_i32 m0, s46, 0x2000
	s_add_u32 s44, s44, 0x100080
	v_lshl_add_u64 v[164:165], v[208:209], 0, s[56:57]
	s_addc_u32 s45, s45, 0
	s_add_i32 s46, s64, s76
	global_load_lds_dwordx4 v[164:165], off
	s_mov_b32 m0, s46
	s_nop 0
	global_load_lds_dwordx4 v126, s[44:45]
	s_add_i32 m0, s46, 0x2000
	s_nop 0
	global_load_lds_dwordx4 v122, s[44:45]
	s_mov_b32 m0, s79
	v_lshl_add_u64 v[164:165], v[240:241], 0, s[56:57]
	global_load_lds_dwordx4 v[164:165], off
	s_mov_b32 m0, s80
	v_lshl_add_u64 v[164:165], v[242:243], 0, s[56:57]
	global_load_lds_dwordx4 v[164:165], off
	s_waitcnt vmcnt(8)
	s_waitcnt lgkmcnt(0)
	s_barrier
	s_setprio 1
	s_waitcnt lgkmcnt(0)
	v_mfma_f32_16x16x32_bf16 v[62:65], v[148:151], v[184:187], v[62:65]
	v_mfma_f32_16x16x32_bf16 v[58:61], v[156:159], v[184:187], v[58:61]
	v_mfma_f32_16x16x32_bf16 v[46:49], v[148:151], v[192:195], v[46:49]
	v_mfma_f32_16x16x32_bf16 v[42:45], v[156:159], v[192:195], v[42:45]
	v_mfma_f32_16x16x32_bf16 v[30:33], v[148:151], v[200:203], v[30:33]
	v_mfma_f32_16x16x32_bf16 v[26:29], v[156:159], v[200:203], v[26:29]
	v_mfma_f32_16x16x32_bf16 v[14:17], v[148:151], v[216:219], v[14:17]
	v_mfma_f32_16x16x32_bf16 v[10:13], v[156:159], v[216:219], v[10:13]
	v_mfma_f32_16x16x32_bf16 v[62:65], v[152:155], v[188:191], v[62:65]
	v_mfma_f32_16x16x32_bf16 v[58:61], v[160:163], v[188:191], v[58:61]
	v_mfma_f32_16x16x32_bf16 v[46:49], v[152:155], v[196:199], v[46:49]
	v_mfma_f32_16x16x32_bf16 v[42:45], v[160:163], v[196:199], v[42:45]
	v_mfma_f32_16x16x32_bf16 v[30:33], v[152:155], v[204:207], v[30:33]
	v_mfma_f32_16x16x32_bf16 v[26:29], v[160:163], v[204:207], v[26:29]
	v_mfma_f32_16x16x32_bf16 v[14:17], v[152:155], v[220:223], v[14:17]
	v_mfma_f32_16x16x32_bf16 v[10:13], v[160:163], v[220:223], v[10:13]
	s_setprio 0
	s_setprio 1
	v_mfma_f32_16x16x32_bf16 v[54:57], v[168:171], v[184:187], v[54:57]
	v_mfma_f32_16x16x32_bf16 v[50:53], v[176:179], v[184:187], v[50:53]
	v_mfma_f32_16x16x32_bf16 v[38:41], v[168:171], v[192:195], v[38:41]
	v_mfma_f32_16x16x32_bf16 v[34:37], v[176:179], v[192:195], v[34:37]
	v_mfma_f32_16x16x32_bf16 v[22:25], v[168:171], v[200:203], v[22:25]
	v_mfma_f32_16x16x32_bf16 v[18:21], v[176:179], v[200:203], v[18:21]
	v_mfma_f32_16x16x32_bf16 v[6:9], v[168:171], v[216:219], v[6:9]
	v_mfma_f32_16x16x32_bf16 v[2:5], v[176:179], v[216:219], v[2:5]
	v_mfma_f32_16x16x32_bf16 v[54:57], v[172:175], v[188:191], v[54:57]
	v_mfma_f32_16x16x32_bf16 v[50:53], v[180:183], v[188:191], v[50:53]
	v_mfma_f32_16x16x32_bf16 v[38:41], v[172:175], v[196:199], v[38:41]
	v_mfma_f32_16x16x32_bf16 v[34:37], v[180:183], v[196:199], v[34:37]
	v_mfma_f32_16x16x32_bf16 v[22:25], v[172:175], v[204:207], v[22:25]
	v_mfma_f32_16x16x32_bf16 v[18:21], v[180:183], v[204:207], v[18:21]
	v_mfma_f32_16x16x32_bf16 v[6:9], v[172:175], v[220:223], v[6:9]
	v_mfma_f32_16x16x32_bf16 v[2:5], v[180:183], v[220:223], v[2:5]
	s_setprio 0
	s_barrier
	s_add_i32 s84, s84, 2
	s_add_u32 s36, s36, 0x100
	s_addc_u32 s37, s37, 0
	s_cmp_gt_u32 s84, 61
	s_cbranch_scc0 .LBB0_2891
	s_add_u32 s36, s59, 0xffffff00
	s_addc_u32 s37, s81, -1
	s_andn2_b64 vcc, exec, s[42:43]
	s_cbranch_vccnz .LBB0_2894
	v_mov_b32_e32 v2, 0
	s_mov_b32 s20, s26
	s_mov_b32 s52, s28
	s_mov_b64 s[24:25], s[34:35]
	s_mov_b32 s68, s58
	v_mov_b32_e32 v3, v2
	v_mov_b32_e32 v4, v2
	v_mov_b32_e32 v5, v2
	v_mov_b32_e32 v6, v2
	v_mov_b32_e32 v7, v2
	v_mov_b32_e32 v8, v2
	v_mov_b32_e32 v9, v2
	v_mov_b32_e32 v18, v2
	v_mov_b32_e32 v19, v2
	v_mov_b32_e32 v20, v2
	v_mov_b32_e32 v21, v2
	v_mov_b32_e32 v22, v2
	v_mov_b32_e32 v23, v2
	v_mov_b32_e32 v24, v2
	v_mov_b32_e32 v25, v2
	v_mov_b32_e32 v34, v2
	v_mov_b32_e32 v35, v2
	v_mov_b32_e32 v36, v2
	v_mov_b32_e32 v37, v2
	v_mov_b32_e32 v38, v2
	v_mov_b32_e32 v39, v2
	v_mov_b32_e32 v40, v2
	v_mov_b32_e32 v41, v2
	v_mov_b32_e32 v50, v2
	v_mov_b32_e32 v51, v2
	v_mov_b32_e32 v52, v2
	v_mov_b32_e32 v53, v2
	v_mov_b32_e32 v54, v2
	v_mov_b32_e32 v55, v2
	v_mov_b32_e32 v56, v2
	v_mov_b32_e32 v57, v2
	v_mov_b32_e32 v10, v2
	v_mov_b32_e32 v11, v2
	v_mov_b32_e32 v12, v2
	v_mov_b32_e32 v13, v2
	v_mov_b32_e32 v14, v2
	v_mov_b32_e32 v15, v2
	v_mov_b32_e32 v16, v2
	v_mov_b32_e32 v17, v2
	v_mov_b32_e32 v26, v2
	v_mov_b32_e32 v27, v2
	v_mov_b32_e32 v28, v2
	v_mov_b32_e32 v29, v2
	v_mov_b32_e32 v30, v2
	v_mov_b32_e32 v31, v2
	v_mov_b32_e32 v32, v2
	v_mov_b32_e32 v33, v2
	v_mov_b32_e32 v42, v2
	v_mov_b32_e32 v43, v2
	v_mov_b32_e32 v44, v2
	v_mov_b32_e32 v45, v2
	v_mov_b32_e32 v46, v2
	v_mov_b32_e32 v47, v2
	v_mov_b32_e32 v48, v2
	v_mov_b32_e32 v49, v2
	v_mov_b32_e32 v58, v2
	v_mov_b32_e32 v59, v2
	v_mov_b32_e32 v60, v2
	v_mov_b32_e32 v61, v2
	v_mov_b32_e32 v62, v2
	v_mov_b32_e32 v63, v2
	v_mov_b32_e32 v64, v2
	v_mov_b32_e32 v65, v2
	v_mov_b32_e32 v66, v2
	v_mov_b32_e32 v67, v2
	v_mov_b32_e32 v68, v2
	v_mov_b32_e32 v69, v2
	v_mov_b32_e32 v70, v2
	v_mov_b32_e32 v71, v2
	v_mov_b32_e32 v72, v2
	v_mov_b32_e32 v73, v2
	v_mov_b32_e32 v82, v2
	v_mov_b32_e32 v83, v2
	v_mov_b32_e32 v84, v2
	v_mov_b32_e32 v85, v2
	v_mov_b32_e32 v86, v2
	v_mov_b32_e32 v87, v2
	v_mov_b32_e32 v88, v2
	v_mov_b32_e32 v89, v2
	v_mov_b32_e32 v98, v2
	v_mov_b32_e32 v99, v2
	v_mov_b32_e32 v100, v2
	v_mov_b32_e32 v101, v2
	v_mov_b32_e32 v102, v2
	v_mov_b32_e32 v103, v2
	v_mov_b32_e32 v104, v2
	v_mov_b32_e32 v105, v2
	v_mov_b32_e32 v114, v2
	v_mov_b32_e32 v115, v2
	v_mov_b32_e32 v116, v2
	v_mov_b32_e32 v117, v2
	v_mov_b32_e32 v118, v2
	v_mov_b32_e32 v119, v2
	v_mov_b32_e32 v120, v2
	v_mov_b32_e32 v121, v2
	v_mov_b32_e32 v74, v2
	v_mov_b32_e32 v75, v2
	v_mov_b32_e32 v76, v2
	v_mov_b32_e32 v77, v2
	v_mov_b32_e32 v78, v2
	v_mov_b32_e32 v79, v2
	v_mov_b32_e32 v80, v2
	v_mov_b32_e32 v81, v2
	v_mov_b32_e32 v90, v2
	v_mov_b32_e32 v91, v2
	v_mov_b32_e32 v92, v2
	v_mov_b32_e32 v93, v2
	v_mov_b32_e32 v94, v2
	v_mov_b32_e32 v95, v2
	v_mov_b32_e32 v96, v2
	v_mov_b32_e32 v97, v2
	v_mov_b32_e32 v106, v2
	v_mov_b32_e32 v107, v2
	v_mov_b32_e32 v108, v2
	v_mov_b32_e32 v109, v2
	v_mov_b32_e32 v110, v2
	v_mov_b32_e32 v111, v2
	v_mov_b32_e32 v112, v2
	v_mov_b32_e32 v113, v2
	v_mov_b32_e32 v130, v2
	v_mov_b32_e32 v131, v2
	v_mov_b32_e32 v132, v2
	v_mov_b32_e32 v133, v2
	v_mov_b32_e32 v134, v2
	v_mov_b32_e32 v135, v2
	v_mov_b32_e32 v136, v2
	v_mov_b32_e32 v137, v2
	s_movk_i32 s92, 0x2b20
	s_andn2_b64 vcc, exec, s[40:41]
	s_cbranch_vccnz .LBB0_2895
	s_branch .LBB0_2896

.LBB0_2974:
	v_mov_b32_e32 v127, v1
	v_lshl_add_u64 v[8:9], s[36:37], 0, v[126:127]
	v_mov_b32_e32 v123, v1
	v_lshl_add_u64 v[10:11], s[36:37], 0, v[122:123]
	v_mov_b32_e32 v129, v1
	s_and_b32 s48, s21, 3
	s_add_i32 m0, s4, 0x18000
	v_lshl_add_u64 v[8:9], v[8:9], 0, s[56:57]
	v_lshl_add_u64 v[12:13], s[24:25], 0, v[128:129]
	v_mov_b32_e32 v125, v1
	s_lshl_b32 s20, s47, 13
	s_lshl_b32 s28, s48, 12
	s_waitcnt vmcnt(2)
	s_barrier
	global_load_lds_dwordx4 v[8:9], off
	v_lshl_add_u64 v[8:9], v[10:11], 0, s[56:57]
	s_add_i32 m0, s4, 0x1a000
	s_add_i32 s76, s4, 0x8000
	s_add_i32 s77, s4, 0xa000
	v_lshl_add_u64 v[14:15], s[24:25], 0, v[124:125]
	global_load_lds_dwordx4 v[8:9], off
	v_lshl_add_u64 v[8:9], v[12:13], 0, s[56:57]
	s_mov_b32 m0, s76
	s_add_u32 s26, s36, 0x100080
	global_load_lds_dwordx4 v[8:9], off
	v_lshl_add_u64 v[8:9], v[14:15], 0, s[56:57]
	s_mov_b32 m0, s77
	s_addc_u32 s27, s37, 0
	global_load_lds_dwordx4 v[8:9], off
	s_add_i32 m0, s4, 0x1c000
	s_nop 0
	global_load_lds_dwordx4 v126, s[26:27]
	v_lshl_add_u64 v[8:9], s[26:27], 0, v[122:123]
	s_add_i32 m0, s4, 0x1e000
	v_and_b32_e32 v0, 15, v239
	global_load_lds_dwordx4 v122, s[26:27]
	v_and_b32_e32 v8, 48, v239
	v_lshlrev_b32_e32 v9, 2, v239
	v_lshl_or_b32 v8, v0, 6, v8
	v_and_b32_e32 v9, 32, v9
	v_bitop3_b32 v10, v8, s20, v9 bitop3:0xde
	v_bitop3_b32 v146, v8, s28, v9 bitop3:0xde
	v_lshlrev_b32_e32 v8, 16, v2
	v_and_b32_e32 v8, 0xfffe0000, v8
	v_lshl_add_u32 v3, v3, 13, v8
	v_and_b32_e32 v2, 1, v2
	v_lshl_or_b32 v2, v2, 6, v3
	v_lshl_add_u32 v138, v4, 1, v2
	v_lshlrev_b32_e32 v2, 16, v6
	v_and_b32_e32 v2, 0xfffe0000, v2
	v_lshl_add_u32 v2, v5, 13, v2
	v_and_b32_e32 v3, 1, v6
	s_waitcnt vmcnt(6)
	v_lshl_or_b32 v2, v3, 6, v2
	v_mov_b32_e32 v4, v1
	v_mov_b32_e32 v5, v1
	v_lshl_add_u32 v140, v7, 1, v2
	v_mov_b32_e32 v2, v1
	v_mov_b32_e32 v3, v1
	v_add_u32_e32 v147, 0, v10
	v_mov_b64_e32 v[8:9], v[4:5]
	v_mov_b64_e32 v[20:21], v[4:5]
	v_mov_b64_e32 v[24:25], v[4:5]
	v_mov_b64_e32 v[36:37], v[4:5]
	v_mov_b64_e32 v[40:41], v[4:5]
	v_mov_b64_e32 v[52:53], v[4:5]
	v_mov_b64_e32 v[56:57], v[4:5]
	v_mov_b64_e32 v[12:13], v[4:5]
	v_mov_b64_e32 v[16:17], v[4:5]
	v_mov_b64_e32 v[28:29], v[4:5]
	v_mov_b64_e32 v[32:33], v[4:5]
	v_mov_b64_e32 v[44:45], v[4:5]
	v_mov_b64_e32 v[48:49], v[4:5]
	v_mov_b64_e32 v[60:61], v[4:5]
	v_mov_b64_e32 v[64:65], v[4:5]
	v_mov_b64_e32 v[68:69], v[4:5]
	v_mov_b64_e32 v[72:73], v[4:5]
	v_mov_b64_e32 v[84:85], v[4:5]
	v_mov_b64_e32 v[88:89], v[4:5]
	v_mov_b64_e32 v[100:101], v[4:5]
	v_mov_b64_e32 v[104:105], v[4:5]
	v_mov_b64_e32 v[116:117], v[4:5]
	v_mov_b64_e32 v[120:121], v[4:5]
	v_mov_b64_e32 v[76:77], v[4:5]
	v_mov_b64_e32 v[80:81], v[4:5]
	v_mov_b64_e32 v[92:93], v[4:5]
	v_mov_b64_e32 v[96:97], v[4:5]
	v_mov_b64_e32 v[108:109], v[4:5]
	v_mov_b64_e32 v[112:113], v[4:5]
	v_mov_b64_e32 v[132:133], v[4:5]
	v_mov_b64_e32 v[136:137], v[4:5]
	v_readlane_b32 s26, v254, 54
	v_lshl_or_b32 v224, s47, 6, v0
	v_mov_b32_e32 v139, v1
	v_mov_b32_e32 v141, v1
	s_mov_b32 s68, 0
	v_mov_b64_e32 v[6:7], v[2:3]
	v_mov_b64_e32 v[18:19], v[2:3]
	v_mov_b64_e32 v[22:23], v[2:3]
	v_mov_b64_e32 v[34:35], v[2:3]
	v_mov_b64_e32 v[38:39], v[2:3]
	v_mov_b64_e32 v[50:51], v[2:3]
	v_mov_b64_e32 v[54:55], v[2:3]
	v_mov_b64_e32 v[10:11], v[2:3]
	v_mov_b64_e32 v[14:15], v[2:3]
	v_mov_b64_e32 v[26:27], v[2:3]
	v_mov_b64_e32 v[30:31], v[2:3]
	v_mov_b64_e32 v[42:43], v[2:3]
	v_mov_b64_e32 v[46:47], v[2:3]
	v_mov_b64_e32 v[58:59], v[2:3]
	v_mov_b64_e32 v[62:63], v[2:3]
	v_mov_b64_e32 v[66:67], v[2:3]
	v_mov_b64_e32 v[70:71], v[2:3]
	v_mov_b64_e32 v[82:83], v[2:3]
	v_mov_b64_e32 v[86:87], v[2:3]
	v_mov_b64_e32 v[98:99], v[2:3]
	v_mov_b64_e32 v[102:103], v[2:3]
	v_mov_b64_e32 v[114:115], v[2:3]
	v_mov_b64_e32 v[118:119], v[2:3]
	v_mov_b64_e32 v[74:75], v[2:3]
	v_mov_b64_e32 v[78:79], v[2:3]
	v_mov_b64_e32 v[90:91], v[2:3]
	v_mov_b64_e32 v[94:95], v[2:3]
	v_mov_b64_e32 v[106:107], v[2:3]
	v_mov_b64_e32 v[110:111], v[2:3]
	v_mov_b64_e32 v[130:131], v[2:3]
	v_mov_b64_e32 v[134:135], v[2:3]
	v_readlane_b32 s20, v254, 58
	s_mov_b32 s78, s26
	s_barrier
	v_readlane_b32 s27, v254, 55

.LBB0_2982:
	s_add_u32 s42, s24, s36
	s_addc_u32 s43, s25, s37
	s_add_u32 s42, s42, 0x100
	s_addc_u32 s43, s43, 0
	s_add_u32 s50, s59, s36
	s_addc_u32 s64, s79, s37
	s_add_i32 s65, 0, 0x10000
	s_cmpk_eq_i32 s36, 0x1f00
	s_cselect_b32 s45, s29, s43
	s_cselect_b32 s44, s80, s42
	s_cselect_b32 s43, s27, s64
	s_cselect_b32 s42, s81, s50
	s_add_i32 s50, 0, 0x14000
	v_add_u32_e32 v160, s65, v146
	v_add_u32_e32 v176, s50, v146
	ds_read_b128 v[148:151], v160
	ds_read_b128 v[152:155], v160 offset:1024
	ds_read_b128 v[156:159], v160 offset:2048
	ds_read_b128 v[160:163], v160 offset:3072
	ds_read_b128 v[164:167], v176
	ds_read_b128 v[168:171], v176 offset:1024
	ds_read_b128 v[172:175], v176 offset:2048
	ds_read_b128 v[176:179], v176 offset:3072
	v_lshl_add_u64 v[208:209], v[144:145], 0, s[36:37]
	s_add_i32 m0, s4, 0xc000
	ds_read_b128 v[180:183], v147
	ds_read_b128 v[184:187], v147 offset:1024
	ds_read_b128 v[188:191], v147 offset:2048
	ds_read_b128 v[192:195], v147 offset:3072
	ds_read_b128 v[196:199], v147 offset:4096
	ds_read_b128 v[200:203], v147 offset:5120
	ds_read_b128 v[204:207], v147 offset:6144
	ds_read_b128 v[216:219], v147 offset:7168
	global_load_lds_dwordx4 v[208:209], off
	s_add_i32 m0, s4, 0xe000
	v_lshl_add_u64 v[208:209], v[142:143], 0, s[36:37]
	global_load_lds_dwordx4 v[208:209], off
	s_waitcnt vmcnt(8)
	s_waitcnt lgkmcnt(0)
	s_barrier
	s_setprio 1
	s_waitcnt lgkmcnt(0)
	v_mfma_f32_16x16x32_bf16 v[134:137], v[148:151], v[180:183], v[134:137]
	v_mfma_f32_16x16x32_bf16 v[130:133], v[156:159], v[180:183], v[130:133]
	v_mfma_f32_16x16x32_bf16 v[110:113], v[148:151], v[188:191], v[110:113]
	v_mfma_f32_16x16x32_bf16 v[106:109], v[156:159], v[188:191], v[106:109]
	v_mfma_f32_16x16x32_bf16 v[94:97], v[148:151], v[196:199], v[94:97]
	v_mfma_f32_16x16x32_bf16 v[90:93], v[156:159], v[196:199], v[90:93]
	v_mfma_f32_16x16x32_bf16 v[78:81], v[148:151], v[204:207], v[78:81]
	v_mfma_f32_16x16x32_bf16 v[74:77], v[156:159], v[204:207], v[74:77]
	v_mfma_f32_16x16x32_bf16 v[134:137], v[152:155], v[184:187], v[134:137]
	v_mfma_f32_16x16x32_bf16 v[130:133], v[160:163], v[184:187], v[130:133]
	v_mfma_f32_16x16x32_bf16 v[110:113], v[152:155], v[192:195], v[110:113]
	v_mfma_f32_16x16x32_bf16 v[106:109], v[160:163], v[192:195], v[106:109]
	v_mfma_f32_16x16x32_bf16 v[94:97], v[152:155], v[200:203], v[94:97]
	v_mfma_f32_16x16x32_bf16 v[90:93], v[160:163], v[200:203], v[90:93]
	v_mfma_f32_16x16x32_bf16 v[78:81], v[152:155], v[216:219], v[78:81]
	v_mfma_f32_16x16x32_bf16 v[74:77], v[160:163], v[216:219], v[74:77]
	s_setprio 0
	s_setprio 1
	v_mfma_f32_16x16x32_bf16 v[118:121], v[164:167], v[180:183], v[118:121]
	v_mfma_f32_16x16x32_bf16 v[114:117], v[172:175], v[180:183], v[114:117]
	v_mfma_f32_16x16x32_bf16 v[102:105], v[164:167], v[188:191], v[102:105]
	v_mfma_f32_16x16x32_bf16 v[98:101], v[172:175], v[188:191], v[98:101]
	v_mfma_f32_16x16x32_bf16 v[86:89], v[164:167], v[196:199], v[86:89]
	v_mfma_f32_16x16x32_bf16 v[82:85], v[172:175], v[196:199], v[82:85]
	v_mfma_f32_16x16x32_bf16 v[70:73], v[164:167], v[204:207], v[70:73]
	v_mfma_f32_16x16x32_bf16 v[66:69], v[172:175], v[204:207], v[66:69]
	v_mfma_f32_16x16x32_bf16 v[118:121], v[168:171], v[184:187], v[118:121]
	v_mfma_f32_16x16x32_bf16 v[114:117], v[176:179], v[184:187], v[114:117]
	v_mfma_f32_16x16x32_bf16 v[102:105], v[168:171], v[192:195], v[102:105]
	v_mfma_f32_16x16x32_bf16 v[98:101], v[176:179], v[192:195], v[98:101]
	v_mfma_f32_16x16x32_bf16 v[86:89], v[168:171], v[200:203], v[86:89]
	v_mfma_f32_16x16x32_bf16 v[82:85], v[176:179], v[200:203], v[82:85]
	v_mfma_f32_16x16x32_bf16 v[70:73], v[168:171], v[216:219], v[70:73]
	v_mfma_f32_16x16x32_bf16 v[66:69], v[176:179], v[216:219], v[66:69]
	s_setprio 0
	s_barrier
	s_add_i32 s64, s65, s63
	v_lshl_add_u64 v[208:209], s[42:43], 0, v[126:127]
	s_mov_b32 m0, s64
	ds_read_b128 v[180:183], v147 offset:16384
	ds_read_b128 v[184:187], v147 offset:17408
	ds_read_b128 v[188:191], v147 offset:18432
	ds_read_b128 v[192:195], v147 offset:19456
	ds_read_b128 v[196:199], v147 offset:20480
	ds_read_b128 v[200:203], v147 offset:21504
	ds_read_b128 v[204:207], v147 offset:22528
	ds_read_b128 v[216:219], v147 offset:23552
	global_load_lds_dwordx4 v126, s[42:43]
	s_add_i32 m0, s64, 0x2000
	s_add_u32 s84, s42, 0x100000
	v_lshl_add_u64 v[220:221], s[42:43], 0, v[122:123]
	s_addc_u32 s85, s43, 0
	s_add_i32 s50, s50, s63
	global_load_lds_dwordx4 v122, s[42:43]
	s_mov_b32 m0, s50
	v_lshl_add_u64 v[240:241], s[44:45], 0, v[124:125]
	global_load_lds_dwordx4 v126, s[84:85]
	s_add_i32 m0, s50, 0x2000
	s_nop 0
	global_load_lds_dwordx4 v122, s[84:85]
	s_mov_b32 m0, s4
	v_lshl_add_u64 v[222:223], s[44:45], 0, v[128:129]
	global_load_lds_dwordx4 v128, s[44:45]
	s_mov_b32 m0, s33
	s_nop 0
	global_load_lds_dwordx4 v124, s[44:45]
	s_waitcnt vmcnt(8)
	s_waitcnt lgkmcnt(0)
	s_barrier
	s_setprio 1
	s_waitcnt lgkmcnt(0)
	v_mfma_f32_16x16x32_bf16 v[62:65], v[148:151], v[180:183], v[62:65]
	v_mfma_f32_16x16x32_bf16 v[58:61], v[156:159], v[180:183], v[58:61]
	v_mfma_f32_16x16x32_bf16 v[46:49], v[148:151], v[188:191], v[46:49]
	v_mfma_f32_16x16x32_bf16 v[42:45], v[156:159], v[188:191], v[42:45]
	v_mfma_f32_16x16x32_bf16 v[30:33], v[148:151], v[196:199], v[30:33]
	v_mfma_f32_16x16x32_bf16 v[26:29], v[156:159], v[196:199], v[26:29]
	v_mfma_f32_16x16x32_bf16 v[14:17], v[148:151], v[204:207], v[14:17]
	v_mfma_f32_16x16x32_bf16 v[10:13], v[156:159], v[204:207], v[10:13]
	v_mfma_f32_16x16x32_bf16 v[62:65], v[152:155], v[184:187], v[62:65]
	v_mfma_f32_16x16x32_bf16 v[58:61], v[160:163], v[184:187], v[58:61]
	v_mfma_f32_16x16x32_bf16 v[46:49], v[152:155], v[192:195], v[46:49]
	v_mfma_f32_16x16x32_bf16 v[42:45], v[160:163], v[192:195], v[42:45]
	v_mfma_f32_16x16x32_bf16 v[30:33], v[152:155], v[200:203], v[30:33]
	v_mfma_f32_16x16x32_bf16 v[26:29], v[160:163], v[200:203], v[26:29]
	v_mfma_f32_16x16x32_bf16 v[14:17], v[152:155], v[216:219], v[14:17]
	v_mfma_f32_16x16x32_bf16 v[10:13], v[160:163], v[216:219], v[10:13]
	s_setprio 0
	s_setprio 1
	v_mfma_f32_16x16x32_bf16 v[54:57], v[164:167], v[180:183], v[54:57]
	v_mfma_f32_16x16x32_bf16 v[50:53], v[172:175], v[180:183], v[50:53]
	v_mfma_f32_16x16x32_bf16 v[38:41], v[164:167], v[188:191], v[38:41]
	v_mfma_f32_16x16x32_bf16 v[34:37], v[172:175], v[188:191], v[34:37]
	v_mfma_f32_16x16x32_bf16 v[22:25], v[164:167], v[196:199], v[22:25]
	v_mfma_f32_16x16x32_bf16 v[18:21], v[172:175], v[196:199], v[18:21]
	v_mfma_f32_16x16x32_bf16 v[6:9], v[164:167], v[204:207], v[6:9]
	v_mfma_f32_16x16x32_bf16 v[2:5], v[172:175], v[204:207], v[2:5]
	v_mfma_f32_16x16x32_bf16 v[54:57], v[168:171], v[184:187], v[54:57]
	v_mfma_f32_16x16x32_bf16 v[50:53], v[176:179], v[184:187], v[50:53]
	v_mfma_f32_16x16x32_bf16 v[38:41], v[168:171], v[192:195], v[38:41]
	v_mfma_f32_16x16x32_bf16 v[34:37], v[176:179], v[192:195], v[34:37]
	v_mfma_f32_16x16x32_bf16 v[22:25], v[168:171], v[200:203], v[22:25]
	v_mfma_f32_16x16x32_bf16 v[18:21], v[176:179], v[200:203], v[18:21]
	v_mfma_f32_16x16x32_bf16 v[6:9], v[168:171], v[216:219], v[6:9]
	v_mfma_f32_16x16x32_bf16 v[2:5], v[176:179], v[216:219], v[2:5]
	s_setprio 0
	s_barrier
	s_add_i32 s50, 0, 0x18000
	s_add_i32 s64, 0, 0x1c000
	v_add_u32_e32 v160, s50, v146
	v_add_u32_e32 v176, s64, v146
	ds_read_b128 v[148:151], v160
	ds_read_b128 v[152:155], v160 offset:1024
	ds_read_b128 v[156:159], v160 offset:2048
	ds_read_b128 v[160:163], v160 offset:3072
	ds_read_b128 v[164:167], v176
	ds_read_b128 v[168:171], v176 offset:1024
	ds_read_b128 v[172:175], v176 offset:2048
	ds_read_b128 v[176:179], v176 offset:3072
	s_add_u32 s44, s44, 0x100000
	s_addc_u32 s45, s45, 0
	s_mov_b32 m0, s70
	ds_read_b128 v[180:183], v147 offset:32768
	ds_read_b128 v[184:187], v147 offset:33792
	ds_read_b128 v[188:191], v147 offset:34816
	ds_read_b128 v[192:195], v147 offset:35840
	ds_read_b128 v[196:199], v147 offset:36864
	ds_read_b128 v[200:203], v147 offset:37888
	ds_read_b128 v[204:207], v147 offset:38912
	ds_read_b128 v[216:219], v147 offset:39936
	global_load_lds_dwordx4 v128, s[44:45]
	s_mov_b32 m0, s71
	v_lshl_add_u64 v[242:243], s[44:45], 0, v[124:125]
	global_load_lds_dwordx4 v124, s[44:45]
	s_waitcnt vmcnt(8)
	s_waitcnt lgkmcnt(0)
	s_barrier
	s_setprio 1
	s_waitcnt lgkmcnt(0)
	v_mfma_f32_16x16x32_bf16 v[134:137], v[148:151], v[180:183], v[134:137]
	v_mfma_f32_16x16x32_bf16 v[130:133], v[156:159], v[180:183], v[130:133]
	v_mfma_f32_16x16x32_bf16 v[110:113], v[148:151], v[188:191], v[110:113]
	v_mfma_f32_16x16x32_bf16 v[106:109], v[156:159], v[188:191], v[106:109]
	v_mfma_f32_16x16x32_bf16 v[94:97], v[148:151], v[196:199], v[94:97]
	v_mfma_f32_16x16x32_bf16 v[90:93], v[156:159], v[196:199], v[90:93]
	v_mfma_f32_16x16x32_bf16 v[78:81], v[148:151], v[204:207], v[78:81]
	v_mfma_f32_16x16x32_bf16 v[74:77], v[156:159], v[204:207], v[74:77]
	v_mfma_f32_16x16x32_bf16 v[134:137], v[152:155], v[184:187], v[134:137]
	v_mfma_f32_16x16x32_bf16 v[130:133], v[160:163], v[184:187], v[130:133]
	v_mfma_f32_16x16x32_bf16 v[110:113], v[152:155], v[192:195], v[110:113]
	v_mfma_f32_16x16x32_bf16 v[106:109], v[160:163], v[192:195], v[106:109]
	v_mfma_f32_16x16x32_bf16 v[94:97], v[152:155], v[200:203], v[94:97]
	v_mfma_f32_16x16x32_bf16 v[90:93], v[160:163], v[200:203], v[90:93]
	v_mfma_f32_16x16x32_bf16 v[78:81], v[152:155], v[216:219], v[78:81]
	v_mfma_f32_16x16x32_bf16 v[74:77], v[160:163], v[216:219], v[74:77]
	s_setprio 0
	s_setprio 1
	v_mfma_f32_16x16x32_bf16 v[118:121], v[164:167], v[180:183], v[118:121]
	v_mfma_f32_16x16x32_bf16 v[114:117], v[172:175], v[180:183], v[114:117]
	v_mfma_f32_16x16x32_bf16 v[102:105], v[164:167], v[188:191], v[102:105]
	v_mfma_f32_16x16x32_bf16 v[98:101], v[172:175], v[188:191], v[98:101]
	v_mfma_f32_16x16x32_bf16 v[86:89], v[164:167], v[196:199], v[86:89]
	v_mfma_f32_16x16x32_bf16 v[82:85], v[172:175], v[196:199], v[82:85]
	v_mfma_f32_16x16x32_bf16 v[70:73], v[164:167], v[204:207], v[70:73]
	v_mfma_f32_16x16x32_bf16 v[66:69], v[172:175], v[204:207], v[66:69]
	v_mfma_f32_16x16x32_bf16 v[118:121], v[168:171], v[184:187], v[118:121]
	v_mfma_f32_16x16x32_bf16 v[114:117], v[176:179], v[184:187], v[114:117]
	v_mfma_f32_16x16x32_bf16 v[102:105], v[168:171], v[192:195], v[102:105]
	v_mfma_f32_16x16x32_bf16 v[98:101], v[176:179], v[192:195], v[98:101]
	v_mfma_f32_16x16x32_bf16 v[86:89], v[168:171], v[200:203], v[86:89]
	v_mfma_f32_16x16x32_bf16 v[82:85], v[176:179], v[200:203], v[82:85]
	v_mfma_f32_16x16x32_bf16 v[70:73], v[168:171], v[216:219], v[70:73]
	v_mfma_f32_16x16x32_bf16 v[66:69], v[176:179], v[216:219], v[66:69]
	s_setprio 0
	s_barrier
	s_add_i32 s44, s50, s63
	v_lshl_add_u64 v[208:209], v[208:209], 0, s[56:57]
	s_mov_b32 m0, s44
	ds_read_b128 v[180:183], v147 offset:49152
	ds_read_b128 v[184:187], v147 offset:50176
	ds_read_b128 v[188:191], v147 offset:51200
	ds_read_b128 v[192:195], v147 offset:52224
	ds_read_b128 v[196:199], v147 offset:53248
	ds_read_b128 v[200:203], v147 offset:54272
	ds_read_b128 v[204:207], v147 offset:55296
	ds_read_b128 v[216:219], v147 offset:56320
	global_load_lds_dwordx4 v[208:209], off
	s_add_i32 m0, s44, 0x2000
	s_add_u32 s42, s42, 0x100080
	v_lshl_add_u64 v[208:209], v[220:221], 0, s[56:57]
	s_addc_u32 s43, s43, 0
	s_add_i32 s44, s64, s63
	global_load_lds_dwordx4 v[208:209], off
	s_mov_b32 m0, s44
	s_nop 0
	global_load_lds_dwordx4 v126, s[42:43]
	s_add_i32 m0, s44, 0x2000
	s_nop 0
	global_load_lds_dwordx4 v122, s[42:43]
	s_mov_b32 m0, s76
	v_lshl_add_u64 v[208:209], v[222:223], 0, s[56:57]
	global_load_lds_dwordx4 v[208:209], off
	s_mov_b32 m0, s77
	v_lshl_add_u64 v[208:209], v[240:241], 0, s[56:57]
	global_load_lds_dwordx4 v[208:209], off
	s_waitcnt vmcnt(8)
	s_waitcnt lgkmcnt(0)
	s_barrier
	s_setprio 1
	s_waitcnt lgkmcnt(0)
	v_mfma_f32_16x16x32_bf16 v[62:65], v[148:151], v[180:183], v[62:65]
	v_mfma_f32_16x16x32_bf16 v[58:61], v[156:159], v[180:183], v[58:61]
	v_mfma_f32_16x16x32_bf16 v[46:49], v[148:151], v[188:191], v[46:49]
	v_mfma_f32_16x16x32_bf16 v[42:45], v[156:159], v[188:191], v[42:45]
	v_mfma_f32_16x16x32_bf16 v[30:33], v[148:151], v[196:199], v[30:33]
	v_mfma_f32_16x16x32_bf16 v[26:29], v[156:159], v[196:199], v[26:29]
	v_mfma_f32_16x16x32_bf16 v[14:17], v[148:151], v[204:207], v[14:17]
	v_mfma_f32_16x16x32_bf16 v[10:13], v[156:159], v[204:207], v[10:13]
	v_mfma_f32_16x16x32_bf16 v[62:65], v[152:155], v[184:187], v[62:65]
	v_mfma_f32_16x16x32_bf16 v[58:61], v[160:163], v[184:187], v[58:61]
	v_mfma_f32_16x16x32_bf16 v[46:49], v[152:155], v[192:195], v[46:49]
	v_mfma_f32_16x16x32_bf16 v[42:45], v[160:163], v[192:195], v[42:45]
	v_mfma_f32_16x16x32_bf16 v[30:33], v[152:155], v[200:203], v[30:33]
	v_mfma_f32_16x16x32_bf16 v[26:29], v[160:163], v[200:203], v[26:29]
	v_mfma_f32_16x16x32_bf16 v[14:17], v[152:155], v[216:219], v[14:17]
	v_mfma_f32_16x16x32_bf16 v[10:13], v[160:163], v[216:219], v[10:13]
	s_setprio 0
	s_setprio 1
	v_mfma_f32_16x16x32_bf16 v[54:57], v[164:167], v[180:183], v[54:57]
	v_mfma_f32_16x16x32_bf16 v[50:53], v[172:175], v[180:183], v[50:53]
	v_mfma_f32_16x16x32_bf16 v[38:41], v[164:167], v[188:191], v[38:41]
	v_mfma_f32_16x16x32_bf16 v[34:37], v[172:175], v[188:191], v[34:37]
	v_mfma_f32_16x16x32_bf16 v[22:25], v[164:167], v[196:199], v[22:25]
	v_mfma_f32_16x16x32_bf16 v[18:21], v[172:175], v[196:199], v[18:21]
	v_mfma_f32_16x16x32_bf16 v[6:9], v[164:167], v[204:207], v[6:9]
	v_mfma_f32_16x16x32_bf16 v[2:5], v[172:175], v[204:207], v[2:5]
	v_mfma_f32_16x16x32_bf16 v[54:57], v[168:171], v[184:187], v[54:57]
	v_mfma_f32_16x16x32_bf16 v[50:53], v[176:179], v[184:187], v[50:53]
	v_mfma_f32_16x16x32_bf16 v[38:41], v[168:171], v[192:195], v[38:41]
	v_mfma_f32_16x16x32_bf16 v[34:37], v[176:179], v[192:195], v[34:37]
	v_mfma_f32_16x16x32_bf16 v[22:25], v[168:171], v[200:203], v[22:25]
	v_mfma_f32_16x16x32_bf16 v[18:21], v[176:179], v[200:203], v[18:21]
	v_mfma_f32_16x16x32_bf16 v[6:9], v[168:171], v[216:219], v[6:9]
	v_mfma_f32_16x16x32_bf16 v[2:5], v[176:179], v[216:219], v[2:5]
	s_setprio 0
	s_barrier
	s_add_i32 s82, s82, 2
	s_add_u32 s36, s36, 0x100
	s_addc_u32 s37, s37, 0
	s_cmp_gt_u32 s82, 61
	s_cbranch_scc0 .LBB0_2982
	s_add_u32 s36, s59, 0xffffff00
	s_addc_u32 s37, s79, -1
	s_andn2_b64 vcc, exec, s[40:41]
	s_cbranch_vccnz .LBB0_2985
	v_mov_b32_e32 v2, 0
	s_mov_b32 s20, s26
	s_mov_b32 s78, s28
	s_mov_b64 s[24:25], s[34:35]
	s_mov_b32 s68, s58
	v_mov_b32_e32 v3, v2
	v_mov_b32_e32 v4, v2
	v_mov_b32_e32 v5, v2
	v_mov_b32_e32 v6, v2
	v_mov_b32_e32 v7, v2
	v_mov_b32_e32 v8, v2
	v_mov_b32_e32 v9, v2
	v_mov_b32_e32 v18, v2
	v_mov_b32_e32 v19, v2
	v_mov_b32_e32 v20, v2
	v_mov_b32_e32 v21, v2
	v_mov_b32_e32 v22, v2
	v_mov_b32_e32 v23, v2
	v_mov_b32_e32 v24, v2
	v_mov_b32_e32 v25, v2
	v_mov_b32_e32 v34, v2
	v_mov_b32_e32 v35, v2
	v_mov_b32_e32 v36, v2
	v_mov_b32_e32 v37, v2
	v_mov_b32_e32 v38, v2
	v_mov_b32_e32 v39, v2
	v_mov_b32_e32 v40, v2
	v_mov_b32_e32 v41, v2
	v_mov_b32_e32 v50, v2
	v_mov_b32_e32 v51, v2
	v_mov_b32_e32 v52, v2
	v_mov_b32_e32 v53, v2
	v_mov_b32_e32 v54, v2
	v_mov_b32_e32 v55, v2
	v_mov_b32_e32 v56, v2
	v_mov_b32_e32 v57, v2
	v_mov_b32_e32 v10, v2
	v_mov_b32_e32 v11, v2
	v_mov_b32_e32 v12, v2
	v_mov_b32_e32 v13, v2
	v_mov_b32_e32 v14, v2
	v_mov_b32_e32 v15, v2
	v_mov_b32_e32 v16, v2
	v_mov_b32_e32 v17, v2
	v_mov_b32_e32 v26, v2
	v_mov_b32_e32 v27, v2
	v_mov_b32_e32 v28, v2
	v_mov_b32_e32 v29, v2
	v_mov_b32_e32 v30, v2
	v_mov_b32_e32 v31, v2
	v_mov_b32_e32 v32, v2
	v_mov_b32_e32 v33, v2
	v_mov_b32_e32 v42, v2
	v_mov_b32_e32 v43, v2
	v_mov_b32_e32 v44, v2
	v_mov_b32_e32 v45, v2
	v_mov_b32_e32 v46, v2
	v_mov_b32_e32 v47, v2
	v_mov_b32_e32 v48, v2
	v_mov_b32_e32 v49, v2
	v_mov_b32_e32 v58, v2
	v_mov_b32_e32 v59, v2
	v_mov_b32_e32 v60, v2
	v_mov_b32_e32 v61, v2
	v_mov_b32_e32 v62, v2
	v_mov_b32_e32 v63, v2
	v_mov_b32_e32 v64, v2
	v_mov_b32_e32 v65, v2
	v_mov_b32_e32 v66, v2
	v_mov_b32_e32 v67, v2
	v_mov_b32_e32 v68, v2
	v_mov_b32_e32 v69, v2
	v_mov_b32_e32 v70, v2
	v_mov_b32_e32 v71, v2
	v_mov_b32_e32 v72, v2
	v_mov_b32_e32 v73, v2
	v_mov_b32_e32 v82, v2
	v_mov_b32_e32 v83, v2
	v_mov_b32_e32 v84, v2
	v_mov_b32_e32 v85, v2
	v_mov_b32_e32 v86, v2
	v_mov_b32_e32 v87, v2
	v_mov_b32_e32 v88, v2
	v_mov_b32_e32 v89, v2
	v_mov_b32_e32 v98, v2
	v_mov_b32_e32 v99, v2
	v_mov_b32_e32 v100, v2
	v_mov_b32_e32 v101, v2
	v_mov_b32_e32 v102, v2
	v_mov_b32_e32 v103, v2
	v_mov_b32_e32 v104, v2
	v_mov_b32_e32 v105, v2
	v_mov_b32_e32 v114, v2
	v_mov_b32_e32 v115, v2
	v_mov_b32_e32 v116, v2
	v_mov_b32_e32 v117, v2
	v_mov_b32_e32 v118, v2
	v_mov_b32_e32 v119, v2
	v_mov_b32_e32 v120, v2
	v_mov_b32_e32 v121, v2
	v_mov_b32_e32 v74, v2
	v_mov_b32_e32 v75, v2
	v_mov_b32_e32 v76, v2
	v_mov_b32_e32 v77, v2
	v_mov_b32_e32 v78, v2
	v_mov_b32_e32 v79, v2
	v_mov_b32_e32 v80, v2
	v_mov_b32_e32 v81, v2
	v_mov_b32_e32 v90, v2
	v_mov_b32_e32 v91, v2
	v_mov_b32_e32 v92, v2
	v_mov_b32_e32 v93, v2
	v_mov_b32_e32 v94, v2
	v_mov_b32_e32 v95, v2
	v_mov_b32_e32 v96, v2
	v_mov_b32_e32 v97, v2
	v_mov_b32_e32 v106, v2
	v_mov_b32_e32 v107, v2
	v_mov_b32_e32 v108, v2
	v_mov_b32_e32 v109, v2
	v_mov_b32_e32 v110, v2
	v_mov_b32_e32 v111, v2
	v_mov_b32_e32 v112, v2
	v_mov_b32_e32 v113, v2
	v_mov_b32_e32 v130, v2
	v_mov_b32_e32 v131, v2
	v_mov_b32_e32 v132, v2
	v_mov_b32_e32 v133, v2
	v_mov_b32_e32 v134, v2
	v_mov_b32_e32 v135, v2
	v_mov_b32_e32 v136, v2
	v_mov_b32_e32 v137, v2
	s_andn2_b64 vcc, exec, s[38:39]
	s_cbranch_vccnz .LBB0_2986
	s_branch .LBB0_2987
